# speedup vs baseline: 1.0034x; 1.0034x over previous
.Lpf_vQ:
	s_lshl_b32 s25, s25, 6
	s_add_u32 s29, s10, s25
	s_lshr_b32 s29, s29, 4
	v_add_u32_e32 v5, s25, v3
	v_lshlrev_b32_e32 v5, 7, v5
	v_add_u32_e32 v15, v5, v6
	v_add_u32_e32 v16, v5, v7
	v_add_u32_e32 v5, 0x8000, v9
	v_add_u32_e32 v17, v5, v6
	v_add_u32_e32 v18, v5, v7
	v_add_u32_e32 v19, 0x18000, v15
	v_add_u32_e32 v20, 0x18000, v16
	v_add_u32_e32 v21, 0x18000, v17
	v_add_u32_e32 v22, 0x18000, v18
	v_lshlrev_b32_e32 v5, 4, v4
	global_load_dwordx4 v[24:27], v5, s[14:15] offset:0
	global_load_dwordx4 v[28:31], v5, s[14:15] offset:64
	global_load_dwordx4 v[32:35], v5, s[14:15] offset:128
	global_load_dwordx4 v[36:39], v5, s[14:15] offset:192
	global_load_dwordx4 v[40:43], v5, s[16:17] offset:0
	global_load_dwordx4 v[44:47], v5, s[16:17] offset:64
	global_load_dwordx4 v[48:51], v5, s[16:17] offset:128
	global_load_dwordx4 v[52:55], v5, s[16:17] offset:192
	s_add_u32 m0, s28, 0x0
	s_nop 0
	global_load_lds_dwordx4 v10, s[4:5]
	s_add_u32 m0, s28, 0x2000
	s_nop 0
	global_load_lds_dwordx4 v11, s[4:5]
	s_add_u32 m0, s28, 0x4000
	s_nop 0
	global_load_lds_dwordx4 v12, s[4:5]
	s_add_u32 m0, s28, 0x6000
	s_nop 0
	global_load_lds_dwordx4 v13, s[4:5]
	s_add_u32 s4, s4, s20
	s_addc_u32 s5, s5, 0
	s_add_u32 m0, s28, 0x8000
	s_nop 0
	global_load_lds_dwordx4 v10, s[6:7]
	s_add_u32 m0, s28, 0xa000
	s_nop 0
	global_load_lds_dwordx4 v11, s[6:7]
	s_add_u32 s6, s6, s20
	s_addc_u32 s7, s7, 0
	s_add_u32 m0, s28, 0xc000
	s_nop 0
	global_load_lds_dwordx4 v10, s[4:5]
	s_add_u32 m0, s28, 0xe000
	s_nop 0
	global_load_lds_dwordx4 v11, s[4:5]
	s_add_u32 m0, s28, 0x10000
	s_nop 0
	global_load_lds_dwordx4 v12, s[4:5]
	s_add_u32 m0, s28, 0x12000
	s_nop 0
	global_load_lds_dwordx4 v13, s[4:5]
	s_add_u32 s4, s4, s20
	s_addc_u32 s5, s5, 0
	s_add_u32 m0, s28, 0x14000
	s_nop 0
	global_load_lds_dwordx4 v10, s[6:7]
	s_add_u32 m0, s28, 0x16000
	s_nop 0
	global_load_lds_dwordx4 v11, s[6:7]
	s_add_u32 s6, s6, s20
	s_addc_u32 s7, s7, 0
	s_add_u32 m0, s28, 0x18000
	s_nop 0
	global_load_lds_dwordx4 v10, s[4:5]
	s_add_u32 m0, s28, 0x1a000
	s_nop 0
	global_load_lds_dwordx4 v11, s[4:5]
	s_add_u32 m0, s28, 0x1c000
	s_nop 0
	global_load_lds_dwordx4 v12, s[4:5]
	s_add_u32 m0, s28, 0x1e000
	s_nop 0
	global_load_lds_dwordx4 v13, s[4:5]
	s_add_u32 s4, s4, s20
	s_addc_u32 s5, s5, 0
	s_add_u32 m0, s28, 0x20000
	s_nop 0
	global_load_lds_dwordx4 v10, s[6:7]
	s_add_u32 m0, s28, 0x22000
	s_nop 0
	global_load_lds_dwordx4 v11, s[6:7]
	s_add_u32 s6, s6, s20
	s_addc_u32 s7, s7, 0
	s_waitcnt vmcnt(12) lgkmcnt(0)
	s_barrier
	s_waitcnt lgkmcnt(7)
	ds_read_b128 v[136:139], v15
	ds_read_b128 v[156:159], v17
	ds_read_b128 v[160:163], v17 offset:2048
	ds_read_b128 v[164:167], v17 offset:4096
	ds_read_b128 v[168:171], v17 offset:6144
	ds_read_b128 v[140:143], v15 offset:2048
	ds_read_b128 v[144:147], v15 offset:4096
	ds_read_b128 v[148:151], v15 offset:6144
	s_waitcnt lgkmcnt(7)
	ds_read_b128 v[172:175], v16
	ds_read_b128 v[192:195], v18
	ds_read_b128 v[196:199], v18 offset:2048
	ds_read_b128 v[200:203], v18 offset:4096
	ds_read_b128 v[204:207], v18 offset:6144
	ds_read_b128 v[176:179], v16 offset:2048
	ds_read_b128 v[180:183], v16 offset:4096
	ds_read_b128 v[184:187], v16 offset:6144
	s_waitcnt lgkmcnt(14)
	v_mfma_f32_16x16x32_f16 v[56:59], v[156:159], v[136:139], 0
	s_waitcnt lgkmcnt(13)
	v_mfma_f32_16x16x32_f16 v[60:63], v[160:163], v[136:139], 0
	s_waitcnt lgkmcnt(12)
	v_mfma_f32_16x16x32_f16 v[64:67], v[164:167], v[136:139], 0
	s_waitcnt lgkmcnt(11)
	v_mfma_f32_16x16x32_f16 v[68:71], v[168:171], v[136:139], 0
	s_waitcnt lgkmcnt(10)
	v_mfma_f32_16x16x32_f16 v[72:75], v[156:159], v[140:143], 0
	v_mfma_f32_16x16x32_f16 v[76:79], v[160:163], v[140:143], 0
	v_mfma_f32_16x16x32_f16 v[80:83], v[164:167], v[140:143], 0
	v_mfma_f32_16x16x32_f16 v[84:87], v[168:171], v[140:143], 0
	s_waitcnt lgkmcnt(9)
	v_mfma_f32_16x16x32_f16 v[88:91], v[156:159], v[144:147], 0
	v_mfma_f32_16x16x32_f16 v[92:95], v[160:163], v[144:147], 0
	v_mfma_f32_16x16x32_f16 v[96:99], v[164:167], v[144:147], 0
	v_mfma_f32_16x16x32_f16 v[100:103], v[168:171], v[144:147], 0
	s_waitcnt lgkmcnt(8)
	v_mfma_f32_16x16x32_f16 v[104:107], v[156:159], v[148:151], 0
	v_mfma_f32_16x16x32_f16 v[108:111], v[160:163], v[148:151], 0
	v_mfma_f32_16x16x32_f16 v[112:115], v[164:167], v[148:151], 0
	v_mfma_f32_16x16x32_f16 v[116:119], v[168:171], v[148:151], 0
	s_waitcnt vmcnt(6) lgkmcnt(0)
	s_barrier
	s_waitcnt lgkmcnt(7)
	ds_read_b128 v[136:139], v15 offset:49152
	ds_read_b128 v[156:159], v17 offset:49152
	ds_read_b128 v[160:163], v17 offset:51200
	ds_read_b128 v[164:167], v17 offset:53248
	ds_read_b128 v[168:171], v17 offset:55296
	ds_read_b128 v[140:143], v15 offset:51200
	ds_read_b128 v[144:147], v15 offset:53248
	ds_read_b128 v[148:151], v15 offset:55296
	s_waitcnt lgkmcnt(14)
	v_mfma_f32_16x16x32_f16 v[56:59], v[192:195], v[172:175], v[56:59]
	s_add_u32 m0, s28, 0x0
	s_nop 0
	global_load_lds_dwordx4 v10, s[4:5]
	s_waitcnt lgkmcnt(13)
	v_mfma_f32_16x16x32_f16 v[60:63], v[196:199], v[172:175], v[60:63]
	s_waitcnt lgkmcnt(12)
	v_mfma_f32_16x16x32_f16 v[64:67], v[200:203], v[172:175], v[64:67]
	s_waitcnt lgkmcnt(11)
	v_mfma_f32_16x16x32_f16 v[68:71], v[204:207], v[172:175], v[68:71]
	s_waitcnt lgkmcnt(10)
	v_mfma_f32_16x16x32_f16 v[72:75], v[192:195], v[176:179], v[72:75]
	v_mfma_f32_16x16x32_f16 v[76:79], v[196:199], v[176:179], v[76:79]
	s_add_u32 m0, s28, 0x2000
	s_nop 0
	global_load_lds_dwordx4 v11, s[4:5]
	v_mfma_f32_16x16x32_f16 v[80:83], v[200:203], v[176:179], v[80:83]
	v_mfma_f32_16x16x32_f16 v[84:87], v[204:207], v[176:179], v[84:87]
	s_waitcnt lgkmcnt(9)
	v_mfma_f32_16x16x32_f16 v[88:91], v[192:195], v[180:183], v[88:91]
	v_mfma_f32_16x16x32_f16 v[92:95], v[196:199], v[180:183], v[92:95]
	v_mfma_f32_16x16x32_f16 v[96:99], v[200:203], v[180:183], v[96:99]
	s_add_u32 m0, s28, 0x4000
	s_nop 0
	global_load_lds_dwordx4 v12, s[4:5]
	v_mfma_f32_16x16x32_f16 v[100:103], v[204:207], v[180:183], v[100:103]
	s_waitcnt lgkmcnt(8)
	v_mfma_f32_16x16x32_f16 v[104:107], v[192:195], v[184:187], v[104:107]
	v_mfma_f32_16x16x32_f16 v[108:111], v[196:199], v[184:187], v[108:111]
	v_mfma_f32_16x16x32_f16 v[112:115], v[200:203], v[184:187], v[112:115]
	v_mfma_f32_16x16x32_f16 v[116:119], v[204:207], v[184:187], v[116:119]
	s_waitcnt lgkmcnt(7)
	ds_read_b128 v[172:175], v16 offset:49152
	ds_read_b128 v[192:195], v18 offset:49152
	ds_read_b128 v[196:199], v18 offset:51200
	ds_read_b128 v[200:203], v18 offset:53248
	ds_read_b128 v[204:207], v18 offset:55296
	ds_read_b128 v[176:179], v16 offset:51200
	ds_read_b128 v[180:183], v16 offset:53248
	ds_read_b128 v[184:187], v16 offset:55296
	s_waitcnt lgkmcnt(14)
	v_mfma_f32_16x16x32_f16 v[56:59], v[156:159], v[136:139], v[56:59]
	s_add_u32 m0, s28, 0x6000
	s_nop 0
	global_load_lds_dwordx4 v13, s[4:5]
	s_add_u32 s4, s4, s20
	s_addc_u32 s5, s5, 0
	s_waitcnt lgkmcnt(13)
	v_mfma_f32_16x16x32_f16 v[60:63], v[160:163], v[136:139], v[60:63]
	s_waitcnt lgkmcnt(12)
	v_mfma_f32_16x16x32_f16 v[64:67], v[164:167], v[136:139], v[64:67]
	s_waitcnt lgkmcnt(11)
	v_mfma_f32_16x16x32_f16 v[68:71], v[168:171], v[136:139], v[68:71]
	s_waitcnt lgkmcnt(10)
	v_mfma_f32_16x16x32_f16 v[72:75], v[156:159], v[140:143], v[72:75]
	v_mfma_f32_16x16x32_f16 v[76:79], v[160:163], v[140:143], v[76:79]
	s_add_u32 m0, s28, 0x8000
	s_nop 0
	global_load_lds_dwordx4 v10, s[6:7]
	v_mfma_f32_16x16x32_f16 v[80:83], v[164:167], v[140:143], v[80:83]
	v_mfma_f32_16x16x32_f16 v[84:87], v[168:171], v[140:143], v[84:87]
	s_waitcnt lgkmcnt(9)
	v_mfma_f32_16x16x32_f16 v[88:91], v[156:159], v[144:147], v[88:91]
	v_mfma_f32_16x16x32_f16 v[92:95], v[160:163], v[144:147], v[92:95]
	v_mfma_f32_16x16x32_f16 v[96:99], v[164:167], v[144:147], v[96:99]
	s_add_u32 m0, s28, 0xa000
	s_nop 0
	global_load_lds_dwordx4 v11, s[6:7]
	s_add_u32 s6, s6, s20
	s_addc_u32 s7, s7, 0
	v_mfma_f32_16x16x32_f16 v[100:103], v[168:171], v[144:147], v[100:103]
	s_waitcnt lgkmcnt(8)
	v_mfma_f32_16x16x32_f16 v[104:107], v[156:159], v[148:151], v[104:107]
	v_mfma_f32_16x16x32_f16 v[108:111], v[160:163], v[148:151], v[108:111]
	v_mfma_f32_16x16x32_f16 v[112:115], v[164:167], v[148:151], v[112:115]
	v_mfma_f32_16x16x32_f16 v[116:119], v[168:171], v[148:151], v[116:119]
	s_waitcnt vmcnt(6) lgkmcnt(0)
	s_barrier
	s_waitcnt lgkmcnt(7)
	ds_read_b128 v[136:139], v19
	ds_read_b128 v[156:159], v21
	ds_read_b128 v[160:163], v21 offset:2048
	ds_read_b128 v[164:167], v21 offset:4096
	ds_read_b128 v[168:171], v21 offset:6144
	ds_read_b128 v[140:143], v19 offset:2048
	ds_read_b128 v[144:147], v19 offset:4096
	ds_read_b128 v[148:151], v19 offset:6144
	s_waitcnt lgkmcnt(14)
	v_mfma_f32_16x16x32_f16 v[56:59], v[192:195], v[172:175], v[56:59]
	s_add_u32 m0, s28, 0xc000
	s_nop 0
	global_load_lds_dwordx4 v10, s[4:5]
	s_waitcnt lgkmcnt(13)
	v_mfma_f32_16x16x32_f16 v[60:63], v[196:199], v[172:175], v[60:63]
	s_waitcnt lgkmcnt(12)
	v_mfma_f32_16x16x32_f16 v[64:67], v[200:203], v[172:175], v[64:67]
	s_waitcnt lgkmcnt(11)
	v_mfma_f32_16x16x32_f16 v[68:71], v[204:207], v[172:175], v[68:71]
	s_waitcnt lgkmcnt(10)
	v_mfma_f32_16x16x32_f16 v[72:75], v[192:195], v[176:179], v[72:75]
	v_mfma_f32_16x16x32_f16 v[76:79], v[196:199], v[176:179], v[76:79]
	s_add_u32 m0, s28, 0xe000
	s_nop 0
	global_load_lds_dwordx4 v11, s[4:5]
	v_mfma_f32_16x16x32_f16 v[80:83], v[200:203], v[176:179], v[80:83]
	v_mfma_f32_16x16x32_f16 v[84:87], v[204:207], v[176:179], v[84:87]
	s_waitcnt lgkmcnt(9)
	v_mfma_f32_16x16x32_f16 v[88:91], v[192:195], v[180:183], v[88:91]
	v_mfma_f32_16x16x32_f16 v[92:95], v[196:199], v[180:183], v[92:95]
	v_mfma_f32_16x16x32_f16 v[96:99], v[200:203], v[180:183], v[96:99]
	s_add_u32 m0, s28, 0x10000
	s_nop 0
	global_load_lds_dwordx4 v12, s[4:5]
	v_mfma_f32_16x16x32_f16 v[100:103], v[204:207], v[180:183], v[100:103]
	s_waitcnt lgkmcnt(8)
	v_mfma_f32_16x16x32_f16 v[104:107], v[192:195], v[184:187], v[104:107]
	v_mfma_f32_16x16x32_f16 v[108:111], v[196:199], v[184:187], v[108:111]
	v_mfma_f32_16x16x32_f16 v[112:115], v[200:203], v[184:187], v[112:115]
	v_mfma_f32_16x16x32_f16 v[116:119], v[204:207], v[184:187], v[116:119]
	s_waitcnt lgkmcnt(7)
	ds_read_b128 v[172:175], v20
	ds_read_b128 v[192:195], v22
	ds_read_b128 v[196:199], v22 offset:2048
	ds_read_b128 v[200:203], v22 offset:4096
	ds_read_b128 v[204:207], v22 offset:6144
	ds_read_b128 v[176:179], v20 offset:2048
	ds_read_b128 v[180:183], v20 offset:4096
	ds_read_b128 v[184:187], v20 offset:6144
	s_waitcnt lgkmcnt(14)
	v_mfma_f32_16x16x32_f16 v[56:59], v[156:159], v[136:139], v[56:59]
	s_add_u32 m0, s28, 0x12000
	s_nop 0
	global_load_lds_dwordx4 v13, s[4:5]
	s_add_u32 s4, s4, s20
	s_addc_u32 s5, s5, 0
	s_waitcnt lgkmcnt(13)
	v_mfma_f32_16x16x32_f16 v[60:63], v[160:163], v[136:139], v[60:63]
	s_waitcnt lgkmcnt(12)
	v_mfma_f32_16x16x32_f16 v[64:67], v[164:167], v[136:139], v[64:67]
	s_waitcnt lgkmcnt(11)
	v_mfma_f32_16x16x32_f16 v[68:71], v[168:171], v[136:139], v[68:71]
	s_waitcnt lgkmcnt(10)
	v_mfma_f32_16x16x32_f16 v[72:75], v[156:159], v[140:143], v[72:75]
	v_mfma_f32_16x16x32_f16 v[76:79], v[160:163], v[140:143], v[76:79]
	s_add_u32 m0, s28, 0x14000
	s_nop 0
	global_load_lds_dwordx4 v10, s[6:7]
	v_mfma_f32_16x16x32_f16 v[80:83], v[164:167], v[140:143], v[80:83]
	v_mfma_f32_16x16x32_f16 v[84:87], v[168:171], v[140:143], v[84:87]
	s_waitcnt lgkmcnt(9)
	v_mfma_f32_16x16x32_f16 v[88:91], v[156:159], v[144:147], v[88:91]
	v_mfma_f32_16x16x32_f16 v[92:95], v[160:163], v[144:147], v[92:95]
	v_mfma_f32_16x16x32_f16 v[96:99], v[164:167], v[144:147], v[96:99]
	s_add_u32 m0, s28, 0x16000
	s_nop 0
	global_load_lds_dwordx4 v11, s[6:7]
	s_add_u32 s6, s6, s20
	s_addc_u32 s7, s7, 0
	v_mfma_f32_16x16x32_f16 v[100:103], v[168:171], v[144:147], v[100:103]
	s_waitcnt lgkmcnt(8)
	v_mfma_f32_16x16x32_f16 v[104:107], v[156:159], v[148:151], v[104:107]
	v_mfma_f32_16x16x32_f16 v[108:111], v[160:163], v[148:151], v[108:111]
	v_mfma_f32_16x16x32_f16 v[112:115], v[164:167], v[148:151], v[112:115]
	v_mfma_f32_16x16x32_f16 v[116:119], v[168:171], v[148:151], v[116:119]
	s_waitcnt vmcnt(6) lgkmcnt(0)
	s_barrier
	s_waitcnt lgkmcnt(7)
	ds_read_b128 v[136:139], v15
	ds_read_b128 v[156:159], v17
	ds_read_b128 v[160:163], v17 offset:2048
	ds_read_b128 v[164:167], v17 offset:4096
	ds_read_b128 v[168:171], v17 offset:6144
	ds_read_b128 v[140:143], v15 offset:2048
	ds_read_b128 v[144:147], v15 offset:4096
	ds_read_b128 v[148:151], v15 offset:6144
	s_waitcnt lgkmcnt(14)
	v_mfma_f32_16x16x32_f16 v[56:59], v[192:195], v[172:175], v[56:59]
	s_add_u32 m0, s28, 0x18000
	s_nop 0
	global_load_lds_dwordx4 v10, s[4:5]
	s_waitcnt lgkmcnt(13)
	v_mfma_f32_16x16x32_f16 v[60:63], v[196:199], v[172:175], v[60:63]
	s_waitcnt lgkmcnt(12)
	v_mfma_f32_16x16x32_f16 v[64:67], v[200:203], v[172:175], v[64:67]
	s_waitcnt lgkmcnt(11)
	v_mfma_f32_16x16x32_f16 v[68:71], v[204:207], v[172:175], v[68:71]
	s_waitcnt lgkmcnt(10)
	v_mfma_f32_16x16x32_f16 v[72:75], v[192:195], v[176:179], v[72:75]
	v_mfma_f32_16x16x32_f16 v[76:79], v[196:199], v[176:179], v[76:79]
	s_add_u32 m0, s28, 0x1a000
	s_nop 0
	global_load_lds_dwordx4 v11, s[4:5]
	v_mfma_f32_16x16x32_f16 v[80:83], v[200:203], v[176:179], v[80:83]
	v_mfma_f32_16x16x32_f16 v[84:87], v[204:207], v[176:179], v[84:87]
	s_waitcnt lgkmcnt(9)
	v_mfma_f32_16x16x32_f16 v[88:91], v[192:195], v[180:183], v[88:91]
	v_mfma_f32_16x16x32_f16 v[92:95], v[196:199], v[180:183], v[92:95]
	v_mfma_f32_16x16x32_f16 v[96:99], v[200:203], v[180:183], v[96:99]
	s_add_u32 m0, s28, 0x1c000
	s_nop 0
	global_load_lds_dwordx4 v12, s[4:5]
	v_mfma_f32_16x16x32_f16 v[100:103], v[204:207], v[180:183], v[100:103]
	s_waitcnt lgkmcnt(8)
	v_mfma_f32_16x16x32_f16 v[104:107], v[192:195], v[184:187], v[104:107]
	v_mfma_f32_16x16x32_f16 v[108:111], v[196:199], v[184:187], v[108:111]
	v_mfma_f32_16x16x32_f16 v[112:115], v[200:203], v[184:187], v[112:115]
	v_mfma_f32_16x16x32_f16 v[116:119], v[204:207], v[184:187], v[116:119]
	s_waitcnt lgkmcnt(7)
	ds_read_b128 v[172:175], v16
	ds_read_b128 v[192:195], v18
	ds_read_b128 v[196:199], v18 offset:2048
	ds_read_b128 v[200:203], v18 offset:4096
	ds_read_b128 v[204:207], v18 offset:6144
	ds_read_b128 v[176:179], v16 offset:2048
	ds_read_b128 v[180:183], v16 offset:4096
	ds_read_b128 v[184:187], v16 offset:6144
	s_waitcnt lgkmcnt(14)
	v_mfma_f32_16x16x32_f16 v[56:59], v[156:159], v[136:139], v[56:59]
	s_add_u32 m0, s28, 0x1e000
	s_nop 0
	global_load_lds_dwordx4 v13, s[4:5]
	s_add_u32 s4, s4, s20
	s_addc_u32 s5, s5, 0
	s_waitcnt lgkmcnt(13)
	v_mfma_f32_16x16x32_f16 v[60:63], v[160:163], v[136:139], v[60:63]
	s_waitcnt lgkmcnt(12)
	v_mfma_f32_16x16x32_f16 v[64:67], v[164:167], v[136:139], v[64:67]
	s_waitcnt lgkmcnt(11)
	v_mfma_f32_16x16x32_f16 v[68:71], v[168:171], v[136:139], v[68:71]
	s_waitcnt lgkmcnt(10)
	v_mfma_f32_16x16x32_f16 v[72:75], v[156:159], v[140:143], v[72:75]
	v_mfma_f32_16x16x32_f16 v[76:79], v[160:163], v[140:143], v[76:79]
	s_add_u32 m0, s28, 0x20000
	s_nop 0
	global_load_lds_dwordx4 v10, s[6:7]
	v_mfma_f32_16x16x32_f16 v[80:83], v[164:167], v[140:143], v[80:83]
	v_mfma_f32_16x16x32_f16 v[84:87], v[168:171], v[140:143], v[84:87]
	s_waitcnt lgkmcnt(9)
	v_mfma_f32_16x16x32_f16 v[88:91], v[156:159], v[144:147], v[88:91]
	v_mfma_f32_16x16x32_f16 v[92:95], v[160:163], v[144:147], v[92:95]
	v_mfma_f32_16x16x32_f16 v[96:99], v[164:167], v[144:147], v[96:99]
	s_add_u32 m0, s28, 0x22000
	s_nop 0
	global_load_lds_dwordx4 v11, s[6:7]
	s_add_u32 s6, s6, s20
	s_addc_u32 s7, s7, 0
	v_mfma_f32_16x16x32_f16 v[100:103], v[168:171], v[144:147], v[100:103]
	s_waitcnt lgkmcnt(8)
	v_mfma_f32_16x16x32_f16 v[104:107], v[156:159], v[148:151], v[104:107]
	v_mfma_f32_16x16x32_f16 v[108:111], v[160:163], v[148:151], v[108:111]
	v_mfma_f32_16x16x32_f16 v[112:115], v[164:167], v[148:151], v[112:115]
	v_mfma_f32_16x16x32_f16 v[116:119], v[168:171], v[148:151], v[116:119]
	s_waitcnt vmcnt(6) lgkmcnt(0)
	s_barrier
	s_waitcnt lgkmcnt(7)
	ds_read_b128 v[136:139], v15 offset:49152
	ds_read_b128 v[156:159], v17 offset:49152
	ds_read_b128 v[160:163], v17 offset:51200
	ds_read_b128 v[164:167], v17 offset:53248
	ds_read_b128 v[168:171], v17 offset:55296
	ds_read_b128 v[140:143], v15 offset:51200
	ds_read_b128 v[144:147], v15 offset:53248
	ds_read_b128 v[148:151], v15 offset:55296
	s_waitcnt lgkmcnt(14)
	v_mfma_f32_16x16x32_f16 v[56:59], v[192:195], v[172:175], v[56:59]
	s_add_u32 m0, s28, 0x0
	s_nop 0
	global_load_lds_dwordx4 v10, s[4:5]
	s_waitcnt lgkmcnt(13)
	v_mfma_f32_16x16x32_f16 v[60:63], v[196:199], v[172:175], v[60:63]
	s_waitcnt lgkmcnt(12)
	v_mfma_f32_16x16x32_f16 v[64:67], v[200:203], v[172:175], v[64:67]
	s_waitcnt lgkmcnt(11)
	v_mfma_f32_16x16x32_f16 v[68:71], v[204:207], v[172:175], v[68:71]
	s_waitcnt lgkmcnt(10)
	v_mfma_f32_16x16x32_f16 v[72:75], v[192:195], v[176:179], v[72:75]
	v_mfma_f32_16x16x32_f16 v[76:79], v[196:199], v[176:179], v[76:79]
	s_add_u32 m0, s28, 0x2000
	s_nop 0
	global_load_lds_dwordx4 v11, s[4:5]
	v_mfma_f32_16x16x32_f16 v[80:83], v[200:203], v[176:179], v[80:83]
	v_mfma_f32_16x16x32_f16 v[84:87], v[204:207], v[176:179], v[84:87]
	s_waitcnt lgkmcnt(9)
	v_mfma_f32_16x16x32_f16 v[88:91], v[192:195], v[180:183], v[88:91]
	v_mfma_f32_16x16x32_f16 v[92:95], v[196:199], v[180:183], v[92:95]
	v_mfma_f32_16x16x32_f16 v[96:99], v[200:203], v[180:183], v[96:99]
	s_add_u32 m0, s28, 0x4000
	s_nop 0
	global_load_lds_dwordx4 v12, s[4:5]
	v_mfma_f32_16x16x32_f16 v[100:103], v[204:207], v[180:183], v[100:103]
	s_waitcnt lgkmcnt(8)
	v_mfma_f32_16x16x32_f16 v[104:107], v[192:195], v[184:187], v[104:107]
	v_mfma_f32_16x16x32_f16 v[108:111], v[196:199], v[184:187], v[108:111]
	v_mfma_f32_16x16x32_f16 v[112:115], v[200:203], v[184:187], v[112:115]
	v_mfma_f32_16x16x32_f16 v[116:119], v[204:207], v[184:187], v[116:119]
	s_waitcnt lgkmcnt(7)
	ds_read_b128 v[172:175], v16 offset:49152
	ds_read_b128 v[192:195], v18 offset:49152
	ds_read_b128 v[196:199], v18 offset:51200
	ds_read_b128 v[200:203], v18 offset:53248
	ds_read_b128 v[204:207], v18 offset:55296
	ds_read_b128 v[176:179], v16 offset:51200
	ds_read_b128 v[180:183], v16 offset:53248
	ds_read_b128 v[184:187], v16 offset:55296
	s_waitcnt lgkmcnt(14)
	v_mfma_f32_16x16x32_f16 v[56:59], v[156:159], v[136:139], v[56:59]
	s_add_u32 m0, s28, 0x6000
	s_nop 0
	global_load_lds_dwordx4 v13, s[4:5]
	s_add_u32 s4, s4, s20
	s_addc_u32 s5, s5, 0
	s_waitcnt lgkmcnt(13)
	v_mfma_f32_16x16x32_f16 v[60:63], v[160:163], v[136:139], v[60:63]
	s_waitcnt lgkmcnt(12)
	v_mfma_f32_16x16x32_f16 v[64:67], v[164:167], v[136:139], v[64:67]
	s_waitcnt lgkmcnt(11)
	v_mfma_f32_16x16x32_f16 v[68:71], v[168:171], v[136:139], v[68:71]
	s_waitcnt lgkmcnt(10)
	v_mfma_f32_16x16x32_f16 v[72:75], v[156:159], v[140:143], v[72:75]
	v_mfma_f32_16x16x32_f16 v[76:79], v[160:163], v[140:143], v[76:79]
	s_add_u32 m0, s28, 0x8000
	s_nop 0
	global_load_lds_dwordx4 v10, s[6:7]
	v_mfma_f32_16x16x32_f16 v[80:83], v[164:167], v[140:143], v[80:83]
	v_mfma_f32_16x16x32_f16 v[84:87], v[168:171], v[140:143], v[84:87]
	s_waitcnt lgkmcnt(9)
	v_mfma_f32_16x16x32_f16 v[88:91], v[156:159], v[144:147], v[88:91]
	v_mfma_f32_16x16x32_f16 v[92:95], v[160:163], v[144:147], v[92:95]
	v_mfma_f32_16x16x32_f16 v[96:99], v[164:167], v[144:147], v[96:99]
	s_add_u32 m0, s28, 0xa000
	s_nop 0
	global_load_lds_dwordx4 v11, s[6:7]
	s_add_u32 s6, s6, s20
	s_addc_u32 s7, s7, 0
	v_mfma_f32_16x16x32_f16 v[100:103], v[168:171], v[144:147], v[100:103]
	s_waitcnt lgkmcnt(8)
	v_mfma_f32_16x16x32_f16 v[104:107], v[156:159], v[148:151], v[104:107]
	v_mfma_f32_16x16x32_f16 v[108:111], v[160:163], v[148:151], v[108:111]
	v_mfma_f32_16x16x32_f16 v[112:115], v[164:167], v[148:151], v[112:115]
	v_mfma_f32_16x16x32_f16 v[116:119], v[168:171], v[148:151], v[116:119]
	s_waitcnt vmcnt(6) lgkmcnt(0)
	s_barrier
	s_waitcnt lgkmcnt(7)
	ds_read_b128 v[136:139], v19
	ds_read_b128 v[156:159], v21
	ds_read_b128 v[160:163], v21 offset:2048
	ds_read_b128 v[164:167], v21 offset:4096
	ds_read_b128 v[168:171], v21 offset:6144
	ds_read_b128 v[140:143], v19 offset:2048
	ds_read_b128 v[144:147], v19 offset:4096
	ds_read_b128 v[148:151], v19 offset:6144
	s_waitcnt lgkmcnt(14)
	v_mfma_f32_16x16x32_f16 v[56:59], v[192:195], v[172:175], v[56:59]
	s_add_u32 m0, s28, 0xc000
	s_nop 0
	global_load_lds_dwordx4 v10, s[4:5]
	s_waitcnt lgkmcnt(13)
	v_mfma_f32_16x16x32_f16 v[60:63], v[196:199], v[172:175], v[60:63]
	s_waitcnt lgkmcnt(12)
	v_mfma_f32_16x16x32_f16 v[64:67], v[200:203], v[172:175], v[64:67]
	s_waitcnt lgkmcnt(11)
	v_mfma_f32_16x16x32_f16 v[68:71], v[204:207], v[172:175], v[68:71]
	s_waitcnt lgkmcnt(10)
	v_mfma_f32_16x16x32_f16 v[72:75], v[192:195], v[176:179], v[72:75]
	v_mfma_f32_16x16x32_f16 v[76:79], v[196:199], v[176:179], v[76:79]
	s_add_u32 m0, s28, 0xe000
	s_nop 0
	global_load_lds_dwordx4 v11, s[4:5]
	v_mfma_f32_16x16x32_f16 v[80:83], v[200:203], v[176:179], v[80:83]
	v_mfma_f32_16x16x32_f16 v[84:87], v[204:207], v[176:179], v[84:87]
	s_waitcnt lgkmcnt(9)
	v_mfma_f32_16x16x32_f16 v[88:91], v[192:195], v[180:183], v[88:91]
	v_mfma_f32_16x16x32_f16 v[92:95], v[196:199], v[180:183], v[92:95]
	v_mfma_f32_16x16x32_f16 v[96:99], v[200:203], v[180:183], v[96:99]
	s_add_u32 m0, s28, 0x10000
	s_nop 0
	global_load_lds_dwordx4 v12, s[4:5]
	v_mfma_f32_16x16x32_f16 v[100:103], v[204:207], v[180:183], v[100:103]
	s_waitcnt lgkmcnt(8)
	v_mfma_f32_16x16x32_f16 v[104:107], v[192:195], v[184:187], v[104:107]
	v_mfma_f32_16x16x32_f16 v[108:111], v[196:199], v[184:187], v[108:111]
	v_mfma_f32_16x16x32_f16 v[112:115], v[200:203], v[184:187], v[112:115]
	v_mfma_f32_16x16x32_f16 v[116:119], v[204:207], v[184:187], v[116:119]
	s_waitcnt lgkmcnt(7)
	ds_read_b128 v[172:175], v20
	ds_read_b128 v[192:195], v22
	ds_read_b128 v[196:199], v22 offset:2048
	ds_read_b128 v[200:203], v22 offset:4096
	ds_read_b128 v[204:207], v22 offset:6144
	ds_read_b128 v[176:179], v20 offset:2048
	ds_read_b128 v[180:183], v20 offset:4096
	ds_read_b128 v[184:187], v20 offset:6144
	s_waitcnt lgkmcnt(14)
	v_mfma_f32_16x16x32_f16 v[56:59], v[156:159], v[136:139], v[56:59]
	s_add_u32 m0, s28, 0x12000
	s_nop 0
	global_load_lds_dwordx4 v13, s[4:5]
	s_add_u32 s4, s4, s20
	s_addc_u32 s5, s5, 0
	s_waitcnt lgkmcnt(13)
	v_mfma_f32_16x16x32_f16 v[60:63], v[160:163], v[136:139], v[60:63]
	s_waitcnt lgkmcnt(12)
	v_mfma_f32_16x16x32_f16 v[64:67], v[164:167], v[136:139], v[64:67]
	s_waitcnt lgkmcnt(11)
	v_mfma_f32_16x16x32_f16 v[68:71], v[168:171], v[136:139], v[68:71]
	s_waitcnt lgkmcnt(10)
	v_mfma_f32_16x16x32_f16 v[72:75], v[156:159], v[140:143], v[72:75]
	v_mfma_f32_16x16x32_f16 v[76:79], v[160:163], v[140:143], v[76:79]
	s_add_u32 m0, s28, 0x14000
	s_nop 0
	global_load_lds_dwordx4 v10, s[6:7]
	v_mfma_f32_16x16x32_f16 v[80:83], v[164:167], v[140:143], v[80:83]
	v_mfma_f32_16x16x32_f16 v[84:87], v[168:171], v[140:143], v[84:87]
	s_waitcnt lgkmcnt(9)
	v_mfma_f32_16x16x32_f16 v[88:91], v[156:159], v[144:147], v[88:91]
	v_mfma_f32_16x16x32_f16 v[92:95], v[160:163], v[144:147], v[92:95]
	v_mfma_f32_16x16x32_f16 v[96:99], v[164:167], v[144:147], v[96:99]
	s_add_u32 m0, s28, 0x16000
	s_nop 0
	global_load_lds_dwordx4 v11, s[6:7]
	s_add_u32 s6, s6, s20
	s_addc_u32 s7, s7, 0
	v_mfma_f32_16x16x32_f16 v[100:103], v[168:171], v[144:147], v[100:103]
	s_waitcnt lgkmcnt(8)
	v_mfma_f32_16x16x32_f16 v[104:107], v[156:159], v[148:151], v[104:107]
	v_mfma_f32_16x16x32_f16 v[108:111], v[160:163], v[148:151], v[108:111]
	v_mfma_f32_16x16x32_f16 v[112:115], v[164:167], v[148:151], v[112:115]
	v_mfma_f32_16x16x32_f16 v[116:119], v[168:171], v[148:151], v[116:119]
	s_waitcnt vmcnt(6) lgkmcnt(0)
	s_barrier
	s_waitcnt lgkmcnt(7)
	ds_read_b128 v[136:139], v15
	ds_read_b128 v[156:159], v17
	ds_read_b128 v[160:163], v17 offset:2048
	ds_read_b128 v[164:167], v17 offset:4096
	ds_read_b128 v[168:171], v17 offset:6144
	ds_read_b128 v[140:143], v15 offset:2048
	ds_read_b128 v[144:147], v15 offset:4096
	ds_read_b128 v[148:151], v15 offset:6144
	s_waitcnt lgkmcnt(14)
	v_mfma_f32_16x16x32_f16 v[56:59], v[192:195], v[172:175], v[56:59]
	s_add_u32 m0, s28, 0x18000
	s_nop 0
	global_load_lds_dwordx4 v10, s[4:5]
	s_waitcnt lgkmcnt(13)
	v_mfma_f32_16x16x32_f16 v[60:63], v[196:199], v[172:175], v[60:63]
	s_waitcnt lgkmcnt(12)
	v_mfma_f32_16x16x32_f16 v[64:67], v[200:203], v[172:175], v[64:67]
	s_waitcnt lgkmcnt(11)
	v_mfma_f32_16x16x32_f16 v[68:71], v[204:207], v[172:175], v[68:71]
	s_waitcnt lgkmcnt(10)
	v_mfma_f32_16x16x32_f16 v[72:75], v[192:195], v[176:179], v[72:75]
	v_mfma_f32_16x16x32_f16 v[76:79], v[196:199], v[176:179], v[76:79]
	s_add_u32 m0, s28, 0x1a000
	s_nop 0
	global_load_lds_dwordx4 v11, s[4:5]
	v_mfma_f32_16x16x32_f16 v[80:83], v[200:203], v[176:179], v[80:83]
	v_mfma_f32_16x16x32_f16 v[84:87], v[204:207], v[176:179], v[84:87]
	s_waitcnt lgkmcnt(9)
	v_mfma_f32_16x16x32_f16 v[88:91], v[192:195], v[180:183], v[88:91]
	v_mfma_f32_16x16x32_f16 v[92:95], v[196:199], v[180:183], v[92:95]
	v_mfma_f32_16x16x32_f16 v[96:99], v[200:203], v[180:183], v[96:99]
	s_add_u32 m0, s28, 0x1c000
	s_nop 0
	global_load_lds_dwordx4 v12, s[4:5]
	v_mfma_f32_16x16x32_f16 v[100:103], v[204:207], v[180:183], v[100:103]
	s_waitcnt lgkmcnt(8)
	v_mfma_f32_16x16x32_f16 v[104:107], v[192:195], v[184:187], v[104:107]
	v_mfma_f32_16x16x32_f16 v[108:111], v[196:199], v[184:187], v[108:111]
	v_mfma_f32_16x16x32_f16 v[112:115], v[200:203], v[184:187], v[112:115]
	v_mfma_f32_16x16x32_f16 v[116:119], v[204:207], v[184:187], v[116:119]
	s_waitcnt lgkmcnt(7)
	ds_read_b128 v[172:175], v16
	ds_read_b128 v[192:195], v18
	ds_read_b128 v[196:199], v18 offset:2048
	ds_read_b128 v[200:203], v18 offset:4096
	ds_read_b128 v[204:207], v18 offset:6144
	ds_read_b128 v[176:179], v16 offset:2048
	ds_read_b128 v[180:183], v16 offset:4096
	ds_read_b128 v[184:187], v16 offset:6144
	s_waitcnt lgkmcnt(14)
	v_mfma_f32_16x16x32_f16 v[56:59], v[156:159], v[136:139], v[56:59]
	s_add_u32 m0, s28, 0x1e000
	s_nop 0
	global_load_lds_dwordx4 v13, s[4:5]
	s_add_u32 s4, s4, s20
	s_addc_u32 s5, s5, 0
	s_waitcnt lgkmcnt(13)
	v_mfma_f32_16x16x32_f16 v[60:63], v[160:163], v[136:139], v[60:63]
	s_waitcnt lgkmcnt(12)
	v_mfma_f32_16x16x32_f16 v[64:67], v[164:167], v[136:139], v[64:67]
	s_waitcnt lgkmcnt(11)
	v_mfma_f32_16x16x32_f16 v[68:71], v[168:171], v[136:139], v[68:71]
	s_waitcnt lgkmcnt(10)
	v_mfma_f32_16x16x32_f16 v[72:75], v[156:159], v[140:143], v[72:75]
	v_mfma_f32_16x16x32_f16 v[76:79], v[160:163], v[140:143], v[76:79]
	s_add_u32 m0, s28, 0x20000
	s_nop 0
	global_load_lds_dwordx4 v10, s[6:7]
	v_mfma_f32_16x16x32_f16 v[80:83], v[164:167], v[140:143], v[80:83]
	v_mfma_f32_16x16x32_f16 v[84:87], v[168:171], v[140:143], v[84:87]
	s_waitcnt lgkmcnt(9)
	v_mfma_f32_16x16x32_f16 v[88:91], v[156:159], v[144:147], v[88:91]
	v_mfma_f32_16x16x32_f16 v[92:95], v[160:163], v[144:147], v[92:95]
	v_mfma_f32_16x16x32_f16 v[96:99], v[164:167], v[144:147], v[96:99]
	s_add_u32 m0, s28, 0x22000
	s_nop 0
	global_load_lds_dwordx4 v11, s[6:7]
	s_add_u32 s6, s6, s20
	s_addc_u32 s7, s7, 0
	v_mfma_f32_16x16x32_f16 v[100:103], v[168:171], v[144:147], v[100:103]
	s_waitcnt lgkmcnt(8)
	v_mfma_f32_16x16x32_f16 v[104:107], v[156:159], v[148:151], v[104:107]
	v_mfma_f32_16x16x32_f16 v[108:111], v[160:163], v[148:151], v[108:111]
	v_mfma_f32_16x16x32_f16 v[112:115], v[164:167], v[148:151], v[112:115]
	v_mfma_f32_16x16x32_f16 v[116:119], v[168:171], v[148:151], v[116:119]
	s_waitcnt vmcnt(6) lgkmcnt(0)
	s_barrier
	s_waitcnt lgkmcnt(7)
	ds_read_b128 v[136:139], v15 offset:49152
	ds_read_b128 v[156:159], v17 offset:49152
	ds_read_b128 v[160:163], v17 offset:51200
	ds_read_b128 v[164:167], v17 offset:53248
	ds_read_b128 v[168:171], v17 offset:55296
	ds_read_b128 v[140:143], v15 offset:51200
	ds_read_b128 v[144:147], v15 offset:53248
	ds_read_b128 v[148:151], v15 offset:55296
	s_waitcnt lgkmcnt(14)
	v_mfma_f32_16x16x32_f16 v[56:59], v[192:195], v[172:175], v[56:59]
	s_add_u32 m0, s28, 0x0
	s_nop 0
	global_load_lds_dwordx4 v10, s[4:5]
	s_waitcnt lgkmcnt(13)
	v_mfma_f32_16x16x32_f16 v[60:63], v[196:199], v[172:175], v[60:63]
	s_waitcnt lgkmcnt(12)
	v_mfma_f32_16x16x32_f16 v[64:67], v[200:203], v[172:175], v[64:67]
	s_waitcnt lgkmcnt(11)
	v_mfma_f32_16x16x32_f16 v[68:71], v[204:207], v[172:175], v[68:71]
	s_waitcnt lgkmcnt(10)
	v_mfma_f32_16x16x32_f16 v[72:75], v[192:195], v[176:179], v[72:75]
	v_mfma_f32_16x16x32_f16 v[76:79], v[196:199], v[176:179], v[76:79]
	s_add_u32 m0, s28, 0x2000
	s_nop 0
	global_load_lds_dwordx4 v11, s[4:5]
	v_mfma_f32_16x16x32_f16 v[80:83], v[200:203], v[176:179], v[80:83]
	v_mfma_f32_16x16x32_f16 v[84:87], v[204:207], v[176:179], v[84:87]
	s_waitcnt lgkmcnt(9)
	v_mfma_f32_16x16x32_f16 v[88:91], v[192:195], v[180:183], v[88:91]
	v_mfma_f32_16x16x32_f16 v[92:95], v[196:199], v[180:183], v[92:95]
	v_mfma_f32_16x16x32_f16 v[96:99], v[200:203], v[180:183], v[96:99]
	s_add_u32 m0, s28, 0x4000
	s_nop 0
	global_load_lds_dwordx4 v12, s[4:5]
	v_mfma_f32_16x16x32_f16 v[100:103], v[204:207], v[180:183], v[100:103]
	s_waitcnt lgkmcnt(8)
	v_mfma_f32_16x16x32_f16 v[104:107], v[192:195], v[184:187], v[104:107]
	v_mfma_f32_16x16x32_f16 v[108:111], v[196:199], v[184:187], v[108:111]
	v_mfma_f32_16x16x32_f16 v[112:115], v[200:203], v[184:187], v[112:115]
	v_mfma_f32_16x16x32_f16 v[116:119], v[204:207], v[184:187], v[116:119]
	s_waitcnt lgkmcnt(7)
	ds_read_b128 v[172:175], v16 offset:49152
	ds_read_b128 v[192:195], v18 offset:49152
	ds_read_b128 v[196:199], v18 offset:51200
	ds_read_b128 v[200:203], v18 offset:53248
	ds_read_b128 v[204:207], v18 offset:55296
	ds_read_b128 v[176:179], v16 offset:51200
	ds_read_b128 v[180:183], v16 offset:53248
	ds_read_b128 v[184:187], v16 offset:55296
	s_waitcnt lgkmcnt(14)
	v_mfma_f32_16x16x32_f16 v[56:59], v[156:159], v[136:139], v[56:59]
	s_add_u32 m0, s28, 0x6000
	s_nop 0
	global_load_lds_dwordx4 v13, s[4:5]
	s_add_u32 s4, s4, s20
	s_addc_u32 s5, s5, 0
	s_waitcnt lgkmcnt(13)
	v_mfma_f32_16x16x32_f16 v[60:63], v[160:163], v[136:139], v[60:63]
	s_waitcnt lgkmcnt(12)
	v_mfma_f32_16x16x32_f16 v[64:67], v[164:167], v[136:139], v[64:67]
	s_waitcnt lgkmcnt(11)
	v_mfma_f32_16x16x32_f16 v[68:71], v[168:171], v[136:139], v[68:71]
	s_waitcnt lgkmcnt(10)
	v_mfma_f32_16x16x32_f16 v[72:75], v[156:159], v[140:143], v[72:75]
	v_mfma_f32_16x16x32_f16 v[76:79], v[160:163], v[140:143], v[76:79]
	s_add_u32 m0, s28, 0x8000
	s_nop 0
	global_load_lds_dwordx4 v10, s[6:7]
	v_mfma_f32_16x16x32_f16 v[80:83], v[164:167], v[140:143], v[80:83]
	v_mfma_f32_16x16x32_f16 v[84:87], v[168:171], v[140:143], v[84:87]
	s_waitcnt lgkmcnt(9)
	v_mfma_f32_16x16x32_f16 v[88:91], v[156:159], v[144:147], v[88:91]
	v_mfma_f32_16x16x32_f16 v[92:95], v[160:163], v[144:147], v[92:95]
	v_mfma_f32_16x16x32_f16 v[96:99], v[164:167], v[144:147], v[96:99]
	s_add_u32 m0, s28, 0xa000
	s_nop 0
	global_load_lds_dwordx4 v11, s[6:7]
	s_add_u32 s6, s6, s20
	s_addc_u32 s7, s7, 0
	v_mfma_f32_16x16x32_f16 v[100:103], v[168:171], v[144:147], v[100:103]
	s_waitcnt lgkmcnt(8)
	v_mfma_f32_16x16x32_f16 v[104:107], v[156:159], v[148:151], v[104:107]
	v_mfma_f32_16x16x32_f16 v[108:111], v[160:163], v[148:151], v[108:111]
	v_mfma_f32_16x16x32_f16 v[112:115], v[164:167], v[148:151], v[112:115]
	v_mfma_f32_16x16x32_f16 v[116:119], v[168:171], v[148:151], v[116:119]
	s_waitcnt vmcnt(6) lgkmcnt(0)
	s_barrier
	s_waitcnt lgkmcnt(7)
	ds_read_b128 v[136:139], v19
	ds_read_b128 v[156:159], v21
	ds_read_b128 v[160:163], v21 offset:2048
	ds_read_b128 v[164:167], v21 offset:4096
	ds_read_b128 v[168:171], v21 offset:6144
	ds_read_b128 v[140:143], v19 offset:2048
	ds_read_b128 v[144:147], v19 offset:4096
	ds_read_b128 v[148:151], v19 offset:6144
	s_waitcnt lgkmcnt(14)
	v_mfma_f32_16x16x32_f16 v[56:59], v[192:195], v[172:175], v[56:59]
	s_add_u32 m0, s28, 0xc000
	s_nop 0
	global_load_lds_dwordx4 v10, s[4:5]
	s_waitcnt lgkmcnt(13)
	v_mfma_f32_16x16x32_f16 v[60:63], v[196:199], v[172:175], v[60:63]
	s_waitcnt lgkmcnt(12)
	v_mfma_f32_16x16x32_f16 v[64:67], v[200:203], v[172:175], v[64:67]
	s_waitcnt lgkmcnt(11)
	v_mfma_f32_16x16x32_f16 v[68:71], v[204:207], v[172:175], v[68:71]
	s_waitcnt lgkmcnt(10)
	v_mfma_f32_16x16x32_f16 v[72:75], v[192:195], v[176:179], v[72:75]
	v_mfma_f32_16x16x32_f16 v[76:79], v[196:199], v[176:179], v[76:79]
	s_add_u32 m0, s28, 0xe000
	s_nop 0
	global_load_lds_dwordx4 v11, s[4:5]
	v_mfma_f32_16x16x32_f16 v[80:83], v[200:203], v[176:179], v[80:83]
	v_mfma_f32_16x16x32_f16 v[84:87], v[204:207], v[176:179], v[84:87]
	s_waitcnt lgkmcnt(9)
	v_mfma_f32_16x16x32_f16 v[88:91], v[192:195], v[180:183], v[88:91]
	v_mfma_f32_16x16x32_f16 v[92:95], v[196:199], v[180:183], v[92:95]
	v_mfma_f32_16x16x32_f16 v[96:99], v[200:203], v[180:183], v[96:99]
	s_add_u32 m0, s28, 0x10000
	s_nop 0
	global_load_lds_dwordx4 v12, s[4:5]
	v_mfma_f32_16x16x32_f16 v[100:103], v[204:207], v[180:183], v[100:103]
	s_waitcnt lgkmcnt(8)
	v_mfma_f32_16x16x32_f16 v[104:107], v[192:195], v[184:187], v[104:107]
	v_mfma_f32_16x16x32_f16 v[108:111], v[196:199], v[184:187], v[108:111]
	v_mfma_f32_16x16x32_f16 v[112:115], v[200:203], v[184:187], v[112:115]
	v_mfma_f32_16x16x32_f16 v[116:119], v[204:207], v[184:187], v[116:119]
	s_waitcnt lgkmcnt(7)
	ds_read_b128 v[172:175], v20
	ds_read_b128 v[192:195], v22
	ds_read_b128 v[196:199], v22 offset:2048
	ds_read_b128 v[200:203], v22 offset:4096
	ds_read_b128 v[204:207], v22 offset:6144
	ds_read_b128 v[176:179], v20 offset:2048
	ds_read_b128 v[180:183], v20 offset:4096
	ds_read_b128 v[184:187], v20 offset:6144
	s_waitcnt lgkmcnt(14)
	v_mfma_f32_16x16x32_f16 v[56:59], v[156:159], v[136:139], v[56:59]
	s_add_u32 m0, s28, 0x12000
	s_nop 0
	global_load_lds_dwordx4 v13, s[4:5]
	s_add_u32 s4, s4, s20
	s_addc_u32 s5, s5, 0
	s_waitcnt lgkmcnt(13)
	v_mfma_f32_16x16x32_f16 v[60:63], v[160:163], v[136:139], v[60:63]
	s_waitcnt lgkmcnt(12)
	v_mfma_f32_16x16x32_f16 v[64:67], v[164:167], v[136:139], v[64:67]
	s_waitcnt lgkmcnt(11)
	v_mfma_f32_16x16x32_f16 v[68:71], v[168:171], v[136:139], v[68:71]
	s_waitcnt lgkmcnt(10)
	v_mfma_f32_16x16x32_f16 v[72:75], v[156:159], v[140:143], v[72:75]
	v_mfma_f32_16x16x32_f16 v[76:79], v[160:163], v[140:143], v[76:79]
	s_add_u32 m0, s28, 0x14000
	s_nop 0
	global_load_lds_dwordx4 v10, s[6:7]
	v_mfma_f32_16x16x32_f16 v[80:83], v[164:167], v[140:143], v[80:83]
	v_mfma_f32_16x16x32_f16 v[84:87], v[168:171], v[140:143], v[84:87]
	s_waitcnt lgkmcnt(9)
	v_mfma_f32_16x16x32_f16 v[88:91], v[156:159], v[144:147], v[88:91]
	v_mfma_f32_16x16x32_f16 v[92:95], v[160:163], v[144:147], v[92:95]
	v_mfma_f32_16x16x32_f16 v[96:99], v[164:167], v[144:147], v[96:99]
	s_add_u32 m0, s28, 0x16000
	s_nop 0
	global_load_lds_dwordx4 v11, s[6:7]
	s_add_u32 s6, s6, s20
	s_addc_u32 s7, s7, 0
	v_mfma_f32_16x16x32_f16 v[100:103], v[168:171], v[144:147], v[100:103]
	s_waitcnt lgkmcnt(8)
	v_mfma_f32_16x16x32_f16 v[104:107], v[156:159], v[148:151], v[104:107]
	v_mfma_f32_16x16x32_f16 v[108:111], v[160:163], v[148:151], v[108:111]
	v_mfma_f32_16x16x32_f16 v[112:115], v[164:167], v[148:151], v[112:115]
	v_mfma_f32_16x16x32_f16 v[116:119], v[168:171], v[148:151], v[116:119]
	s_waitcnt vmcnt(6) lgkmcnt(0)
	s_barrier
	s_waitcnt lgkmcnt(7)
	ds_read_b128 v[136:139], v15
	ds_read_b128 v[156:159], v17
	ds_read_b128 v[160:163], v17 offset:2048
	ds_read_b128 v[164:167], v17 offset:4096
	ds_read_b128 v[168:171], v17 offset:6144
	ds_read_b128 v[140:143], v15 offset:2048
	ds_read_b128 v[144:147], v15 offset:4096
	ds_read_b128 v[148:151], v15 offset:6144
	s_waitcnt lgkmcnt(14)
	v_mfma_f32_16x16x32_f16 v[56:59], v[192:195], v[172:175], v[56:59]
	s_add_u32 m0, s28, 0x18000
	s_nop 0
	global_load_lds_dwordx4 v10, s[4:5]
	s_waitcnt lgkmcnt(13)
	v_mfma_f32_16x16x32_f16 v[60:63], v[196:199], v[172:175], v[60:63]
	s_waitcnt lgkmcnt(12)
	v_mfma_f32_16x16x32_f16 v[64:67], v[200:203], v[172:175], v[64:67]
	s_waitcnt lgkmcnt(11)
	v_mfma_f32_16x16x32_f16 v[68:71], v[204:207], v[172:175], v[68:71]
	s_waitcnt lgkmcnt(10)
	v_mfma_f32_16x16x32_f16 v[72:75], v[192:195], v[176:179], v[72:75]
	v_mfma_f32_16x16x32_f16 v[76:79], v[196:199], v[176:179], v[76:79]
	s_add_u32 m0, s28, 0x1a000
	s_nop 0
	global_load_lds_dwordx4 v11, s[4:5]
	v_mfma_f32_16x16x32_f16 v[80:83], v[200:203], v[176:179], v[80:83]
	v_mfma_f32_16x16x32_f16 v[84:87], v[204:207], v[176:179], v[84:87]
	s_waitcnt lgkmcnt(9)
	v_mfma_f32_16x16x32_f16 v[88:91], v[192:195], v[180:183], v[88:91]
	v_mfma_f32_16x16x32_f16 v[92:95], v[196:199], v[180:183], v[92:95]
	v_mfma_f32_16x16x32_f16 v[96:99], v[200:203], v[180:183], v[96:99]
	s_add_u32 m0, s28, 0x1c000
	s_nop 0
	global_load_lds_dwordx4 v12, s[4:5]
	v_mfma_f32_16x16x32_f16 v[100:103], v[204:207], v[180:183], v[100:103]
	s_waitcnt lgkmcnt(8)
	v_mfma_f32_16x16x32_f16 v[104:107], v[192:195], v[184:187], v[104:107]
	v_mfma_f32_16x16x32_f16 v[108:111], v[196:199], v[184:187], v[108:111]
	v_mfma_f32_16x16x32_f16 v[112:115], v[200:203], v[184:187], v[112:115]
	v_mfma_f32_16x16x32_f16 v[116:119], v[204:207], v[184:187], v[116:119]
	s_waitcnt lgkmcnt(7)
	ds_read_b128 v[172:175], v16
	ds_read_b128 v[192:195], v18
	ds_read_b128 v[196:199], v18 offset:2048
	ds_read_b128 v[200:203], v18 offset:4096
	ds_read_b128 v[204:207], v18 offset:6144
	ds_read_b128 v[176:179], v16 offset:2048
	ds_read_b128 v[180:183], v16 offset:4096
	ds_read_b128 v[184:187], v16 offset:6144
	s_waitcnt lgkmcnt(14)
	v_mfma_f32_16x16x32_f16 v[56:59], v[156:159], v[136:139], v[56:59]
	s_add_u32 m0, s28, 0x1e000
	s_nop 0
	global_load_lds_dwordx4 v13, s[4:5]
	s_add_u32 s4, s4, s20
	s_addc_u32 s5, s5, 0
	s_waitcnt lgkmcnt(13)
	v_mfma_f32_16x16x32_f16 v[60:63], v[160:163], v[136:139], v[60:63]
	s_waitcnt lgkmcnt(12)
	v_mfma_f32_16x16x32_f16 v[64:67], v[164:167], v[136:139], v[64:67]
	s_waitcnt lgkmcnt(11)
	v_mfma_f32_16x16x32_f16 v[68:71], v[168:171], v[136:139], v[68:71]
	s_waitcnt lgkmcnt(10)
	v_mfma_f32_16x16x32_f16 v[72:75], v[156:159], v[140:143], v[72:75]
	v_mfma_f32_16x16x32_f16 v[76:79], v[160:163], v[140:143], v[76:79]
	s_add_u32 m0, s28, 0x20000
	s_nop 0
	global_load_lds_dwordx4 v10, s[6:7]
	v_mfma_f32_16x16x32_f16 v[80:83], v[164:167], v[140:143], v[80:83]
	v_mfma_f32_16x16x32_f16 v[84:87], v[168:171], v[140:143], v[84:87]
	s_waitcnt lgkmcnt(9)
	v_mfma_f32_16x16x32_f16 v[88:91], v[156:159], v[144:147], v[88:91]
	v_mfma_f32_16x16x32_f16 v[92:95], v[160:163], v[144:147], v[92:95]
	v_mfma_f32_16x16x32_f16 v[96:99], v[164:167], v[144:147], v[96:99]
	s_add_u32 m0, s28, 0x22000
	s_nop 0
	global_load_lds_dwordx4 v11, s[6:7]
	s_add_u32 s6, s6, s20
	s_addc_u32 s7, s7, 0
	v_mfma_f32_16x16x32_f16 v[100:103], v[168:171], v[144:147], v[100:103]
	s_waitcnt lgkmcnt(8)
	v_mfma_f32_16x16x32_f16 v[104:107], v[156:159], v[148:151], v[104:107]
	v_mfma_f32_16x16x32_f16 v[108:111], v[160:163], v[148:151], v[108:111]
	v_mfma_f32_16x16x32_f16 v[112:115], v[164:167], v[148:151], v[112:115]
	v_mfma_f32_16x16x32_f16 v[116:119], v[168:171], v[148:151], v[116:119]
	s_waitcnt vmcnt(6) lgkmcnt(0)
	s_barrier
	s_waitcnt lgkmcnt(7)
	ds_read_b128 v[136:139], v15 offset:49152
	ds_read_b128 v[156:159], v17 offset:49152
	ds_read_b128 v[160:163], v17 offset:51200
	ds_read_b128 v[164:167], v17 offset:53248
	ds_read_b128 v[168:171], v17 offset:55296
	ds_read_b128 v[140:143], v15 offset:51200
	ds_read_b128 v[144:147], v15 offset:53248
	ds_read_b128 v[148:151], v15 offset:55296
	s_waitcnt lgkmcnt(14)
	v_mfma_f32_16x16x32_f16 v[56:59], v[192:195], v[172:175], v[56:59]
	s_add_u32 m0, s28, 0x0
	s_nop 0
	global_load_lds_dwordx4 v10, s[4:5]
	s_waitcnt lgkmcnt(13)
	v_mfma_f32_16x16x32_f16 v[60:63], v[196:199], v[172:175], v[60:63]
	s_waitcnt lgkmcnt(12)
	v_mfma_f32_16x16x32_f16 v[64:67], v[200:203], v[172:175], v[64:67]
	s_waitcnt lgkmcnt(11)
	v_mfma_f32_16x16x32_f16 v[68:71], v[204:207], v[172:175], v[68:71]
	s_waitcnt lgkmcnt(10)
	v_mfma_f32_16x16x32_f16 v[72:75], v[192:195], v[176:179], v[72:75]
	v_mfma_f32_16x16x32_f16 v[76:79], v[196:199], v[176:179], v[76:79]
	s_add_u32 m0, s28, 0x2000
	s_nop 0
	global_load_lds_dwordx4 v11, s[4:5]
	v_mfma_f32_16x16x32_f16 v[80:83], v[200:203], v[176:179], v[80:83]
	v_mfma_f32_16x16x32_f16 v[84:87], v[204:207], v[176:179], v[84:87]
	s_waitcnt lgkmcnt(9)
	v_mfma_f32_16x16x32_f16 v[88:91], v[192:195], v[180:183], v[88:91]
	v_mfma_f32_16x16x32_f16 v[92:95], v[196:199], v[180:183], v[92:95]
	v_mfma_f32_16x16x32_f16 v[96:99], v[200:203], v[180:183], v[96:99]
	s_add_u32 m0, s28, 0x4000
	s_nop 0
	global_load_lds_dwordx4 v12, s[4:5]
	v_mfma_f32_16x16x32_f16 v[100:103], v[204:207], v[180:183], v[100:103]
	s_waitcnt lgkmcnt(8)
	v_mfma_f32_16x16x32_f16 v[104:107], v[192:195], v[184:187], v[104:107]
	v_mfma_f32_16x16x32_f16 v[108:111], v[196:199], v[184:187], v[108:111]
	v_mfma_f32_16x16x32_f16 v[112:115], v[200:203], v[184:187], v[112:115]
	v_mfma_f32_16x16x32_f16 v[116:119], v[204:207], v[184:187], v[116:119]
	s_waitcnt lgkmcnt(7)
	ds_read_b128 v[172:175], v16 offset:49152
	ds_read_b128 v[192:195], v18 offset:49152
	ds_read_b128 v[196:199], v18 offset:51200
	ds_read_b128 v[200:203], v18 offset:53248
	ds_read_b128 v[204:207], v18 offset:55296
	ds_read_b128 v[176:179], v16 offset:51200
	ds_read_b128 v[180:183], v16 offset:53248
	ds_read_b128 v[184:187], v16 offset:55296
	s_waitcnt lgkmcnt(14)
	v_mfma_f32_16x16x32_f16 v[56:59], v[156:159], v[136:139], v[56:59]
	s_add_u32 m0, s28, 0x6000
	s_nop 0
	global_load_lds_dwordx4 v13, s[4:5]
	s_add_u32 s4, s4, s20
	s_addc_u32 s5, s5, 0
	s_waitcnt lgkmcnt(13)
	v_mfma_f32_16x16x32_f16 v[60:63], v[160:163], v[136:139], v[60:63]
	s_waitcnt lgkmcnt(12)
	v_mfma_f32_16x16x32_f16 v[64:67], v[164:167], v[136:139], v[64:67]
	s_waitcnt lgkmcnt(11)
	v_mfma_f32_16x16x32_f16 v[68:71], v[168:171], v[136:139], v[68:71]
	s_waitcnt lgkmcnt(10)
	v_mfma_f32_16x16x32_f16 v[72:75], v[156:159], v[140:143], v[72:75]
	v_mfma_f32_16x16x32_f16 v[76:79], v[160:163], v[140:143], v[76:79]
	s_add_u32 m0, s28, 0x8000
	s_nop 0
	global_load_lds_dwordx4 v10, s[6:7]
	v_mfma_f32_16x16x32_f16 v[80:83], v[164:167], v[140:143], v[80:83]
	v_mfma_f32_16x16x32_f16 v[84:87], v[168:171], v[140:143], v[84:87]
	s_waitcnt lgkmcnt(9)
	v_mfma_f32_16x16x32_f16 v[88:91], v[156:159], v[144:147], v[88:91]
	v_mfma_f32_16x16x32_f16 v[92:95], v[160:163], v[144:147], v[92:95]
	v_mfma_f32_16x16x32_f16 v[96:99], v[164:167], v[144:147], v[96:99]
	s_add_u32 m0, s28, 0xa000
	s_nop 0
	global_load_lds_dwordx4 v11, s[6:7]
	s_add_u32 s6, s6, s20
	s_addc_u32 s7, s7, 0
	v_mfma_f32_16x16x32_f16 v[100:103], v[168:171], v[144:147], v[100:103]
	s_waitcnt lgkmcnt(8)
	v_mfma_f32_16x16x32_f16 v[104:107], v[156:159], v[148:151], v[104:107]
	v_mfma_f32_16x16x32_f16 v[108:111], v[160:163], v[148:151], v[108:111]
	v_mfma_f32_16x16x32_f16 v[112:115], v[164:167], v[148:151], v[112:115]
	v_mfma_f32_16x16x32_f16 v[116:119], v[168:171], v[148:151], v[116:119]
	s_waitcnt vmcnt(6) lgkmcnt(0)
	s_barrier
	s_waitcnt lgkmcnt(7)
	ds_read_b128 v[136:139], v19
	ds_read_b128 v[156:159], v21
	ds_read_b128 v[160:163], v21 offset:2048
	ds_read_b128 v[164:167], v21 offset:4096
	ds_read_b128 v[168:171], v21 offset:6144
	ds_read_b128 v[140:143], v19 offset:2048
	ds_read_b128 v[144:147], v19 offset:4096
	ds_read_b128 v[148:151], v19 offset:6144
	s_waitcnt lgkmcnt(14)
	v_mfma_f32_16x16x32_f16 v[56:59], v[192:195], v[172:175], v[56:59]
	s_add_u32 m0, s28, 0xc000
	s_nop 0
	global_load_lds_dwordx4 v10, s[4:5]
	s_waitcnt lgkmcnt(13)
	v_mfma_f32_16x16x32_f16 v[60:63], v[196:199], v[172:175], v[60:63]
	s_waitcnt lgkmcnt(12)
	v_mfma_f32_16x16x32_f16 v[64:67], v[200:203], v[172:175], v[64:67]
	s_waitcnt lgkmcnt(11)
	v_mfma_f32_16x16x32_f16 v[68:71], v[204:207], v[172:175], v[68:71]
	s_waitcnt lgkmcnt(10)
	v_mfma_f32_16x16x32_f16 v[72:75], v[192:195], v[176:179], v[72:75]
	v_mfma_f32_16x16x32_f16 v[76:79], v[196:199], v[176:179], v[76:79]
	s_add_u32 m0, s28, 0xe000
	s_nop 0
	global_load_lds_dwordx4 v11, s[4:5]
	v_mfma_f32_16x16x32_f16 v[80:83], v[200:203], v[176:179], v[80:83]
	v_mfma_f32_16x16x32_f16 v[84:87], v[204:207], v[176:179], v[84:87]
	s_waitcnt lgkmcnt(9)
	v_mfma_f32_16x16x32_f16 v[88:91], v[192:195], v[180:183], v[88:91]
	v_mfma_f32_16x16x32_f16 v[92:95], v[196:199], v[180:183], v[92:95]
	v_mfma_f32_16x16x32_f16 v[96:99], v[200:203], v[180:183], v[96:99]
	s_add_u32 m0, s28, 0x10000
	s_nop 0
	global_load_lds_dwordx4 v12, s[4:5]
	v_mfma_f32_16x16x32_f16 v[100:103], v[204:207], v[180:183], v[100:103]
	s_waitcnt lgkmcnt(8)
	v_mfma_f32_16x16x32_f16 v[104:107], v[192:195], v[184:187], v[104:107]
	v_mfma_f32_16x16x32_f16 v[108:111], v[196:199], v[184:187], v[108:111]
	v_mfma_f32_16x16x32_f16 v[112:115], v[200:203], v[184:187], v[112:115]
	v_mfma_f32_16x16x32_f16 v[116:119], v[204:207], v[184:187], v[116:119]
	s_waitcnt lgkmcnt(7)
	ds_read_b128 v[172:175], v20
	ds_read_b128 v[192:195], v22
	ds_read_b128 v[196:199], v22 offset:2048
	ds_read_b128 v[200:203], v22 offset:4096
	ds_read_b128 v[204:207], v22 offset:6144
	ds_read_b128 v[176:179], v20 offset:2048
	ds_read_b128 v[180:183], v20 offset:4096
	ds_read_b128 v[184:187], v20 offset:6144
	s_waitcnt lgkmcnt(14)
	v_mfma_f32_16x16x32_f16 v[56:59], v[156:159], v[136:139], v[56:59]
	s_add_u32 m0, s28, 0x12000
	s_nop 0
	global_load_lds_dwordx4 v13, s[4:5]
	s_add_u32 s4, s4, s20
	s_addc_u32 s5, s5, 0
	s_waitcnt lgkmcnt(13)
	v_mfma_f32_16x16x32_f16 v[60:63], v[160:163], v[136:139], v[60:63]
	s_waitcnt lgkmcnt(12)
	v_mfma_f32_16x16x32_f16 v[64:67], v[164:167], v[136:139], v[64:67]
	s_waitcnt lgkmcnt(11)
	v_mfma_f32_16x16x32_f16 v[68:71], v[168:171], v[136:139], v[68:71]
	s_waitcnt lgkmcnt(10)
	v_mfma_f32_16x16x32_f16 v[72:75], v[156:159], v[140:143], v[72:75]
	v_mfma_f32_16x16x32_f16 v[76:79], v[160:163], v[140:143], v[76:79]
	s_add_u32 m0, s28, 0x14000
	s_nop 0
	global_load_lds_dwordx4 v10, s[6:7]
	v_mfma_f32_16x16x32_f16 v[80:83], v[164:167], v[140:143], v[80:83]
	v_mfma_f32_16x16x32_f16 v[84:87], v[168:171], v[140:143], v[84:87]
	s_waitcnt lgkmcnt(9)
	v_mfma_f32_16x16x32_f16 v[88:91], v[156:159], v[144:147], v[88:91]
	v_mfma_f32_16x16x32_f16 v[92:95], v[160:163], v[144:147], v[92:95]
	v_mfma_f32_16x16x32_f16 v[96:99], v[164:167], v[144:147], v[96:99]
	s_add_u32 m0, s28, 0x16000
	s_nop 0
	global_load_lds_dwordx4 v11, s[6:7]
	s_add_u32 s6, s6, s20
	s_addc_u32 s7, s7, 0
	v_mfma_f32_16x16x32_f16 v[100:103], v[168:171], v[144:147], v[100:103]
	s_waitcnt lgkmcnt(8)
	v_mfma_f32_16x16x32_f16 v[104:107], v[156:159], v[148:151], v[104:107]
	v_mfma_f32_16x16x32_f16 v[108:111], v[160:163], v[148:151], v[108:111]
	v_mfma_f32_16x16x32_f16 v[112:115], v[164:167], v[148:151], v[112:115]
	v_mfma_f32_16x16x32_f16 v[116:119], v[168:171], v[148:151], v[116:119]
	s_waitcnt vmcnt(6) lgkmcnt(0)
	s_barrier
	s_waitcnt lgkmcnt(7)
	ds_read_b128 v[136:139], v15
	ds_read_b128 v[156:159], v17
	ds_read_b128 v[160:163], v17 offset:2048
	ds_read_b128 v[164:167], v17 offset:4096
	ds_read_b128 v[168:171], v17 offset:6144
	ds_read_b128 v[140:143], v15 offset:2048
	ds_read_b128 v[144:147], v15 offset:4096
	ds_read_b128 v[148:151], v15 offset:6144
	s_waitcnt lgkmcnt(14)
	v_mfma_f32_16x16x32_f16 v[56:59], v[192:195], v[172:175], v[56:59]
	s_add_u32 m0, s28, 0x18000
	s_nop 0
	global_load_lds_dwordx4 v10, s[4:5]
	s_waitcnt lgkmcnt(13)
	v_mfma_f32_16x16x32_f16 v[60:63], v[196:199], v[172:175], v[60:63]
	s_waitcnt lgkmcnt(12)
	v_mfma_f32_16x16x32_f16 v[64:67], v[200:203], v[172:175], v[64:67]
	s_waitcnt lgkmcnt(11)
	v_mfma_f32_16x16x32_f16 v[68:71], v[204:207], v[172:175], v[68:71]
	s_waitcnt lgkmcnt(10)
	v_mfma_f32_16x16x32_f16 v[72:75], v[192:195], v[176:179], v[72:75]
	v_mfma_f32_16x16x32_f16 v[76:79], v[196:199], v[176:179], v[76:79]
	s_add_u32 m0, s28, 0x1a000
	s_nop 0
	global_load_lds_dwordx4 v11, s[4:5]
	v_mfma_f32_16x16x32_f16 v[80:83], v[200:203], v[176:179], v[80:83]
	v_mfma_f32_16x16x32_f16 v[84:87], v[204:207], v[176:179], v[84:87]
	s_waitcnt lgkmcnt(9)
	v_mfma_f32_16x16x32_f16 v[88:91], v[192:195], v[180:183], v[88:91]
	v_mfma_f32_16x16x32_f16 v[92:95], v[196:199], v[180:183], v[92:95]
	v_mfma_f32_16x16x32_f16 v[96:99], v[200:203], v[180:183], v[96:99]
	s_add_u32 m0, s28, 0x1c000
	s_nop 0
	global_load_lds_dwordx4 v12, s[4:5]
	v_mfma_f32_16x16x32_f16 v[100:103], v[204:207], v[180:183], v[100:103]
	s_waitcnt lgkmcnt(8)
	v_mfma_f32_16x16x32_f16 v[104:107], v[192:195], v[184:187], v[104:107]
	v_mfma_f32_16x16x32_f16 v[108:111], v[196:199], v[184:187], v[108:111]
	v_mfma_f32_16x16x32_f16 v[112:115], v[200:203], v[184:187], v[112:115]
	v_mfma_f32_16x16x32_f16 v[116:119], v[204:207], v[184:187], v[116:119]
	s_waitcnt lgkmcnt(7)
	ds_read_b128 v[172:175], v16
	ds_read_b128 v[192:195], v18
	ds_read_b128 v[196:199], v18 offset:2048
	ds_read_b128 v[200:203], v18 offset:4096
	ds_read_b128 v[204:207], v18 offset:6144
	ds_read_b128 v[176:179], v16 offset:2048
	ds_read_b128 v[180:183], v16 offset:4096
	ds_read_b128 v[184:187], v16 offset:6144
	s_waitcnt lgkmcnt(14)
	v_mfma_f32_16x16x32_f16 v[56:59], v[156:159], v[136:139], v[56:59]
	s_add_u32 m0, s28, 0x1e000
	s_nop 0
	global_load_lds_dwordx4 v13, s[4:5]
	s_add_u32 s4, s4, s20
	s_addc_u32 s5, s5, 0
	s_waitcnt lgkmcnt(13)
	v_mfma_f32_16x16x32_f16 v[60:63], v[160:163], v[136:139], v[60:63]
	s_waitcnt lgkmcnt(12)
	v_mfma_f32_16x16x32_f16 v[64:67], v[164:167], v[136:139], v[64:67]
	s_waitcnt lgkmcnt(11)
	v_mfma_f32_16x16x32_f16 v[68:71], v[168:171], v[136:139], v[68:71]
	s_waitcnt lgkmcnt(10)
	v_mfma_f32_16x16x32_f16 v[72:75], v[156:159], v[140:143], v[72:75]
	v_mfma_f32_16x16x32_f16 v[76:79], v[160:163], v[140:143], v[76:79]
	s_add_u32 m0, s28, 0x20000
	s_nop 0
	global_load_lds_dwordx4 v10, s[6:7]
	v_mfma_f32_16x16x32_f16 v[80:83], v[164:167], v[140:143], v[80:83]
	v_mfma_f32_16x16x32_f16 v[84:87], v[168:171], v[140:143], v[84:87]
	s_waitcnt lgkmcnt(9)
	v_mfma_f32_16x16x32_f16 v[88:91], v[156:159], v[144:147], v[88:91]
	v_mfma_f32_16x16x32_f16 v[92:95], v[160:163], v[144:147], v[92:95]
	v_mfma_f32_16x16x32_f16 v[96:99], v[164:167], v[144:147], v[96:99]
	s_add_u32 m0, s28, 0x22000
	s_nop 0
	global_load_lds_dwordx4 v11, s[6:7]
	s_add_u32 s6, s6, s20
	s_addc_u32 s7, s7, 0
	v_mfma_f32_16x16x32_f16 v[100:103], v[168:171], v[144:147], v[100:103]
	s_waitcnt lgkmcnt(8)
	v_mfma_f32_16x16x32_f16 v[104:107], v[156:159], v[148:151], v[104:107]
	v_mfma_f32_16x16x32_f16 v[108:111], v[160:163], v[148:151], v[108:111]
	v_mfma_f32_16x16x32_f16 v[112:115], v[164:167], v[148:151], v[112:115]
	v_mfma_f32_16x16x32_f16 v[116:119], v[168:171], v[148:151], v[116:119]
	s_waitcnt vmcnt(6) lgkmcnt(0)
	s_barrier
	s_waitcnt lgkmcnt(7)
	ds_read_b128 v[136:139], v15 offset:49152
	ds_read_b128 v[156:159], v17 offset:49152
	ds_read_b128 v[160:163], v17 offset:51200
	ds_read_b128 v[164:167], v17 offset:53248
	ds_read_b128 v[168:171], v17 offset:55296
	ds_read_b128 v[140:143], v15 offset:51200
	ds_read_b128 v[144:147], v15 offset:53248
	ds_read_b128 v[148:151], v15 offset:55296
	s_waitcnt lgkmcnt(14)
	v_mfma_f32_16x16x32_f16 v[56:59], v[192:195], v[172:175], v[56:59]
	s_add_u32 m0, s28, 0x0
	s_nop 0
	global_load_lds_dwordx4 v10, s[4:5]
	s_waitcnt lgkmcnt(13)
	v_mfma_f32_16x16x32_f16 v[60:63], v[196:199], v[172:175], v[60:63]
	s_waitcnt lgkmcnt(12)
	v_mfma_f32_16x16x32_f16 v[64:67], v[200:203], v[172:175], v[64:67]
	s_waitcnt lgkmcnt(11)
	v_mfma_f32_16x16x32_f16 v[68:71], v[204:207], v[172:175], v[68:71]
	s_waitcnt lgkmcnt(10)
	v_mfma_f32_16x16x32_f16 v[72:75], v[192:195], v[176:179], v[72:75]
	v_mfma_f32_16x16x32_f16 v[76:79], v[196:199], v[176:179], v[76:79]
	s_add_u32 m0, s28, 0x2000
	s_nop 0
	global_load_lds_dwordx4 v11, s[4:5]
	v_mfma_f32_16x16x32_f16 v[80:83], v[200:203], v[176:179], v[80:83]
	v_mfma_f32_16x16x32_f16 v[84:87], v[204:207], v[176:179], v[84:87]
	s_waitcnt lgkmcnt(9)
	v_mfma_f32_16x16x32_f16 v[88:91], v[192:195], v[180:183], v[88:91]
	v_mfma_f32_16x16x32_f16 v[92:95], v[196:199], v[180:183], v[92:95]
	v_mfma_f32_16x16x32_f16 v[96:99], v[200:203], v[180:183], v[96:99]
	s_add_u32 m0, s28, 0x4000
	s_nop 0
	global_load_lds_dwordx4 v12, s[4:5]
	v_mfma_f32_16x16x32_f16 v[100:103], v[204:207], v[180:183], v[100:103]
	s_waitcnt lgkmcnt(8)
	v_mfma_f32_16x16x32_f16 v[104:107], v[192:195], v[184:187], v[104:107]
	v_mfma_f32_16x16x32_f16 v[108:111], v[196:199], v[184:187], v[108:111]
	v_mfma_f32_16x16x32_f16 v[112:115], v[200:203], v[184:187], v[112:115]
	v_mfma_f32_16x16x32_f16 v[116:119], v[204:207], v[184:187], v[116:119]
	s_waitcnt lgkmcnt(7)
	ds_read_b128 v[172:175], v16 offset:49152
	ds_read_b128 v[192:195], v18 offset:49152
	ds_read_b128 v[196:199], v18 offset:51200
	ds_read_b128 v[200:203], v18 offset:53248
	ds_read_b128 v[204:207], v18 offset:55296
	ds_read_b128 v[176:179], v16 offset:51200
	ds_read_b128 v[180:183], v16 offset:53248
	ds_read_b128 v[184:187], v16 offset:55296
	s_waitcnt lgkmcnt(14)
	v_mfma_f32_16x16x32_f16 v[56:59], v[156:159], v[136:139], v[56:59]
	s_add_u32 m0, s28, 0x6000
	s_nop 0
	global_load_lds_dwordx4 v13, s[4:5]
	s_add_u32 s4, s4, s20
	s_addc_u32 s5, s5, 0
	s_waitcnt lgkmcnt(13)
	v_mfma_f32_16x16x32_f16 v[60:63], v[160:163], v[136:139], v[60:63]
	s_waitcnt lgkmcnt(12)
	v_mfma_f32_16x16x32_f16 v[64:67], v[164:167], v[136:139], v[64:67]
	s_waitcnt lgkmcnt(11)
	v_mfma_f32_16x16x32_f16 v[68:71], v[168:171], v[136:139], v[68:71]
	s_waitcnt lgkmcnt(10)
	v_mfma_f32_16x16x32_f16 v[72:75], v[156:159], v[140:143], v[72:75]
	v_mfma_f32_16x16x32_f16 v[76:79], v[160:163], v[140:143], v[76:79]
	s_add_u32 m0, s28, 0x8000
	s_nop 0
	global_load_lds_dwordx4 v10, s[6:7]
	v_mfma_f32_16x16x32_f16 v[80:83], v[164:167], v[140:143], v[80:83]
	v_mfma_f32_16x16x32_f16 v[84:87], v[168:171], v[140:143], v[84:87]
	s_waitcnt lgkmcnt(9)
	v_mfma_f32_16x16x32_f16 v[88:91], v[156:159], v[144:147], v[88:91]
	v_mfma_f32_16x16x32_f16 v[92:95], v[160:163], v[144:147], v[92:95]
	v_mfma_f32_16x16x32_f16 v[96:99], v[164:167], v[144:147], v[96:99]
	s_add_u32 m0, s28, 0xa000
	s_nop 0
	global_load_lds_dwordx4 v11, s[6:7]
	s_add_u32 s6, s6, s20
	s_addc_u32 s7, s7, 0
	v_mfma_f32_16x16x32_f16 v[100:103], v[168:171], v[144:147], v[100:103]
	s_waitcnt lgkmcnt(8)
	v_mfma_f32_16x16x32_f16 v[104:107], v[156:159], v[148:151], v[104:107]
	v_mfma_f32_16x16x32_f16 v[108:111], v[160:163], v[148:151], v[108:111]
	v_mfma_f32_16x16x32_f16 v[112:115], v[164:167], v[148:151], v[112:115]
	v_mfma_f32_16x16x32_f16 v[116:119], v[168:171], v[148:151], v[116:119]
	s_waitcnt vmcnt(6) lgkmcnt(0)
	s_barrier
	s_waitcnt lgkmcnt(7)
	ds_read_b128 v[136:139], v19
	ds_read_b128 v[156:159], v21
	ds_read_b128 v[160:163], v21 offset:2048
	ds_read_b128 v[164:167], v21 offset:4096
	ds_read_b128 v[168:171], v21 offset:6144
	ds_read_b128 v[140:143], v19 offset:2048
	ds_read_b128 v[144:147], v19 offset:4096
	ds_read_b128 v[148:151], v19 offset:6144
	s_waitcnt lgkmcnt(14)
	v_mfma_f32_16x16x32_f16 v[56:59], v[192:195], v[172:175], v[56:59]
	s_waitcnt lgkmcnt(13)
	v_mfma_f32_16x16x32_f16 v[60:63], v[196:199], v[172:175], v[60:63]
	s_waitcnt lgkmcnt(12)
	v_mfma_f32_16x16x32_f16 v[64:67], v[200:203], v[172:175], v[64:67]
	s_waitcnt lgkmcnt(11)
	v_mfma_f32_16x16x32_f16 v[68:71], v[204:207], v[172:175], v[68:71]
	s_waitcnt lgkmcnt(10)
	v_mfma_f32_16x16x32_f16 v[72:75], v[192:195], v[176:179], v[72:75]
	v_mfma_f32_16x16x32_f16 v[76:79], v[196:199], v[176:179], v[76:79]
	v_mfma_f32_16x16x32_f16 v[80:83], v[200:203], v[176:179], v[80:83]
	v_mfma_f32_16x16x32_f16 v[84:87], v[204:207], v[176:179], v[84:87]
	s_waitcnt lgkmcnt(9)
	v_mfma_f32_16x16x32_f16 v[88:91], v[192:195], v[180:183], v[88:91]
	v_mfma_f32_16x16x32_f16 v[92:95], v[196:199], v[180:183], v[92:95]
	v_mfma_f32_16x16x32_f16 v[96:99], v[200:203], v[180:183], v[96:99]
	v_mfma_f32_16x16x32_f16 v[100:103], v[204:207], v[180:183], v[100:103]
	s_waitcnt lgkmcnt(8)
	v_mfma_f32_16x16x32_f16 v[104:107], v[192:195], v[184:187], v[104:107]
	v_mfma_f32_16x16x32_f16 v[108:111], v[196:199], v[184:187], v[108:111]
	v_mfma_f32_16x16x32_f16 v[112:115], v[200:203], v[184:187], v[112:115]
	v_mfma_f32_16x16x32_f16 v[116:119], v[204:207], v[184:187], v[116:119]
	s_waitcnt lgkmcnt(7)
	ds_read_b128 v[172:175], v20
	ds_read_b128 v[192:195], v22
	ds_read_b128 v[196:199], v22 offset:2048
	ds_read_b128 v[200:203], v22 offset:4096
	ds_read_b128 v[204:207], v22 offset:6144
	ds_read_b128 v[176:179], v20 offset:2048
	ds_read_b128 v[180:183], v20 offset:4096
	ds_read_b128 v[184:187], v20 offset:6144
	s_waitcnt lgkmcnt(14)
	v_mfma_f32_16x16x32_f16 v[56:59], v[156:159], v[136:139], v[56:59]
	s_waitcnt lgkmcnt(13)
	v_mfma_f32_16x16x32_f16 v[60:63], v[160:163], v[136:139], v[60:63]
	s_waitcnt lgkmcnt(12)
	v_mfma_f32_16x16x32_f16 v[64:67], v[164:167], v[136:139], v[64:67]
	s_waitcnt lgkmcnt(11)
	v_mfma_f32_16x16x32_f16 v[68:71], v[168:171], v[136:139], v[68:71]
	s_waitcnt lgkmcnt(10)
	v_mfma_f32_16x16x32_f16 v[72:75], v[156:159], v[140:143], v[72:75]
	v_mfma_f32_16x16x32_f16 v[76:79], v[160:163], v[140:143], v[76:79]
	v_mfma_f32_16x16x32_f16 v[80:83], v[164:167], v[140:143], v[80:83]
	v_mfma_f32_16x16x32_f16 v[84:87], v[168:171], v[140:143], v[84:87]
	s_waitcnt lgkmcnt(9)
	v_mfma_f32_16x16x32_f16 v[88:91], v[156:159], v[144:147], v[88:91]
	v_mfma_f32_16x16x32_f16 v[92:95], v[160:163], v[144:147], v[92:95]
	v_mfma_f32_16x16x32_f16 v[96:99], v[164:167], v[144:147], v[96:99]
	v_mfma_f32_16x16x32_f16 v[100:103], v[168:171], v[144:147], v[100:103]
	s_waitcnt lgkmcnt(8)
	v_mfma_f32_16x16x32_f16 v[104:107], v[156:159], v[148:151], v[104:107]
	v_mfma_f32_16x16x32_f16 v[108:111], v[160:163], v[148:151], v[108:111]
	v_mfma_f32_16x16x32_f16 v[112:115], v[164:167], v[148:151], v[112:115]
	v_mfma_f32_16x16x32_f16 v[116:119], v[168:171], v[148:151], v[116:119]
	s_waitcnt vmcnt(0) lgkmcnt(0)
	s_barrier
	s_waitcnt lgkmcnt(7)
	ds_read_b128 v[136:139], v15
	ds_read_b128 v[156:159], v17
	ds_read_b128 v[160:163], v17 offset:2048
	ds_read_b128 v[164:167], v17 offset:4096
	ds_read_b128 v[168:171], v17 offset:6144
	ds_read_b128 v[140:143], v15 offset:2048
	ds_read_b128 v[144:147], v15 offset:4096
	ds_read_b128 v[148:151], v15 offset:6144
	s_waitcnt lgkmcnt(14)
	v_mfma_f32_16x16x32_f16 v[56:59], v[192:195], v[172:175], v[56:59]
	s_waitcnt lgkmcnt(13)
	v_mfma_f32_16x16x32_f16 v[60:63], v[196:199], v[172:175], v[60:63]
	s_waitcnt lgkmcnt(12)
	v_mfma_f32_16x16x32_f16 v[64:67], v[200:203], v[172:175], v[64:67]
	s_waitcnt lgkmcnt(11)
	v_mfma_f32_16x16x32_f16 v[68:71], v[204:207], v[172:175], v[68:71]
	s_waitcnt lgkmcnt(10)
	v_mfma_f32_16x16x32_f16 v[72:75], v[192:195], v[176:179], v[72:75]
	v_mfma_f32_16x16x32_f16 v[76:79], v[196:199], v[176:179], v[76:79]
	v_mfma_f32_16x16x32_f16 v[80:83], v[200:203], v[176:179], v[80:83]
	v_mfma_f32_16x16x32_f16 v[84:87], v[204:207], v[176:179], v[84:87]
	s_waitcnt lgkmcnt(9)
	v_mfma_f32_16x16x32_f16 v[88:91], v[192:195], v[180:183], v[88:91]
	v_mfma_f32_16x16x32_f16 v[92:95], v[196:199], v[180:183], v[92:95]
	v_mfma_f32_16x16x32_f16 v[96:99], v[200:203], v[180:183], v[96:99]
	v_mfma_f32_16x16x32_f16 v[100:103], v[204:207], v[180:183], v[100:103]
	s_waitcnt lgkmcnt(8)
	v_mfma_f32_16x16x32_f16 v[104:107], v[192:195], v[184:187], v[104:107]
	v_mfma_f32_16x16x32_f16 v[108:111], v[196:199], v[184:187], v[108:111]
	v_mfma_f32_16x16x32_f16 v[112:115], v[200:203], v[184:187], v[112:115]
	v_mfma_f32_16x16x32_f16 v[116:119], v[204:207], v[184:187], v[116:119]
	s_waitcnt lgkmcnt(7)
	ds_read_b128 v[172:175], v16
	ds_read_b128 v[192:195], v18
	ds_read_b128 v[196:199], v18 offset:2048
	ds_read_b128 v[200:203], v18 offset:4096
	ds_read_b128 v[204:207], v18 offset:6144
	ds_read_b128 v[176:179], v16 offset:2048
	ds_read_b128 v[180:183], v16 offset:4096
	ds_read_b128 v[184:187], v16 offset:6144
	s_waitcnt lgkmcnt(14)
	v_mfma_f32_16x16x32_f16 v[56:59], v[156:159], v[136:139], v[56:59]
	s_waitcnt lgkmcnt(13)
	v_mfma_f32_16x16x32_f16 v[60:63], v[160:163], v[136:139], v[60:63]
	s_waitcnt lgkmcnt(12)
	v_mfma_f32_16x16x32_f16 v[64:67], v[164:167], v[136:139], v[64:67]
	s_waitcnt lgkmcnt(11)
	v_mfma_f32_16x16x32_f16 v[68:71], v[168:171], v[136:139], v[68:71]
	s_waitcnt lgkmcnt(10)
	v_mfma_f32_16x16x32_f16 v[72:75], v[156:159], v[140:143], v[72:75]
	v_mfma_f32_16x16x32_f16 v[76:79], v[160:163], v[140:143], v[76:79]
	v_mfma_f32_16x16x32_f16 v[80:83], v[164:167], v[140:143], v[80:83]
	v_mfma_f32_16x16x32_f16 v[84:87], v[168:171], v[140:143], v[84:87]
	s_waitcnt lgkmcnt(9)
	v_mfma_f32_16x16x32_f16 v[88:91], v[156:159], v[144:147], v[88:91]
	v_mfma_f32_16x16x32_f16 v[92:95], v[160:163], v[144:147], v[92:95]
	v_mfma_f32_16x16x32_f16 v[96:99], v[164:167], v[144:147], v[96:99]
	v_mfma_f32_16x16x32_f16 v[100:103], v[168:171], v[144:147], v[100:103]
	s_waitcnt lgkmcnt(8)
	v_mfma_f32_16x16x32_f16 v[104:107], v[156:159], v[148:151], v[104:107]
	v_mfma_f32_16x16x32_f16 v[108:111], v[160:163], v[148:151], v[108:111]
	v_mfma_f32_16x16x32_f16 v[112:115], v[164:167], v[148:151], v[112:115]
	v_mfma_f32_16x16x32_f16 v[116:119], v[168:171], v[148:151], v[116:119]
	s_waitcnt lgkmcnt(6)
	v_mfma_f32_16x16x32_f16 v[56:59], v[192:195], v[172:175], v[56:59]
	s_waitcnt lgkmcnt(5)
	v_mfma_f32_16x16x32_f16 v[60:63], v[196:199], v[172:175], v[60:63]
	s_waitcnt lgkmcnt(4)
	v_mfma_f32_16x16x32_f16 v[64:67], v[200:203], v[172:175], v[64:67]
	s_waitcnt lgkmcnt(3)
	v_mfma_f32_16x16x32_f16 v[68:71], v[204:207], v[172:175], v[68:71]
	s_waitcnt lgkmcnt(2)
	v_mfma_f32_16x16x32_f16 v[72:75], v[192:195], v[176:179], v[72:75]
	v_mfma_f32_16x16x32_f16 v[76:79], v[196:199], v[176:179], v[76:79]
	v_mfma_f32_16x16x32_f16 v[80:83], v[200:203], v[176:179], v[80:83]
	v_mfma_f32_16x16x32_f16 v[84:87], v[204:207], v[176:179], v[84:87]
	s_waitcnt lgkmcnt(1)
	v_mfma_f32_16x16x32_f16 v[88:91], v[192:195], v[180:183], v[88:91]
	v_mfma_f32_16x16x32_f16 v[92:95], v[196:199], v[180:183], v[92:95]
	v_mfma_f32_16x16x32_f16 v[96:99], v[200:203], v[180:183], v[96:99]
	v_mfma_f32_16x16x32_f16 v[100:103], v[204:207], v[180:183], v[100:103]
	s_waitcnt lgkmcnt(0)
	v_mfma_f32_16x16x32_f16 v[104:107], v[192:195], v[184:187], v[104:107]
	v_mfma_f32_16x16x32_f16 v[108:111], v[196:199], v[184:187], v[108:111]
	v_mfma_f32_16x16x32_f16 v[112:115], v[200:203], v[184:187], v[112:115]
	v_mfma_f32_16x16x32_f16 v[116:119], v[204:207], v[184:187], v[116:119]
	s_nop 7
	s_nop 1
	v_mov_b32_e32 v213, s19
	v_pk_add_f32 v[56:57], v[56:57], v[24:25]
	v_pk_add_f32 v[58:59], v[58:59], v[26:27]
	v_pk_add_f32 v[60:61], v[60:61], v[28:29]
	v_pk_add_f32 v[62:63], v[62:63], v[30:31]
	v_pk_add_f32 v[64:65], v[64:65], v[32:33]
	v_pk_add_f32 v[66:67], v[66:67], v[34:35]
	v_pk_add_f32 v[68:69], v[68:69], v[36:37]
	v_pk_add_f32 v[70:71], v[70:71], v[38:39]
	v_pk_mul_f32 v[208:209], v[56:57], v[56:57]
	v_pk_fma_f32 v[208:209], v[58:59], v[58:59], v[208:209]
	v_pk_fma_f32 v[208:209], v[60:61], v[60:61], v[208:209]
	v_pk_fma_f32 v[208:209], v[62:63], v[62:63], v[208:209]
	v_pk_fma_f32 v[208:209], v[64:65], v[64:65], v[208:209]
	v_pk_fma_f32 v[208:209], v[66:67], v[66:67], v[208:209]
	v_pk_fma_f32 v[208:209], v[68:69], v[68:69], v[208:209]
	v_pk_fma_f32 v[208:209], v[70:71], v[70:71], v[208:209]
	v_add_f32_e32 v208, v208, v209
	v_mov_b32_e32 v209, v208
	s_nop 1
	v_permlane16_swap_b32_e32 v208, v209
	v_add_f32_e32 v208, v208, v209
	v_mov_b32_e32 v209, v208
	s_nop 1
	v_permlane32_swap_b32_e32 v208, v209
	v_add_f32_e32 v208, v208, v209
	v_mov_b32_e32 v210, 0x358637bd
	v_fmac_f32_e32 v210, 0x3c800000, v208
	v_rsq_f32_e32 v210, v210
	s_add_u32 s24, s29, 0
	s_lshr_b32 s8, s24, 1
	s_lshl_b32 s8, s8, 12
	s_and_b32 s24, s24, 1
	s_lshl_b32 s24, s24, 8
	s_add_u32 s8, s8, s24
	v_mul_f32_e32 v210, v213, v210
	v_add_u32_e32 v212, s8, v23
	v_pk_mul_f32 v[56:57], v[56:57], v[210:211] op_sel_hi:[1,0]
	v_pk_mul_f32 v[58:59], v[58:59], v[210:211] op_sel_hi:[1,0]
	v_pk_mul_f32 v[56:57], v[56:57], v[40:41]
	v_pk_mul_f32 v[58:59], v[58:59], v[42:43]
	v_cvt_pk_f16_f32 v56, v56, v57
	v_cvt_pk_f16_f32 v57, v58, v59
	global_store_dwordx2 v212, v[56:57], s[22:23] offset:0
	v_pk_mul_f32 v[60:61], v[60:61], v[210:211] op_sel_hi:[1,0]
	v_pk_mul_f32 v[62:63], v[62:63], v[210:211] op_sel_hi:[1,0]
	v_pk_mul_f32 v[60:61], v[60:61], v[44:45]
	v_pk_mul_f32 v[62:63], v[62:63], v[46:47]
	v_cvt_pk_f16_f32 v60, v60, v61
	v_cvt_pk_f16_f32 v61, v62, v63
	global_store_dwordx2 v212, v[60:61], s[22:23] offset:1024
	v_pk_mul_f32 v[64:65], v[64:65], v[210:211] op_sel_hi:[1,0]
	v_pk_mul_f32 v[66:67], v[66:67], v[210:211] op_sel_hi:[1,0]
	v_pk_mul_f32 v[64:65], v[64:65], v[48:49]
	v_pk_mul_f32 v[66:67], v[66:67], v[50:51]
	v_cvt_pk_f16_f32 v64, v64, v65
	v_cvt_pk_f16_f32 v65, v66, v67
	global_store_dwordx2 v212, v[64:65], s[22:23] offset:2048
	v_pk_mul_f32 v[68:69], v[68:69], v[210:211] op_sel_hi:[1,0]
	v_pk_mul_f32 v[70:71], v[70:71], v[210:211] op_sel_hi:[1,0]
	v_pk_mul_f32 v[68:69], v[68:69], v[52:53]
	v_pk_mul_f32 v[70:71], v[70:71], v[54:55]
	v_cvt_pk_f16_f32 v68, v68, v69
	v_cvt_pk_f16_f32 v69, v70, v71
	global_store_dwordx2 v212, v[68:69], s[22:23] offset:3072
	v_pk_add_f32 v[72:73], v[72:73], v[24:25]
	v_pk_add_f32 v[74:75], v[74:75], v[26:27]
	v_pk_add_f32 v[76:77], v[76:77], v[28:29]
	v_pk_add_f32 v[78:79], v[78:79], v[30:31]
	v_pk_add_f32 v[80:81], v[80:81], v[32:33]
	v_pk_add_f32 v[82:83], v[82:83], v[34:35]
	v_pk_add_f32 v[84:85], v[84:85], v[36:37]
	v_pk_add_f32 v[86:87], v[86:87], v[38:39]
	v_pk_mul_f32 v[208:209], v[72:73], v[72:73]
	v_pk_fma_f32 v[208:209], v[74:75], v[74:75], v[208:209]
	v_pk_fma_f32 v[208:209], v[76:77], v[76:77], v[208:209]
	v_pk_fma_f32 v[208:209], v[78:79], v[78:79], v[208:209]
	v_pk_fma_f32 v[208:209], v[80:81], v[80:81], v[208:209]
	v_pk_fma_f32 v[208:209], v[82:83], v[82:83], v[208:209]
	v_pk_fma_f32 v[208:209], v[84:85], v[84:85], v[208:209]
	v_pk_fma_f32 v[208:209], v[86:87], v[86:87], v[208:209]
	v_add_f32_e32 v208, v208, v209
	v_mov_b32_e32 v209, v208
	s_nop 1
	v_permlane16_swap_b32_e32 v208, v209
	v_add_f32_e32 v208, v208, v209
	v_mov_b32_e32 v209, v208
	s_nop 1
	v_permlane32_swap_b32_e32 v208, v209
	v_add_f32_e32 v208, v208, v209
	v_mov_b32_e32 v210, 0x358637bd
	v_fmac_f32_e32 v210, 0x3c800000, v208
	v_rsq_f32_e32 v210, v210
	s_add_u32 s24, s29, 1
	s_lshr_b32 s8, s24, 1
	s_lshl_b32 s8, s8, 12
	s_and_b32 s24, s24, 1
	s_lshl_b32 s24, s24, 8
	s_add_u32 s8, s8, s24
	v_mul_f32_e32 v210, v213, v210
	v_add_u32_e32 v212, s8, v23
	v_pk_mul_f32 v[72:73], v[72:73], v[210:211] op_sel_hi:[1,0]
	v_pk_mul_f32 v[74:75], v[74:75], v[210:211] op_sel_hi:[1,0]
	v_pk_mul_f32 v[72:73], v[72:73], v[40:41]
	v_pk_mul_f32 v[74:75], v[74:75], v[42:43]
	v_cvt_pk_f16_f32 v72, v72, v73
	v_cvt_pk_f16_f32 v73, v74, v75
	global_store_dwordx2 v212, v[72:73], s[22:23] offset:0
	v_pk_mul_f32 v[76:77], v[76:77], v[210:211] op_sel_hi:[1,0]
	v_pk_mul_f32 v[78:79], v[78:79], v[210:211] op_sel_hi:[1,0]
	v_pk_mul_f32 v[76:77], v[76:77], v[44:45]
	v_pk_mul_f32 v[78:79], v[78:79], v[46:47]
	v_cvt_pk_f16_f32 v76, v76, v77
	v_cvt_pk_f16_f32 v77, v78, v79
	global_store_dwordx2 v212, v[76:77], s[22:23] offset:1024
	v_pk_mul_f32 v[80:81], v[80:81], v[210:211] op_sel_hi:[1,0]
	v_pk_mul_f32 v[82:83], v[82:83], v[210:211] op_sel_hi:[1,0]
	v_pk_mul_f32 v[80:81], v[80:81], v[48:49]
	v_pk_mul_f32 v[82:83], v[82:83], v[50:51]
	v_cvt_pk_f16_f32 v80, v80, v81
	v_cvt_pk_f16_f32 v81, v82, v83
	global_store_dwordx2 v212, v[80:81], s[22:23] offset:2048
	v_pk_mul_f32 v[84:85], v[84:85], v[210:211] op_sel_hi:[1,0]
	v_pk_mul_f32 v[86:87], v[86:87], v[210:211] op_sel_hi:[1,0]
	v_pk_mul_f32 v[84:85], v[84:85], v[52:53]
	v_pk_mul_f32 v[86:87], v[86:87], v[54:55]
	v_cvt_pk_f16_f32 v84, v84, v85
	v_cvt_pk_f16_f32 v85, v86, v87
	global_store_dwordx2 v212, v[84:85], s[22:23] offset:3072
	v_pk_add_f32 v[88:89], v[88:89], v[24:25]
	v_pk_add_f32 v[90:91], v[90:91], v[26:27]
	v_pk_add_f32 v[92:93], v[92:93], v[28:29]
	v_pk_add_f32 v[94:95], v[94:95], v[30:31]
	v_pk_add_f32 v[96:97], v[96:97], v[32:33]
	v_pk_add_f32 v[98:99], v[98:99], v[34:35]
	v_pk_add_f32 v[100:101], v[100:101], v[36:37]
	v_pk_add_f32 v[102:103], v[102:103], v[38:39]
	v_pk_mul_f32 v[208:209], v[88:89], v[88:89]
	v_pk_fma_f32 v[208:209], v[90:91], v[90:91], v[208:209]
	v_pk_fma_f32 v[208:209], v[92:93], v[92:93], v[208:209]
	v_pk_fma_f32 v[208:209], v[94:95], v[94:95], v[208:209]
	v_pk_fma_f32 v[208:209], v[96:97], v[96:97], v[208:209]
	v_pk_fma_f32 v[208:209], v[98:99], v[98:99], v[208:209]
	v_pk_fma_f32 v[208:209], v[100:101], v[100:101], v[208:209]
	v_pk_fma_f32 v[208:209], v[102:103], v[102:103], v[208:209]
	v_add_f32_e32 v208, v208, v209
	v_mov_b32_e32 v209, v208
	s_nop 1
	v_permlane16_swap_b32_e32 v208, v209
	v_add_f32_e32 v208, v208, v209
	v_mov_b32_e32 v209, v208
	s_nop 1
	v_permlane32_swap_b32_e32 v208, v209
	v_add_f32_e32 v208, v208, v209
	v_mov_b32_e32 v210, 0x358637bd
	v_fmac_f32_e32 v210, 0x3c800000, v208
	v_rsq_f32_e32 v210, v210
	s_add_u32 s24, s29, 2
	s_lshr_b32 s8, s24, 1
	s_lshl_b32 s8, s8, 12
	s_and_b32 s24, s24, 1
	s_lshl_b32 s24, s24, 8
	s_add_u32 s8, s8, s24
	v_mul_f32_e32 v210, v213, v210
	v_add_u32_e32 v212, s8, v23
	v_pk_mul_f32 v[88:89], v[88:89], v[210:211] op_sel_hi:[1,0]
	v_pk_mul_f32 v[90:91], v[90:91], v[210:211] op_sel_hi:[1,0]
	v_pk_mul_f32 v[88:89], v[88:89], v[40:41]
	v_pk_mul_f32 v[90:91], v[90:91], v[42:43]
	v_cvt_pk_f16_f32 v88, v88, v89
	v_cvt_pk_f16_f32 v89, v90, v91
	global_store_dwordx2 v212, v[88:89], s[22:23] offset:0
	v_pk_mul_f32 v[92:93], v[92:93], v[210:211] op_sel_hi:[1,0]
	v_pk_mul_f32 v[94:95], v[94:95], v[210:211] op_sel_hi:[1,0]
	v_pk_mul_f32 v[92:93], v[92:93], v[44:45]
	v_pk_mul_f32 v[94:95], v[94:95], v[46:47]
	v_cvt_pk_f16_f32 v92, v92, v93
	v_cvt_pk_f16_f32 v93, v94, v95
	global_store_dwordx2 v212, v[92:93], s[22:23] offset:1024
	v_pk_mul_f32 v[96:97], v[96:97], v[210:211] op_sel_hi:[1,0]
	v_pk_mul_f32 v[98:99], v[98:99], v[210:211] op_sel_hi:[1,0]
	v_pk_mul_f32 v[96:97], v[96:97], v[48:49]
	v_pk_mul_f32 v[98:99], v[98:99], v[50:51]
	v_cvt_pk_f16_f32 v96, v96, v97
	v_cvt_pk_f16_f32 v97, v98, v99
	global_store_dwordx2 v212, v[96:97], s[22:23] offset:2048
	v_pk_mul_f32 v[100:101], v[100:101], v[210:211] op_sel_hi:[1,0]
	v_pk_mul_f32 v[102:103], v[102:103], v[210:211] op_sel_hi:[1,0]
	v_pk_mul_f32 v[100:101], v[100:101], v[52:53]
	v_pk_mul_f32 v[102:103], v[102:103], v[54:55]
	v_cvt_pk_f16_f32 v100, v100, v101
	v_cvt_pk_f16_f32 v101, v102, v103
	global_store_dwordx2 v212, v[100:101], s[22:23] offset:3072
	v_pk_add_f32 v[104:105], v[104:105], v[24:25]
	v_pk_add_f32 v[106:107], v[106:107], v[26:27]
	v_pk_add_f32 v[108:109], v[108:109], v[28:29]
	v_pk_add_f32 v[110:111], v[110:111], v[30:31]
	v_pk_add_f32 v[112:113], v[112:113], v[32:33]
	v_pk_add_f32 v[114:115], v[114:115], v[34:35]
	v_pk_add_f32 v[116:117], v[116:117], v[36:37]
	v_pk_add_f32 v[118:119], v[118:119], v[38:39]
	v_pk_mul_f32 v[208:209], v[104:105], v[104:105]
	v_pk_fma_f32 v[208:209], v[106:107], v[106:107], v[208:209]
	v_pk_fma_f32 v[208:209], v[108:109], v[108:109], v[208:209]
	v_pk_fma_f32 v[208:209], v[110:111], v[110:111], v[208:209]
	v_pk_fma_f32 v[208:209], v[112:113], v[112:113], v[208:209]
	v_pk_fma_f32 v[208:209], v[114:115], v[114:115], v[208:209]
	v_pk_fma_f32 v[208:209], v[116:117], v[116:117], v[208:209]
	v_pk_fma_f32 v[208:209], v[118:119], v[118:119], v[208:209]
	v_add_f32_e32 v208, v208, v209
	v_mov_b32_e32 v209, v208
	s_nop 1
	v_permlane16_swap_b32_e32 v208, v209
	v_add_f32_e32 v208, v208, v209
	v_mov_b32_e32 v209, v208
	s_nop 1
	v_permlane32_swap_b32_e32 v208, v209
	v_add_f32_e32 v208, v208, v209
	v_mov_b32_e32 v210, 0x358637bd
	v_fmac_f32_e32 v210, 0x3c800000, v208
	v_rsq_f32_e32 v210, v210
	s_add_u32 s24, s29, 3
	s_lshr_b32 s8, s24, 1
	s_lshl_b32 s8, s8, 12
	s_and_b32 s24, s24, 1
	s_lshl_b32 s24, s24, 8
	s_add_u32 s8, s8, s24
	v_mul_f32_e32 v210, v213, v210
	v_add_u32_e32 v212, s8, v23
	v_pk_mul_f32 v[104:105], v[104:105], v[210:211] op_sel_hi:[1,0]
	v_pk_mul_f32 v[106:107], v[106:107], v[210:211] op_sel_hi:[1,0]
	v_pk_mul_f32 v[104:105], v[104:105], v[40:41]
	v_pk_mul_f32 v[106:107], v[106:107], v[42:43]
	v_cvt_pk_f16_f32 v104, v104, v105
	v_cvt_pk_f16_f32 v105, v106, v107
	global_store_dwordx2 v212, v[104:105], s[22:23] offset:0
	v_pk_mul_f32 v[108:109], v[108:109], v[210:211] op_sel_hi:[1,0]
	v_pk_mul_f32 v[110:111], v[110:111], v[210:211] op_sel_hi:[1,0]
	v_pk_mul_f32 v[108:109], v[108:109], v[44:45]
	v_pk_mul_f32 v[110:111], v[110:111], v[46:47]
	v_cvt_pk_f16_f32 v108, v108, v109
	v_cvt_pk_f16_f32 v109, v110, v111
	global_store_dwordx2 v212, v[108:109], s[22:23] offset:1024
	v_pk_mul_f32 v[112:113], v[112:113], v[210:211] op_sel_hi:[1,0]
	v_pk_mul_f32 v[114:115], v[114:115], v[210:211] op_sel_hi:[1,0]
	v_pk_mul_f32 v[112:113], v[112:113], v[48:49]
	v_pk_mul_f32 v[114:115], v[114:115], v[50:51]
	v_cvt_pk_f16_f32 v112, v112, v113
	v_cvt_pk_f16_f32 v113, v114, v115
	global_store_dwordx2 v212, v[112:113], s[22:23] offset:2048
	v_pk_mul_f32 v[116:117], v[116:117], v[210:211] op_sel_hi:[1,0]
	v_pk_mul_f32 v[118:119], v[118:119], v[210:211] op_sel_hi:[1,0]
	v_pk_mul_f32 v[116:117], v[116:117], v[52:53]
	v_pk_mul_f32 v[118:119], v[118:119], v[54:55]
	v_cvt_pk_f16_f32 v116, v116, v117
	v_cvt_pk_f16_f32 v117, v118, v119
	global_store_dwordx2 v212, v[116:117], s[22:23] offset:3072
	s_branch .Lpf_done
.Lpf_vKA:
	s_mul_i32 s25, s25, 0x50
	s_add_u32 s29, s10, s25
	s_lshr_b32 s29, s29, 4
	v_add_u32_e32 v5, s25, v3
	v_lshlrev_b32_e32 v5, 7, v5
	v_add_u32_e32 v15, v5, v6
	v_add_u32_e32 v16, v5, v7
	v_add_u32_e32 v5, 0x9000, v9
	v_add_u32_e32 v17, v5, v6
	v_add_u32_e32 v18, v5, v7
	v_add_u32_e32 v19, 0x1a000, v15
	v_add_u32_e32 v20, 0x1a000, v16
	v_add_u32_e32 v21, 0x1a000, v17
	v_add_u32_e32 v22, 0x1a000, v18
	v_lshlrev_b32_e32 v5, 4, v4
	global_load_dwordx4 v[24:27], v5, s[14:15] offset:0
	global_load_dwordx4 v[28:31], v5, s[14:15] offset:64
	global_load_dwordx4 v[32:35], v5, s[14:15] offset:128
	global_load_dwordx4 v[36:39], v5, s[14:15] offset:192
	global_load_dwordx4 v[40:43], v5, s[16:17] offset:0
	global_load_dwordx4 v[44:47], v5, s[16:17] offset:64
	global_load_dwordx4 v[48:51], v5, s[16:17] offset:128
	global_load_dwordx4 v[52:55], v5, s[16:17] offset:192
	s_add_u32 m0, s28, 0x0
	s_nop 0
	global_load_lds_dwordx4 v10, s[4:5]
	s_add_u32 m0, s28, 0x2000
	s_nop 0
	global_load_lds_dwordx4 v11, s[4:5]
	s_add_u32 m0, s28, 0x4000
	s_nop 0
	global_load_lds_dwordx4 v12, s[4:5]
	s_add_u32 m0, s28, 0x6000
	s_nop 0
	global_load_lds_dwordx4 v13, s[4:5]
	s_add_u32 m0, s28, 0x8000
	s_nop 0
	global_load_lds_dwordx4 v14, s[4:5]
	s_add_u32 s4, s4, s20
	s_addc_u32 s5, s5, 0
	s_add_u32 m0, s28, 0x9000
	s_nop 0
	global_load_lds_dwordx4 v10, s[6:7]
	s_add_u32 m0, s28, 0xb000
	s_nop 0
	global_load_lds_dwordx4 v11, s[6:7]
	s_add_u32 s6, s6, s20
	s_addc_u32 s7, s7, 0
	s_add_u32 m0, s28, 0xd000
	s_nop 0
	global_load_lds_dwordx4 v10, s[4:5]
	s_add_u32 m0, s28, 0xf000
	s_nop 0
	global_load_lds_dwordx4 v11, s[4:5]
	s_add_u32 m0, s28, 0x11000
	s_nop 0
	global_load_lds_dwordx4 v12, s[4:5]
	s_add_u32 m0, s28, 0x13000
	s_nop 0
	global_load_lds_dwordx4 v13, s[4:5]
	s_add_u32 m0, s28, 0x15000
	s_nop 0
	global_load_lds_dwordx4 v14, s[4:5]
	s_add_u32 s4, s4, s20
	s_addc_u32 s5, s5, 0
	s_add_u32 m0, s28, 0x16000
	s_nop 0
	global_load_lds_dwordx4 v10, s[6:7]
	s_add_u32 m0, s28, 0x18000
	s_nop 0
	global_load_lds_dwordx4 v11, s[6:7]
	s_add_u32 s6, s6, s20
	s_addc_u32 s7, s7, 0
	s_add_u32 m0, s28, 0x1a000
	s_nop 0
	global_load_lds_dwordx4 v10, s[4:5]
	s_add_u32 m0, s28, 0x1c000
	s_nop 0
	global_load_lds_dwordx4 v11, s[4:5]
	s_add_u32 m0, s28, 0x1e000
	s_nop 0
	global_load_lds_dwordx4 v12, s[4:5]
	s_add_u32 m0, s28, 0x20000
	s_nop 0
	global_load_lds_dwordx4 v13, s[4:5]
	s_add_u32 m0, s28, 0x22000
	s_nop 0
	global_load_lds_dwordx4 v14, s[4:5]
	s_add_u32 s4, s4, s20
	s_addc_u32 s5, s5, 0
	s_add_u32 m0, s28, 0x23000
	s_nop 0
	global_load_lds_dwordx4 v10, s[6:7]
	s_add_u32 m0, s28, 0x25000
	s_nop 0
	global_load_lds_dwordx4 v11, s[6:7]
	s_add_u32 s6, s6, s20
	s_addc_u32 s7, s7, 0
	s_waitcnt vmcnt(14) lgkmcnt(0)
	s_barrier
	s_waitcnt lgkmcnt(6)
	ds_read_b128 v[136:139], v15
	ds_read_b128 v[156:159], v17
	ds_read_b128 v[160:163], v17 offset:2048
	ds_read_b128 v[164:167], v17 offset:4096
	ds_read_b128 v[168:171], v17 offset:6144
	ds_read_b128 v[140:143], v15 offset:2048
	ds_read_b128 v[144:147], v15 offset:4096
	ds_read_b128 v[148:151], v15 offset:6144
	ds_read_b128 v[152:155], v15 offset:8192
	s_waitcnt lgkmcnt(6)
	ds_read_b128 v[172:175], v16
	ds_read_b128 v[192:195], v18
	ds_read_b128 v[196:199], v18 offset:2048
	ds_read_b128 v[200:203], v18 offset:4096
	ds_read_b128 v[204:207], v18 offset:6144
	ds_read_b128 v[176:179], v16 offset:2048
	ds_read_b128 v[180:183], v16 offset:4096
	ds_read_b128 v[184:187], v16 offset:6144
	ds_read_b128 v[188:191], v16 offset:8192
	v_mfma_f32_16x16x32_f16 v[56:59], v[156:159], v[136:139], 0
	s_waitcnt lgkmcnt(15)
	v_mfma_f32_16x16x32_f16 v[60:63], v[160:163], v[136:139], 0
	s_waitcnt lgkmcnt(14)
	v_mfma_f32_16x16x32_f16 v[64:67], v[164:167], v[136:139], 0
	s_waitcnt lgkmcnt(13)
	v_mfma_f32_16x16x32_f16 v[68:71], v[168:171], v[136:139], 0
	s_waitcnt lgkmcnt(12)
	v_mfma_f32_16x16x32_f16 v[72:75], v[156:159], v[140:143], 0
	v_mfma_f32_16x16x32_f16 v[76:79], v[160:163], v[140:143], 0
	v_mfma_f32_16x16x32_f16 v[80:83], v[164:167], v[140:143], 0
	v_mfma_f32_16x16x32_f16 v[84:87], v[168:171], v[140:143], 0
	s_waitcnt lgkmcnt(11)
	v_mfma_f32_16x16x32_f16 v[88:91], v[156:159], v[144:147], 0
	v_mfma_f32_16x16x32_f16 v[92:95], v[160:163], v[144:147], 0
	v_mfma_f32_16x16x32_f16 v[96:99], v[164:167], v[144:147], 0
	v_mfma_f32_16x16x32_f16 v[100:103], v[168:171], v[144:147], 0
	s_waitcnt lgkmcnt(10)
	v_mfma_f32_16x16x32_f16 v[104:107], v[156:159], v[148:151], 0
	v_mfma_f32_16x16x32_f16 v[108:111], v[160:163], v[148:151], 0
	v_mfma_f32_16x16x32_f16 v[112:115], v[164:167], v[148:151], 0
	v_mfma_f32_16x16x32_f16 v[116:119], v[168:171], v[148:151], 0
	s_waitcnt lgkmcnt(9)
	v_mfma_f32_16x16x32_f16 v[120:123], v[156:159], v[152:155], 0
	v_mfma_f32_16x16x32_f16 v[124:127], v[160:163], v[152:155], 0
	v_mfma_f32_16x16x32_f16 v[128:131], v[164:167], v[152:155], 0
	v_mfma_f32_16x16x32_f16 v[132:135], v[168:171], v[152:155], 0
	s_waitcnt vmcnt(7) lgkmcnt(0)
	s_barrier
	s_waitcnt lgkmcnt(6)
	ds_read_b128 v[136:139], v15 offset:53248
	ds_read_b128 v[156:159], v17 offset:53248
	ds_read_b128 v[160:163], v17 offset:55296
	ds_read_b128 v[164:167], v17 offset:57344
	ds_read_b128 v[168:171], v17 offset:59392
	ds_read_b128 v[140:143], v15 offset:55296
	ds_read_b128 v[144:147], v15 offset:57344
	ds_read_b128 v[148:151], v15 offset:59392
	ds_read_b128 v[152:155], v15 offset:61440
	v_mfma_f32_16x16x32_f16 v[56:59], v[192:195], v[172:175], v[56:59]
	s_add_u32 m0, s28, 0x0
	s_nop 0
	global_load_lds_dwordx4 v10, s[4:5]
	s_waitcnt lgkmcnt(15)
	v_mfma_f32_16x16x32_f16 v[60:63], v[196:199], v[172:175], v[60:63]
	s_waitcnt lgkmcnt(14)
	v_mfma_f32_16x16x32_f16 v[64:67], v[200:203], v[172:175], v[64:67]
	s_waitcnt lgkmcnt(13)
	v_mfma_f32_16x16x32_f16 v[68:71], v[204:207], v[172:175], v[68:71]
	s_waitcnt lgkmcnt(12)
	v_mfma_f32_16x16x32_f16 v[72:75], v[192:195], v[176:179], v[72:75]
	v_mfma_f32_16x16x32_f16 v[76:79], v[196:199], v[176:179], v[76:79]
	s_add_u32 m0, s28, 0x2000
	s_nop 0
	global_load_lds_dwordx4 v11, s[4:5]
	v_mfma_f32_16x16x32_f16 v[80:83], v[200:203], v[176:179], v[80:83]
	v_mfma_f32_16x16x32_f16 v[84:87], v[204:207], v[176:179], v[84:87]
	s_waitcnt lgkmcnt(11)
	v_mfma_f32_16x16x32_f16 v[88:91], v[192:195], v[180:183], v[88:91]
	v_mfma_f32_16x16x32_f16 v[92:95], v[196:199], v[180:183], v[92:95]
	v_mfma_f32_16x16x32_f16 v[96:99], v[200:203], v[180:183], v[96:99]
	s_add_u32 m0, s28, 0x4000
	s_nop 0
	global_load_lds_dwordx4 v12, s[4:5]
	v_mfma_f32_16x16x32_f16 v[100:103], v[204:207], v[180:183], v[100:103]
	s_waitcnt lgkmcnt(10)
	v_mfma_f32_16x16x32_f16 v[104:107], v[192:195], v[184:187], v[104:107]
	v_mfma_f32_16x16x32_f16 v[108:111], v[196:199], v[184:187], v[108:111]
	v_mfma_f32_16x16x32_f16 v[112:115], v[200:203], v[184:187], v[112:115]
	v_mfma_f32_16x16x32_f16 v[116:119], v[204:207], v[184:187], v[116:119]
	s_add_u32 m0, s28, 0x6000
	s_nop 0
	global_load_lds_dwordx4 v13, s[4:5]
	s_waitcnt lgkmcnt(9)
	v_mfma_f32_16x16x32_f16 v[120:123], v[192:195], v[188:191], v[120:123]
	v_mfma_f32_16x16x32_f16 v[124:127], v[196:199], v[188:191], v[124:127]
	v_mfma_f32_16x16x32_f16 v[128:131], v[200:203], v[188:191], v[128:131]
	v_mfma_f32_16x16x32_f16 v[132:135], v[204:207], v[188:191], v[132:135]
	s_waitcnt lgkmcnt(6)
	ds_read_b128 v[172:175], v16 offset:53248
	ds_read_b128 v[192:195], v18 offset:53248
	ds_read_b128 v[196:199], v18 offset:55296
	ds_read_b128 v[200:203], v18 offset:57344
	ds_read_b128 v[204:207], v18 offset:59392
	ds_read_b128 v[176:179], v16 offset:55296
	ds_read_b128 v[180:183], v16 offset:57344
	ds_read_b128 v[184:187], v16 offset:59392
	ds_read_b128 v[188:191], v16 offset:61440
	v_mfma_f32_16x16x32_f16 v[56:59], v[156:159], v[136:139], v[56:59]
	s_add_u32 m0, s28, 0x8000
	s_nop 0
	global_load_lds_dwordx4 v14, s[4:5]
	s_add_u32 s4, s4, s20
	s_addc_u32 s5, s5, 0
	s_waitcnt lgkmcnt(15)
	v_mfma_f32_16x16x32_f16 v[60:63], v[160:163], v[136:139], v[60:63]
	s_waitcnt lgkmcnt(14)
	v_mfma_f32_16x16x32_f16 v[64:67], v[164:167], v[136:139], v[64:67]
	s_waitcnt lgkmcnt(13)
	v_mfma_f32_16x16x32_f16 v[68:71], v[168:171], v[136:139], v[68:71]
	s_waitcnt lgkmcnt(12)
	v_mfma_f32_16x16x32_f16 v[72:75], v[156:159], v[140:143], v[72:75]
	v_mfma_f32_16x16x32_f16 v[76:79], v[160:163], v[140:143], v[76:79]
	v_mfma_f32_16x16x32_f16 v[80:83], v[164:167], v[140:143], v[80:83]
	s_add_u32 m0, s28, 0x9000
	s_nop 0
	global_load_lds_dwordx4 v10, s[6:7]
	v_mfma_f32_16x16x32_f16 v[84:87], v[168:171], v[140:143], v[84:87]
	s_waitcnt lgkmcnt(11)
	v_mfma_f32_16x16x32_f16 v[88:91], v[156:159], v[144:147], v[88:91]
	v_mfma_f32_16x16x32_f16 v[92:95], v[160:163], v[144:147], v[92:95]
	v_mfma_f32_16x16x32_f16 v[96:99], v[164:167], v[144:147], v[96:99]
	v_mfma_f32_16x16x32_f16 v[100:103], v[168:171], v[144:147], v[100:103]
	s_waitcnt lgkmcnt(10)
	v_mfma_f32_16x16x32_f16 v[104:107], v[156:159], v[148:151], v[104:107]
	v_mfma_f32_16x16x32_f16 v[108:111], v[160:163], v[148:151], v[108:111]
	s_add_u32 m0, s28, 0xb000
	s_nop 0
	global_load_lds_dwordx4 v11, s[6:7]
	s_add_u32 s6, s6, s20
	s_addc_u32 s7, s7, 0
	v_mfma_f32_16x16x32_f16 v[112:115], v[164:167], v[148:151], v[112:115]
	v_mfma_f32_16x16x32_f16 v[116:119], v[168:171], v[148:151], v[116:119]
	s_waitcnt lgkmcnt(9)
	v_mfma_f32_16x16x32_f16 v[120:123], v[156:159], v[152:155], v[120:123]
	v_mfma_f32_16x16x32_f16 v[124:127], v[160:163], v[152:155], v[124:127]
	v_mfma_f32_16x16x32_f16 v[128:131], v[164:167], v[152:155], v[128:131]
	v_mfma_f32_16x16x32_f16 v[132:135], v[168:171], v[152:155], v[132:135]
	s_waitcnt vmcnt(7) lgkmcnt(0)
	s_barrier
	s_waitcnt lgkmcnt(6)
	ds_read_b128 v[136:139], v19
	ds_read_b128 v[156:159], v21
	ds_read_b128 v[160:163], v21 offset:2048
	ds_read_b128 v[164:167], v21 offset:4096
	ds_read_b128 v[168:171], v21 offset:6144
	ds_read_b128 v[140:143], v19 offset:2048
	ds_read_b128 v[144:147], v19 offset:4096
	ds_read_b128 v[148:151], v19 offset:6144
	ds_read_b128 v[152:155], v19 offset:8192
	v_mfma_f32_16x16x32_f16 v[56:59], v[192:195], v[172:175], v[56:59]
	s_add_u32 m0, s28, 0xd000
	s_nop 0
	global_load_lds_dwordx4 v10, s[4:5]
	s_waitcnt lgkmcnt(15)
	v_mfma_f32_16x16x32_f16 v[60:63], v[196:199], v[172:175], v[60:63]
	s_waitcnt lgkmcnt(14)
	v_mfma_f32_16x16x32_f16 v[64:67], v[200:203], v[172:175], v[64:67]
	s_waitcnt lgkmcnt(13)
	v_mfma_f32_16x16x32_f16 v[68:71], v[204:207], v[172:175], v[68:71]
	s_waitcnt lgkmcnt(12)
	v_mfma_f32_16x16x32_f16 v[72:75], v[192:195], v[176:179], v[72:75]
	v_mfma_f32_16x16x32_f16 v[76:79], v[196:199], v[176:179], v[76:79]
	s_add_u32 m0, s28, 0xf000
	s_nop 0
	global_load_lds_dwordx4 v11, s[4:5]
	v_mfma_f32_16x16x32_f16 v[80:83], v[200:203], v[176:179], v[80:83]
	v_mfma_f32_16x16x32_f16 v[84:87], v[204:207], v[176:179], v[84:87]
	s_waitcnt lgkmcnt(11)
	v_mfma_f32_16x16x32_f16 v[88:91], v[192:195], v[180:183], v[88:91]
	v_mfma_f32_16x16x32_f16 v[92:95], v[196:199], v[180:183], v[92:95]
	v_mfma_f32_16x16x32_f16 v[96:99], v[200:203], v[180:183], v[96:99]
	s_add_u32 m0, s28, 0x11000
	s_nop 0
	global_load_lds_dwordx4 v12, s[4:5]
	v_mfma_f32_16x16x32_f16 v[100:103], v[204:207], v[180:183], v[100:103]
	s_waitcnt lgkmcnt(10)
	v_mfma_f32_16x16x32_f16 v[104:107], v[192:195], v[184:187], v[104:107]
	v_mfma_f32_16x16x32_f16 v[108:111], v[196:199], v[184:187], v[108:111]
	v_mfma_f32_16x16x32_f16 v[112:115], v[200:203], v[184:187], v[112:115]
	v_mfma_f32_16x16x32_f16 v[116:119], v[204:207], v[184:187], v[116:119]
	s_add_u32 m0, s28, 0x13000
	s_nop 0
	global_load_lds_dwordx4 v13, s[4:5]
	s_waitcnt lgkmcnt(9)
	v_mfma_f32_16x16x32_f16 v[120:123], v[192:195], v[188:191], v[120:123]
	v_mfma_f32_16x16x32_f16 v[124:127], v[196:199], v[188:191], v[124:127]
	v_mfma_f32_16x16x32_f16 v[128:131], v[200:203], v[188:191], v[128:131]
	v_mfma_f32_16x16x32_f16 v[132:135], v[204:207], v[188:191], v[132:135]
	s_waitcnt lgkmcnt(6)
	ds_read_b128 v[172:175], v20
	ds_read_b128 v[192:195], v22
	ds_read_b128 v[196:199], v22 offset:2048
	ds_read_b128 v[200:203], v22 offset:4096
	ds_read_b128 v[204:207], v22 offset:6144
	ds_read_b128 v[176:179], v20 offset:2048
	ds_read_b128 v[180:183], v20 offset:4096
	ds_read_b128 v[184:187], v20 offset:6144
	ds_read_b128 v[188:191], v20 offset:8192
	v_mfma_f32_16x16x32_f16 v[56:59], v[156:159], v[136:139], v[56:59]
	s_add_u32 m0, s28, 0x15000
	s_nop 0
	global_load_lds_dwordx4 v14, s[4:5]
	s_add_u32 s4, s4, s20
	s_addc_u32 s5, s5, 0
	s_waitcnt lgkmcnt(15)
	v_mfma_f32_16x16x32_f16 v[60:63], v[160:163], v[136:139], v[60:63]
	s_waitcnt lgkmcnt(14)
	v_mfma_f32_16x16x32_f16 v[64:67], v[164:167], v[136:139], v[64:67]
	s_waitcnt lgkmcnt(13)
	v_mfma_f32_16x16x32_f16 v[68:71], v[168:171], v[136:139], v[68:71]
	s_waitcnt lgkmcnt(12)
	v_mfma_f32_16x16x32_f16 v[72:75], v[156:159], v[140:143], v[72:75]
	v_mfma_f32_16x16x32_f16 v[76:79], v[160:163], v[140:143], v[76:79]
	v_mfma_f32_16x16x32_f16 v[80:83], v[164:167], v[140:143], v[80:83]
	s_add_u32 m0, s28, 0x16000
	s_nop 0
	global_load_lds_dwordx4 v10, s[6:7]
	v_mfma_f32_16x16x32_f16 v[84:87], v[168:171], v[140:143], v[84:87]
	s_waitcnt lgkmcnt(11)
	v_mfma_f32_16x16x32_f16 v[88:91], v[156:159], v[144:147], v[88:91]
	v_mfma_f32_16x16x32_f16 v[92:95], v[160:163], v[144:147], v[92:95]
	v_mfma_f32_16x16x32_f16 v[96:99], v[164:167], v[144:147], v[96:99]
	v_mfma_f32_16x16x32_f16 v[100:103], v[168:171], v[144:147], v[100:103]
	s_waitcnt lgkmcnt(10)
	v_mfma_f32_16x16x32_f16 v[104:107], v[156:159], v[148:151], v[104:107]
	v_mfma_f32_16x16x32_f16 v[108:111], v[160:163], v[148:151], v[108:111]
	s_add_u32 m0, s28, 0x18000
	s_nop 0
	global_load_lds_dwordx4 v11, s[6:7]
	s_add_u32 s6, s6, s20
	s_addc_u32 s7, s7, 0
	v_mfma_f32_16x16x32_f16 v[112:115], v[164:167], v[148:151], v[112:115]
	v_mfma_f32_16x16x32_f16 v[116:119], v[168:171], v[148:151], v[116:119]
	s_waitcnt lgkmcnt(9)
	v_mfma_f32_16x16x32_f16 v[120:123], v[156:159], v[152:155], v[120:123]
	v_mfma_f32_16x16x32_f16 v[124:127], v[160:163], v[152:155], v[124:127]
	v_mfma_f32_16x16x32_f16 v[128:131], v[164:167], v[152:155], v[128:131]
	v_mfma_f32_16x16x32_f16 v[132:135], v[168:171], v[152:155], v[132:135]
	s_waitcnt vmcnt(7) lgkmcnt(0)
	s_barrier
	s_waitcnt lgkmcnt(6)
	ds_read_b128 v[136:139], v15
	ds_read_b128 v[156:159], v17
	ds_read_b128 v[160:163], v17 offset:2048
	ds_read_b128 v[164:167], v17 offset:4096
	ds_read_b128 v[168:171], v17 offset:6144
	ds_read_b128 v[140:143], v15 offset:2048
	ds_read_b128 v[144:147], v15 offset:4096
	ds_read_b128 v[148:151], v15 offset:6144
	ds_read_b128 v[152:155], v15 offset:8192
	v_mfma_f32_16x16x32_f16 v[56:59], v[192:195], v[172:175], v[56:59]
	s_add_u32 m0, s28, 0x1a000
	s_nop 0
	global_load_lds_dwordx4 v10, s[4:5]
	s_waitcnt lgkmcnt(15)
	v_mfma_f32_16x16x32_f16 v[60:63], v[196:199], v[172:175], v[60:63]
	s_waitcnt lgkmcnt(14)
	v_mfma_f32_16x16x32_f16 v[64:67], v[200:203], v[172:175], v[64:67]
	s_waitcnt lgkmcnt(13)
	v_mfma_f32_16x16x32_f16 v[68:71], v[204:207], v[172:175], v[68:71]
	s_waitcnt lgkmcnt(12)
	v_mfma_f32_16x16x32_f16 v[72:75], v[192:195], v[176:179], v[72:75]
	v_mfma_f32_16x16x32_f16 v[76:79], v[196:199], v[176:179], v[76:79]
	s_add_u32 m0, s28, 0x1c000
	s_nop 0
	global_load_lds_dwordx4 v11, s[4:5]
	v_mfma_f32_16x16x32_f16 v[80:83], v[200:203], v[176:179], v[80:83]
	v_mfma_f32_16x16x32_f16 v[84:87], v[204:207], v[176:179], v[84:87]
	s_waitcnt lgkmcnt(11)
	v_mfma_f32_16x16x32_f16 v[88:91], v[192:195], v[180:183], v[88:91]
	v_mfma_f32_16x16x32_f16 v[92:95], v[196:199], v[180:183], v[92:95]
	v_mfma_f32_16x16x32_f16 v[96:99], v[200:203], v[180:183], v[96:99]
	s_add_u32 m0, s28, 0x1e000
	s_nop 0
	global_load_lds_dwordx4 v12, s[4:5]
	v_mfma_f32_16x16x32_f16 v[100:103], v[204:207], v[180:183], v[100:103]
	s_waitcnt lgkmcnt(10)
	v_mfma_f32_16x16x32_f16 v[104:107], v[192:195], v[184:187], v[104:107]
	v_mfma_f32_16x16x32_f16 v[108:111], v[196:199], v[184:187], v[108:111]
	v_mfma_f32_16x16x32_f16 v[112:115], v[200:203], v[184:187], v[112:115]
	v_mfma_f32_16x16x32_f16 v[116:119], v[204:207], v[184:187], v[116:119]
	s_add_u32 m0, s28, 0x20000
	s_nop 0
	global_load_lds_dwordx4 v13, s[4:5]
	s_waitcnt lgkmcnt(9)
	v_mfma_f32_16x16x32_f16 v[120:123], v[192:195], v[188:191], v[120:123]
	v_mfma_f32_16x16x32_f16 v[124:127], v[196:199], v[188:191], v[124:127]
	v_mfma_f32_16x16x32_f16 v[128:131], v[200:203], v[188:191], v[128:131]
	v_mfma_f32_16x16x32_f16 v[132:135], v[204:207], v[188:191], v[132:135]
	s_waitcnt lgkmcnt(6)
	ds_read_b128 v[172:175], v16
	ds_read_b128 v[192:195], v18
	ds_read_b128 v[196:199], v18 offset:2048
	ds_read_b128 v[200:203], v18 offset:4096
	ds_read_b128 v[204:207], v18 offset:6144
	ds_read_b128 v[176:179], v16 offset:2048
	ds_read_b128 v[180:183], v16 offset:4096
	ds_read_b128 v[184:187], v16 offset:6144
	ds_read_b128 v[188:191], v16 offset:8192
	v_mfma_f32_16x16x32_f16 v[56:59], v[156:159], v[136:139], v[56:59]
	s_add_u32 m0, s28, 0x22000
	s_nop 0
	global_load_lds_dwordx4 v14, s[4:5]
	s_add_u32 s4, s4, s20
	s_addc_u32 s5, s5, 0
	s_waitcnt lgkmcnt(15)
	v_mfma_f32_16x16x32_f16 v[60:63], v[160:163], v[136:139], v[60:63]
	s_waitcnt lgkmcnt(14)
	v_mfma_f32_16x16x32_f16 v[64:67], v[164:167], v[136:139], v[64:67]
	s_waitcnt lgkmcnt(13)
	v_mfma_f32_16x16x32_f16 v[68:71], v[168:171], v[136:139], v[68:71]
	s_waitcnt lgkmcnt(12)
	v_mfma_f32_16x16x32_f16 v[72:75], v[156:159], v[140:143], v[72:75]
	v_mfma_f32_16x16x32_f16 v[76:79], v[160:163], v[140:143], v[76:79]
	v_mfma_f32_16x16x32_f16 v[80:83], v[164:167], v[140:143], v[80:83]
	s_add_u32 m0, s28, 0x23000
	s_nop 0
	global_load_lds_dwordx4 v10, s[6:7]
	v_mfma_f32_16x16x32_f16 v[84:87], v[168:171], v[140:143], v[84:87]
	s_waitcnt lgkmcnt(11)
	v_mfma_f32_16x16x32_f16 v[88:91], v[156:159], v[144:147], v[88:91]
	v_mfma_f32_16x16x32_f16 v[92:95], v[160:163], v[144:147], v[92:95]
	v_mfma_f32_16x16x32_f16 v[96:99], v[164:167], v[144:147], v[96:99]
	v_mfma_f32_16x16x32_f16 v[100:103], v[168:171], v[144:147], v[100:103]
	s_waitcnt lgkmcnt(10)
	v_mfma_f32_16x16x32_f16 v[104:107], v[156:159], v[148:151], v[104:107]
	v_mfma_f32_16x16x32_f16 v[108:111], v[160:163], v[148:151], v[108:111]
	s_add_u32 m0, s28, 0x25000
	s_nop 0
	global_load_lds_dwordx4 v11, s[6:7]
	s_add_u32 s6, s6, s20
	s_addc_u32 s7, s7, 0
	v_mfma_f32_16x16x32_f16 v[112:115], v[164:167], v[148:151], v[112:115]
	v_mfma_f32_16x16x32_f16 v[116:119], v[168:171], v[148:151], v[116:119]
	s_waitcnt lgkmcnt(9)
	v_mfma_f32_16x16x32_f16 v[120:123], v[156:159], v[152:155], v[120:123]
	v_mfma_f32_16x16x32_f16 v[124:127], v[160:163], v[152:155], v[124:127]
	v_mfma_f32_16x16x32_f16 v[128:131], v[164:167], v[152:155], v[128:131]
	v_mfma_f32_16x16x32_f16 v[132:135], v[168:171], v[152:155], v[132:135]
	s_waitcnt vmcnt(7) lgkmcnt(0)
	s_barrier
	s_waitcnt lgkmcnt(6)
	ds_read_b128 v[136:139], v15 offset:53248
	ds_read_b128 v[156:159], v17 offset:53248
	ds_read_b128 v[160:163], v17 offset:55296
	ds_read_b128 v[164:167], v17 offset:57344
	ds_read_b128 v[168:171], v17 offset:59392
	ds_read_b128 v[140:143], v15 offset:55296
	ds_read_b128 v[144:147], v15 offset:57344
	ds_read_b128 v[148:151], v15 offset:59392
	ds_read_b128 v[152:155], v15 offset:61440
	v_mfma_f32_16x16x32_f16 v[56:59], v[192:195], v[172:175], v[56:59]
	s_add_u32 m0, s28, 0x0
	s_nop 0
	global_load_lds_dwordx4 v10, s[4:5]
	s_waitcnt lgkmcnt(15)
	v_mfma_f32_16x16x32_f16 v[60:63], v[196:199], v[172:175], v[60:63]
	s_waitcnt lgkmcnt(14)
	v_mfma_f32_16x16x32_f16 v[64:67], v[200:203], v[172:175], v[64:67]
	s_waitcnt lgkmcnt(13)
	v_mfma_f32_16x16x32_f16 v[68:71], v[204:207], v[172:175], v[68:71]
	s_waitcnt lgkmcnt(12)
	v_mfma_f32_16x16x32_f16 v[72:75], v[192:195], v[176:179], v[72:75]
	v_mfma_f32_16x16x32_f16 v[76:79], v[196:199], v[176:179], v[76:79]
	s_add_u32 m0, s28, 0x2000
	s_nop 0
	global_load_lds_dwordx4 v11, s[4:5]
	v_mfma_f32_16x16x32_f16 v[80:83], v[200:203], v[176:179], v[80:83]
	v_mfma_f32_16x16x32_f16 v[84:87], v[204:207], v[176:179], v[84:87]
	s_waitcnt lgkmcnt(11)
	v_mfma_f32_16x16x32_f16 v[88:91], v[192:195], v[180:183], v[88:91]
	v_mfma_f32_16x16x32_f16 v[92:95], v[196:199], v[180:183], v[92:95]
	v_mfma_f32_16x16x32_f16 v[96:99], v[200:203], v[180:183], v[96:99]
	s_add_u32 m0, s28, 0x4000
	s_nop 0
	global_load_lds_dwordx4 v12, s[4:5]
	v_mfma_f32_16x16x32_f16 v[100:103], v[204:207], v[180:183], v[100:103]
	s_waitcnt lgkmcnt(10)
	v_mfma_f32_16x16x32_f16 v[104:107], v[192:195], v[184:187], v[104:107]
	v_mfma_f32_16x16x32_f16 v[108:111], v[196:199], v[184:187], v[108:111]
	v_mfma_f32_16x16x32_f16 v[112:115], v[200:203], v[184:187], v[112:115]
	v_mfma_f32_16x16x32_f16 v[116:119], v[204:207], v[184:187], v[116:119]
	s_add_u32 m0, s28, 0x6000
	s_nop 0
	global_load_lds_dwordx4 v13, s[4:5]
	s_waitcnt lgkmcnt(9)
	v_mfma_f32_16x16x32_f16 v[120:123], v[192:195], v[188:191], v[120:123]
	v_mfma_f32_16x16x32_f16 v[124:127], v[196:199], v[188:191], v[124:127]
	v_mfma_f32_16x16x32_f16 v[128:131], v[200:203], v[188:191], v[128:131]
	v_mfma_f32_16x16x32_f16 v[132:135], v[204:207], v[188:191], v[132:135]
	s_waitcnt lgkmcnt(6)
	ds_read_b128 v[172:175], v16 offset:53248
	ds_read_b128 v[192:195], v18 offset:53248
	ds_read_b128 v[196:199], v18 offset:55296
	ds_read_b128 v[200:203], v18 offset:57344
	ds_read_b128 v[204:207], v18 offset:59392
	ds_read_b128 v[176:179], v16 offset:55296
	ds_read_b128 v[180:183], v16 offset:57344
	ds_read_b128 v[184:187], v16 offset:59392
	ds_read_b128 v[188:191], v16 offset:61440
	v_mfma_f32_16x16x32_f16 v[56:59], v[156:159], v[136:139], v[56:59]
	s_add_u32 m0, s28, 0x8000
	s_nop 0
	global_load_lds_dwordx4 v14, s[4:5]
	s_add_u32 s4, s4, s20
	s_addc_u32 s5, s5, 0
	s_waitcnt lgkmcnt(15)
	v_mfma_f32_16x16x32_f16 v[60:63], v[160:163], v[136:139], v[60:63]
	s_waitcnt lgkmcnt(14)
	v_mfma_f32_16x16x32_f16 v[64:67], v[164:167], v[136:139], v[64:67]
	s_waitcnt lgkmcnt(13)
	v_mfma_f32_16x16x32_f16 v[68:71], v[168:171], v[136:139], v[68:71]
	s_waitcnt lgkmcnt(12)
	v_mfma_f32_16x16x32_f16 v[72:75], v[156:159], v[140:143], v[72:75]
	v_mfma_f32_16x16x32_f16 v[76:79], v[160:163], v[140:143], v[76:79]
	v_mfma_f32_16x16x32_f16 v[80:83], v[164:167], v[140:143], v[80:83]
	s_add_u32 m0, s28, 0x9000
	s_nop 0
	global_load_lds_dwordx4 v10, s[6:7]
	v_mfma_f32_16x16x32_f16 v[84:87], v[168:171], v[140:143], v[84:87]
	s_waitcnt lgkmcnt(11)
	v_mfma_f32_16x16x32_f16 v[88:91], v[156:159], v[144:147], v[88:91]
	v_mfma_f32_16x16x32_f16 v[92:95], v[160:163], v[144:147], v[92:95]
	v_mfma_f32_16x16x32_f16 v[96:99], v[164:167], v[144:147], v[96:99]
	v_mfma_f32_16x16x32_f16 v[100:103], v[168:171], v[144:147], v[100:103]
	s_waitcnt lgkmcnt(10)
	v_mfma_f32_16x16x32_f16 v[104:107], v[156:159], v[148:151], v[104:107]
	v_mfma_f32_16x16x32_f16 v[108:111], v[160:163], v[148:151], v[108:111]
	s_add_u32 m0, s28, 0xb000
	s_nop 0
	global_load_lds_dwordx4 v11, s[6:7]
	s_add_u32 s6, s6, s20
	s_addc_u32 s7, s7, 0
	v_mfma_f32_16x16x32_f16 v[112:115], v[164:167], v[148:151], v[112:115]
	v_mfma_f32_16x16x32_f16 v[116:119], v[168:171], v[148:151], v[116:119]
	s_waitcnt lgkmcnt(9)
	v_mfma_f32_16x16x32_f16 v[120:123], v[156:159], v[152:155], v[120:123]
	v_mfma_f32_16x16x32_f16 v[124:127], v[160:163], v[152:155], v[124:127]
	v_mfma_f32_16x16x32_f16 v[128:131], v[164:167], v[152:155], v[128:131]
	v_mfma_f32_16x16x32_f16 v[132:135], v[168:171], v[152:155], v[132:135]
	s_waitcnt vmcnt(7) lgkmcnt(0)
	s_barrier
	s_waitcnt lgkmcnt(6)
	ds_read_b128 v[136:139], v19
	ds_read_b128 v[156:159], v21
	ds_read_b128 v[160:163], v21 offset:2048
	ds_read_b128 v[164:167], v21 offset:4096
	ds_read_b128 v[168:171], v21 offset:6144
	ds_read_b128 v[140:143], v19 offset:2048
	ds_read_b128 v[144:147], v19 offset:4096
	ds_read_b128 v[148:151], v19 offset:6144
	ds_read_b128 v[152:155], v19 offset:8192
	v_mfma_f32_16x16x32_f16 v[56:59], v[192:195], v[172:175], v[56:59]
	s_add_u32 m0, s28, 0xd000
	s_nop 0
	global_load_lds_dwordx4 v10, s[4:5]
	s_waitcnt lgkmcnt(15)
	v_mfma_f32_16x16x32_f16 v[60:63], v[196:199], v[172:175], v[60:63]
	s_waitcnt lgkmcnt(14)
	v_mfma_f32_16x16x32_f16 v[64:67], v[200:203], v[172:175], v[64:67]
	s_waitcnt lgkmcnt(13)
	v_mfma_f32_16x16x32_f16 v[68:71], v[204:207], v[172:175], v[68:71]
	s_waitcnt lgkmcnt(12)
	v_mfma_f32_16x16x32_f16 v[72:75], v[192:195], v[176:179], v[72:75]
	v_mfma_f32_16x16x32_f16 v[76:79], v[196:199], v[176:179], v[76:79]
	s_add_u32 m0, s28, 0xf000
	s_nop 0
	global_load_lds_dwordx4 v11, s[4:5]
	v_mfma_f32_16x16x32_f16 v[80:83], v[200:203], v[176:179], v[80:83]
	v_mfma_f32_16x16x32_f16 v[84:87], v[204:207], v[176:179], v[84:87]
	s_waitcnt lgkmcnt(11)
	v_mfma_f32_16x16x32_f16 v[88:91], v[192:195], v[180:183], v[88:91]
	v_mfma_f32_16x16x32_f16 v[92:95], v[196:199], v[180:183], v[92:95]
	v_mfma_f32_16x16x32_f16 v[96:99], v[200:203], v[180:183], v[96:99]
	s_add_u32 m0, s28, 0x11000
	s_nop 0
	global_load_lds_dwordx4 v12, s[4:5]
	v_mfma_f32_16x16x32_f16 v[100:103], v[204:207], v[180:183], v[100:103]
	s_waitcnt lgkmcnt(10)
	v_mfma_f32_16x16x32_f16 v[104:107], v[192:195], v[184:187], v[104:107]
	v_mfma_f32_16x16x32_f16 v[108:111], v[196:199], v[184:187], v[108:111]
	v_mfma_f32_16x16x32_f16 v[112:115], v[200:203], v[184:187], v[112:115]
	v_mfma_f32_16x16x32_f16 v[116:119], v[204:207], v[184:187], v[116:119]
	s_add_u32 m0, s28, 0x13000
	s_nop 0
	global_load_lds_dwordx4 v13, s[4:5]
	s_waitcnt lgkmcnt(9)
	v_mfma_f32_16x16x32_f16 v[120:123], v[192:195], v[188:191], v[120:123]
	v_mfma_f32_16x16x32_f16 v[124:127], v[196:199], v[188:191], v[124:127]
	v_mfma_f32_16x16x32_f16 v[128:131], v[200:203], v[188:191], v[128:131]
	v_mfma_f32_16x16x32_f16 v[132:135], v[204:207], v[188:191], v[132:135]
	s_waitcnt lgkmcnt(6)
	ds_read_b128 v[172:175], v20
	ds_read_b128 v[192:195], v22
	ds_read_b128 v[196:199], v22 offset:2048
	ds_read_b128 v[200:203], v22 offset:4096
	ds_read_b128 v[204:207], v22 offset:6144
	ds_read_b128 v[176:179], v20 offset:2048
	ds_read_b128 v[180:183], v20 offset:4096
	ds_read_b128 v[184:187], v20 offset:6144
	ds_read_b128 v[188:191], v20 offset:8192
	v_mfma_f32_16x16x32_f16 v[56:59], v[156:159], v[136:139], v[56:59]
	s_add_u32 m0, s28, 0x15000
	s_nop 0
	global_load_lds_dwordx4 v14, s[4:5]
	s_add_u32 s4, s4, s20
	s_addc_u32 s5, s5, 0
	s_waitcnt lgkmcnt(15)
	v_mfma_f32_16x16x32_f16 v[60:63], v[160:163], v[136:139], v[60:63]
	s_waitcnt lgkmcnt(14)
	v_mfma_f32_16x16x32_f16 v[64:67], v[164:167], v[136:139], v[64:67]
	s_waitcnt lgkmcnt(13)
	v_mfma_f32_16x16x32_f16 v[68:71], v[168:171], v[136:139], v[68:71]
	s_waitcnt lgkmcnt(12)
	v_mfma_f32_16x16x32_f16 v[72:75], v[156:159], v[140:143], v[72:75]
	v_mfma_f32_16x16x32_f16 v[76:79], v[160:163], v[140:143], v[76:79]
	v_mfma_f32_16x16x32_f16 v[80:83], v[164:167], v[140:143], v[80:83]
	s_add_u32 m0, s28, 0x16000
	s_nop 0
	global_load_lds_dwordx4 v10, s[6:7]
	v_mfma_f32_16x16x32_f16 v[84:87], v[168:171], v[140:143], v[84:87]
	s_waitcnt lgkmcnt(11)
	v_mfma_f32_16x16x32_f16 v[88:91], v[156:159], v[144:147], v[88:91]
	v_mfma_f32_16x16x32_f16 v[92:95], v[160:163], v[144:147], v[92:95]
	v_mfma_f32_16x16x32_f16 v[96:99], v[164:167], v[144:147], v[96:99]
	v_mfma_f32_16x16x32_f16 v[100:103], v[168:171], v[144:147], v[100:103]
	s_waitcnt lgkmcnt(10)
	v_mfma_f32_16x16x32_f16 v[104:107], v[156:159], v[148:151], v[104:107]
	v_mfma_f32_16x16x32_f16 v[108:111], v[160:163], v[148:151], v[108:111]
	s_add_u32 m0, s28, 0x18000
	s_nop 0
	global_load_lds_dwordx4 v11, s[6:7]
	s_add_u32 s6, s6, s20
	s_addc_u32 s7, s7, 0
	v_mfma_f32_16x16x32_f16 v[112:115], v[164:167], v[148:151], v[112:115]
	v_mfma_f32_16x16x32_f16 v[116:119], v[168:171], v[148:151], v[116:119]
	s_waitcnt lgkmcnt(9)
	v_mfma_f32_16x16x32_f16 v[120:123], v[156:159], v[152:155], v[120:123]
	v_mfma_f32_16x16x32_f16 v[124:127], v[160:163], v[152:155], v[124:127]
	v_mfma_f32_16x16x32_f16 v[128:131], v[164:167], v[152:155], v[128:131]
	v_mfma_f32_16x16x32_f16 v[132:135], v[168:171], v[152:155], v[132:135]
	s_waitcnt vmcnt(7) lgkmcnt(0)
	s_barrier
	s_waitcnt lgkmcnt(6)
	ds_read_b128 v[136:139], v15
	ds_read_b128 v[156:159], v17
	ds_read_b128 v[160:163], v17 offset:2048
	ds_read_b128 v[164:167], v17 offset:4096
	ds_read_b128 v[168:171], v17 offset:6144
	ds_read_b128 v[140:143], v15 offset:2048
	ds_read_b128 v[144:147], v15 offset:4096
	ds_read_b128 v[148:151], v15 offset:6144
	ds_read_b128 v[152:155], v15 offset:8192
	v_mfma_f32_16x16x32_f16 v[56:59], v[192:195], v[172:175], v[56:59]
	s_add_u32 m0, s28, 0x1a000
	s_nop 0
	global_load_lds_dwordx4 v10, s[4:5]
	s_waitcnt lgkmcnt(15)
	v_mfma_f32_16x16x32_f16 v[60:63], v[196:199], v[172:175], v[60:63]
	s_waitcnt lgkmcnt(14)
	v_mfma_f32_16x16x32_f16 v[64:67], v[200:203], v[172:175], v[64:67]
	s_waitcnt lgkmcnt(13)
	v_mfma_f32_16x16x32_f16 v[68:71], v[204:207], v[172:175], v[68:71]
	s_waitcnt lgkmcnt(12)
	v_mfma_f32_16x16x32_f16 v[72:75], v[192:195], v[176:179], v[72:75]
	v_mfma_f32_16x16x32_f16 v[76:79], v[196:199], v[176:179], v[76:79]
	s_add_u32 m0, s28, 0x1c000
	s_nop 0
	global_load_lds_dwordx4 v11, s[4:5]
	v_mfma_f32_16x16x32_f16 v[80:83], v[200:203], v[176:179], v[80:83]
	v_mfma_f32_16x16x32_f16 v[84:87], v[204:207], v[176:179], v[84:87]
	s_waitcnt lgkmcnt(11)
	v_mfma_f32_16x16x32_f16 v[88:91], v[192:195], v[180:183], v[88:91]
	v_mfma_f32_16x16x32_f16 v[92:95], v[196:199], v[180:183], v[92:95]
	v_mfma_f32_16x16x32_f16 v[96:99], v[200:203], v[180:183], v[96:99]
	s_add_u32 m0, s28, 0x1e000
	s_nop 0
	global_load_lds_dwordx4 v12, s[4:5]
	v_mfma_f32_16x16x32_f16 v[100:103], v[204:207], v[180:183], v[100:103]
	s_waitcnt lgkmcnt(10)
	v_mfma_f32_16x16x32_f16 v[104:107], v[192:195], v[184:187], v[104:107]
	v_mfma_f32_16x16x32_f16 v[108:111], v[196:199], v[184:187], v[108:111]
	v_mfma_f32_16x16x32_f16 v[112:115], v[200:203], v[184:187], v[112:115]
	v_mfma_f32_16x16x32_f16 v[116:119], v[204:207], v[184:187], v[116:119]
	s_add_u32 m0, s28, 0x20000
	s_nop 0
	global_load_lds_dwordx4 v13, s[4:5]
	s_waitcnt lgkmcnt(9)
	v_mfma_f32_16x16x32_f16 v[120:123], v[192:195], v[188:191], v[120:123]
	v_mfma_f32_16x16x32_f16 v[124:127], v[196:199], v[188:191], v[124:127]
	v_mfma_f32_16x16x32_f16 v[128:131], v[200:203], v[188:191], v[128:131]
	v_mfma_f32_16x16x32_f16 v[132:135], v[204:207], v[188:191], v[132:135]
	s_waitcnt lgkmcnt(6)
	ds_read_b128 v[172:175], v16
	ds_read_b128 v[192:195], v18
	ds_read_b128 v[196:199], v18 offset:2048
	ds_read_b128 v[200:203], v18 offset:4096
	ds_read_b128 v[204:207], v18 offset:6144
	ds_read_b128 v[176:179], v16 offset:2048
	ds_read_b128 v[180:183], v16 offset:4096
	ds_read_b128 v[184:187], v16 offset:6144
	ds_read_b128 v[188:191], v16 offset:8192
	v_mfma_f32_16x16x32_f16 v[56:59], v[156:159], v[136:139], v[56:59]
	s_add_u32 m0, s28, 0x22000
	s_nop 0
	global_load_lds_dwordx4 v14, s[4:5]
	s_add_u32 s4, s4, s20
	s_addc_u32 s5, s5, 0
	s_waitcnt lgkmcnt(15)
	v_mfma_f32_16x16x32_f16 v[60:63], v[160:163], v[136:139], v[60:63]
	s_waitcnt lgkmcnt(14)
	v_mfma_f32_16x16x32_f16 v[64:67], v[164:167], v[136:139], v[64:67]
	s_waitcnt lgkmcnt(13)
	v_mfma_f32_16x16x32_f16 v[68:71], v[168:171], v[136:139], v[68:71]
	s_waitcnt lgkmcnt(12)
	v_mfma_f32_16x16x32_f16 v[72:75], v[156:159], v[140:143], v[72:75]
	v_mfma_f32_16x16x32_f16 v[76:79], v[160:163], v[140:143], v[76:79]
	v_mfma_f32_16x16x32_f16 v[80:83], v[164:167], v[140:143], v[80:83]
	s_add_u32 m0, s28, 0x23000
	s_nop 0
	global_load_lds_dwordx4 v10, s[6:7]
	v_mfma_f32_16x16x32_f16 v[84:87], v[168:171], v[140:143], v[84:87]
	s_waitcnt lgkmcnt(11)
	v_mfma_f32_16x16x32_f16 v[88:91], v[156:159], v[144:147], v[88:91]
	v_mfma_f32_16x16x32_f16 v[92:95], v[160:163], v[144:147], v[92:95]
	v_mfma_f32_16x16x32_f16 v[96:99], v[164:167], v[144:147], v[96:99]
	v_mfma_f32_16x16x32_f16 v[100:103], v[168:171], v[144:147], v[100:103]
	s_waitcnt lgkmcnt(10)
	v_mfma_f32_16x16x32_f16 v[104:107], v[156:159], v[148:151], v[104:107]
	v_mfma_f32_16x16x32_f16 v[108:111], v[160:163], v[148:151], v[108:111]
	s_add_u32 m0, s28, 0x25000
	s_nop 0
	global_load_lds_dwordx4 v11, s[6:7]
	s_add_u32 s6, s6, s20
	s_addc_u32 s7, s7, 0
	v_mfma_f32_16x16x32_f16 v[112:115], v[164:167], v[148:151], v[112:115]
	v_mfma_f32_16x16x32_f16 v[116:119], v[168:171], v[148:151], v[116:119]
	s_waitcnt lgkmcnt(9)
	v_mfma_f32_16x16x32_f16 v[120:123], v[156:159], v[152:155], v[120:123]
	v_mfma_f32_16x16x32_f16 v[124:127], v[160:163], v[152:155], v[124:127]
	v_mfma_f32_16x16x32_f16 v[128:131], v[164:167], v[152:155], v[128:131]
	v_mfma_f32_16x16x32_f16 v[132:135], v[168:171], v[152:155], v[132:135]
	s_waitcnt vmcnt(7) lgkmcnt(0)
	s_barrier
	s_waitcnt lgkmcnt(6)
	ds_read_b128 v[136:139], v15 offset:53248
	ds_read_b128 v[156:159], v17 offset:53248
	ds_read_b128 v[160:163], v17 offset:55296
	ds_read_b128 v[164:167], v17 offset:57344
	ds_read_b128 v[168:171], v17 offset:59392
	ds_read_b128 v[140:143], v15 offset:55296
	ds_read_b128 v[144:147], v15 offset:57344
	ds_read_b128 v[148:151], v15 offset:59392
	ds_read_b128 v[152:155], v15 offset:61440
	v_mfma_f32_16x16x32_f16 v[56:59], v[192:195], v[172:175], v[56:59]
	s_add_u32 m0, s28, 0x0
	s_nop 0
	global_load_lds_dwordx4 v10, s[4:5]
	s_waitcnt lgkmcnt(15)
	v_mfma_f32_16x16x32_f16 v[60:63], v[196:199], v[172:175], v[60:63]
	s_waitcnt lgkmcnt(14)
	v_mfma_f32_16x16x32_f16 v[64:67], v[200:203], v[172:175], v[64:67]
	s_waitcnt lgkmcnt(13)
	v_mfma_f32_16x16x32_f16 v[68:71], v[204:207], v[172:175], v[68:71]
	s_waitcnt lgkmcnt(12)
	v_mfma_f32_16x16x32_f16 v[72:75], v[192:195], v[176:179], v[72:75]
	v_mfma_f32_16x16x32_f16 v[76:79], v[196:199], v[176:179], v[76:79]
	s_add_u32 m0, s28, 0x2000
	s_nop 0
	global_load_lds_dwordx4 v11, s[4:5]
	v_mfma_f32_16x16x32_f16 v[80:83], v[200:203], v[176:179], v[80:83]
	v_mfma_f32_16x16x32_f16 v[84:87], v[204:207], v[176:179], v[84:87]
	s_waitcnt lgkmcnt(11)
	v_mfma_f32_16x16x32_f16 v[88:91], v[192:195], v[180:183], v[88:91]
	v_mfma_f32_16x16x32_f16 v[92:95], v[196:199], v[180:183], v[92:95]
	v_mfma_f32_16x16x32_f16 v[96:99], v[200:203], v[180:183], v[96:99]
	s_add_u32 m0, s28, 0x4000
	s_nop 0
	global_load_lds_dwordx4 v12, s[4:5]
	v_mfma_f32_16x16x32_f16 v[100:103], v[204:207], v[180:183], v[100:103]
	s_waitcnt lgkmcnt(10)
	v_mfma_f32_16x16x32_f16 v[104:107], v[192:195], v[184:187], v[104:107]
	v_mfma_f32_16x16x32_f16 v[108:111], v[196:199], v[184:187], v[108:111]
	v_mfma_f32_16x16x32_f16 v[112:115], v[200:203], v[184:187], v[112:115]
	v_mfma_f32_16x16x32_f16 v[116:119], v[204:207], v[184:187], v[116:119]
	s_add_u32 m0, s28, 0x6000
	s_nop 0
	global_load_lds_dwordx4 v13, s[4:5]
	s_waitcnt lgkmcnt(9)
	v_mfma_f32_16x16x32_f16 v[120:123], v[192:195], v[188:191], v[120:123]
	v_mfma_f32_16x16x32_f16 v[124:127], v[196:199], v[188:191], v[124:127]
	v_mfma_f32_16x16x32_f16 v[128:131], v[200:203], v[188:191], v[128:131]
	v_mfma_f32_16x16x32_f16 v[132:135], v[204:207], v[188:191], v[132:135]
	s_waitcnt lgkmcnt(6)
	ds_read_b128 v[172:175], v16 offset:53248
	ds_read_b128 v[192:195], v18 offset:53248
	ds_read_b128 v[196:199], v18 offset:55296
	ds_read_b128 v[200:203], v18 offset:57344
	ds_read_b128 v[204:207], v18 offset:59392
	ds_read_b128 v[176:179], v16 offset:55296
	ds_read_b128 v[180:183], v16 offset:57344
	ds_read_b128 v[184:187], v16 offset:59392
	ds_read_b128 v[188:191], v16 offset:61440
	v_mfma_f32_16x16x32_f16 v[56:59], v[156:159], v[136:139], v[56:59]
	s_add_u32 m0, s28, 0x8000
	s_nop 0
	global_load_lds_dwordx4 v14, s[4:5]
	s_add_u32 s4, s4, s20
	s_addc_u32 s5, s5, 0
	s_waitcnt lgkmcnt(15)
	v_mfma_f32_16x16x32_f16 v[60:63], v[160:163], v[136:139], v[60:63]
	s_waitcnt lgkmcnt(14)
	v_mfma_f32_16x16x32_f16 v[64:67], v[164:167], v[136:139], v[64:67]
	s_waitcnt lgkmcnt(13)
	v_mfma_f32_16x16x32_f16 v[68:71], v[168:171], v[136:139], v[68:71]
	s_waitcnt lgkmcnt(12)
	v_mfma_f32_16x16x32_f16 v[72:75], v[156:159], v[140:143], v[72:75]
	v_mfma_f32_16x16x32_f16 v[76:79], v[160:163], v[140:143], v[76:79]
	v_mfma_f32_16x16x32_f16 v[80:83], v[164:167], v[140:143], v[80:83]
	s_add_u32 m0, s28, 0x9000
	s_nop 0
	global_load_lds_dwordx4 v10, s[6:7]
	v_mfma_f32_16x16x32_f16 v[84:87], v[168:171], v[140:143], v[84:87]
	s_waitcnt lgkmcnt(11)
	v_mfma_f32_16x16x32_f16 v[88:91], v[156:159], v[144:147], v[88:91]
	v_mfma_f32_16x16x32_f16 v[92:95], v[160:163], v[144:147], v[92:95]
	v_mfma_f32_16x16x32_f16 v[96:99], v[164:167], v[144:147], v[96:99]
	v_mfma_f32_16x16x32_f16 v[100:103], v[168:171], v[144:147], v[100:103]
	s_waitcnt lgkmcnt(10)
	v_mfma_f32_16x16x32_f16 v[104:107], v[156:159], v[148:151], v[104:107]
	v_mfma_f32_16x16x32_f16 v[108:111], v[160:163], v[148:151], v[108:111]
	s_add_u32 m0, s28, 0xb000
	s_nop 0
	global_load_lds_dwordx4 v11, s[6:7]
	s_add_u32 s6, s6, s20
	s_addc_u32 s7, s7, 0
	v_mfma_f32_16x16x32_f16 v[112:115], v[164:167], v[148:151], v[112:115]
	v_mfma_f32_16x16x32_f16 v[116:119], v[168:171], v[148:151], v[116:119]
	s_waitcnt lgkmcnt(9)
	v_mfma_f32_16x16x32_f16 v[120:123], v[156:159], v[152:155], v[120:123]
	v_mfma_f32_16x16x32_f16 v[124:127], v[160:163], v[152:155], v[124:127]
	v_mfma_f32_16x16x32_f16 v[128:131], v[164:167], v[152:155], v[128:131]
	v_mfma_f32_16x16x32_f16 v[132:135], v[168:171], v[152:155], v[132:135]
	s_waitcnt vmcnt(7) lgkmcnt(0)
	s_barrier
	s_waitcnt lgkmcnt(6)
	ds_read_b128 v[136:139], v19
	ds_read_b128 v[156:159], v21
	ds_read_b128 v[160:163], v21 offset:2048
	ds_read_b128 v[164:167], v21 offset:4096
	ds_read_b128 v[168:171], v21 offset:6144
	ds_read_b128 v[140:143], v19 offset:2048
	ds_read_b128 v[144:147], v19 offset:4096
	ds_read_b128 v[148:151], v19 offset:6144
	ds_read_b128 v[152:155], v19 offset:8192
	v_mfma_f32_16x16x32_f16 v[56:59], v[192:195], v[172:175], v[56:59]
	s_add_u32 m0, s28, 0xd000
	s_nop 0
	global_load_lds_dwordx4 v10, s[4:5]
	s_waitcnt lgkmcnt(15)
	v_mfma_f32_16x16x32_f16 v[60:63], v[196:199], v[172:175], v[60:63]
	s_waitcnt lgkmcnt(14)
	v_mfma_f32_16x16x32_f16 v[64:67], v[200:203], v[172:175], v[64:67]
	s_waitcnt lgkmcnt(13)
	v_mfma_f32_16x16x32_f16 v[68:71], v[204:207], v[172:175], v[68:71]
	s_waitcnt lgkmcnt(12)
	v_mfma_f32_16x16x32_f16 v[72:75], v[192:195], v[176:179], v[72:75]
	v_mfma_f32_16x16x32_f16 v[76:79], v[196:199], v[176:179], v[76:79]
	s_add_u32 m0, s28, 0xf000
	s_nop 0
	global_load_lds_dwordx4 v11, s[4:5]
	v_mfma_f32_16x16x32_f16 v[80:83], v[200:203], v[176:179], v[80:83]
	v_mfma_f32_16x16x32_f16 v[84:87], v[204:207], v[176:179], v[84:87]
	s_waitcnt lgkmcnt(11)
	v_mfma_f32_16x16x32_f16 v[88:91], v[192:195], v[180:183], v[88:91]
	v_mfma_f32_16x16x32_f16 v[92:95], v[196:199], v[180:183], v[92:95]
	v_mfma_f32_16x16x32_f16 v[96:99], v[200:203], v[180:183], v[96:99]
	s_add_u32 m0, s28, 0x11000
	s_nop 0
	global_load_lds_dwordx4 v12, s[4:5]
	v_mfma_f32_16x16x32_f16 v[100:103], v[204:207], v[180:183], v[100:103]
	s_waitcnt lgkmcnt(10)
	v_mfma_f32_16x16x32_f16 v[104:107], v[192:195], v[184:187], v[104:107]
	v_mfma_f32_16x16x32_f16 v[108:111], v[196:199], v[184:187], v[108:111]
	v_mfma_f32_16x16x32_f16 v[112:115], v[200:203], v[184:187], v[112:115]
	v_mfma_f32_16x16x32_f16 v[116:119], v[204:207], v[184:187], v[116:119]
	s_add_u32 m0, s28, 0x13000
	s_nop 0
	global_load_lds_dwordx4 v13, s[4:5]
	s_waitcnt lgkmcnt(9)
	v_mfma_f32_16x16x32_f16 v[120:123], v[192:195], v[188:191], v[120:123]
	v_mfma_f32_16x16x32_f16 v[124:127], v[196:199], v[188:191], v[124:127]
	v_mfma_f32_16x16x32_f16 v[128:131], v[200:203], v[188:191], v[128:131]
	v_mfma_f32_16x16x32_f16 v[132:135], v[204:207], v[188:191], v[132:135]
	s_waitcnt lgkmcnt(6)
	ds_read_b128 v[172:175], v20
	ds_read_b128 v[192:195], v22
	ds_read_b128 v[196:199], v22 offset:2048
	ds_read_b128 v[200:203], v22 offset:4096
	ds_read_b128 v[204:207], v22 offset:6144
	ds_read_b128 v[176:179], v20 offset:2048
	ds_read_b128 v[180:183], v20 offset:4096
	ds_read_b128 v[184:187], v20 offset:6144
	ds_read_b128 v[188:191], v20 offset:8192
	v_mfma_f32_16x16x32_f16 v[56:59], v[156:159], v[136:139], v[56:59]
	s_add_u32 m0, s28, 0x15000
	s_nop 0
	global_load_lds_dwordx4 v14, s[4:5]
	s_add_u32 s4, s4, s20
	s_addc_u32 s5, s5, 0
	s_waitcnt lgkmcnt(15)
	v_mfma_f32_16x16x32_f16 v[60:63], v[160:163], v[136:139], v[60:63]
	s_waitcnt lgkmcnt(14)
	v_mfma_f32_16x16x32_f16 v[64:67], v[164:167], v[136:139], v[64:67]
	s_waitcnt lgkmcnt(13)
	v_mfma_f32_16x16x32_f16 v[68:71], v[168:171], v[136:139], v[68:71]
	s_waitcnt lgkmcnt(12)
	v_mfma_f32_16x16x32_f16 v[72:75], v[156:159], v[140:143], v[72:75]
	v_mfma_f32_16x16x32_f16 v[76:79], v[160:163], v[140:143], v[76:79]
	v_mfma_f32_16x16x32_f16 v[80:83], v[164:167], v[140:143], v[80:83]
	s_add_u32 m0, s28, 0x16000
	s_nop 0
	global_load_lds_dwordx4 v10, s[6:7]
	v_mfma_f32_16x16x32_f16 v[84:87], v[168:171], v[140:143], v[84:87]
	s_waitcnt lgkmcnt(11)
	v_mfma_f32_16x16x32_f16 v[88:91], v[156:159], v[144:147], v[88:91]
	v_mfma_f32_16x16x32_f16 v[92:95], v[160:163], v[144:147], v[92:95]
	v_mfma_f32_16x16x32_f16 v[96:99], v[164:167], v[144:147], v[96:99]
	v_mfma_f32_16x16x32_f16 v[100:103], v[168:171], v[144:147], v[100:103]
	s_waitcnt lgkmcnt(10)
	v_mfma_f32_16x16x32_f16 v[104:107], v[156:159], v[148:151], v[104:107]
	v_mfma_f32_16x16x32_f16 v[108:111], v[160:163], v[148:151], v[108:111]
	s_add_u32 m0, s28, 0x18000
	s_nop 0
	global_load_lds_dwordx4 v11, s[6:7]
	s_add_u32 s6, s6, s20
	s_addc_u32 s7, s7, 0
	v_mfma_f32_16x16x32_f16 v[112:115], v[164:167], v[148:151], v[112:115]
	v_mfma_f32_16x16x32_f16 v[116:119], v[168:171], v[148:151], v[116:119]
	s_waitcnt lgkmcnt(9)
	v_mfma_f32_16x16x32_f16 v[120:123], v[156:159], v[152:155], v[120:123]
	v_mfma_f32_16x16x32_f16 v[124:127], v[160:163], v[152:155], v[124:127]
	v_mfma_f32_16x16x32_f16 v[128:131], v[164:167], v[152:155], v[128:131]
	v_mfma_f32_16x16x32_f16 v[132:135], v[168:171], v[152:155], v[132:135]
	s_waitcnt vmcnt(7) lgkmcnt(0)
	s_barrier
	s_waitcnt lgkmcnt(6)
	ds_read_b128 v[136:139], v15
	ds_read_b128 v[156:159], v17
	ds_read_b128 v[160:163], v17 offset:2048
	ds_read_b128 v[164:167], v17 offset:4096
	ds_read_b128 v[168:171], v17 offset:6144
	ds_read_b128 v[140:143], v15 offset:2048
	ds_read_b128 v[144:147], v15 offset:4096
	ds_read_b128 v[148:151], v15 offset:6144
	ds_read_b128 v[152:155], v15 offset:8192
	v_mfma_f32_16x16x32_f16 v[56:59], v[192:195], v[172:175], v[56:59]
	s_add_u32 m0, s28, 0x1a000
	s_nop 0
	global_load_lds_dwordx4 v10, s[4:5]
	s_waitcnt lgkmcnt(15)
	v_mfma_f32_16x16x32_f16 v[60:63], v[196:199], v[172:175], v[60:63]
	s_waitcnt lgkmcnt(14)
	v_mfma_f32_16x16x32_f16 v[64:67], v[200:203], v[172:175], v[64:67]
	s_waitcnt lgkmcnt(13)
	v_mfma_f32_16x16x32_f16 v[68:71], v[204:207], v[172:175], v[68:71]
	s_waitcnt lgkmcnt(12)
	v_mfma_f32_16x16x32_f16 v[72:75], v[192:195], v[176:179], v[72:75]
	v_mfma_f32_16x16x32_f16 v[76:79], v[196:199], v[176:179], v[76:79]
	s_add_u32 m0, s28, 0x1c000
	s_nop 0
	global_load_lds_dwordx4 v11, s[4:5]
	v_mfma_f32_16x16x32_f16 v[80:83], v[200:203], v[176:179], v[80:83]
	v_mfma_f32_16x16x32_f16 v[84:87], v[204:207], v[176:179], v[84:87]
	s_waitcnt lgkmcnt(11)
	v_mfma_f32_16x16x32_f16 v[88:91], v[192:195], v[180:183], v[88:91]
	v_mfma_f32_16x16x32_f16 v[92:95], v[196:199], v[180:183], v[92:95]
	v_mfma_f32_16x16x32_f16 v[96:99], v[200:203], v[180:183], v[96:99]
	s_add_u32 m0, s28, 0x1e000
	s_nop 0
	global_load_lds_dwordx4 v12, s[4:5]
	v_mfma_f32_16x16x32_f16 v[100:103], v[204:207], v[180:183], v[100:103]
	s_waitcnt lgkmcnt(10)
	v_mfma_f32_16x16x32_f16 v[104:107], v[192:195], v[184:187], v[104:107]
	v_mfma_f32_16x16x32_f16 v[108:111], v[196:199], v[184:187], v[108:111]
	v_mfma_f32_16x16x32_f16 v[112:115], v[200:203], v[184:187], v[112:115]
	v_mfma_f32_16x16x32_f16 v[116:119], v[204:207], v[184:187], v[116:119]
	s_add_u32 m0, s28, 0x20000
	s_nop 0
	global_load_lds_dwordx4 v13, s[4:5]
	s_waitcnt lgkmcnt(9)
	v_mfma_f32_16x16x32_f16 v[120:123], v[192:195], v[188:191], v[120:123]
	v_mfma_f32_16x16x32_f16 v[124:127], v[196:199], v[188:191], v[124:127]
	v_mfma_f32_16x16x32_f16 v[128:131], v[200:203], v[188:191], v[128:131]
	v_mfma_f32_16x16x32_f16 v[132:135], v[204:207], v[188:191], v[132:135]
	s_waitcnt lgkmcnt(6)
	ds_read_b128 v[172:175], v16
	ds_read_b128 v[192:195], v18
	ds_read_b128 v[196:199], v18 offset:2048
	ds_read_b128 v[200:203], v18 offset:4096
	ds_read_b128 v[204:207], v18 offset:6144
	ds_read_b128 v[176:179], v16 offset:2048
	ds_read_b128 v[180:183], v16 offset:4096
	ds_read_b128 v[184:187], v16 offset:6144
	ds_read_b128 v[188:191], v16 offset:8192
	v_mfma_f32_16x16x32_f16 v[56:59], v[156:159], v[136:139], v[56:59]
	s_add_u32 m0, s28, 0x22000
	s_nop 0
	global_load_lds_dwordx4 v14, s[4:5]
	s_add_u32 s4, s4, s20
	s_addc_u32 s5, s5, 0
	s_waitcnt lgkmcnt(15)
	v_mfma_f32_16x16x32_f16 v[60:63], v[160:163], v[136:139], v[60:63]
	s_waitcnt lgkmcnt(14)
	v_mfma_f32_16x16x32_f16 v[64:67], v[164:167], v[136:139], v[64:67]
	s_waitcnt lgkmcnt(13)
	v_mfma_f32_16x16x32_f16 v[68:71], v[168:171], v[136:139], v[68:71]
	s_waitcnt lgkmcnt(12)
	v_mfma_f32_16x16x32_f16 v[72:75], v[156:159], v[140:143], v[72:75]
	v_mfma_f32_16x16x32_f16 v[76:79], v[160:163], v[140:143], v[76:79]
	v_mfma_f32_16x16x32_f16 v[80:83], v[164:167], v[140:143], v[80:83]
	s_add_u32 m0, s28, 0x23000
	s_nop 0
	global_load_lds_dwordx4 v10, s[6:7]
	v_mfma_f32_16x16x32_f16 v[84:87], v[168:171], v[140:143], v[84:87]
	s_waitcnt lgkmcnt(11)
	v_mfma_f32_16x16x32_f16 v[88:91], v[156:159], v[144:147], v[88:91]
	v_mfma_f32_16x16x32_f16 v[92:95], v[160:163], v[144:147], v[92:95]
	v_mfma_f32_16x16x32_f16 v[96:99], v[164:167], v[144:147], v[96:99]
	v_mfma_f32_16x16x32_f16 v[100:103], v[168:171], v[144:147], v[100:103]
	s_waitcnt lgkmcnt(10)
	v_mfma_f32_16x16x32_f16 v[104:107], v[156:159], v[148:151], v[104:107]
	v_mfma_f32_16x16x32_f16 v[108:111], v[160:163], v[148:151], v[108:111]
	s_add_u32 m0, s28, 0x25000
	s_nop 0
	global_load_lds_dwordx4 v11, s[6:7]
	s_add_u32 s6, s6, s20
	s_addc_u32 s7, s7, 0
	v_mfma_f32_16x16x32_f16 v[112:115], v[164:167], v[148:151], v[112:115]
	v_mfma_f32_16x16x32_f16 v[116:119], v[168:171], v[148:151], v[116:119]
	s_waitcnt lgkmcnt(9)
	v_mfma_f32_16x16x32_f16 v[120:123], v[156:159], v[152:155], v[120:123]
	v_mfma_f32_16x16x32_f16 v[124:127], v[160:163], v[152:155], v[124:127]
	v_mfma_f32_16x16x32_f16 v[128:131], v[164:167], v[152:155], v[128:131]
	v_mfma_f32_16x16x32_f16 v[132:135], v[168:171], v[152:155], v[132:135]
	s_waitcnt vmcnt(7) lgkmcnt(0)
	s_barrier
	s_waitcnt lgkmcnt(6)
	ds_read_b128 v[136:139], v15 offset:53248
	ds_read_b128 v[156:159], v17 offset:53248
	ds_read_b128 v[160:163], v17 offset:55296
	ds_read_b128 v[164:167], v17 offset:57344
	ds_read_b128 v[168:171], v17 offset:59392
	ds_read_b128 v[140:143], v15 offset:55296
	ds_read_b128 v[144:147], v15 offset:57344
	ds_read_b128 v[148:151], v15 offset:59392
	ds_read_b128 v[152:155], v15 offset:61440
	v_mfma_f32_16x16x32_f16 v[56:59], v[192:195], v[172:175], v[56:59]
	s_add_u32 m0, s28, 0x0
	s_nop 0
	global_load_lds_dwordx4 v10, s[4:5]
	s_waitcnt lgkmcnt(15)
	v_mfma_f32_16x16x32_f16 v[60:63], v[196:199], v[172:175], v[60:63]
	s_waitcnt lgkmcnt(14)
	v_mfma_f32_16x16x32_f16 v[64:67], v[200:203], v[172:175], v[64:67]
	s_waitcnt lgkmcnt(13)
	v_mfma_f32_16x16x32_f16 v[68:71], v[204:207], v[172:175], v[68:71]
	s_waitcnt lgkmcnt(12)
	v_mfma_f32_16x16x32_f16 v[72:75], v[192:195], v[176:179], v[72:75]
	v_mfma_f32_16x16x32_f16 v[76:79], v[196:199], v[176:179], v[76:79]
	s_add_u32 m0, s28, 0x2000
	s_nop 0
	global_load_lds_dwordx4 v11, s[4:5]
	v_mfma_f32_16x16x32_f16 v[80:83], v[200:203], v[176:179], v[80:83]
	v_mfma_f32_16x16x32_f16 v[84:87], v[204:207], v[176:179], v[84:87]
	s_waitcnt lgkmcnt(11)
	v_mfma_f32_16x16x32_f16 v[88:91], v[192:195], v[180:183], v[88:91]
	v_mfma_f32_16x16x32_f16 v[92:95], v[196:199], v[180:183], v[92:95]
	v_mfma_f32_16x16x32_f16 v[96:99], v[200:203], v[180:183], v[96:99]
	s_add_u32 m0, s28, 0x4000
	s_nop 0
	global_load_lds_dwordx4 v12, s[4:5]
	v_mfma_f32_16x16x32_f16 v[100:103], v[204:207], v[180:183], v[100:103]
	s_waitcnt lgkmcnt(10)
	v_mfma_f32_16x16x32_f16 v[104:107], v[192:195], v[184:187], v[104:107]
	v_mfma_f32_16x16x32_f16 v[108:111], v[196:199], v[184:187], v[108:111]
	v_mfma_f32_16x16x32_f16 v[112:115], v[200:203], v[184:187], v[112:115]
	v_mfma_f32_16x16x32_f16 v[116:119], v[204:207], v[184:187], v[116:119]
	s_add_u32 m0, s28, 0x6000
	s_nop 0
	global_load_lds_dwordx4 v13, s[4:5]
	s_waitcnt lgkmcnt(9)
	v_mfma_f32_16x16x32_f16 v[120:123], v[192:195], v[188:191], v[120:123]
	v_mfma_f32_16x16x32_f16 v[124:127], v[196:199], v[188:191], v[124:127]
	v_mfma_f32_16x16x32_f16 v[128:131], v[200:203], v[188:191], v[128:131]
	v_mfma_f32_16x16x32_f16 v[132:135], v[204:207], v[188:191], v[132:135]
	s_waitcnt lgkmcnt(6)
	ds_read_b128 v[172:175], v16 offset:53248
	ds_read_b128 v[192:195], v18 offset:53248
	ds_read_b128 v[196:199], v18 offset:55296
	ds_read_b128 v[200:203], v18 offset:57344
	ds_read_b128 v[204:207], v18 offset:59392
	ds_read_b128 v[176:179], v16 offset:55296
	ds_read_b128 v[180:183], v16 offset:57344
	ds_read_b128 v[184:187], v16 offset:59392
	ds_read_b128 v[188:191], v16 offset:61440
	v_mfma_f32_16x16x32_f16 v[56:59], v[156:159], v[136:139], v[56:59]
	s_add_u32 m0, s28, 0x8000
	s_nop 0
	global_load_lds_dwordx4 v14, s[4:5]
	s_add_u32 s4, s4, s20
	s_addc_u32 s5, s5, 0
	s_waitcnt lgkmcnt(15)
	v_mfma_f32_16x16x32_f16 v[60:63], v[160:163], v[136:139], v[60:63]
	s_waitcnt lgkmcnt(14)
	v_mfma_f32_16x16x32_f16 v[64:67], v[164:167], v[136:139], v[64:67]
	s_waitcnt lgkmcnt(13)
	v_mfma_f32_16x16x32_f16 v[68:71], v[168:171], v[136:139], v[68:71]
	s_waitcnt lgkmcnt(12)
	v_mfma_f32_16x16x32_f16 v[72:75], v[156:159], v[140:143], v[72:75]
	v_mfma_f32_16x16x32_f16 v[76:79], v[160:163], v[140:143], v[76:79]
	v_mfma_f32_16x16x32_f16 v[80:83], v[164:167], v[140:143], v[80:83]
	s_add_u32 m0, s28, 0x9000
	s_nop 0
	global_load_lds_dwordx4 v10, s[6:7]
	v_mfma_f32_16x16x32_f16 v[84:87], v[168:171], v[140:143], v[84:87]
	s_waitcnt lgkmcnt(11)
	v_mfma_f32_16x16x32_f16 v[88:91], v[156:159], v[144:147], v[88:91]
	v_mfma_f32_16x16x32_f16 v[92:95], v[160:163], v[144:147], v[92:95]
	v_mfma_f32_16x16x32_f16 v[96:99], v[164:167], v[144:147], v[96:99]
	v_mfma_f32_16x16x32_f16 v[100:103], v[168:171], v[144:147], v[100:103]
	s_waitcnt lgkmcnt(10)
	v_mfma_f32_16x16x32_f16 v[104:107], v[156:159], v[148:151], v[104:107]
	v_mfma_f32_16x16x32_f16 v[108:111], v[160:163], v[148:151], v[108:111]
	s_add_u32 m0, s28, 0xb000
	s_nop 0
	global_load_lds_dwordx4 v11, s[6:7]
	s_add_u32 s6, s6, s20
	s_addc_u32 s7, s7, 0
	v_mfma_f32_16x16x32_f16 v[112:115], v[164:167], v[148:151], v[112:115]
	v_mfma_f32_16x16x32_f16 v[116:119], v[168:171], v[148:151], v[116:119]
	s_waitcnt lgkmcnt(9)
	v_mfma_f32_16x16x32_f16 v[120:123], v[156:159], v[152:155], v[120:123]
	v_mfma_f32_16x16x32_f16 v[124:127], v[160:163], v[152:155], v[124:127]
	v_mfma_f32_16x16x32_f16 v[128:131], v[164:167], v[152:155], v[128:131]
	v_mfma_f32_16x16x32_f16 v[132:135], v[168:171], v[152:155], v[132:135]
	s_waitcnt vmcnt(7) lgkmcnt(0)
	s_barrier
	s_waitcnt lgkmcnt(6)
	ds_read_b128 v[136:139], v19
	ds_read_b128 v[156:159], v21
	ds_read_b128 v[160:163], v21 offset:2048
	ds_read_b128 v[164:167], v21 offset:4096
	ds_read_b128 v[168:171], v21 offset:6144
	ds_read_b128 v[140:143], v19 offset:2048
	ds_read_b128 v[144:147], v19 offset:4096
	ds_read_b128 v[148:151], v19 offset:6144
	ds_read_b128 v[152:155], v19 offset:8192
	v_mfma_f32_16x16x32_f16 v[56:59], v[192:195], v[172:175], v[56:59]
	s_add_u32 m0, s28, 0xd000
	s_nop 0
	global_load_lds_dwordx4 v10, s[4:5]
	s_waitcnt lgkmcnt(15)
	v_mfma_f32_16x16x32_f16 v[60:63], v[196:199], v[172:175], v[60:63]
	s_waitcnt lgkmcnt(14)
	v_mfma_f32_16x16x32_f16 v[64:67], v[200:203], v[172:175], v[64:67]
	s_waitcnt lgkmcnt(13)
	v_mfma_f32_16x16x32_f16 v[68:71], v[204:207], v[172:175], v[68:71]
	s_waitcnt lgkmcnt(12)
	v_mfma_f32_16x16x32_f16 v[72:75], v[192:195], v[176:179], v[72:75]
	v_mfma_f32_16x16x32_f16 v[76:79], v[196:199], v[176:179], v[76:79]
	s_add_u32 m0, s28, 0xf000
	s_nop 0
	global_load_lds_dwordx4 v11, s[4:5]
	v_mfma_f32_16x16x32_f16 v[80:83], v[200:203], v[176:179], v[80:83]
	v_mfma_f32_16x16x32_f16 v[84:87], v[204:207], v[176:179], v[84:87]
	s_waitcnt lgkmcnt(11)
	v_mfma_f32_16x16x32_f16 v[88:91], v[192:195], v[180:183], v[88:91]
	v_mfma_f32_16x16x32_f16 v[92:95], v[196:199], v[180:183], v[92:95]
	v_mfma_f32_16x16x32_f16 v[96:99], v[200:203], v[180:183], v[96:99]
	s_add_u32 m0, s28, 0x11000
	s_nop 0
	global_load_lds_dwordx4 v12, s[4:5]
	v_mfma_f32_16x16x32_f16 v[100:103], v[204:207], v[180:183], v[100:103]
	s_waitcnt lgkmcnt(10)
	v_mfma_f32_16x16x32_f16 v[104:107], v[192:195], v[184:187], v[104:107]
	v_mfma_f32_16x16x32_f16 v[108:111], v[196:199], v[184:187], v[108:111]
	v_mfma_f32_16x16x32_f16 v[112:115], v[200:203], v[184:187], v[112:115]
	v_mfma_f32_16x16x32_f16 v[116:119], v[204:207], v[184:187], v[116:119]
	s_add_u32 m0, s28, 0x13000
	s_nop 0
	global_load_lds_dwordx4 v13, s[4:5]
	s_waitcnt lgkmcnt(9)
	v_mfma_f32_16x16x32_f16 v[120:123], v[192:195], v[188:191], v[120:123]
	v_mfma_f32_16x16x32_f16 v[124:127], v[196:199], v[188:191], v[124:127]
	v_mfma_f32_16x16x32_f16 v[128:131], v[200:203], v[188:191], v[128:131]
	v_mfma_f32_16x16x32_f16 v[132:135], v[204:207], v[188:191], v[132:135]
	s_waitcnt lgkmcnt(6)
	ds_read_b128 v[172:175], v20
	ds_read_b128 v[192:195], v22
	ds_read_b128 v[196:199], v22 offset:2048
	ds_read_b128 v[200:203], v22 offset:4096
	ds_read_b128 v[204:207], v22 offset:6144
	ds_read_b128 v[176:179], v20 offset:2048
	ds_read_b128 v[180:183], v20 offset:4096
	ds_read_b128 v[184:187], v20 offset:6144
	ds_read_b128 v[188:191], v20 offset:8192
	v_mfma_f32_16x16x32_f16 v[56:59], v[156:159], v[136:139], v[56:59]
	s_add_u32 m0, s28, 0x15000
	s_nop 0
	global_load_lds_dwordx4 v14, s[4:5]
	s_add_u32 s4, s4, s20
	s_addc_u32 s5, s5, 0
	s_waitcnt lgkmcnt(15)
	v_mfma_f32_16x16x32_f16 v[60:63], v[160:163], v[136:139], v[60:63]
	s_waitcnt lgkmcnt(14)
	v_mfma_f32_16x16x32_f16 v[64:67], v[164:167], v[136:139], v[64:67]
	s_waitcnt lgkmcnt(13)
	v_mfma_f32_16x16x32_f16 v[68:71], v[168:171], v[136:139], v[68:71]
	s_waitcnt lgkmcnt(12)
	v_mfma_f32_16x16x32_f16 v[72:75], v[156:159], v[140:143], v[72:75]
	v_mfma_f32_16x16x32_f16 v[76:79], v[160:163], v[140:143], v[76:79]
	v_mfma_f32_16x16x32_f16 v[80:83], v[164:167], v[140:143], v[80:83]
	s_add_u32 m0, s28, 0x16000
	s_nop 0
	global_load_lds_dwordx4 v10, s[6:7]
	v_mfma_f32_16x16x32_f16 v[84:87], v[168:171], v[140:143], v[84:87]
	s_waitcnt lgkmcnt(11)
	v_mfma_f32_16x16x32_f16 v[88:91], v[156:159], v[144:147], v[88:91]
	v_mfma_f32_16x16x32_f16 v[92:95], v[160:163], v[144:147], v[92:95]
	v_mfma_f32_16x16x32_f16 v[96:99], v[164:167], v[144:147], v[96:99]
	v_mfma_f32_16x16x32_f16 v[100:103], v[168:171], v[144:147], v[100:103]
	s_waitcnt lgkmcnt(10)
	v_mfma_f32_16x16x32_f16 v[104:107], v[156:159], v[148:151], v[104:107]
	v_mfma_f32_16x16x32_f16 v[108:111], v[160:163], v[148:151], v[108:111]
	s_add_u32 m0, s28, 0x18000
	s_nop 0
	global_load_lds_dwordx4 v11, s[6:7]
	s_add_u32 s6, s6, s20
	s_addc_u32 s7, s7, 0
	v_mfma_f32_16x16x32_f16 v[112:115], v[164:167], v[148:151], v[112:115]
	v_mfma_f32_16x16x32_f16 v[116:119], v[168:171], v[148:151], v[116:119]
	s_waitcnt lgkmcnt(9)
	v_mfma_f32_16x16x32_f16 v[120:123], v[156:159], v[152:155], v[120:123]
	v_mfma_f32_16x16x32_f16 v[124:127], v[160:163], v[152:155], v[124:127]
	v_mfma_f32_16x16x32_f16 v[128:131], v[164:167], v[152:155], v[128:131]
	v_mfma_f32_16x16x32_f16 v[132:135], v[168:171], v[152:155], v[132:135]
	s_waitcnt vmcnt(7) lgkmcnt(0)
	s_barrier
	s_waitcnt lgkmcnt(6)
	ds_read_b128 v[136:139], v15
	ds_read_b128 v[156:159], v17
	ds_read_b128 v[160:163], v17 offset:2048
	ds_read_b128 v[164:167], v17 offset:4096
	ds_read_b128 v[168:171], v17 offset:6144
	ds_read_b128 v[140:143], v15 offset:2048
	ds_read_b128 v[144:147], v15 offset:4096
	ds_read_b128 v[148:151], v15 offset:6144
	ds_read_b128 v[152:155], v15 offset:8192
	v_mfma_f32_16x16x32_f16 v[56:59], v[192:195], v[172:175], v[56:59]
	s_add_u32 m0, s28, 0x1a000
	s_nop 0
	global_load_lds_dwordx4 v10, s[4:5]
	s_waitcnt lgkmcnt(15)
	v_mfma_f32_16x16x32_f16 v[60:63], v[196:199], v[172:175], v[60:63]
	s_waitcnt lgkmcnt(14)
	v_mfma_f32_16x16x32_f16 v[64:67], v[200:203], v[172:175], v[64:67]
	s_waitcnt lgkmcnt(13)
	v_mfma_f32_16x16x32_f16 v[68:71], v[204:207], v[172:175], v[68:71]
	s_waitcnt lgkmcnt(12)
	v_mfma_f32_16x16x32_f16 v[72:75], v[192:195], v[176:179], v[72:75]
	v_mfma_f32_16x16x32_f16 v[76:79], v[196:199], v[176:179], v[76:79]
	s_add_u32 m0, s28, 0x1c000
	s_nop 0
	global_load_lds_dwordx4 v11, s[4:5]
	v_mfma_f32_16x16x32_f16 v[80:83], v[200:203], v[176:179], v[80:83]
	v_mfma_f32_16x16x32_f16 v[84:87], v[204:207], v[176:179], v[84:87]
	s_waitcnt lgkmcnt(11)
	v_mfma_f32_16x16x32_f16 v[88:91], v[192:195], v[180:183], v[88:91]
	v_mfma_f32_16x16x32_f16 v[92:95], v[196:199], v[180:183], v[92:95]
	v_mfma_f32_16x16x32_f16 v[96:99], v[200:203], v[180:183], v[96:99]
	s_add_u32 m0, s28, 0x1e000
	s_nop 0
	global_load_lds_dwordx4 v12, s[4:5]
	v_mfma_f32_16x16x32_f16 v[100:103], v[204:207], v[180:183], v[100:103]
	s_waitcnt lgkmcnt(10)
	v_mfma_f32_16x16x32_f16 v[104:107], v[192:195], v[184:187], v[104:107]
	v_mfma_f32_16x16x32_f16 v[108:111], v[196:199], v[184:187], v[108:111]
	v_mfma_f32_16x16x32_f16 v[112:115], v[200:203], v[184:187], v[112:115]
	v_mfma_f32_16x16x32_f16 v[116:119], v[204:207], v[184:187], v[116:119]
	s_add_u32 m0, s28, 0x20000
	s_nop 0
	global_load_lds_dwordx4 v13, s[4:5]
	s_waitcnt lgkmcnt(9)
	v_mfma_f32_16x16x32_f16 v[120:123], v[192:195], v[188:191], v[120:123]
	v_mfma_f32_16x16x32_f16 v[124:127], v[196:199], v[188:191], v[124:127]
	v_mfma_f32_16x16x32_f16 v[128:131], v[200:203], v[188:191], v[128:131]
	v_mfma_f32_16x16x32_f16 v[132:135], v[204:207], v[188:191], v[132:135]
	s_waitcnt lgkmcnt(6)
	ds_read_b128 v[172:175], v16
	ds_read_b128 v[192:195], v18
	ds_read_b128 v[196:199], v18 offset:2048
	ds_read_b128 v[200:203], v18 offset:4096
	ds_read_b128 v[204:207], v18 offset:6144
	ds_read_b128 v[176:179], v16 offset:2048
	ds_read_b128 v[180:183], v16 offset:4096
	ds_read_b128 v[184:187], v16 offset:6144
	ds_read_b128 v[188:191], v16 offset:8192
	v_mfma_f32_16x16x32_f16 v[56:59], v[156:159], v[136:139], v[56:59]
	s_add_u32 m0, s28, 0x22000
	s_nop 0
	global_load_lds_dwordx4 v14, s[4:5]
	s_add_u32 s4, s4, s20
	s_addc_u32 s5, s5, 0
	s_waitcnt lgkmcnt(15)
	v_mfma_f32_16x16x32_f16 v[60:63], v[160:163], v[136:139], v[60:63]
	s_waitcnt lgkmcnt(14)
	v_mfma_f32_16x16x32_f16 v[64:67], v[164:167], v[136:139], v[64:67]
	s_waitcnt lgkmcnt(13)
	v_mfma_f32_16x16x32_f16 v[68:71], v[168:171], v[136:139], v[68:71]
	s_waitcnt lgkmcnt(12)
	v_mfma_f32_16x16x32_f16 v[72:75], v[156:159], v[140:143], v[72:75]
	v_mfma_f32_16x16x32_f16 v[76:79], v[160:163], v[140:143], v[76:79]
	v_mfma_f32_16x16x32_f16 v[80:83], v[164:167], v[140:143], v[80:83]
	s_add_u32 m0, s28, 0x23000
	s_nop 0
	global_load_lds_dwordx4 v10, s[6:7]
	v_mfma_f32_16x16x32_f16 v[84:87], v[168:171], v[140:143], v[84:87]
	s_waitcnt lgkmcnt(11)
	v_mfma_f32_16x16x32_f16 v[88:91], v[156:159], v[144:147], v[88:91]
	v_mfma_f32_16x16x32_f16 v[92:95], v[160:163], v[144:147], v[92:95]
	v_mfma_f32_16x16x32_f16 v[96:99], v[164:167], v[144:147], v[96:99]
	v_mfma_f32_16x16x32_f16 v[100:103], v[168:171], v[144:147], v[100:103]
	s_waitcnt lgkmcnt(10)
	v_mfma_f32_16x16x32_f16 v[104:107], v[156:159], v[148:151], v[104:107]
	v_mfma_f32_16x16x32_f16 v[108:111], v[160:163], v[148:151], v[108:111]
	s_add_u32 m0, s28, 0x25000
	s_nop 0
	global_load_lds_dwordx4 v11, s[6:7]
	s_add_u32 s6, s6, s20
	s_addc_u32 s7, s7, 0
	v_mfma_f32_16x16x32_f16 v[112:115], v[164:167], v[148:151], v[112:115]
	v_mfma_f32_16x16x32_f16 v[116:119], v[168:171], v[148:151], v[116:119]
	s_waitcnt lgkmcnt(9)
	v_mfma_f32_16x16x32_f16 v[120:123], v[156:159], v[152:155], v[120:123]
	v_mfma_f32_16x16x32_f16 v[124:127], v[160:163], v[152:155], v[124:127]
	v_mfma_f32_16x16x32_f16 v[128:131], v[164:167], v[152:155], v[128:131]
	v_mfma_f32_16x16x32_f16 v[132:135], v[168:171], v[152:155], v[132:135]
	s_waitcnt vmcnt(7) lgkmcnt(0)
	s_barrier
	s_waitcnt lgkmcnt(6)
	ds_read_b128 v[136:139], v15 offset:53248
	ds_read_b128 v[156:159], v17 offset:53248
	ds_read_b128 v[160:163], v17 offset:55296
	ds_read_b128 v[164:167], v17 offset:57344
	ds_read_b128 v[168:171], v17 offset:59392
	ds_read_b128 v[140:143], v15 offset:55296
	ds_read_b128 v[144:147], v15 offset:57344
	ds_read_b128 v[148:151], v15 offset:59392
	ds_read_b128 v[152:155], v15 offset:61440
	v_mfma_f32_16x16x32_f16 v[56:59], v[192:195], v[172:175], v[56:59]
	s_add_u32 m0, s28, 0x0
	s_nop 0
	global_load_lds_dwordx4 v10, s[4:5]
	s_waitcnt lgkmcnt(15)
	v_mfma_f32_16x16x32_f16 v[60:63], v[196:199], v[172:175], v[60:63]
	s_waitcnt lgkmcnt(14)
	v_mfma_f32_16x16x32_f16 v[64:67], v[200:203], v[172:175], v[64:67]
	s_waitcnt lgkmcnt(13)
	v_mfma_f32_16x16x32_f16 v[68:71], v[204:207], v[172:175], v[68:71]
	s_waitcnt lgkmcnt(12)
	v_mfma_f32_16x16x32_f16 v[72:75], v[192:195], v[176:179], v[72:75]
	v_mfma_f32_16x16x32_f16 v[76:79], v[196:199], v[176:179], v[76:79]
	s_add_u32 m0, s28, 0x2000
	s_nop 0
	global_load_lds_dwordx4 v11, s[4:5]
	v_mfma_f32_16x16x32_f16 v[80:83], v[200:203], v[176:179], v[80:83]
	v_mfma_f32_16x16x32_f16 v[84:87], v[204:207], v[176:179], v[84:87]
	s_waitcnt lgkmcnt(11)
	v_mfma_f32_16x16x32_f16 v[88:91], v[192:195], v[180:183], v[88:91]
	v_mfma_f32_16x16x32_f16 v[92:95], v[196:199], v[180:183], v[92:95]
	v_mfma_f32_16x16x32_f16 v[96:99], v[200:203], v[180:183], v[96:99]
	s_add_u32 m0, s28, 0x4000
	s_nop 0
	global_load_lds_dwordx4 v12, s[4:5]
	v_mfma_f32_16x16x32_f16 v[100:103], v[204:207], v[180:183], v[100:103]
	s_waitcnt lgkmcnt(10)
	v_mfma_f32_16x16x32_f16 v[104:107], v[192:195], v[184:187], v[104:107]
	v_mfma_f32_16x16x32_f16 v[108:111], v[196:199], v[184:187], v[108:111]
	v_mfma_f32_16x16x32_f16 v[112:115], v[200:203], v[184:187], v[112:115]
	v_mfma_f32_16x16x32_f16 v[116:119], v[204:207], v[184:187], v[116:119]
	s_add_u32 m0, s28, 0x6000
	s_nop 0
	global_load_lds_dwordx4 v13, s[4:5]
	s_waitcnt lgkmcnt(9)
	v_mfma_f32_16x16x32_f16 v[120:123], v[192:195], v[188:191], v[120:123]
	v_mfma_f32_16x16x32_f16 v[124:127], v[196:199], v[188:191], v[124:127]
	v_mfma_f32_16x16x32_f16 v[128:131], v[200:203], v[188:191], v[128:131]
	v_mfma_f32_16x16x32_f16 v[132:135], v[204:207], v[188:191], v[132:135]
	s_waitcnt lgkmcnt(6)
	ds_read_b128 v[172:175], v16 offset:53248
	ds_read_b128 v[192:195], v18 offset:53248
	ds_read_b128 v[196:199], v18 offset:55296
	ds_read_b128 v[200:203], v18 offset:57344
	ds_read_b128 v[204:207], v18 offset:59392
	ds_read_b128 v[176:179], v16 offset:55296
	ds_read_b128 v[180:183], v16 offset:57344
	ds_read_b128 v[184:187], v16 offset:59392
	ds_read_b128 v[188:191], v16 offset:61440
	v_mfma_f32_16x16x32_f16 v[56:59], v[156:159], v[136:139], v[56:59]
	s_add_u32 m0, s28, 0x8000
	s_nop 0
	global_load_lds_dwordx4 v14, s[4:5]
	s_add_u32 s4, s4, s20
	s_addc_u32 s5, s5, 0
	s_waitcnt lgkmcnt(15)
	v_mfma_f32_16x16x32_f16 v[60:63], v[160:163], v[136:139], v[60:63]
	s_waitcnt lgkmcnt(14)
	v_mfma_f32_16x16x32_f16 v[64:67], v[164:167], v[136:139], v[64:67]
	s_waitcnt lgkmcnt(13)
	v_mfma_f32_16x16x32_f16 v[68:71], v[168:171], v[136:139], v[68:71]
	s_waitcnt lgkmcnt(12)
	v_mfma_f32_16x16x32_f16 v[72:75], v[156:159], v[140:143], v[72:75]
	v_mfma_f32_16x16x32_f16 v[76:79], v[160:163], v[140:143], v[76:79]
	v_mfma_f32_16x16x32_f16 v[80:83], v[164:167], v[140:143], v[80:83]
	s_add_u32 m0, s28, 0x9000
	s_nop 0
	global_load_lds_dwordx4 v10, s[6:7]
	v_mfma_f32_16x16x32_f16 v[84:87], v[168:171], v[140:143], v[84:87]
	s_waitcnt lgkmcnt(11)
	v_mfma_f32_16x16x32_f16 v[88:91], v[156:159], v[144:147], v[88:91]
	v_mfma_f32_16x16x32_f16 v[92:95], v[160:163], v[144:147], v[92:95]
	v_mfma_f32_16x16x32_f16 v[96:99], v[164:167], v[144:147], v[96:99]
	v_mfma_f32_16x16x32_f16 v[100:103], v[168:171], v[144:147], v[100:103]
	s_waitcnt lgkmcnt(10)
	v_mfma_f32_16x16x32_f16 v[104:107], v[156:159], v[148:151], v[104:107]
	v_mfma_f32_16x16x32_f16 v[108:111], v[160:163], v[148:151], v[108:111]
	s_add_u32 m0, s28, 0xb000
	s_nop 0
	global_load_lds_dwordx4 v11, s[6:7]
	s_add_u32 s6, s6, s20
	s_addc_u32 s7, s7, 0
	v_mfma_f32_16x16x32_f16 v[112:115], v[164:167], v[148:151], v[112:115]
	v_mfma_f32_16x16x32_f16 v[116:119], v[168:171], v[148:151], v[116:119]
	s_waitcnt lgkmcnt(9)
	v_mfma_f32_16x16x32_f16 v[120:123], v[156:159], v[152:155], v[120:123]
	v_mfma_f32_16x16x32_f16 v[124:127], v[160:163], v[152:155], v[124:127]
	v_mfma_f32_16x16x32_f16 v[128:131], v[164:167], v[152:155], v[128:131]
	v_mfma_f32_16x16x32_f16 v[132:135], v[168:171], v[152:155], v[132:135]
	s_waitcnt vmcnt(7) lgkmcnt(0)
	s_barrier
	s_waitcnt lgkmcnt(6)
	ds_read_b128 v[136:139], v19
	ds_read_b128 v[156:159], v21
	ds_read_b128 v[160:163], v21 offset:2048
	ds_read_b128 v[164:167], v21 offset:4096
	ds_read_b128 v[168:171], v21 offset:6144
	ds_read_b128 v[140:143], v19 offset:2048
	ds_read_b128 v[144:147], v19 offset:4096
	ds_read_b128 v[148:151], v19 offset:6144
	ds_read_b128 v[152:155], v19 offset:8192
	v_mfma_f32_16x16x32_f16 v[56:59], v[192:195], v[172:175], v[56:59]
	s_waitcnt lgkmcnt(15)
	v_mfma_f32_16x16x32_f16 v[60:63], v[196:199], v[172:175], v[60:63]
	s_waitcnt lgkmcnt(14)
	v_mfma_f32_16x16x32_f16 v[64:67], v[200:203], v[172:175], v[64:67]
	s_waitcnt lgkmcnt(13)
	v_mfma_f32_16x16x32_f16 v[68:71], v[204:207], v[172:175], v[68:71]
	s_waitcnt lgkmcnt(12)
	v_mfma_f32_16x16x32_f16 v[72:75], v[192:195], v[176:179], v[72:75]
	v_mfma_f32_16x16x32_f16 v[76:79], v[196:199], v[176:179], v[76:79]
	v_mfma_f32_16x16x32_f16 v[80:83], v[200:203], v[176:179], v[80:83]
	v_mfma_f32_16x16x32_f16 v[84:87], v[204:207], v[176:179], v[84:87]
	s_waitcnt lgkmcnt(11)
	v_mfma_f32_16x16x32_f16 v[88:91], v[192:195], v[180:183], v[88:91]
	v_mfma_f32_16x16x32_f16 v[92:95], v[196:199], v[180:183], v[92:95]
	v_mfma_f32_16x16x32_f16 v[96:99], v[200:203], v[180:183], v[96:99]
	v_mfma_f32_16x16x32_f16 v[100:103], v[204:207], v[180:183], v[100:103]
	s_waitcnt lgkmcnt(10)
	v_mfma_f32_16x16x32_f16 v[104:107], v[192:195], v[184:187], v[104:107]
	v_mfma_f32_16x16x32_f16 v[108:111], v[196:199], v[184:187], v[108:111]
	v_mfma_f32_16x16x32_f16 v[112:115], v[200:203], v[184:187], v[112:115]
	v_mfma_f32_16x16x32_f16 v[116:119], v[204:207], v[184:187], v[116:119]
	s_waitcnt lgkmcnt(9)
	v_mfma_f32_16x16x32_f16 v[120:123], v[192:195], v[188:191], v[120:123]
	v_mfma_f32_16x16x32_f16 v[124:127], v[196:199], v[188:191], v[124:127]
	v_mfma_f32_16x16x32_f16 v[128:131], v[200:203], v[188:191], v[128:131]
	v_mfma_f32_16x16x32_f16 v[132:135], v[204:207], v[188:191], v[132:135]
	s_waitcnt lgkmcnt(6)
	ds_read_b128 v[172:175], v20
	ds_read_b128 v[192:195], v22
	ds_read_b128 v[196:199], v22 offset:2048
	ds_read_b128 v[200:203], v22 offset:4096
	ds_read_b128 v[204:207], v22 offset:6144
	ds_read_b128 v[176:179], v20 offset:2048
	ds_read_b128 v[180:183], v20 offset:4096
	ds_read_b128 v[184:187], v20 offset:6144
	ds_read_b128 v[188:191], v20 offset:8192
	v_mfma_f32_16x16x32_f16 v[56:59], v[156:159], v[136:139], v[56:59]
	s_waitcnt lgkmcnt(15)
	v_mfma_f32_16x16x32_f16 v[60:63], v[160:163], v[136:139], v[60:63]
	s_waitcnt lgkmcnt(14)
	v_mfma_f32_16x16x32_f16 v[64:67], v[164:167], v[136:139], v[64:67]
	s_waitcnt lgkmcnt(13)
	v_mfma_f32_16x16x32_f16 v[68:71], v[168:171], v[136:139], v[68:71]
	s_waitcnt lgkmcnt(12)
	v_mfma_f32_16x16x32_f16 v[72:75], v[156:159], v[140:143], v[72:75]
	v_mfma_f32_16x16x32_f16 v[76:79], v[160:163], v[140:143], v[76:79]
	v_mfma_f32_16x16x32_f16 v[80:83], v[164:167], v[140:143], v[80:83]
	v_mfma_f32_16x16x32_f16 v[84:87], v[168:171], v[140:143], v[84:87]
	s_waitcnt lgkmcnt(11)
	v_mfma_f32_16x16x32_f16 v[88:91], v[156:159], v[144:147], v[88:91]
	v_mfma_f32_16x16x32_f16 v[92:95], v[160:163], v[144:147], v[92:95]
	v_mfma_f32_16x16x32_f16 v[96:99], v[164:167], v[144:147], v[96:99]
	v_mfma_f32_16x16x32_f16 v[100:103], v[168:171], v[144:147], v[100:103]
	s_waitcnt lgkmcnt(10)
	v_mfma_f32_16x16x32_f16 v[104:107], v[156:159], v[148:151], v[104:107]
	v_mfma_f32_16x16x32_f16 v[108:111], v[160:163], v[148:151], v[108:111]
	v_mfma_f32_16x16x32_f16 v[112:115], v[164:167], v[148:151], v[112:115]
	v_mfma_f32_16x16x32_f16 v[116:119], v[168:171], v[148:151], v[116:119]
	s_waitcnt lgkmcnt(9)
	v_mfma_f32_16x16x32_f16 v[120:123], v[156:159], v[152:155], v[120:123]
	v_mfma_f32_16x16x32_f16 v[124:127], v[160:163], v[152:155], v[124:127]
	v_mfma_f32_16x16x32_f16 v[128:131], v[164:167], v[152:155], v[128:131]
	v_mfma_f32_16x16x32_f16 v[132:135], v[168:171], v[152:155], v[132:135]
	s_waitcnt vmcnt(0) lgkmcnt(0)
	s_barrier
	s_waitcnt lgkmcnt(6)
	ds_read_b128 v[136:139], v15
	ds_read_b128 v[156:159], v17
	ds_read_b128 v[160:163], v17 offset:2048
	ds_read_b128 v[164:167], v17 offset:4096
	ds_read_b128 v[168:171], v17 offset:6144
	ds_read_b128 v[140:143], v15 offset:2048
	ds_read_b128 v[144:147], v15 offset:4096
	ds_read_b128 v[148:151], v15 offset:6144
	ds_read_b128 v[152:155], v15 offset:8192
	v_mfma_f32_16x16x32_f16 v[56:59], v[192:195], v[172:175], v[56:59]
	s_waitcnt lgkmcnt(15)
	v_mfma_f32_16x16x32_f16 v[60:63], v[196:199], v[172:175], v[60:63]
	s_waitcnt lgkmcnt(14)
	v_mfma_f32_16x16x32_f16 v[64:67], v[200:203], v[172:175], v[64:67]
	s_waitcnt lgkmcnt(13)
	v_mfma_f32_16x16x32_f16 v[68:71], v[204:207], v[172:175], v[68:71]
	s_waitcnt lgkmcnt(12)
	v_mfma_f32_16x16x32_f16 v[72:75], v[192:195], v[176:179], v[72:75]
	v_mfma_f32_16x16x32_f16 v[76:79], v[196:199], v[176:179], v[76:79]
	v_mfma_f32_16x16x32_f16 v[80:83], v[200:203], v[176:179], v[80:83]
	v_mfma_f32_16x16x32_f16 v[84:87], v[204:207], v[176:179], v[84:87]
	s_waitcnt lgkmcnt(11)
	v_mfma_f32_16x16x32_f16 v[88:91], v[192:195], v[180:183], v[88:91]
	v_mfma_f32_16x16x32_f16 v[92:95], v[196:199], v[180:183], v[92:95]
	v_mfma_f32_16x16x32_f16 v[96:99], v[200:203], v[180:183], v[96:99]
	v_mfma_f32_16x16x32_f16 v[100:103], v[204:207], v[180:183], v[100:103]
	s_waitcnt lgkmcnt(10)
	v_mfma_f32_16x16x32_f16 v[104:107], v[192:195], v[184:187], v[104:107]
	v_mfma_f32_16x16x32_f16 v[108:111], v[196:199], v[184:187], v[108:111]
	v_mfma_f32_16x16x32_f16 v[112:115], v[200:203], v[184:187], v[112:115]
	v_mfma_f32_16x16x32_f16 v[116:119], v[204:207], v[184:187], v[116:119]
	s_waitcnt lgkmcnt(9)
	v_mfma_f32_16x16x32_f16 v[120:123], v[192:195], v[188:191], v[120:123]
	v_mfma_f32_16x16x32_f16 v[124:127], v[196:199], v[188:191], v[124:127]
	v_mfma_f32_16x16x32_f16 v[128:131], v[200:203], v[188:191], v[128:131]
	v_mfma_f32_16x16x32_f16 v[132:135], v[204:207], v[188:191], v[132:135]
	s_waitcnt lgkmcnt(6)
	ds_read_b128 v[172:175], v16
	ds_read_b128 v[192:195], v18
	ds_read_b128 v[196:199], v18 offset:2048
	ds_read_b128 v[200:203], v18 offset:4096
	ds_read_b128 v[204:207], v18 offset:6144
	ds_read_b128 v[176:179], v16 offset:2048
	ds_read_b128 v[180:183], v16 offset:4096
	ds_read_b128 v[184:187], v16 offset:6144
	ds_read_b128 v[188:191], v16 offset:8192
	v_mfma_f32_16x16x32_f16 v[56:59], v[156:159], v[136:139], v[56:59]
	s_waitcnt lgkmcnt(15)
	v_mfma_f32_16x16x32_f16 v[60:63], v[160:163], v[136:139], v[60:63]
	s_waitcnt lgkmcnt(14)
	v_mfma_f32_16x16x32_f16 v[64:67], v[164:167], v[136:139], v[64:67]
	s_waitcnt lgkmcnt(13)
	v_mfma_f32_16x16x32_f16 v[68:71], v[168:171], v[136:139], v[68:71]
	s_waitcnt lgkmcnt(12)
	v_mfma_f32_16x16x32_f16 v[72:75], v[156:159], v[140:143], v[72:75]
	v_mfma_f32_16x16x32_f16 v[76:79], v[160:163], v[140:143], v[76:79]
	v_mfma_f32_16x16x32_f16 v[80:83], v[164:167], v[140:143], v[80:83]
	v_mfma_f32_16x16x32_f16 v[84:87], v[168:171], v[140:143], v[84:87]
	s_waitcnt lgkmcnt(11)
	v_mfma_f32_16x16x32_f16 v[88:91], v[156:159], v[144:147], v[88:91]
	v_mfma_f32_16x16x32_f16 v[92:95], v[160:163], v[144:147], v[92:95]
	v_mfma_f32_16x16x32_f16 v[96:99], v[164:167], v[144:147], v[96:99]
	v_mfma_f32_16x16x32_f16 v[100:103], v[168:171], v[144:147], v[100:103]
	s_waitcnt lgkmcnt(10)
	v_mfma_f32_16x16x32_f16 v[104:107], v[156:159], v[148:151], v[104:107]
	v_mfma_f32_16x16x32_f16 v[108:111], v[160:163], v[148:151], v[108:111]
	v_mfma_f32_16x16x32_f16 v[112:115], v[164:167], v[148:151], v[112:115]
	v_mfma_f32_16x16x32_f16 v[116:119], v[168:171], v[148:151], v[116:119]
	s_waitcnt lgkmcnt(9)
	v_mfma_f32_16x16x32_f16 v[120:123], v[156:159], v[152:155], v[120:123]
	v_mfma_f32_16x16x32_f16 v[124:127], v[160:163], v[152:155], v[124:127]
	v_mfma_f32_16x16x32_f16 v[128:131], v[164:167], v[152:155], v[128:131]
	v_mfma_f32_16x16x32_f16 v[132:135], v[168:171], v[152:155], v[132:135]
	s_waitcnt lgkmcnt(7)
	v_mfma_f32_16x16x32_f16 v[56:59], v[192:195], v[172:175], v[56:59]
	s_waitcnt lgkmcnt(6)
	v_mfma_f32_16x16x32_f16 v[60:63], v[196:199], v[172:175], v[60:63]
	s_waitcnt lgkmcnt(5)
	v_mfma_f32_16x16x32_f16 v[64:67], v[200:203], v[172:175], v[64:67]
	s_waitcnt lgkmcnt(4)
	v_mfma_f32_16x16x32_f16 v[68:71], v[204:207], v[172:175], v[68:71]
	s_waitcnt lgkmcnt(3)
	v_mfma_f32_16x16x32_f16 v[72:75], v[192:195], v[176:179], v[72:75]
	v_mfma_f32_16x16x32_f16 v[76:79], v[196:199], v[176:179], v[76:79]
	v_mfma_f32_16x16x32_f16 v[80:83], v[200:203], v[176:179], v[80:83]
	v_mfma_f32_16x16x32_f16 v[84:87], v[204:207], v[176:179], v[84:87]
	s_waitcnt lgkmcnt(2)
	v_mfma_f32_16x16x32_f16 v[88:91], v[192:195], v[180:183], v[88:91]
	v_mfma_f32_16x16x32_f16 v[92:95], v[196:199], v[180:183], v[92:95]
	v_mfma_f32_16x16x32_f16 v[96:99], v[200:203], v[180:183], v[96:99]
	v_mfma_f32_16x16x32_f16 v[100:103], v[204:207], v[180:183], v[100:103]
	s_waitcnt lgkmcnt(1)
	v_mfma_f32_16x16x32_f16 v[104:107], v[192:195], v[184:187], v[104:107]
	v_mfma_f32_16x16x32_f16 v[108:111], v[196:199], v[184:187], v[108:111]
	v_mfma_f32_16x16x32_f16 v[112:115], v[200:203], v[184:187], v[112:115]
	v_mfma_f32_16x16x32_f16 v[116:119], v[204:207], v[184:187], v[116:119]
	s_waitcnt lgkmcnt(0)
	v_mfma_f32_16x16x32_f16 v[120:123], v[192:195], v[188:191], v[120:123]
	v_mfma_f32_16x16x32_f16 v[124:127], v[196:199], v[188:191], v[124:127]
	v_mfma_f32_16x16x32_f16 v[128:131], v[200:203], v[188:191], v[128:131]
	v_mfma_f32_16x16x32_f16 v[132:135], v[204:207], v[188:191], v[132:135]
	s_nop 7
	s_nop 1
	v_mov_b32_e32 v213, s19
	v_pk_add_f32 v[56:57], v[56:57], v[24:25]
	v_pk_add_f32 v[58:59], v[58:59], v[26:27]
	v_pk_add_f32 v[60:61], v[60:61], v[28:29]
	v_pk_add_f32 v[62:63], v[62:63], v[30:31]
	v_pk_add_f32 v[64:65], v[64:65], v[32:33]
	v_pk_add_f32 v[66:67], v[66:67], v[34:35]
	v_pk_add_f32 v[68:69], v[68:69], v[36:37]
	v_pk_add_f32 v[70:71], v[70:71], v[38:39]
	v_pk_mul_f32 v[208:209], v[56:57], v[56:57]
	v_pk_fma_f32 v[208:209], v[58:59], v[58:59], v[208:209]
	v_pk_fma_f32 v[208:209], v[60:61], v[60:61], v[208:209]
	v_pk_fma_f32 v[208:209], v[62:63], v[62:63], v[208:209]
	v_pk_fma_f32 v[208:209], v[64:65], v[64:65], v[208:209]
	v_pk_fma_f32 v[208:209], v[66:67], v[66:67], v[208:209]
	v_pk_fma_f32 v[208:209], v[68:69], v[68:69], v[208:209]
	v_pk_fma_f32 v[208:209], v[70:71], v[70:71], v[208:209]
	v_add_f32_e32 v208, v208, v209
	v_mov_b32_e32 v209, v208
	s_nop 1
	v_permlane16_swap_b32_e32 v208, v209
	v_add_f32_e32 v208, v208, v209
	v_mov_b32_e32 v209, v208
	s_nop 1
	v_permlane32_swap_b32_e32 v208, v209
	v_add_f32_e32 v208, v208, v209
	v_mov_b32_e32 v210, 0x358637bd
	v_fmac_f32_e32 v210, 0x3c800000, v208
	v_rsq_f32_e32 v210, v210
	s_add_u32 s24, s29, 0
	s_lshr_b32 s8, s24, 1
	s_lshl_b32 s8, s8, 12
	s_and_b32 s24, s24, 1
	s_lshl_b32 s24, s24, 8
	s_add_u32 s8, s8, s24
	v_mul_f32_e32 v210, v213, v210
	v_add_u32_e32 v212, s8, v23
	v_pk_mul_f32 v[56:57], v[56:57], v[210:211] op_sel_hi:[1,0]
	v_pk_mul_f32 v[58:59], v[58:59], v[210:211] op_sel_hi:[1,0]
	v_pk_mul_f32 v[56:57], v[56:57], v[40:41]
	v_pk_mul_f32 v[58:59], v[58:59], v[42:43]
	v_cvt_pk_f16_f32 v56, v56, v57
	v_cvt_pk_f16_f32 v57, v58, v59
	global_store_dwordx2 v212, v[56:57], s[22:23] offset:0
	v_pk_mul_f32 v[60:61], v[60:61], v[210:211] op_sel_hi:[1,0]
	v_pk_mul_f32 v[62:63], v[62:63], v[210:211] op_sel_hi:[1,0]
	v_pk_mul_f32 v[60:61], v[60:61], v[44:45]
	v_pk_mul_f32 v[62:63], v[62:63], v[46:47]
	v_cvt_pk_f16_f32 v60, v60, v61
	v_cvt_pk_f16_f32 v61, v62, v63
	global_store_dwordx2 v212, v[60:61], s[22:23] offset:1024
	v_pk_mul_f32 v[64:65], v[64:65], v[210:211] op_sel_hi:[1,0]
	v_pk_mul_f32 v[66:67], v[66:67], v[210:211] op_sel_hi:[1,0]
	v_pk_mul_f32 v[64:65], v[64:65], v[48:49]
	v_pk_mul_f32 v[66:67], v[66:67], v[50:51]
	v_cvt_pk_f16_f32 v64, v64, v65
	v_cvt_pk_f16_f32 v65, v66, v67
	global_store_dwordx2 v212, v[64:65], s[22:23] offset:2048
	v_pk_mul_f32 v[68:69], v[68:69], v[210:211] op_sel_hi:[1,0]
	v_pk_mul_f32 v[70:71], v[70:71], v[210:211] op_sel_hi:[1,0]
	v_pk_mul_f32 v[68:69], v[68:69], v[52:53]
	v_pk_mul_f32 v[70:71], v[70:71], v[54:55]
	v_cvt_pk_f16_f32 v68, v68, v69
	v_cvt_pk_f16_f32 v69, v70, v71
	global_store_dwordx2 v212, v[68:69], s[22:23] offset:3072
	v_pk_add_f32 v[72:73], v[72:73], v[24:25]
	v_pk_add_f32 v[74:75], v[74:75], v[26:27]
	v_pk_add_f32 v[76:77], v[76:77], v[28:29]
	v_pk_add_f32 v[78:79], v[78:79], v[30:31]
	v_pk_add_f32 v[80:81], v[80:81], v[32:33]
	v_pk_add_f32 v[82:83], v[82:83], v[34:35]
	v_pk_add_f32 v[84:85], v[84:85], v[36:37]
	v_pk_add_f32 v[86:87], v[86:87], v[38:39]
	v_pk_mul_f32 v[208:209], v[72:73], v[72:73]
	v_pk_fma_f32 v[208:209], v[74:75], v[74:75], v[208:209]
	v_pk_fma_f32 v[208:209], v[76:77], v[76:77], v[208:209]
	v_pk_fma_f32 v[208:209], v[78:79], v[78:79], v[208:209]
	v_pk_fma_f32 v[208:209], v[80:81], v[80:81], v[208:209]
	v_pk_fma_f32 v[208:209], v[82:83], v[82:83], v[208:209]
	v_pk_fma_f32 v[208:209], v[84:85], v[84:85], v[208:209]
	v_pk_fma_f32 v[208:209], v[86:87], v[86:87], v[208:209]
	v_add_f32_e32 v208, v208, v209
	v_mov_b32_e32 v209, v208
	s_nop 1
	v_permlane16_swap_b32_e32 v208, v209
	v_add_f32_e32 v208, v208, v209
	v_mov_b32_e32 v209, v208
	s_nop 1
	v_permlane32_swap_b32_e32 v208, v209
	v_add_f32_e32 v208, v208, v209
	v_mov_b32_e32 v210, 0x358637bd
	v_fmac_f32_e32 v210, 0x3c800000, v208
	v_rsq_f32_e32 v210, v210
	s_add_u32 s24, s29, 1
	s_lshr_b32 s8, s24, 1
	s_lshl_b32 s8, s8, 12
	s_and_b32 s24, s24, 1
	s_lshl_b32 s24, s24, 8
	s_add_u32 s8, s8, s24
	v_mul_f32_e32 v210, v213, v210
	v_add_u32_e32 v212, s8, v23
	v_pk_mul_f32 v[72:73], v[72:73], v[210:211] op_sel_hi:[1,0]
	v_pk_mul_f32 v[74:75], v[74:75], v[210:211] op_sel_hi:[1,0]
	v_pk_mul_f32 v[72:73], v[72:73], v[40:41]
	v_pk_mul_f32 v[74:75], v[74:75], v[42:43]
	v_cvt_pk_f16_f32 v72, v72, v73
	v_cvt_pk_f16_f32 v73, v74, v75
	global_store_dwordx2 v212, v[72:73], s[22:23] offset:0
	v_pk_mul_f32 v[76:77], v[76:77], v[210:211] op_sel_hi:[1,0]
	v_pk_mul_f32 v[78:79], v[78:79], v[210:211] op_sel_hi:[1,0]
	v_pk_mul_f32 v[76:77], v[76:77], v[44:45]
	v_pk_mul_f32 v[78:79], v[78:79], v[46:47]
	v_cvt_pk_f16_f32 v76, v76, v77
	v_cvt_pk_f16_f32 v77, v78, v79
	global_store_dwordx2 v212, v[76:77], s[22:23] offset:1024
	v_pk_mul_f32 v[80:81], v[80:81], v[210:211] op_sel_hi:[1,0]
	v_pk_mul_f32 v[82:83], v[82:83], v[210:211] op_sel_hi:[1,0]
	v_pk_mul_f32 v[80:81], v[80:81], v[48:49]
	v_pk_mul_f32 v[82:83], v[82:83], v[50:51]
	v_cvt_pk_f16_f32 v80, v80, v81
	v_cvt_pk_f16_f32 v81, v82, v83
	global_store_dwordx2 v212, v[80:81], s[22:23] offset:2048
	v_pk_mul_f32 v[84:85], v[84:85], v[210:211] op_sel_hi:[1,0]
	v_pk_mul_f32 v[86:87], v[86:87], v[210:211] op_sel_hi:[1,0]
	v_pk_mul_f32 v[84:85], v[84:85], v[52:53]
	v_pk_mul_f32 v[86:87], v[86:87], v[54:55]
	v_cvt_pk_f16_f32 v84, v84, v85
	v_cvt_pk_f16_f32 v85, v86, v87
	global_store_dwordx2 v212, v[84:85], s[22:23] offset:3072
	v_pk_add_f32 v[88:89], v[88:89], v[24:25]
	v_pk_add_f32 v[90:91], v[90:91], v[26:27]
	v_pk_add_f32 v[92:93], v[92:93], v[28:29]
	v_pk_add_f32 v[94:95], v[94:95], v[30:31]
	v_pk_add_f32 v[96:97], v[96:97], v[32:33]
	v_pk_add_f32 v[98:99], v[98:99], v[34:35]
	v_pk_add_f32 v[100:101], v[100:101], v[36:37]
	v_pk_add_f32 v[102:103], v[102:103], v[38:39]
	v_pk_mul_f32 v[208:209], v[88:89], v[88:89]
	v_pk_fma_f32 v[208:209], v[90:91], v[90:91], v[208:209]
	v_pk_fma_f32 v[208:209], v[92:93], v[92:93], v[208:209]
	v_pk_fma_f32 v[208:209], v[94:95], v[94:95], v[208:209]
	v_pk_fma_f32 v[208:209], v[96:97], v[96:97], v[208:209]
	v_pk_fma_f32 v[208:209], v[98:99], v[98:99], v[208:209]
	v_pk_fma_f32 v[208:209], v[100:101], v[100:101], v[208:209]
	v_pk_fma_f32 v[208:209], v[102:103], v[102:103], v[208:209]
	v_add_f32_e32 v208, v208, v209
	v_mov_b32_e32 v209, v208
	s_nop 1
	v_permlane16_swap_b32_e32 v208, v209
	v_add_f32_e32 v208, v208, v209
	v_mov_b32_e32 v209, v208
	s_nop 1
	v_permlane32_swap_b32_e32 v208, v209
	v_add_f32_e32 v208, v208, v209
	v_mov_b32_e32 v210, 0x358637bd
	v_fmac_f32_e32 v210, 0x3c800000, v208
	v_rsq_f32_e32 v210, v210
	s_add_u32 s24, s29, 2
	s_lshr_b32 s8, s24, 1
	s_lshl_b32 s8, s8, 12
	s_and_b32 s24, s24, 1
	s_lshl_b32 s24, s24, 8
	s_add_u32 s8, s8, s24
	v_mul_f32_e32 v210, v213, v210
	v_add_u32_e32 v212, s8, v23
	v_pk_mul_f32 v[88:89], v[88:89], v[210:211] op_sel_hi:[1,0]
	v_pk_mul_f32 v[90:91], v[90:91], v[210:211] op_sel_hi:[1,0]
	v_pk_mul_f32 v[88:89], v[88:89], v[40:41]
	v_pk_mul_f32 v[90:91], v[90:91], v[42:43]
	v_cvt_pk_f16_f32 v88, v88, v89
	v_cvt_pk_f16_f32 v89, v90, v91
	global_store_dwordx2 v212, v[88:89], s[22:23] offset:0
	v_pk_mul_f32 v[92:93], v[92:93], v[210:211] op_sel_hi:[1,0]
	v_pk_mul_f32 v[94:95], v[94:95], v[210:211] op_sel_hi:[1,0]
	v_pk_mul_f32 v[92:93], v[92:93], v[44:45]
	v_pk_mul_f32 v[94:95], v[94:95], v[46:47]
	v_cvt_pk_f16_f32 v92, v92, v93
	v_cvt_pk_f16_f32 v93, v94, v95
	global_store_dwordx2 v212, v[92:93], s[22:23] offset:1024
	v_pk_mul_f32 v[96:97], v[96:97], v[210:211] op_sel_hi:[1,0]
	v_pk_mul_f32 v[98:99], v[98:99], v[210:211] op_sel_hi:[1,0]
	v_pk_mul_f32 v[96:97], v[96:97], v[48:49]
	v_pk_mul_f32 v[98:99], v[98:99], v[50:51]
	v_cvt_pk_f16_f32 v96, v96, v97
	v_cvt_pk_f16_f32 v97, v98, v99
	global_store_dwordx2 v212, v[96:97], s[22:23] offset:2048
	v_pk_mul_f32 v[100:101], v[100:101], v[210:211] op_sel_hi:[1,0]
	v_pk_mul_f32 v[102:103], v[102:103], v[210:211] op_sel_hi:[1,0]
	v_pk_mul_f32 v[100:101], v[100:101], v[52:53]
	v_pk_mul_f32 v[102:103], v[102:103], v[54:55]
	v_cvt_pk_f16_f32 v100, v100, v101
	v_cvt_pk_f16_f32 v101, v102, v103
	global_store_dwordx2 v212, v[100:101], s[22:23] offset:3072
	v_pk_add_f32 v[104:105], v[104:105], v[24:25]
	v_pk_add_f32 v[106:107], v[106:107], v[26:27]
	v_pk_add_f32 v[108:109], v[108:109], v[28:29]
	v_pk_add_f32 v[110:111], v[110:111], v[30:31]
	v_pk_add_f32 v[112:113], v[112:113], v[32:33]
	v_pk_add_f32 v[114:115], v[114:115], v[34:35]
	v_pk_add_f32 v[116:117], v[116:117], v[36:37]
	v_pk_add_f32 v[118:119], v[118:119], v[38:39]
	v_pk_mul_f32 v[208:209], v[104:105], v[104:105]
	v_pk_fma_f32 v[208:209], v[106:107], v[106:107], v[208:209]
	v_pk_fma_f32 v[208:209], v[108:109], v[108:109], v[208:209]
	v_pk_fma_f32 v[208:209], v[110:111], v[110:111], v[208:209]
	v_pk_fma_f32 v[208:209], v[112:113], v[112:113], v[208:209]
	v_pk_fma_f32 v[208:209], v[114:115], v[114:115], v[208:209]
	v_pk_fma_f32 v[208:209], v[116:117], v[116:117], v[208:209]
	v_pk_fma_f32 v[208:209], v[118:119], v[118:119], v[208:209]
	v_add_f32_e32 v208, v208, v209
	v_mov_b32_e32 v209, v208
	s_nop 1
	v_permlane16_swap_b32_e32 v208, v209
	v_add_f32_e32 v208, v208, v209
	v_mov_b32_e32 v209, v208
	s_nop 1
	v_permlane32_swap_b32_e32 v208, v209
	v_add_f32_e32 v208, v208, v209
	v_mov_b32_e32 v210, 0x358637bd
	v_fmac_f32_e32 v210, 0x3c800000, v208
	v_rsq_f32_e32 v210, v210
	s_add_u32 s24, s29, 3
	s_lshr_b32 s8, s24, 1
	s_lshl_b32 s8, s8, 12
	s_and_b32 s24, s24, 1
	s_lshl_b32 s24, s24, 8
	s_add_u32 s8, s8, s24
	v_mul_f32_e32 v210, v213, v210
	v_add_u32_e32 v212, s8, v23
	v_pk_mul_f32 v[104:105], v[104:105], v[210:211] op_sel_hi:[1,0]
	v_pk_mul_f32 v[106:107], v[106:107], v[210:211] op_sel_hi:[1,0]
	v_pk_mul_f32 v[104:105], v[104:105], v[40:41]
	v_pk_mul_f32 v[106:107], v[106:107], v[42:43]
	v_cvt_pk_f16_f32 v104, v104, v105
	v_cvt_pk_f16_f32 v105, v106, v107
	global_store_dwordx2 v212, v[104:105], s[22:23] offset:0
	v_pk_mul_f32 v[108:109], v[108:109], v[210:211] op_sel_hi:[1,0]
	v_pk_mul_f32 v[110:111], v[110:111], v[210:211] op_sel_hi:[1,0]
	v_pk_mul_f32 v[108:109], v[108:109], v[44:45]
	v_pk_mul_f32 v[110:111], v[110:111], v[46:47]
	v_cvt_pk_f16_f32 v108, v108, v109
	v_cvt_pk_f16_f32 v109, v110, v111
	global_store_dwordx2 v212, v[108:109], s[22:23] offset:1024
	v_pk_mul_f32 v[112:113], v[112:113], v[210:211] op_sel_hi:[1,0]
	v_pk_mul_f32 v[114:115], v[114:115], v[210:211] op_sel_hi:[1,0]
	v_pk_mul_f32 v[112:113], v[112:113], v[48:49]
	v_pk_mul_f32 v[114:115], v[114:115], v[50:51]
	v_cvt_pk_f16_f32 v112, v112, v113
	v_cvt_pk_f16_f32 v113, v114, v115
	global_store_dwordx2 v212, v[112:113], s[22:23] offset:2048
	v_pk_mul_f32 v[116:117], v[116:117], v[210:211] op_sel_hi:[1,0]
	v_pk_mul_f32 v[118:119], v[118:119], v[210:211] op_sel_hi:[1,0]
	v_pk_mul_f32 v[116:117], v[116:117], v[52:53]
	v_pk_mul_f32 v[118:119], v[118:119], v[54:55]
	v_cvt_pk_f16_f32 v116, v116, v117
	v_cvt_pk_f16_f32 v117, v118, v119
	global_store_dwordx2 v212, v[116:117], s[22:23] offset:3072
	v_pk_add_f32 v[120:121], v[120:121], v[24:25]
	v_pk_add_f32 v[122:123], v[122:123], v[26:27]
	v_pk_add_f32 v[124:125], v[124:125], v[28:29]
	v_pk_add_f32 v[126:127], v[126:127], v[30:31]
	v_pk_add_f32 v[128:129], v[128:129], v[32:33]
	v_pk_add_f32 v[130:131], v[130:131], v[34:35]
	v_pk_add_f32 v[132:133], v[132:133], v[36:37]
	v_pk_add_f32 v[134:135], v[134:135], v[38:39]
	v_pk_mul_f32 v[208:209], v[120:121], v[120:121]
	v_pk_fma_f32 v[208:209], v[122:123], v[122:123], v[208:209]
	v_pk_fma_f32 v[208:209], v[124:125], v[124:125], v[208:209]
	v_pk_fma_f32 v[208:209], v[126:127], v[126:127], v[208:209]
	v_pk_fma_f32 v[208:209], v[128:129], v[128:129], v[208:209]
	v_pk_fma_f32 v[208:209], v[130:131], v[130:131], v[208:209]
	v_pk_fma_f32 v[208:209], v[132:133], v[132:133], v[208:209]
	v_pk_fma_f32 v[208:209], v[134:135], v[134:135], v[208:209]
	v_add_f32_e32 v208, v208, v209
	v_mov_b32_e32 v209, v208
	s_nop 1
	v_permlane16_swap_b32_e32 v208, v209
	v_add_f32_e32 v208, v208, v209
	v_mov_b32_e32 v209, v208
	s_nop 1
	v_permlane32_swap_b32_e32 v208, v209
	v_add_f32_e32 v208, v208, v209
	v_mov_b32_e32 v210, 0x358637bd
	v_fmac_f32_e32 v210, 0x3c800000, v208
	v_rsq_f32_e32 v210, v210
	s_add_u32 s24, s29, 4
	s_lshr_b32 s8, s24, 1
	s_lshl_b32 s8, s8, 12
	s_and_b32 s24, s24, 1
	s_lshl_b32 s24, s24, 8
	s_add_u32 s8, s8, s24
	v_mul_f32_e32 v210, v213, v210
	v_add_u32_e32 v212, s8, v23
	v_pk_mul_f32 v[120:121], v[120:121], v[210:211] op_sel_hi:[1,0]
	v_pk_mul_f32 v[122:123], v[122:123], v[210:211] op_sel_hi:[1,0]
	v_pk_mul_f32 v[120:121], v[120:121], v[40:41]
	v_pk_mul_f32 v[122:123], v[122:123], v[42:43]
	v_cvt_pk_f16_f32 v120, v120, v121
	v_cvt_pk_f16_f32 v121, v122, v123
	global_store_dwordx2 v212, v[120:121], s[22:23] offset:0
	v_pk_mul_f32 v[124:125], v[124:125], v[210:211] op_sel_hi:[1,0]
	v_pk_mul_f32 v[126:127], v[126:127], v[210:211] op_sel_hi:[1,0]
	v_pk_mul_f32 v[124:125], v[124:125], v[44:45]
	v_pk_mul_f32 v[126:127], v[126:127], v[46:47]
	v_cvt_pk_f16_f32 v124, v124, v125
	v_cvt_pk_f16_f32 v125, v126, v127
	global_store_dwordx2 v212, v[124:125], s[22:23] offset:1024
	v_pk_mul_f32 v[128:129], v[128:129], v[210:211] op_sel_hi:[1,0]
	v_pk_mul_f32 v[130:131], v[130:131], v[210:211] op_sel_hi:[1,0]
	v_pk_mul_f32 v[128:129], v[128:129], v[48:49]
	v_pk_mul_f32 v[130:131], v[130:131], v[50:51]
	v_cvt_pk_f16_f32 v128, v128, v129
	v_cvt_pk_f16_f32 v129, v130, v131
	global_store_dwordx2 v212, v[128:129], s[22:23] offset:2048
	v_pk_mul_f32 v[132:133], v[132:133], v[210:211] op_sel_hi:[1,0]
	v_pk_mul_f32 v[134:135], v[134:135], v[210:211] op_sel_hi:[1,0]
	v_pk_mul_f32 v[132:133], v[132:133], v[52:53]
	v_pk_mul_f32 v[134:135], v[134:135], v[54:55]
	v_cvt_pk_f16_f32 v132, v132, v133
	v_cvt_pk_f16_f32 v133, v134, v135
	global_store_dwordx2 v212, v[132:133], s[22:23] offset:3072
	s_branch .Lpf_done
.Lpf_vKB:
	s_lshl_b32 s25, s25, 6
	s_add_u32 s25, s25, 32
	s_add_u32 s29, s10, s25
	s_lshr_b32 s29, s29, 4
	v_add_u32_e32 v5, s25, v3
	v_lshlrev_b32_e32 v5, 7, v5
	v_add_u32_e32 v15, v5, v6
	v_add_u32_e32 v16, v5, v7
	v_add_u32_e32 v5, 0x9000, v9
	v_add_u32_e32 v17, v5, v6
	v_add_u32_e32 v18, v5, v7
	v_add_u32_e32 v19, 0x1a000, v15
	v_add_u32_e32 v20, 0x1a000, v16
	v_add_u32_e32 v21, 0x1a000, v17
	v_add_u32_e32 v22, 0x1a000, v18
	v_lshlrev_b32_e32 v5, 4, v4
	global_load_dwordx4 v[24:27], v5, s[14:15] offset:0
	global_load_dwordx4 v[28:31], v5, s[14:15] offset:64
	global_load_dwordx4 v[32:35], v5, s[14:15] offset:128
	global_load_dwordx4 v[36:39], v5, s[14:15] offset:192
	global_load_dwordx4 v[40:43], v5, s[16:17] offset:0
	global_load_dwordx4 v[44:47], v5, s[16:17] offset:64
	global_load_dwordx4 v[48:51], v5, s[16:17] offset:128
	global_load_dwordx4 v[52:55], v5, s[16:17] offset:192
	s_add_u32 m0, s28, 0x0
	s_nop 0
	global_load_lds_dwordx4 v10, s[4:5]
	s_add_u32 m0, s28, 0x2000
	s_nop 0
	global_load_lds_dwordx4 v11, s[4:5]
	s_add_u32 m0, s28, 0x4000
	s_nop 0
	global_load_lds_dwordx4 v12, s[4:5]
	s_add_u32 m0, s28, 0x6000
	s_nop 0
	global_load_lds_dwordx4 v13, s[4:5]
	s_add_u32 s4, s4, s20
	s_addc_u32 s5, s5, 0
	s_add_u32 m0, s28, 0x9000
	s_nop 0
	global_load_lds_dwordx4 v10, s[6:7]
	s_add_u32 m0, s28, 0xb000
	s_nop 0
	global_load_lds_dwordx4 v11, s[6:7]
	s_add_u32 s6, s6, s20
	s_addc_u32 s7, s7, 0
	s_add_u32 m0, s28, 0xd000
	s_nop 0
	global_load_lds_dwordx4 v10, s[4:5]
	s_add_u32 m0, s28, 0xf000
	s_nop 0
	global_load_lds_dwordx4 v11, s[4:5]
	s_add_u32 m0, s28, 0x11000
	s_nop 0
	global_load_lds_dwordx4 v12, s[4:5]
	s_add_u32 m0, s28, 0x13000
	s_nop 0
	global_load_lds_dwordx4 v13, s[4:5]
	s_add_u32 s4, s4, s20
	s_addc_u32 s5, s5, 0
	s_add_u32 m0, s28, 0x16000
	s_nop 0
	global_load_lds_dwordx4 v10, s[6:7]
	s_add_u32 m0, s28, 0x18000
	s_nop 0
	global_load_lds_dwordx4 v11, s[6:7]
	s_add_u32 s6, s6, s20
	s_addc_u32 s7, s7, 0
	s_add_u32 m0, s28, 0x1a000
	s_nop 0
	global_load_lds_dwordx4 v10, s[4:5]
	s_add_u32 m0, s28, 0x1c000
	s_nop 0
	global_load_lds_dwordx4 v11, s[4:5]
	s_add_u32 m0, s28, 0x1e000
	s_nop 0
	global_load_lds_dwordx4 v12, s[4:5]
	s_add_u32 m0, s28, 0x20000
	s_nop 0
	global_load_lds_dwordx4 v13, s[4:5]
	s_add_u32 s4, s4, s20
	s_addc_u32 s5, s5, 0
	s_add_u32 m0, s28, 0x23000
	s_nop 0
	global_load_lds_dwordx4 v10, s[6:7]
	s_add_u32 m0, s28, 0x25000
	s_nop 0
	global_load_lds_dwordx4 v11, s[6:7]
	s_add_u32 s6, s6, s20
	s_addc_u32 s7, s7, 0
	s_waitcnt vmcnt(12) lgkmcnt(0)
	s_barrier
	s_waitcnt lgkmcnt(7)
	ds_read_b128 v[136:139], v15
	ds_read_b128 v[156:159], v17
	ds_read_b128 v[160:163], v17 offset:2048
	ds_read_b128 v[164:167], v17 offset:4096
	ds_read_b128 v[168:171], v17 offset:6144
	ds_read_b128 v[140:143], v15 offset:2048
	ds_read_b128 v[144:147], v15 offset:4096
	ds_read_b128 v[148:151], v15 offset:6144
	s_waitcnt lgkmcnt(7)
	ds_read_b128 v[172:175], v16
	ds_read_b128 v[192:195], v18
	ds_read_b128 v[196:199], v18 offset:2048
	ds_read_b128 v[200:203], v18 offset:4096
	ds_read_b128 v[204:207], v18 offset:6144
	ds_read_b128 v[176:179], v16 offset:2048
	ds_read_b128 v[180:183], v16 offset:4096
	ds_read_b128 v[184:187], v16 offset:6144
	s_waitcnt lgkmcnt(14)
	v_mfma_f32_16x16x32_f16 v[56:59], v[156:159], v[136:139], 0
	s_waitcnt lgkmcnt(13)
	v_mfma_f32_16x16x32_f16 v[60:63], v[160:163], v[136:139], 0
	s_waitcnt lgkmcnt(12)
	v_mfma_f32_16x16x32_f16 v[64:67], v[164:167], v[136:139], 0
	s_waitcnt lgkmcnt(11)
	v_mfma_f32_16x16x32_f16 v[68:71], v[168:171], v[136:139], 0
	s_waitcnt lgkmcnt(10)
	v_mfma_f32_16x16x32_f16 v[72:75], v[156:159], v[140:143], 0
	v_mfma_f32_16x16x32_f16 v[76:79], v[160:163], v[140:143], 0
	v_mfma_f32_16x16x32_f16 v[80:83], v[164:167], v[140:143], 0
	v_mfma_f32_16x16x32_f16 v[84:87], v[168:171], v[140:143], 0
	s_waitcnt lgkmcnt(9)
	v_mfma_f32_16x16x32_f16 v[88:91], v[156:159], v[144:147], 0
	v_mfma_f32_16x16x32_f16 v[92:95], v[160:163], v[144:147], 0
	v_mfma_f32_16x16x32_f16 v[96:99], v[164:167], v[144:147], 0
	v_mfma_f32_16x16x32_f16 v[100:103], v[168:171], v[144:147], 0
	s_waitcnt lgkmcnt(8)
	v_mfma_f32_16x16x32_f16 v[104:107], v[156:159], v[148:151], 0
	v_mfma_f32_16x16x32_f16 v[108:111], v[160:163], v[148:151], 0
	v_mfma_f32_16x16x32_f16 v[112:115], v[164:167], v[148:151], 0
	v_mfma_f32_16x16x32_f16 v[116:119], v[168:171], v[148:151], 0
	s_waitcnt vmcnt(6) lgkmcnt(0)
	s_barrier
	s_waitcnt lgkmcnt(7)
	ds_read_b128 v[136:139], v15 offset:53248
	ds_read_b128 v[156:159], v17 offset:53248
	ds_read_b128 v[160:163], v17 offset:55296
	ds_read_b128 v[164:167], v17 offset:57344
	ds_read_b128 v[168:171], v17 offset:59392
	ds_read_b128 v[140:143], v15 offset:55296
	ds_read_b128 v[144:147], v15 offset:57344
	ds_read_b128 v[148:151], v15 offset:59392
	s_waitcnt lgkmcnt(14)
	v_mfma_f32_16x16x32_f16 v[56:59], v[192:195], v[172:175], v[56:59]
	s_add_u32 m0, s28, 0x0
	s_nop 0
	global_load_lds_dwordx4 v10, s[4:5]
	s_waitcnt lgkmcnt(13)
	v_mfma_f32_16x16x32_f16 v[60:63], v[196:199], v[172:175], v[60:63]
	s_waitcnt lgkmcnt(12)
	v_mfma_f32_16x16x32_f16 v[64:67], v[200:203], v[172:175], v[64:67]
	s_waitcnt lgkmcnt(11)
	v_mfma_f32_16x16x32_f16 v[68:71], v[204:207], v[172:175], v[68:71]
	s_waitcnt lgkmcnt(10)
	v_mfma_f32_16x16x32_f16 v[72:75], v[192:195], v[176:179], v[72:75]
	v_mfma_f32_16x16x32_f16 v[76:79], v[196:199], v[176:179], v[76:79]
	s_add_u32 m0, s28, 0x2000
	s_nop 0
	global_load_lds_dwordx4 v11, s[4:5]
	v_mfma_f32_16x16x32_f16 v[80:83], v[200:203], v[176:179], v[80:83]
	v_mfma_f32_16x16x32_f16 v[84:87], v[204:207], v[176:179], v[84:87]
	s_waitcnt lgkmcnt(9)
	v_mfma_f32_16x16x32_f16 v[88:91], v[192:195], v[180:183], v[88:91]
	v_mfma_f32_16x16x32_f16 v[92:95], v[196:199], v[180:183], v[92:95]
	v_mfma_f32_16x16x32_f16 v[96:99], v[200:203], v[180:183], v[96:99]
	s_add_u32 m0, s28, 0x4000
	s_nop 0
	global_load_lds_dwordx4 v12, s[4:5]
	v_mfma_f32_16x16x32_f16 v[100:103], v[204:207], v[180:183], v[100:103]
	s_waitcnt lgkmcnt(8)
	v_mfma_f32_16x16x32_f16 v[104:107], v[192:195], v[184:187], v[104:107]
	v_mfma_f32_16x16x32_f16 v[108:111], v[196:199], v[184:187], v[108:111]
	v_mfma_f32_16x16x32_f16 v[112:115], v[200:203], v[184:187], v[112:115]
	v_mfma_f32_16x16x32_f16 v[116:119], v[204:207], v[184:187], v[116:119]
	s_waitcnt lgkmcnt(7)
	ds_read_b128 v[172:175], v16 offset:53248
	ds_read_b128 v[192:195], v18 offset:53248
	ds_read_b128 v[196:199], v18 offset:55296
	ds_read_b128 v[200:203], v18 offset:57344
	ds_read_b128 v[204:207], v18 offset:59392
	ds_read_b128 v[176:179], v16 offset:55296
	ds_read_b128 v[180:183], v16 offset:57344
	ds_read_b128 v[184:187], v16 offset:59392
	s_waitcnt lgkmcnt(14)
	v_mfma_f32_16x16x32_f16 v[56:59], v[156:159], v[136:139], v[56:59]
	s_add_u32 m0, s28, 0x6000
	s_nop 0
	global_load_lds_dwordx4 v13, s[4:5]
	s_add_u32 s4, s4, s20
	s_addc_u32 s5, s5, 0
	s_waitcnt lgkmcnt(13)
	v_mfma_f32_16x16x32_f16 v[60:63], v[160:163], v[136:139], v[60:63]
	s_waitcnt lgkmcnt(12)
	v_mfma_f32_16x16x32_f16 v[64:67], v[164:167], v[136:139], v[64:67]
	s_waitcnt lgkmcnt(11)
	v_mfma_f32_16x16x32_f16 v[68:71], v[168:171], v[136:139], v[68:71]
	s_waitcnt lgkmcnt(10)
	v_mfma_f32_16x16x32_f16 v[72:75], v[156:159], v[140:143], v[72:75]
	v_mfma_f32_16x16x32_f16 v[76:79], v[160:163], v[140:143], v[76:79]
	s_add_u32 m0, s28, 0x9000
	s_nop 0
	global_load_lds_dwordx4 v10, s[6:7]
	v_mfma_f32_16x16x32_f16 v[80:83], v[164:167], v[140:143], v[80:83]
	v_mfma_f32_16x16x32_f16 v[84:87], v[168:171], v[140:143], v[84:87]
	s_waitcnt lgkmcnt(9)
	v_mfma_f32_16x16x32_f16 v[88:91], v[156:159], v[144:147], v[88:91]
	v_mfma_f32_16x16x32_f16 v[92:95], v[160:163], v[144:147], v[92:95]
	v_mfma_f32_16x16x32_f16 v[96:99], v[164:167], v[144:147], v[96:99]
	s_add_u32 m0, s28, 0xb000
	s_nop 0
	global_load_lds_dwordx4 v11, s[6:7]
	s_add_u32 s6, s6, s20
	s_addc_u32 s7, s7, 0
	v_mfma_f32_16x16x32_f16 v[100:103], v[168:171], v[144:147], v[100:103]
	s_waitcnt lgkmcnt(8)
	v_mfma_f32_16x16x32_f16 v[104:107], v[156:159], v[148:151], v[104:107]
	v_mfma_f32_16x16x32_f16 v[108:111], v[160:163], v[148:151], v[108:111]
	v_mfma_f32_16x16x32_f16 v[112:115], v[164:167], v[148:151], v[112:115]
	v_mfma_f32_16x16x32_f16 v[116:119], v[168:171], v[148:151], v[116:119]
	s_waitcnt vmcnt(6) lgkmcnt(0)
	s_barrier
	s_waitcnt lgkmcnt(7)
	ds_read_b128 v[136:139], v19
	ds_read_b128 v[156:159], v21
	ds_read_b128 v[160:163], v21 offset:2048
	ds_read_b128 v[164:167], v21 offset:4096
	ds_read_b128 v[168:171], v21 offset:6144
	ds_read_b128 v[140:143], v19 offset:2048
	ds_read_b128 v[144:147], v19 offset:4096
	ds_read_b128 v[148:151], v19 offset:6144
	s_waitcnt lgkmcnt(14)
	v_mfma_f32_16x16x32_f16 v[56:59], v[192:195], v[172:175], v[56:59]
	s_add_u32 m0, s28, 0xd000
	s_nop 0
	global_load_lds_dwordx4 v10, s[4:5]
	s_waitcnt lgkmcnt(13)
	v_mfma_f32_16x16x32_f16 v[60:63], v[196:199], v[172:175], v[60:63]
	s_waitcnt lgkmcnt(12)
	v_mfma_f32_16x16x32_f16 v[64:67], v[200:203], v[172:175], v[64:67]
	s_waitcnt lgkmcnt(11)
	v_mfma_f32_16x16x32_f16 v[68:71], v[204:207], v[172:175], v[68:71]
	s_waitcnt lgkmcnt(10)
	v_mfma_f32_16x16x32_f16 v[72:75], v[192:195], v[176:179], v[72:75]
	v_mfma_f32_16x16x32_f16 v[76:79], v[196:199], v[176:179], v[76:79]
	s_add_u32 m0, s28, 0xf000
	s_nop 0
	global_load_lds_dwordx4 v11, s[4:5]
	v_mfma_f32_16x16x32_f16 v[80:83], v[200:203], v[176:179], v[80:83]
	v_mfma_f32_16x16x32_f16 v[84:87], v[204:207], v[176:179], v[84:87]
	s_waitcnt lgkmcnt(9)
	v_mfma_f32_16x16x32_f16 v[88:91], v[192:195], v[180:183], v[88:91]
	v_mfma_f32_16x16x32_f16 v[92:95], v[196:199], v[180:183], v[92:95]
	v_mfma_f32_16x16x32_f16 v[96:99], v[200:203], v[180:183], v[96:99]
	s_add_u32 m0, s28, 0x11000
	s_nop 0
	global_load_lds_dwordx4 v12, s[4:5]
	v_mfma_f32_16x16x32_f16 v[100:103], v[204:207], v[180:183], v[100:103]
	s_waitcnt lgkmcnt(8)
	v_mfma_f32_16x16x32_f16 v[104:107], v[192:195], v[184:187], v[104:107]
	v_mfma_f32_16x16x32_f16 v[108:111], v[196:199], v[184:187], v[108:111]
	v_mfma_f32_16x16x32_f16 v[112:115], v[200:203], v[184:187], v[112:115]
	v_mfma_f32_16x16x32_f16 v[116:119], v[204:207], v[184:187], v[116:119]
	s_waitcnt lgkmcnt(7)
	ds_read_b128 v[172:175], v20
	ds_read_b128 v[192:195], v22
	ds_read_b128 v[196:199], v22 offset:2048
	ds_read_b128 v[200:203], v22 offset:4096
	ds_read_b128 v[204:207], v22 offset:6144
	ds_read_b128 v[176:179], v20 offset:2048
	ds_read_b128 v[180:183], v20 offset:4096
	ds_read_b128 v[184:187], v20 offset:6144
	s_waitcnt lgkmcnt(14)
	v_mfma_f32_16x16x32_f16 v[56:59], v[156:159], v[136:139], v[56:59]
	s_add_u32 m0, s28, 0x13000
	s_nop 0
	global_load_lds_dwordx4 v13, s[4:5]
	s_add_u32 s4, s4, s20
	s_addc_u32 s5, s5, 0
	s_waitcnt lgkmcnt(13)
	v_mfma_f32_16x16x32_f16 v[60:63], v[160:163], v[136:139], v[60:63]
	s_waitcnt lgkmcnt(12)
	v_mfma_f32_16x16x32_f16 v[64:67], v[164:167], v[136:139], v[64:67]
	s_waitcnt lgkmcnt(11)
	v_mfma_f32_16x16x32_f16 v[68:71], v[168:171], v[136:139], v[68:71]
	s_waitcnt lgkmcnt(10)
	v_mfma_f32_16x16x32_f16 v[72:75], v[156:159], v[140:143], v[72:75]
	v_mfma_f32_16x16x32_f16 v[76:79], v[160:163], v[140:143], v[76:79]
	s_add_u32 m0, s28, 0x16000
	s_nop 0
	global_load_lds_dwordx4 v10, s[6:7]
	v_mfma_f32_16x16x32_f16 v[80:83], v[164:167], v[140:143], v[80:83]
	v_mfma_f32_16x16x32_f16 v[84:87], v[168:171], v[140:143], v[84:87]
	s_waitcnt lgkmcnt(9)
	v_mfma_f32_16x16x32_f16 v[88:91], v[156:159], v[144:147], v[88:91]
	v_mfma_f32_16x16x32_f16 v[92:95], v[160:163], v[144:147], v[92:95]
	v_mfma_f32_16x16x32_f16 v[96:99], v[164:167], v[144:147], v[96:99]
	s_add_u32 m0, s28, 0x18000
	s_nop 0
	global_load_lds_dwordx4 v11, s[6:7]
	s_add_u32 s6, s6, s20
	s_addc_u32 s7, s7, 0
	v_mfma_f32_16x16x32_f16 v[100:103], v[168:171], v[144:147], v[100:103]
	s_waitcnt lgkmcnt(8)
	v_mfma_f32_16x16x32_f16 v[104:107], v[156:159], v[148:151], v[104:107]
	v_mfma_f32_16x16x32_f16 v[108:111], v[160:163], v[148:151], v[108:111]
	v_mfma_f32_16x16x32_f16 v[112:115], v[164:167], v[148:151], v[112:115]
	v_mfma_f32_16x16x32_f16 v[116:119], v[168:171], v[148:151], v[116:119]
	s_waitcnt vmcnt(6) lgkmcnt(0)
	s_barrier
	s_waitcnt lgkmcnt(7)
	ds_read_b128 v[136:139], v15
	ds_read_b128 v[156:159], v17
	ds_read_b128 v[160:163], v17 offset:2048
	ds_read_b128 v[164:167], v17 offset:4096
	ds_read_b128 v[168:171], v17 offset:6144
	ds_read_b128 v[140:143], v15 offset:2048
	ds_read_b128 v[144:147], v15 offset:4096
	ds_read_b128 v[148:151], v15 offset:6144
	s_waitcnt lgkmcnt(14)
	v_mfma_f32_16x16x32_f16 v[56:59], v[192:195], v[172:175], v[56:59]
	s_add_u32 m0, s28, 0x1a000
	s_nop 0
	global_load_lds_dwordx4 v10, s[4:5]
	s_waitcnt lgkmcnt(13)
	v_mfma_f32_16x16x32_f16 v[60:63], v[196:199], v[172:175], v[60:63]
	s_waitcnt lgkmcnt(12)
	v_mfma_f32_16x16x32_f16 v[64:67], v[200:203], v[172:175], v[64:67]
	s_waitcnt lgkmcnt(11)
	v_mfma_f32_16x16x32_f16 v[68:71], v[204:207], v[172:175], v[68:71]
	s_waitcnt lgkmcnt(10)
	v_mfma_f32_16x16x32_f16 v[72:75], v[192:195], v[176:179], v[72:75]
	v_mfma_f32_16x16x32_f16 v[76:79], v[196:199], v[176:179], v[76:79]
	s_add_u32 m0, s28, 0x1c000
	s_nop 0
	global_load_lds_dwordx4 v11, s[4:5]
	v_mfma_f32_16x16x32_f16 v[80:83], v[200:203], v[176:179], v[80:83]
	v_mfma_f32_16x16x32_f16 v[84:87], v[204:207], v[176:179], v[84:87]
	s_waitcnt lgkmcnt(9)
	v_mfma_f32_16x16x32_f16 v[88:91], v[192:195], v[180:183], v[88:91]
	v_mfma_f32_16x16x32_f16 v[92:95], v[196:199], v[180:183], v[92:95]
	v_mfma_f32_16x16x32_f16 v[96:99], v[200:203], v[180:183], v[96:99]
	s_add_u32 m0, s28, 0x1e000
	s_nop 0
	global_load_lds_dwordx4 v12, s[4:5]
	v_mfma_f32_16x16x32_f16 v[100:103], v[204:207], v[180:183], v[100:103]
	s_waitcnt lgkmcnt(8)
	v_mfma_f32_16x16x32_f16 v[104:107], v[192:195], v[184:187], v[104:107]
	v_mfma_f32_16x16x32_f16 v[108:111], v[196:199], v[184:187], v[108:111]
	v_mfma_f32_16x16x32_f16 v[112:115], v[200:203], v[184:187], v[112:115]
	v_mfma_f32_16x16x32_f16 v[116:119], v[204:207], v[184:187], v[116:119]
	s_waitcnt lgkmcnt(7)
	ds_read_b128 v[172:175], v16
	ds_read_b128 v[192:195], v18
	ds_read_b128 v[196:199], v18 offset:2048
	ds_read_b128 v[200:203], v18 offset:4096
	ds_read_b128 v[204:207], v18 offset:6144
	ds_read_b128 v[176:179], v16 offset:2048
	ds_read_b128 v[180:183], v16 offset:4096
	ds_read_b128 v[184:187], v16 offset:6144
	s_waitcnt lgkmcnt(14)
	v_mfma_f32_16x16x32_f16 v[56:59], v[156:159], v[136:139], v[56:59]
	s_add_u32 m0, s28, 0x20000
	s_nop 0
	global_load_lds_dwordx4 v13, s[4:5]
	s_add_u32 s4, s4, s20
	s_addc_u32 s5, s5, 0
	s_waitcnt lgkmcnt(13)
	v_mfma_f32_16x16x32_f16 v[60:63], v[160:163], v[136:139], v[60:63]
	s_waitcnt lgkmcnt(12)
	v_mfma_f32_16x16x32_f16 v[64:67], v[164:167], v[136:139], v[64:67]
	s_waitcnt lgkmcnt(11)
	v_mfma_f32_16x16x32_f16 v[68:71], v[168:171], v[136:139], v[68:71]
	s_waitcnt lgkmcnt(10)
	v_mfma_f32_16x16x32_f16 v[72:75], v[156:159], v[140:143], v[72:75]
	v_mfma_f32_16x16x32_f16 v[76:79], v[160:163], v[140:143], v[76:79]
	s_add_u32 m0, s28, 0x23000
	s_nop 0
	global_load_lds_dwordx4 v10, s[6:7]
	v_mfma_f32_16x16x32_f16 v[80:83], v[164:167], v[140:143], v[80:83]
	v_mfma_f32_16x16x32_f16 v[84:87], v[168:171], v[140:143], v[84:87]
	s_waitcnt lgkmcnt(9)
	v_mfma_f32_16x16x32_f16 v[88:91], v[156:159], v[144:147], v[88:91]
	v_mfma_f32_16x16x32_f16 v[92:95], v[160:163], v[144:147], v[92:95]
	v_mfma_f32_16x16x32_f16 v[96:99], v[164:167], v[144:147], v[96:99]
	s_add_u32 m0, s28, 0x25000
	s_nop 0
	global_load_lds_dwordx4 v11, s[6:7]
	s_add_u32 s6, s6, s20
	s_addc_u32 s7, s7, 0
	v_mfma_f32_16x16x32_f16 v[100:103], v[168:171], v[144:147], v[100:103]
	s_waitcnt lgkmcnt(8)
	v_mfma_f32_16x16x32_f16 v[104:107], v[156:159], v[148:151], v[104:107]
	v_mfma_f32_16x16x32_f16 v[108:111], v[160:163], v[148:151], v[108:111]
	v_mfma_f32_16x16x32_f16 v[112:115], v[164:167], v[148:151], v[112:115]
	v_mfma_f32_16x16x32_f16 v[116:119], v[168:171], v[148:151], v[116:119]
	s_waitcnt vmcnt(6) lgkmcnt(0)
	s_barrier
	s_waitcnt lgkmcnt(7)
	ds_read_b128 v[136:139], v15 offset:53248
	ds_read_b128 v[156:159], v17 offset:53248
	ds_read_b128 v[160:163], v17 offset:55296
	ds_read_b128 v[164:167], v17 offset:57344
	ds_read_b128 v[168:171], v17 offset:59392
	ds_read_b128 v[140:143], v15 offset:55296
	ds_read_b128 v[144:147], v15 offset:57344
	ds_read_b128 v[148:151], v15 offset:59392
	s_waitcnt lgkmcnt(14)
	v_mfma_f32_16x16x32_f16 v[56:59], v[192:195], v[172:175], v[56:59]
	s_add_u32 m0, s28, 0x0
	s_nop 0
	global_load_lds_dwordx4 v10, s[4:5]
	s_waitcnt lgkmcnt(13)
	v_mfma_f32_16x16x32_f16 v[60:63], v[196:199], v[172:175], v[60:63]
	s_waitcnt lgkmcnt(12)
	v_mfma_f32_16x16x32_f16 v[64:67], v[200:203], v[172:175], v[64:67]
	s_waitcnt lgkmcnt(11)
	v_mfma_f32_16x16x32_f16 v[68:71], v[204:207], v[172:175], v[68:71]
	s_waitcnt lgkmcnt(10)
	v_mfma_f32_16x16x32_f16 v[72:75], v[192:195], v[176:179], v[72:75]
	v_mfma_f32_16x16x32_f16 v[76:79], v[196:199], v[176:179], v[76:79]
	s_add_u32 m0, s28, 0x2000
	s_nop 0
	global_load_lds_dwordx4 v11, s[4:5]
	v_mfma_f32_16x16x32_f16 v[80:83], v[200:203], v[176:179], v[80:83]
	v_mfma_f32_16x16x32_f16 v[84:87], v[204:207], v[176:179], v[84:87]
	s_waitcnt lgkmcnt(9)
	v_mfma_f32_16x16x32_f16 v[88:91], v[192:195], v[180:183], v[88:91]
	v_mfma_f32_16x16x32_f16 v[92:95], v[196:199], v[180:183], v[92:95]
	v_mfma_f32_16x16x32_f16 v[96:99], v[200:203], v[180:183], v[96:99]
	s_add_u32 m0, s28, 0x4000
	s_nop 0
	global_load_lds_dwordx4 v12, s[4:5]
	v_mfma_f32_16x16x32_f16 v[100:103], v[204:207], v[180:183], v[100:103]
	s_waitcnt lgkmcnt(8)
	v_mfma_f32_16x16x32_f16 v[104:107], v[192:195], v[184:187], v[104:107]
	v_mfma_f32_16x16x32_f16 v[108:111], v[196:199], v[184:187], v[108:111]
	v_mfma_f32_16x16x32_f16 v[112:115], v[200:203], v[184:187], v[112:115]
	v_mfma_f32_16x16x32_f16 v[116:119], v[204:207], v[184:187], v[116:119]
	s_waitcnt lgkmcnt(7)
	ds_read_b128 v[172:175], v16 offset:53248
	ds_read_b128 v[192:195], v18 offset:53248
	ds_read_b128 v[196:199], v18 offset:55296
	ds_read_b128 v[200:203], v18 offset:57344
	ds_read_b128 v[204:207], v18 offset:59392
	ds_read_b128 v[176:179], v16 offset:55296
	ds_read_b128 v[180:183], v16 offset:57344
	ds_read_b128 v[184:187], v16 offset:59392
	s_waitcnt lgkmcnt(14)
	v_mfma_f32_16x16x32_f16 v[56:59], v[156:159], v[136:139], v[56:59]
	s_add_u32 m0, s28, 0x6000
	s_nop 0
	global_load_lds_dwordx4 v13, s[4:5]
	s_add_u32 s4, s4, s20
	s_addc_u32 s5, s5, 0
	s_waitcnt lgkmcnt(13)
	v_mfma_f32_16x16x32_f16 v[60:63], v[160:163], v[136:139], v[60:63]
	s_waitcnt lgkmcnt(12)
	v_mfma_f32_16x16x32_f16 v[64:67], v[164:167], v[136:139], v[64:67]
	s_waitcnt lgkmcnt(11)
	v_mfma_f32_16x16x32_f16 v[68:71], v[168:171], v[136:139], v[68:71]
	s_waitcnt lgkmcnt(10)
	v_mfma_f32_16x16x32_f16 v[72:75], v[156:159], v[140:143], v[72:75]
	v_mfma_f32_16x16x32_f16 v[76:79], v[160:163], v[140:143], v[76:79]
	s_add_u32 m0, s28, 0x9000
	s_nop 0
	global_load_lds_dwordx4 v10, s[6:7]
	v_mfma_f32_16x16x32_f16 v[80:83], v[164:167], v[140:143], v[80:83]
	v_mfma_f32_16x16x32_f16 v[84:87], v[168:171], v[140:143], v[84:87]
	s_waitcnt lgkmcnt(9)
	v_mfma_f32_16x16x32_f16 v[88:91], v[156:159], v[144:147], v[88:91]
	v_mfma_f32_16x16x32_f16 v[92:95], v[160:163], v[144:147], v[92:95]
	v_mfma_f32_16x16x32_f16 v[96:99], v[164:167], v[144:147], v[96:99]
	s_add_u32 m0, s28, 0xb000
	s_nop 0
	global_load_lds_dwordx4 v11, s[6:7]
	s_add_u32 s6, s6, s20
	s_addc_u32 s7, s7, 0
	v_mfma_f32_16x16x32_f16 v[100:103], v[168:171], v[144:147], v[100:103]
	s_waitcnt lgkmcnt(8)
	v_mfma_f32_16x16x32_f16 v[104:107], v[156:159], v[148:151], v[104:107]
	v_mfma_f32_16x16x32_f16 v[108:111], v[160:163], v[148:151], v[108:111]
	v_mfma_f32_16x16x32_f16 v[112:115], v[164:167], v[148:151], v[112:115]
	v_mfma_f32_16x16x32_f16 v[116:119], v[168:171], v[148:151], v[116:119]
	s_waitcnt vmcnt(6) lgkmcnt(0)
	s_barrier
	s_waitcnt lgkmcnt(7)
	ds_read_b128 v[136:139], v19
	ds_read_b128 v[156:159], v21
	ds_read_b128 v[160:163], v21 offset:2048
	ds_read_b128 v[164:167], v21 offset:4096
	ds_read_b128 v[168:171], v21 offset:6144
	ds_read_b128 v[140:143], v19 offset:2048
	ds_read_b128 v[144:147], v19 offset:4096
	ds_read_b128 v[148:151], v19 offset:6144
	s_waitcnt lgkmcnt(14)
	v_mfma_f32_16x16x32_f16 v[56:59], v[192:195], v[172:175], v[56:59]
	s_add_u32 m0, s28, 0xd000
	s_nop 0
	global_load_lds_dwordx4 v10, s[4:5]
	s_waitcnt lgkmcnt(13)
	v_mfma_f32_16x16x32_f16 v[60:63], v[196:199], v[172:175], v[60:63]
	s_waitcnt lgkmcnt(12)
	v_mfma_f32_16x16x32_f16 v[64:67], v[200:203], v[172:175], v[64:67]
	s_waitcnt lgkmcnt(11)
	v_mfma_f32_16x16x32_f16 v[68:71], v[204:207], v[172:175], v[68:71]
	s_waitcnt lgkmcnt(10)
	v_mfma_f32_16x16x32_f16 v[72:75], v[192:195], v[176:179], v[72:75]
	v_mfma_f32_16x16x32_f16 v[76:79], v[196:199], v[176:179], v[76:79]
	s_add_u32 m0, s28, 0xf000
	s_nop 0
	global_load_lds_dwordx4 v11, s[4:5]
	v_mfma_f32_16x16x32_f16 v[80:83], v[200:203], v[176:179], v[80:83]
	v_mfma_f32_16x16x32_f16 v[84:87], v[204:207], v[176:179], v[84:87]
	s_waitcnt lgkmcnt(9)
	v_mfma_f32_16x16x32_f16 v[88:91], v[192:195], v[180:183], v[88:91]
	v_mfma_f32_16x16x32_f16 v[92:95], v[196:199], v[180:183], v[92:95]
	v_mfma_f32_16x16x32_f16 v[96:99], v[200:203], v[180:183], v[96:99]
	s_add_u32 m0, s28, 0x11000
	s_nop 0
	global_load_lds_dwordx4 v12, s[4:5]
	v_mfma_f32_16x16x32_f16 v[100:103], v[204:207], v[180:183], v[100:103]
	s_waitcnt lgkmcnt(8)
	v_mfma_f32_16x16x32_f16 v[104:107], v[192:195], v[184:187], v[104:107]
	v_mfma_f32_16x16x32_f16 v[108:111], v[196:199], v[184:187], v[108:111]
	v_mfma_f32_16x16x32_f16 v[112:115], v[200:203], v[184:187], v[112:115]
	v_mfma_f32_16x16x32_f16 v[116:119], v[204:207], v[184:187], v[116:119]
	s_waitcnt lgkmcnt(7)
	ds_read_b128 v[172:175], v20
	ds_read_b128 v[192:195], v22
	ds_read_b128 v[196:199], v22 offset:2048
	ds_read_b128 v[200:203], v22 offset:4096
	ds_read_b128 v[204:207], v22 offset:6144
	ds_read_b128 v[176:179], v20 offset:2048
	ds_read_b128 v[180:183], v20 offset:4096
	ds_read_b128 v[184:187], v20 offset:6144
	s_waitcnt lgkmcnt(14)
	v_mfma_f32_16x16x32_f16 v[56:59], v[156:159], v[136:139], v[56:59]
	s_add_u32 m0, s28, 0x13000
	s_nop 0
	global_load_lds_dwordx4 v13, s[4:5]
	s_add_u32 s4, s4, s20
	s_addc_u32 s5, s5, 0
	s_waitcnt lgkmcnt(13)
	v_mfma_f32_16x16x32_f16 v[60:63], v[160:163], v[136:139], v[60:63]
	s_waitcnt lgkmcnt(12)
	v_mfma_f32_16x16x32_f16 v[64:67], v[164:167], v[136:139], v[64:67]
	s_waitcnt lgkmcnt(11)
	v_mfma_f32_16x16x32_f16 v[68:71], v[168:171], v[136:139], v[68:71]
	s_waitcnt lgkmcnt(10)
	v_mfma_f32_16x16x32_f16 v[72:75], v[156:159], v[140:143], v[72:75]
	v_mfma_f32_16x16x32_f16 v[76:79], v[160:163], v[140:143], v[76:79]
	s_add_u32 m0, s28, 0x16000
	s_nop 0
	global_load_lds_dwordx4 v10, s[6:7]
	v_mfma_f32_16x16x32_f16 v[80:83], v[164:167], v[140:143], v[80:83]
	v_mfma_f32_16x16x32_f16 v[84:87], v[168:171], v[140:143], v[84:87]
	s_waitcnt lgkmcnt(9)
	v_mfma_f32_16x16x32_f16 v[88:91], v[156:159], v[144:147], v[88:91]
	v_mfma_f32_16x16x32_f16 v[92:95], v[160:163], v[144:147], v[92:95]
	v_mfma_f32_16x16x32_f16 v[96:99], v[164:167], v[144:147], v[96:99]
	s_add_u32 m0, s28, 0x18000
	s_nop 0
	global_load_lds_dwordx4 v11, s[6:7]
	s_add_u32 s6, s6, s20
	s_addc_u32 s7, s7, 0
	v_mfma_f32_16x16x32_f16 v[100:103], v[168:171], v[144:147], v[100:103]
	s_waitcnt lgkmcnt(8)
	v_mfma_f32_16x16x32_f16 v[104:107], v[156:159], v[148:151], v[104:107]
	v_mfma_f32_16x16x32_f16 v[108:111], v[160:163], v[148:151], v[108:111]
	v_mfma_f32_16x16x32_f16 v[112:115], v[164:167], v[148:151], v[112:115]
	v_mfma_f32_16x16x32_f16 v[116:119], v[168:171], v[148:151], v[116:119]
	s_waitcnt vmcnt(6) lgkmcnt(0)
	s_barrier
	s_waitcnt lgkmcnt(7)
	ds_read_b128 v[136:139], v15
	ds_read_b128 v[156:159], v17
	ds_read_b128 v[160:163], v17 offset:2048
	ds_read_b128 v[164:167], v17 offset:4096
	ds_read_b128 v[168:171], v17 offset:6144
	ds_read_b128 v[140:143], v15 offset:2048
	ds_read_b128 v[144:147], v15 offset:4096
	ds_read_b128 v[148:151], v15 offset:6144
	s_waitcnt lgkmcnt(14)
	v_mfma_f32_16x16x32_f16 v[56:59], v[192:195], v[172:175], v[56:59]
	s_add_u32 m0, s28, 0x1a000
	s_nop 0
	global_load_lds_dwordx4 v10, s[4:5]
	s_waitcnt lgkmcnt(13)
	v_mfma_f32_16x16x32_f16 v[60:63], v[196:199], v[172:175], v[60:63]
	s_waitcnt lgkmcnt(12)
	v_mfma_f32_16x16x32_f16 v[64:67], v[200:203], v[172:175], v[64:67]
	s_waitcnt lgkmcnt(11)
	v_mfma_f32_16x16x32_f16 v[68:71], v[204:207], v[172:175], v[68:71]
	s_waitcnt lgkmcnt(10)
	v_mfma_f32_16x16x32_f16 v[72:75], v[192:195], v[176:179], v[72:75]
	v_mfma_f32_16x16x32_f16 v[76:79], v[196:199], v[176:179], v[76:79]
	s_add_u32 m0, s28, 0x1c000
	s_nop 0
	global_load_lds_dwordx4 v11, s[4:5]
	v_mfma_f32_16x16x32_f16 v[80:83], v[200:203], v[176:179], v[80:83]
	v_mfma_f32_16x16x32_f16 v[84:87], v[204:207], v[176:179], v[84:87]
	s_waitcnt lgkmcnt(9)
	v_mfma_f32_16x16x32_f16 v[88:91], v[192:195], v[180:183], v[88:91]
	v_mfma_f32_16x16x32_f16 v[92:95], v[196:199], v[180:183], v[92:95]
	v_mfma_f32_16x16x32_f16 v[96:99], v[200:203], v[180:183], v[96:99]
	s_add_u32 m0, s28, 0x1e000
	s_nop 0
	global_load_lds_dwordx4 v12, s[4:5]
	v_mfma_f32_16x16x32_f16 v[100:103], v[204:207], v[180:183], v[100:103]
	s_waitcnt lgkmcnt(8)
	v_mfma_f32_16x16x32_f16 v[104:107], v[192:195], v[184:187], v[104:107]
	v_mfma_f32_16x16x32_f16 v[108:111], v[196:199], v[184:187], v[108:111]
	v_mfma_f32_16x16x32_f16 v[112:115], v[200:203], v[184:187], v[112:115]
	v_mfma_f32_16x16x32_f16 v[116:119], v[204:207], v[184:187], v[116:119]
	s_waitcnt lgkmcnt(7)
	ds_read_b128 v[172:175], v16
	ds_read_b128 v[192:195], v18
	ds_read_b128 v[196:199], v18 offset:2048
	ds_read_b128 v[200:203], v18 offset:4096
	ds_read_b128 v[204:207], v18 offset:6144
	ds_read_b128 v[176:179], v16 offset:2048
	ds_read_b128 v[180:183], v16 offset:4096
	ds_read_b128 v[184:187], v16 offset:6144
	s_waitcnt lgkmcnt(14)
	v_mfma_f32_16x16x32_f16 v[56:59], v[156:159], v[136:139], v[56:59]
	s_add_u32 m0, s28, 0x20000
	s_nop 0
	global_load_lds_dwordx4 v13, s[4:5]
	s_add_u32 s4, s4, s20
	s_addc_u32 s5, s5, 0
	s_waitcnt lgkmcnt(13)
	v_mfma_f32_16x16x32_f16 v[60:63], v[160:163], v[136:139], v[60:63]
	s_waitcnt lgkmcnt(12)
	v_mfma_f32_16x16x32_f16 v[64:67], v[164:167], v[136:139], v[64:67]
	s_waitcnt lgkmcnt(11)
	v_mfma_f32_16x16x32_f16 v[68:71], v[168:171], v[136:139], v[68:71]
	s_waitcnt lgkmcnt(10)
	v_mfma_f32_16x16x32_f16 v[72:75], v[156:159], v[140:143], v[72:75]
	v_mfma_f32_16x16x32_f16 v[76:79], v[160:163], v[140:143], v[76:79]
	s_add_u32 m0, s28, 0x23000
	s_nop 0
	global_load_lds_dwordx4 v10, s[6:7]
	v_mfma_f32_16x16x32_f16 v[80:83], v[164:167], v[140:143], v[80:83]
	v_mfma_f32_16x16x32_f16 v[84:87], v[168:171], v[140:143], v[84:87]
	s_waitcnt lgkmcnt(9)
	v_mfma_f32_16x16x32_f16 v[88:91], v[156:159], v[144:147], v[88:91]
	v_mfma_f32_16x16x32_f16 v[92:95], v[160:163], v[144:147], v[92:95]
	v_mfma_f32_16x16x32_f16 v[96:99], v[164:167], v[144:147], v[96:99]
	s_add_u32 m0, s28, 0x25000
	s_nop 0
	global_load_lds_dwordx4 v11, s[6:7]
	s_add_u32 s6, s6, s20
	s_addc_u32 s7, s7, 0
	v_mfma_f32_16x16x32_f16 v[100:103], v[168:171], v[144:147], v[100:103]
	s_waitcnt lgkmcnt(8)
	v_mfma_f32_16x16x32_f16 v[104:107], v[156:159], v[148:151], v[104:107]
	v_mfma_f32_16x16x32_f16 v[108:111], v[160:163], v[148:151], v[108:111]
	v_mfma_f32_16x16x32_f16 v[112:115], v[164:167], v[148:151], v[112:115]
	v_mfma_f32_16x16x32_f16 v[116:119], v[168:171], v[148:151], v[116:119]
	s_waitcnt vmcnt(6) lgkmcnt(0)
	s_barrier
	s_waitcnt lgkmcnt(7)
	ds_read_b128 v[136:139], v15 offset:53248
	ds_read_b128 v[156:159], v17 offset:53248
	ds_read_b128 v[160:163], v17 offset:55296
	ds_read_b128 v[164:167], v17 offset:57344
	ds_read_b128 v[168:171], v17 offset:59392
	ds_read_b128 v[140:143], v15 offset:55296
	ds_read_b128 v[144:147], v15 offset:57344
	ds_read_b128 v[148:151], v15 offset:59392
	s_waitcnt lgkmcnt(14)
	v_mfma_f32_16x16x32_f16 v[56:59], v[192:195], v[172:175], v[56:59]
	s_add_u32 m0, s28, 0x0
	s_nop 0
	global_load_lds_dwordx4 v10, s[4:5]
	s_waitcnt lgkmcnt(13)
	v_mfma_f32_16x16x32_f16 v[60:63], v[196:199], v[172:175], v[60:63]
	s_waitcnt lgkmcnt(12)
	v_mfma_f32_16x16x32_f16 v[64:67], v[200:203], v[172:175], v[64:67]
	s_waitcnt lgkmcnt(11)
	v_mfma_f32_16x16x32_f16 v[68:71], v[204:207], v[172:175], v[68:71]
	s_waitcnt lgkmcnt(10)
	v_mfma_f32_16x16x32_f16 v[72:75], v[192:195], v[176:179], v[72:75]
	v_mfma_f32_16x16x32_f16 v[76:79], v[196:199], v[176:179], v[76:79]
	s_add_u32 m0, s28, 0x2000
	s_nop 0
	global_load_lds_dwordx4 v11, s[4:5]
	v_mfma_f32_16x16x32_f16 v[80:83], v[200:203], v[176:179], v[80:83]
	v_mfma_f32_16x16x32_f16 v[84:87], v[204:207], v[176:179], v[84:87]
	s_waitcnt lgkmcnt(9)
	v_mfma_f32_16x16x32_f16 v[88:91], v[192:195], v[180:183], v[88:91]
	v_mfma_f32_16x16x32_f16 v[92:95], v[196:199], v[180:183], v[92:95]
	v_mfma_f32_16x16x32_f16 v[96:99], v[200:203], v[180:183], v[96:99]
	s_add_u32 m0, s28, 0x4000
	s_nop 0
	global_load_lds_dwordx4 v12, s[4:5]
	v_mfma_f32_16x16x32_f16 v[100:103], v[204:207], v[180:183], v[100:103]
	s_waitcnt lgkmcnt(8)
	v_mfma_f32_16x16x32_f16 v[104:107], v[192:195], v[184:187], v[104:107]
	v_mfma_f32_16x16x32_f16 v[108:111], v[196:199], v[184:187], v[108:111]
	v_mfma_f32_16x16x32_f16 v[112:115], v[200:203], v[184:187], v[112:115]
	v_mfma_f32_16x16x32_f16 v[116:119], v[204:207], v[184:187], v[116:119]
	s_waitcnt lgkmcnt(7)
	ds_read_b128 v[172:175], v16 offset:53248
	ds_read_b128 v[192:195], v18 offset:53248
	ds_read_b128 v[196:199], v18 offset:55296
	ds_read_b128 v[200:203], v18 offset:57344
	ds_read_b128 v[204:207], v18 offset:59392
	ds_read_b128 v[176:179], v16 offset:55296
	ds_read_b128 v[180:183], v16 offset:57344
	ds_read_b128 v[184:187], v16 offset:59392
	s_waitcnt lgkmcnt(14)
	v_mfma_f32_16x16x32_f16 v[56:59], v[156:159], v[136:139], v[56:59]
	s_add_u32 m0, s28, 0x6000
	s_nop 0
	global_load_lds_dwordx4 v13, s[4:5]
	s_add_u32 s4, s4, s20
	s_addc_u32 s5, s5, 0
	s_waitcnt lgkmcnt(13)
	v_mfma_f32_16x16x32_f16 v[60:63], v[160:163], v[136:139], v[60:63]
	s_waitcnt lgkmcnt(12)
	v_mfma_f32_16x16x32_f16 v[64:67], v[164:167], v[136:139], v[64:67]
	s_waitcnt lgkmcnt(11)
	v_mfma_f32_16x16x32_f16 v[68:71], v[168:171], v[136:139], v[68:71]
	s_waitcnt lgkmcnt(10)
	v_mfma_f32_16x16x32_f16 v[72:75], v[156:159], v[140:143], v[72:75]
	v_mfma_f32_16x16x32_f16 v[76:79], v[160:163], v[140:143], v[76:79]
	s_add_u32 m0, s28, 0x9000
	s_nop 0
	global_load_lds_dwordx4 v10, s[6:7]
	v_mfma_f32_16x16x32_f16 v[80:83], v[164:167], v[140:143], v[80:83]
	v_mfma_f32_16x16x32_f16 v[84:87], v[168:171], v[140:143], v[84:87]
	s_waitcnt lgkmcnt(9)
	v_mfma_f32_16x16x32_f16 v[88:91], v[156:159], v[144:147], v[88:91]
	v_mfma_f32_16x16x32_f16 v[92:95], v[160:163], v[144:147], v[92:95]
	v_mfma_f32_16x16x32_f16 v[96:99], v[164:167], v[144:147], v[96:99]
	s_add_u32 m0, s28, 0xb000
	s_nop 0
	global_load_lds_dwordx4 v11, s[6:7]
	s_add_u32 s6, s6, s20
	s_addc_u32 s7, s7, 0
	v_mfma_f32_16x16x32_f16 v[100:103], v[168:171], v[144:147], v[100:103]
	s_waitcnt lgkmcnt(8)
	v_mfma_f32_16x16x32_f16 v[104:107], v[156:159], v[148:151], v[104:107]
	v_mfma_f32_16x16x32_f16 v[108:111], v[160:163], v[148:151], v[108:111]
	v_mfma_f32_16x16x32_f16 v[112:115], v[164:167], v[148:151], v[112:115]
	v_mfma_f32_16x16x32_f16 v[116:119], v[168:171], v[148:151], v[116:119]
	s_waitcnt vmcnt(6) lgkmcnt(0)
	s_barrier
	s_waitcnt lgkmcnt(7)
	ds_read_b128 v[136:139], v19
	ds_read_b128 v[156:159], v21
	ds_read_b128 v[160:163], v21 offset:2048
	ds_read_b128 v[164:167], v21 offset:4096
	ds_read_b128 v[168:171], v21 offset:6144
	ds_read_b128 v[140:143], v19 offset:2048
	ds_read_b128 v[144:147], v19 offset:4096
	ds_read_b128 v[148:151], v19 offset:6144
	s_waitcnt lgkmcnt(14)
	v_mfma_f32_16x16x32_f16 v[56:59], v[192:195], v[172:175], v[56:59]
	s_add_u32 m0, s28, 0xd000
	s_nop 0
	global_load_lds_dwordx4 v10, s[4:5]
	s_waitcnt lgkmcnt(13)
	v_mfma_f32_16x16x32_f16 v[60:63], v[196:199], v[172:175], v[60:63]
	s_waitcnt lgkmcnt(12)
	v_mfma_f32_16x16x32_f16 v[64:67], v[200:203], v[172:175], v[64:67]
	s_waitcnt lgkmcnt(11)
	v_mfma_f32_16x16x32_f16 v[68:71], v[204:207], v[172:175], v[68:71]
	s_waitcnt lgkmcnt(10)
	v_mfma_f32_16x16x32_f16 v[72:75], v[192:195], v[176:179], v[72:75]
	v_mfma_f32_16x16x32_f16 v[76:79], v[196:199], v[176:179], v[76:79]
	s_add_u32 m0, s28, 0xf000
	s_nop 0
	global_load_lds_dwordx4 v11, s[4:5]
	v_mfma_f32_16x16x32_f16 v[80:83], v[200:203], v[176:179], v[80:83]
	v_mfma_f32_16x16x32_f16 v[84:87], v[204:207], v[176:179], v[84:87]
	s_waitcnt lgkmcnt(9)
	v_mfma_f32_16x16x32_f16 v[88:91], v[192:195], v[180:183], v[88:91]
	v_mfma_f32_16x16x32_f16 v[92:95], v[196:199], v[180:183], v[92:95]
	v_mfma_f32_16x16x32_f16 v[96:99], v[200:203], v[180:183], v[96:99]
	s_add_u32 m0, s28, 0x11000
	s_nop 0
	global_load_lds_dwordx4 v12, s[4:5]
	v_mfma_f32_16x16x32_f16 v[100:103], v[204:207], v[180:183], v[100:103]
	s_waitcnt lgkmcnt(8)
	v_mfma_f32_16x16x32_f16 v[104:107], v[192:195], v[184:187], v[104:107]
	v_mfma_f32_16x16x32_f16 v[108:111], v[196:199], v[184:187], v[108:111]
	v_mfma_f32_16x16x32_f16 v[112:115], v[200:203], v[184:187], v[112:115]
	v_mfma_f32_16x16x32_f16 v[116:119], v[204:207], v[184:187], v[116:119]
	s_waitcnt lgkmcnt(7)
	ds_read_b128 v[172:175], v20
	ds_read_b128 v[192:195], v22
	ds_read_b128 v[196:199], v22 offset:2048
	ds_read_b128 v[200:203], v22 offset:4096
	ds_read_b128 v[204:207], v22 offset:6144
	ds_read_b128 v[176:179], v20 offset:2048
	ds_read_b128 v[180:183], v20 offset:4096
	ds_read_b128 v[184:187], v20 offset:6144
	s_waitcnt lgkmcnt(14)
	v_mfma_f32_16x16x32_f16 v[56:59], v[156:159], v[136:139], v[56:59]
	s_add_u32 m0, s28, 0x13000
	s_nop 0
	global_load_lds_dwordx4 v13, s[4:5]
	s_add_u32 s4, s4, s20
	s_addc_u32 s5, s5, 0
	s_waitcnt lgkmcnt(13)
	v_mfma_f32_16x16x32_f16 v[60:63], v[160:163], v[136:139], v[60:63]
	s_waitcnt lgkmcnt(12)
	v_mfma_f32_16x16x32_f16 v[64:67], v[164:167], v[136:139], v[64:67]
	s_waitcnt lgkmcnt(11)
	v_mfma_f32_16x16x32_f16 v[68:71], v[168:171], v[136:139], v[68:71]
	s_waitcnt lgkmcnt(10)
	v_mfma_f32_16x16x32_f16 v[72:75], v[156:159], v[140:143], v[72:75]
	v_mfma_f32_16x16x32_f16 v[76:79], v[160:163], v[140:143], v[76:79]
	s_add_u32 m0, s28, 0x16000
	s_nop 0
	global_load_lds_dwordx4 v10, s[6:7]
	v_mfma_f32_16x16x32_f16 v[80:83], v[164:167], v[140:143], v[80:83]
	v_mfma_f32_16x16x32_f16 v[84:87], v[168:171], v[140:143], v[84:87]
	s_waitcnt lgkmcnt(9)
	v_mfma_f32_16x16x32_f16 v[88:91], v[156:159], v[144:147], v[88:91]
	v_mfma_f32_16x16x32_f16 v[92:95], v[160:163], v[144:147], v[92:95]
	v_mfma_f32_16x16x32_f16 v[96:99], v[164:167], v[144:147], v[96:99]
	s_add_u32 m0, s28, 0x18000
	s_nop 0
	global_load_lds_dwordx4 v11, s[6:7]
	s_add_u32 s6, s6, s20
	s_addc_u32 s7, s7, 0
	v_mfma_f32_16x16x32_f16 v[100:103], v[168:171], v[144:147], v[100:103]
	s_waitcnt lgkmcnt(8)
	v_mfma_f32_16x16x32_f16 v[104:107], v[156:159], v[148:151], v[104:107]
	v_mfma_f32_16x16x32_f16 v[108:111], v[160:163], v[148:151], v[108:111]
	v_mfma_f32_16x16x32_f16 v[112:115], v[164:167], v[148:151], v[112:115]
	v_mfma_f32_16x16x32_f16 v[116:119], v[168:171], v[148:151], v[116:119]
	s_waitcnt vmcnt(6) lgkmcnt(0)
	s_barrier
	s_waitcnt lgkmcnt(7)
	ds_read_b128 v[136:139], v15
	ds_read_b128 v[156:159], v17
	ds_read_b128 v[160:163], v17 offset:2048
	ds_read_b128 v[164:167], v17 offset:4096
	ds_read_b128 v[168:171], v17 offset:6144
	ds_read_b128 v[140:143], v15 offset:2048
	ds_read_b128 v[144:147], v15 offset:4096
	ds_read_b128 v[148:151], v15 offset:6144
	s_waitcnt lgkmcnt(14)
	v_mfma_f32_16x16x32_f16 v[56:59], v[192:195], v[172:175], v[56:59]
	s_add_u32 m0, s28, 0x1a000
	s_nop 0
	global_load_lds_dwordx4 v10, s[4:5]
	s_waitcnt lgkmcnt(13)
	v_mfma_f32_16x16x32_f16 v[60:63], v[196:199], v[172:175], v[60:63]
	s_waitcnt lgkmcnt(12)
	v_mfma_f32_16x16x32_f16 v[64:67], v[200:203], v[172:175], v[64:67]
	s_waitcnt lgkmcnt(11)
	v_mfma_f32_16x16x32_f16 v[68:71], v[204:207], v[172:175], v[68:71]
	s_waitcnt lgkmcnt(10)
	v_mfma_f32_16x16x32_f16 v[72:75], v[192:195], v[176:179], v[72:75]
	v_mfma_f32_16x16x32_f16 v[76:79], v[196:199], v[176:179], v[76:79]
	s_add_u32 m0, s28, 0x1c000
	s_nop 0
	global_load_lds_dwordx4 v11, s[4:5]
	v_mfma_f32_16x16x32_f16 v[80:83], v[200:203], v[176:179], v[80:83]
	v_mfma_f32_16x16x32_f16 v[84:87], v[204:207], v[176:179], v[84:87]
	s_waitcnt lgkmcnt(9)
	v_mfma_f32_16x16x32_f16 v[88:91], v[192:195], v[180:183], v[88:91]
	v_mfma_f32_16x16x32_f16 v[92:95], v[196:199], v[180:183], v[92:95]
	v_mfma_f32_16x16x32_f16 v[96:99], v[200:203], v[180:183], v[96:99]
	s_add_u32 m0, s28, 0x1e000
	s_nop 0
	global_load_lds_dwordx4 v12, s[4:5]
	v_mfma_f32_16x16x32_f16 v[100:103], v[204:207], v[180:183], v[100:103]
	s_waitcnt lgkmcnt(8)
	v_mfma_f32_16x16x32_f16 v[104:107], v[192:195], v[184:187], v[104:107]
	v_mfma_f32_16x16x32_f16 v[108:111], v[196:199], v[184:187], v[108:111]
	v_mfma_f32_16x16x32_f16 v[112:115], v[200:203], v[184:187], v[112:115]
	v_mfma_f32_16x16x32_f16 v[116:119], v[204:207], v[184:187], v[116:119]
	s_waitcnt lgkmcnt(7)
	ds_read_b128 v[172:175], v16
	ds_read_b128 v[192:195], v18
	ds_read_b128 v[196:199], v18 offset:2048
	ds_read_b128 v[200:203], v18 offset:4096
	ds_read_b128 v[204:207], v18 offset:6144
	ds_read_b128 v[176:179], v16 offset:2048
	ds_read_b128 v[180:183], v16 offset:4096
	ds_read_b128 v[184:187], v16 offset:6144
	s_waitcnt lgkmcnt(14)
	v_mfma_f32_16x16x32_f16 v[56:59], v[156:159], v[136:139], v[56:59]
	s_add_u32 m0, s28, 0x20000
	s_nop 0
	global_load_lds_dwordx4 v13, s[4:5]
	s_add_u32 s4, s4, s20
	s_addc_u32 s5, s5, 0
	s_waitcnt lgkmcnt(13)
	v_mfma_f32_16x16x32_f16 v[60:63], v[160:163], v[136:139], v[60:63]
	s_waitcnt lgkmcnt(12)
	v_mfma_f32_16x16x32_f16 v[64:67], v[164:167], v[136:139], v[64:67]
	s_waitcnt lgkmcnt(11)
	v_mfma_f32_16x16x32_f16 v[68:71], v[168:171], v[136:139], v[68:71]
	s_waitcnt lgkmcnt(10)
	v_mfma_f32_16x16x32_f16 v[72:75], v[156:159], v[140:143], v[72:75]
	v_mfma_f32_16x16x32_f16 v[76:79], v[160:163], v[140:143], v[76:79]
	s_add_u32 m0, s28, 0x23000
	s_nop 0
	global_load_lds_dwordx4 v10, s[6:7]
	v_mfma_f32_16x16x32_f16 v[80:83], v[164:167], v[140:143], v[80:83]
	v_mfma_f32_16x16x32_f16 v[84:87], v[168:171], v[140:143], v[84:87]
	s_waitcnt lgkmcnt(9)
	v_mfma_f32_16x16x32_f16 v[88:91], v[156:159], v[144:147], v[88:91]
	v_mfma_f32_16x16x32_f16 v[92:95], v[160:163], v[144:147], v[92:95]
	v_mfma_f32_16x16x32_f16 v[96:99], v[164:167], v[144:147], v[96:99]
	s_add_u32 m0, s28, 0x25000
	s_nop 0
	global_load_lds_dwordx4 v11, s[6:7]
	s_add_u32 s6, s6, s20
	s_addc_u32 s7, s7, 0
	v_mfma_f32_16x16x32_f16 v[100:103], v[168:171], v[144:147], v[100:103]
	s_waitcnt lgkmcnt(8)
	v_mfma_f32_16x16x32_f16 v[104:107], v[156:159], v[148:151], v[104:107]
	v_mfma_f32_16x16x32_f16 v[108:111], v[160:163], v[148:151], v[108:111]
	v_mfma_f32_16x16x32_f16 v[112:115], v[164:167], v[148:151], v[112:115]
	v_mfma_f32_16x16x32_f16 v[116:119], v[168:171], v[148:151], v[116:119]
	s_waitcnt vmcnt(6) lgkmcnt(0)
	s_barrier
	s_waitcnt lgkmcnt(7)
	ds_read_b128 v[136:139], v15 offset:53248
	ds_read_b128 v[156:159], v17 offset:53248
	ds_read_b128 v[160:163], v17 offset:55296
	ds_read_b128 v[164:167], v17 offset:57344
	ds_read_b128 v[168:171], v17 offset:59392
	ds_read_b128 v[140:143], v15 offset:55296
	ds_read_b128 v[144:147], v15 offset:57344
	ds_read_b128 v[148:151], v15 offset:59392
	s_waitcnt lgkmcnt(14)
	v_mfma_f32_16x16x32_f16 v[56:59], v[192:195], v[172:175], v[56:59]
	s_add_u32 m0, s28, 0x0
	s_nop 0
	global_load_lds_dwordx4 v10, s[4:5]
	s_waitcnt lgkmcnt(13)
	v_mfma_f32_16x16x32_f16 v[60:63], v[196:199], v[172:175], v[60:63]
	s_waitcnt lgkmcnt(12)
	v_mfma_f32_16x16x32_f16 v[64:67], v[200:203], v[172:175], v[64:67]
	s_waitcnt lgkmcnt(11)
	v_mfma_f32_16x16x32_f16 v[68:71], v[204:207], v[172:175], v[68:71]
	s_waitcnt lgkmcnt(10)
	v_mfma_f32_16x16x32_f16 v[72:75], v[192:195], v[176:179], v[72:75]
	v_mfma_f32_16x16x32_f16 v[76:79], v[196:199], v[176:179], v[76:79]
	s_add_u32 m0, s28, 0x2000
	s_nop 0
	global_load_lds_dwordx4 v11, s[4:5]
	v_mfma_f32_16x16x32_f16 v[80:83], v[200:203], v[176:179], v[80:83]
	v_mfma_f32_16x16x32_f16 v[84:87], v[204:207], v[176:179], v[84:87]
	s_waitcnt lgkmcnt(9)
	v_mfma_f32_16x16x32_f16 v[88:91], v[192:195], v[180:183], v[88:91]
	v_mfma_f32_16x16x32_f16 v[92:95], v[196:199], v[180:183], v[92:95]
	v_mfma_f32_16x16x32_f16 v[96:99], v[200:203], v[180:183], v[96:99]
	s_add_u32 m0, s28, 0x4000
	s_nop 0
	global_load_lds_dwordx4 v12, s[4:5]
	v_mfma_f32_16x16x32_f16 v[100:103], v[204:207], v[180:183], v[100:103]
	s_waitcnt lgkmcnt(8)
	v_mfma_f32_16x16x32_f16 v[104:107], v[192:195], v[184:187], v[104:107]
	v_mfma_f32_16x16x32_f16 v[108:111], v[196:199], v[184:187], v[108:111]
	v_mfma_f32_16x16x32_f16 v[112:115], v[200:203], v[184:187], v[112:115]
	v_mfma_f32_16x16x32_f16 v[116:119], v[204:207], v[184:187], v[116:119]
	s_waitcnt lgkmcnt(7)
	ds_read_b128 v[172:175], v16 offset:53248
	ds_read_b128 v[192:195], v18 offset:53248
	ds_read_b128 v[196:199], v18 offset:55296
	ds_read_b128 v[200:203], v18 offset:57344
	ds_read_b128 v[204:207], v18 offset:59392
	ds_read_b128 v[176:179], v16 offset:55296
	ds_read_b128 v[180:183], v16 offset:57344
	ds_read_b128 v[184:187], v16 offset:59392
	s_waitcnt lgkmcnt(14)
	v_mfma_f32_16x16x32_f16 v[56:59], v[156:159], v[136:139], v[56:59]
	s_add_u32 m0, s28, 0x6000
	s_nop 0
	global_load_lds_dwordx4 v13, s[4:5]
	s_add_u32 s4, s4, s20
	s_addc_u32 s5, s5, 0
	s_waitcnt lgkmcnt(13)
	v_mfma_f32_16x16x32_f16 v[60:63], v[160:163], v[136:139], v[60:63]
	s_waitcnt lgkmcnt(12)
	v_mfma_f32_16x16x32_f16 v[64:67], v[164:167], v[136:139], v[64:67]
	s_waitcnt lgkmcnt(11)
	v_mfma_f32_16x16x32_f16 v[68:71], v[168:171], v[136:139], v[68:71]
	s_waitcnt lgkmcnt(10)
	v_mfma_f32_16x16x32_f16 v[72:75], v[156:159], v[140:143], v[72:75]
	v_mfma_f32_16x16x32_f16 v[76:79], v[160:163], v[140:143], v[76:79]
	s_add_u32 m0, s28, 0x9000
	s_nop 0
	global_load_lds_dwordx4 v10, s[6:7]
	v_mfma_f32_16x16x32_f16 v[80:83], v[164:167], v[140:143], v[80:83]
	v_mfma_f32_16x16x32_f16 v[84:87], v[168:171], v[140:143], v[84:87]
	s_waitcnt lgkmcnt(9)
	v_mfma_f32_16x16x32_f16 v[88:91], v[156:159], v[144:147], v[88:91]
	v_mfma_f32_16x16x32_f16 v[92:95], v[160:163], v[144:147], v[92:95]
	v_mfma_f32_16x16x32_f16 v[96:99], v[164:167], v[144:147], v[96:99]
	s_add_u32 m0, s28, 0xb000
	s_nop 0
	global_load_lds_dwordx4 v11, s[6:7]
	s_add_u32 s6, s6, s20
	s_addc_u32 s7, s7, 0
	v_mfma_f32_16x16x32_f16 v[100:103], v[168:171], v[144:147], v[100:103]
	s_waitcnt lgkmcnt(8)
	v_mfma_f32_16x16x32_f16 v[104:107], v[156:159], v[148:151], v[104:107]
	v_mfma_f32_16x16x32_f16 v[108:111], v[160:163], v[148:151], v[108:111]
	v_mfma_f32_16x16x32_f16 v[112:115], v[164:167], v[148:151], v[112:115]
	v_mfma_f32_16x16x32_f16 v[116:119], v[168:171], v[148:151], v[116:119]
	s_waitcnt vmcnt(6) lgkmcnt(0)
	s_barrier
	s_waitcnt lgkmcnt(7)
	ds_read_b128 v[136:139], v19
	ds_read_b128 v[156:159], v21
	ds_read_b128 v[160:163], v21 offset:2048
	ds_read_b128 v[164:167], v21 offset:4096
	ds_read_b128 v[168:171], v21 offset:6144
	ds_read_b128 v[140:143], v19 offset:2048
	ds_read_b128 v[144:147], v19 offset:4096
	ds_read_b128 v[148:151], v19 offset:6144
	s_waitcnt lgkmcnt(14)
	v_mfma_f32_16x16x32_f16 v[56:59], v[192:195], v[172:175], v[56:59]
	s_add_u32 m0, s28, 0xd000
	s_nop 0
	global_load_lds_dwordx4 v10, s[4:5]
	s_waitcnt lgkmcnt(13)
	v_mfma_f32_16x16x32_f16 v[60:63], v[196:199], v[172:175], v[60:63]
	s_waitcnt lgkmcnt(12)
	v_mfma_f32_16x16x32_f16 v[64:67], v[200:203], v[172:175], v[64:67]
	s_waitcnt lgkmcnt(11)
	v_mfma_f32_16x16x32_f16 v[68:71], v[204:207], v[172:175], v[68:71]
	s_waitcnt lgkmcnt(10)
	v_mfma_f32_16x16x32_f16 v[72:75], v[192:195], v[176:179], v[72:75]
	v_mfma_f32_16x16x32_f16 v[76:79], v[196:199], v[176:179], v[76:79]
	s_add_u32 m0, s28, 0xf000
	s_nop 0
	global_load_lds_dwordx4 v11, s[4:5]
	v_mfma_f32_16x16x32_f16 v[80:83], v[200:203], v[176:179], v[80:83]
	v_mfma_f32_16x16x32_f16 v[84:87], v[204:207], v[176:179], v[84:87]
	s_waitcnt lgkmcnt(9)
	v_mfma_f32_16x16x32_f16 v[88:91], v[192:195], v[180:183], v[88:91]
	v_mfma_f32_16x16x32_f16 v[92:95], v[196:199], v[180:183], v[92:95]
	v_mfma_f32_16x16x32_f16 v[96:99], v[200:203], v[180:183], v[96:99]
	s_add_u32 m0, s28, 0x11000
	s_nop 0
	global_load_lds_dwordx4 v12, s[4:5]
	v_mfma_f32_16x16x32_f16 v[100:103], v[204:207], v[180:183], v[100:103]
	s_waitcnt lgkmcnt(8)
	v_mfma_f32_16x16x32_f16 v[104:107], v[192:195], v[184:187], v[104:107]
	v_mfma_f32_16x16x32_f16 v[108:111], v[196:199], v[184:187], v[108:111]
	v_mfma_f32_16x16x32_f16 v[112:115], v[200:203], v[184:187], v[112:115]
	v_mfma_f32_16x16x32_f16 v[116:119], v[204:207], v[184:187], v[116:119]
	s_waitcnt lgkmcnt(7)
	ds_read_b128 v[172:175], v20
	ds_read_b128 v[192:195], v22
	ds_read_b128 v[196:199], v22 offset:2048
	ds_read_b128 v[200:203], v22 offset:4096
	ds_read_b128 v[204:207], v22 offset:6144
	ds_read_b128 v[176:179], v20 offset:2048
	ds_read_b128 v[180:183], v20 offset:4096
	ds_read_b128 v[184:187], v20 offset:6144
	s_waitcnt lgkmcnt(14)
	v_mfma_f32_16x16x32_f16 v[56:59], v[156:159], v[136:139], v[56:59]
	s_add_u32 m0, s28, 0x13000
	s_nop 0
	global_load_lds_dwordx4 v13, s[4:5]
	s_add_u32 s4, s4, s20
	s_addc_u32 s5, s5, 0
	s_waitcnt lgkmcnt(13)
	v_mfma_f32_16x16x32_f16 v[60:63], v[160:163], v[136:139], v[60:63]
	s_waitcnt lgkmcnt(12)
	v_mfma_f32_16x16x32_f16 v[64:67], v[164:167], v[136:139], v[64:67]
	s_waitcnt lgkmcnt(11)
	v_mfma_f32_16x16x32_f16 v[68:71], v[168:171], v[136:139], v[68:71]
	s_waitcnt lgkmcnt(10)
	v_mfma_f32_16x16x32_f16 v[72:75], v[156:159], v[140:143], v[72:75]
	v_mfma_f32_16x16x32_f16 v[76:79], v[160:163], v[140:143], v[76:79]
	s_add_u32 m0, s28, 0x16000
	s_nop 0
	global_load_lds_dwordx4 v10, s[6:7]
	v_mfma_f32_16x16x32_f16 v[80:83], v[164:167], v[140:143], v[80:83]
	v_mfma_f32_16x16x32_f16 v[84:87], v[168:171], v[140:143], v[84:87]
	s_waitcnt lgkmcnt(9)
	v_mfma_f32_16x16x32_f16 v[88:91], v[156:159], v[144:147], v[88:91]
	v_mfma_f32_16x16x32_f16 v[92:95], v[160:163], v[144:147], v[92:95]
	v_mfma_f32_16x16x32_f16 v[96:99], v[164:167], v[144:147], v[96:99]
	s_add_u32 m0, s28, 0x18000
	s_nop 0
	global_load_lds_dwordx4 v11, s[6:7]
	s_add_u32 s6, s6, s20
	s_addc_u32 s7, s7, 0
	v_mfma_f32_16x16x32_f16 v[100:103], v[168:171], v[144:147], v[100:103]
	s_waitcnt lgkmcnt(8)
	v_mfma_f32_16x16x32_f16 v[104:107], v[156:159], v[148:151], v[104:107]
	v_mfma_f32_16x16x32_f16 v[108:111], v[160:163], v[148:151], v[108:111]
	v_mfma_f32_16x16x32_f16 v[112:115], v[164:167], v[148:151], v[112:115]
	v_mfma_f32_16x16x32_f16 v[116:119], v[168:171], v[148:151], v[116:119]
	s_waitcnt vmcnt(6) lgkmcnt(0)
	s_barrier
	s_waitcnt lgkmcnt(7)
	ds_read_b128 v[136:139], v15
	ds_read_b128 v[156:159], v17
	ds_read_b128 v[160:163], v17 offset:2048
	ds_read_b128 v[164:167], v17 offset:4096
	ds_read_b128 v[168:171], v17 offset:6144
	ds_read_b128 v[140:143], v15 offset:2048
	ds_read_b128 v[144:147], v15 offset:4096
	ds_read_b128 v[148:151], v15 offset:6144
	s_waitcnt lgkmcnt(14)
	v_mfma_f32_16x16x32_f16 v[56:59], v[192:195], v[172:175], v[56:59]
	s_add_u32 m0, s28, 0x1a000
	s_nop 0
	global_load_lds_dwordx4 v10, s[4:5]
	s_waitcnt lgkmcnt(13)
	v_mfma_f32_16x16x32_f16 v[60:63], v[196:199], v[172:175], v[60:63]
	s_waitcnt lgkmcnt(12)
	v_mfma_f32_16x16x32_f16 v[64:67], v[200:203], v[172:175], v[64:67]
	s_waitcnt lgkmcnt(11)
	v_mfma_f32_16x16x32_f16 v[68:71], v[204:207], v[172:175], v[68:71]
	s_waitcnt lgkmcnt(10)
	v_mfma_f32_16x16x32_f16 v[72:75], v[192:195], v[176:179], v[72:75]
	v_mfma_f32_16x16x32_f16 v[76:79], v[196:199], v[176:179], v[76:79]
	s_add_u32 m0, s28, 0x1c000
	s_nop 0
	global_load_lds_dwordx4 v11, s[4:5]
	v_mfma_f32_16x16x32_f16 v[80:83], v[200:203], v[176:179], v[80:83]
	v_mfma_f32_16x16x32_f16 v[84:87], v[204:207], v[176:179], v[84:87]
	s_waitcnt lgkmcnt(9)
	v_mfma_f32_16x16x32_f16 v[88:91], v[192:195], v[180:183], v[88:91]
	v_mfma_f32_16x16x32_f16 v[92:95], v[196:199], v[180:183], v[92:95]
	v_mfma_f32_16x16x32_f16 v[96:99], v[200:203], v[180:183], v[96:99]
	s_add_u32 m0, s28, 0x1e000
	s_nop 0
	global_load_lds_dwordx4 v12, s[4:5]
	v_mfma_f32_16x16x32_f16 v[100:103], v[204:207], v[180:183], v[100:103]
	s_waitcnt lgkmcnt(8)
	v_mfma_f32_16x16x32_f16 v[104:107], v[192:195], v[184:187], v[104:107]
	v_mfma_f32_16x16x32_f16 v[108:111], v[196:199], v[184:187], v[108:111]
	v_mfma_f32_16x16x32_f16 v[112:115], v[200:203], v[184:187], v[112:115]
	v_mfma_f32_16x16x32_f16 v[116:119], v[204:207], v[184:187], v[116:119]
	s_waitcnt lgkmcnt(7)
	ds_read_b128 v[172:175], v16
	ds_read_b128 v[192:195], v18
	ds_read_b128 v[196:199], v18 offset:2048
	ds_read_b128 v[200:203], v18 offset:4096
	ds_read_b128 v[204:207], v18 offset:6144
	ds_read_b128 v[176:179], v16 offset:2048
	ds_read_b128 v[180:183], v16 offset:4096
	ds_read_b128 v[184:187], v16 offset:6144
	s_waitcnt lgkmcnt(14)
	v_mfma_f32_16x16x32_f16 v[56:59], v[156:159], v[136:139], v[56:59]
	s_add_u32 m0, s28, 0x20000
	s_nop 0
	global_load_lds_dwordx4 v13, s[4:5]
	s_add_u32 s4, s4, s20
	s_addc_u32 s5, s5, 0
	s_waitcnt lgkmcnt(13)
	v_mfma_f32_16x16x32_f16 v[60:63], v[160:163], v[136:139], v[60:63]
	s_waitcnt lgkmcnt(12)
	v_mfma_f32_16x16x32_f16 v[64:67], v[164:167], v[136:139], v[64:67]
	s_waitcnt lgkmcnt(11)
	v_mfma_f32_16x16x32_f16 v[68:71], v[168:171], v[136:139], v[68:71]
	s_waitcnt lgkmcnt(10)
	v_mfma_f32_16x16x32_f16 v[72:75], v[156:159], v[140:143], v[72:75]
	v_mfma_f32_16x16x32_f16 v[76:79], v[160:163], v[140:143], v[76:79]
	s_add_u32 m0, s28, 0x23000
	s_nop 0
	global_load_lds_dwordx4 v10, s[6:7]
	v_mfma_f32_16x16x32_f16 v[80:83], v[164:167], v[140:143], v[80:83]
	v_mfma_f32_16x16x32_f16 v[84:87], v[168:171], v[140:143], v[84:87]
	s_waitcnt lgkmcnt(9)
	v_mfma_f32_16x16x32_f16 v[88:91], v[156:159], v[144:147], v[88:91]
	v_mfma_f32_16x16x32_f16 v[92:95], v[160:163], v[144:147], v[92:95]
	v_mfma_f32_16x16x32_f16 v[96:99], v[164:167], v[144:147], v[96:99]
	s_add_u32 m0, s28, 0x25000
	s_nop 0
	global_load_lds_dwordx4 v11, s[6:7]
	s_add_u32 s6, s6, s20
	s_addc_u32 s7, s7, 0
	v_mfma_f32_16x16x32_f16 v[100:103], v[168:171], v[144:147], v[100:103]
	s_waitcnt lgkmcnt(8)
	v_mfma_f32_16x16x32_f16 v[104:107], v[156:159], v[148:151], v[104:107]
	v_mfma_f32_16x16x32_f16 v[108:111], v[160:163], v[148:151], v[108:111]
	v_mfma_f32_16x16x32_f16 v[112:115], v[164:167], v[148:151], v[112:115]
	v_mfma_f32_16x16x32_f16 v[116:119], v[168:171], v[148:151], v[116:119]
	s_waitcnt vmcnt(6) lgkmcnt(0)
	s_barrier
	s_waitcnt lgkmcnt(7)
	ds_read_b128 v[136:139], v15 offset:53248
	ds_read_b128 v[156:159], v17 offset:53248
	ds_read_b128 v[160:163], v17 offset:55296
	ds_read_b128 v[164:167], v17 offset:57344
	ds_read_b128 v[168:171], v17 offset:59392
	ds_read_b128 v[140:143], v15 offset:55296
	ds_read_b128 v[144:147], v15 offset:57344
	ds_read_b128 v[148:151], v15 offset:59392
	s_waitcnt lgkmcnt(14)
	v_mfma_f32_16x16x32_f16 v[56:59], v[192:195], v[172:175], v[56:59]
	s_add_u32 m0, s28, 0x0
	s_nop 0
	global_load_lds_dwordx4 v10, s[4:5]
	s_waitcnt lgkmcnt(13)
	v_mfma_f32_16x16x32_f16 v[60:63], v[196:199], v[172:175], v[60:63]
	s_waitcnt lgkmcnt(12)
	v_mfma_f32_16x16x32_f16 v[64:67], v[200:203], v[172:175], v[64:67]
	s_waitcnt lgkmcnt(11)
	v_mfma_f32_16x16x32_f16 v[68:71], v[204:207], v[172:175], v[68:71]
	s_waitcnt lgkmcnt(10)
	v_mfma_f32_16x16x32_f16 v[72:75], v[192:195], v[176:179], v[72:75]
	v_mfma_f32_16x16x32_f16 v[76:79], v[196:199], v[176:179], v[76:79]
	s_add_u32 m0, s28, 0x2000
	s_nop 0
	global_load_lds_dwordx4 v11, s[4:5]
	v_mfma_f32_16x16x32_f16 v[80:83], v[200:203], v[176:179], v[80:83]
	v_mfma_f32_16x16x32_f16 v[84:87], v[204:207], v[176:179], v[84:87]
	s_waitcnt lgkmcnt(9)
	v_mfma_f32_16x16x32_f16 v[88:91], v[192:195], v[180:183], v[88:91]
	v_mfma_f32_16x16x32_f16 v[92:95], v[196:199], v[180:183], v[92:95]
	v_mfma_f32_16x16x32_f16 v[96:99], v[200:203], v[180:183], v[96:99]
	s_add_u32 m0, s28, 0x4000
	s_nop 0
	global_load_lds_dwordx4 v12, s[4:5]
	v_mfma_f32_16x16x32_f16 v[100:103], v[204:207], v[180:183], v[100:103]
	s_waitcnt lgkmcnt(8)
	v_mfma_f32_16x16x32_f16 v[104:107], v[192:195], v[184:187], v[104:107]
	v_mfma_f32_16x16x32_f16 v[108:111], v[196:199], v[184:187], v[108:111]
	v_mfma_f32_16x16x32_f16 v[112:115], v[200:203], v[184:187], v[112:115]
	v_mfma_f32_16x16x32_f16 v[116:119], v[204:207], v[184:187], v[116:119]
	s_waitcnt lgkmcnt(7)
	ds_read_b128 v[172:175], v16 offset:53248
	ds_read_b128 v[192:195], v18 offset:53248
	ds_read_b128 v[196:199], v18 offset:55296
	ds_read_b128 v[200:203], v18 offset:57344
	ds_read_b128 v[204:207], v18 offset:59392
	ds_read_b128 v[176:179], v16 offset:55296
	ds_read_b128 v[180:183], v16 offset:57344
	ds_read_b128 v[184:187], v16 offset:59392
	s_waitcnt lgkmcnt(14)
	v_mfma_f32_16x16x32_f16 v[56:59], v[156:159], v[136:139], v[56:59]
	s_add_u32 m0, s28, 0x6000
	s_nop 0
	global_load_lds_dwordx4 v13, s[4:5]
	s_add_u32 s4, s4, s20
	s_addc_u32 s5, s5, 0
	s_waitcnt lgkmcnt(13)
	v_mfma_f32_16x16x32_f16 v[60:63], v[160:163], v[136:139], v[60:63]
	s_waitcnt lgkmcnt(12)
	v_mfma_f32_16x16x32_f16 v[64:67], v[164:167], v[136:139], v[64:67]
	s_waitcnt lgkmcnt(11)
	v_mfma_f32_16x16x32_f16 v[68:71], v[168:171], v[136:139], v[68:71]
	s_waitcnt lgkmcnt(10)
	v_mfma_f32_16x16x32_f16 v[72:75], v[156:159], v[140:143], v[72:75]
	v_mfma_f32_16x16x32_f16 v[76:79], v[160:163], v[140:143], v[76:79]
	s_add_u32 m0, s28, 0x9000
	s_nop 0
	global_load_lds_dwordx4 v10, s[6:7]
	v_mfma_f32_16x16x32_f16 v[80:83], v[164:167], v[140:143], v[80:83]
	v_mfma_f32_16x16x32_f16 v[84:87], v[168:171], v[140:143], v[84:87]
	s_waitcnt lgkmcnt(9)
	v_mfma_f32_16x16x32_f16 v[88:91], v[156:159], v[144:147], v[88:91]
	v_mfma_f32_16x16x32_f16 v[92:95], v[160:163], v[144:147], v[92:95]
	v_mfma_f32_16x16x32_f16 v[96:99], v[164:167], v[144:147], v[96:99]
	s_add_u32 m0, s28, 0xb000
	s_nop 0
	global_load_lds_dwordx4 v11, s[6:7]
	s_add_u32 s6, s6, s20
	s_addc_u32 s7, s7, 0
	v_mfma_f32_16x16x32_f16 v[100:103], v[168:171], v[144:147], v[100:103]
	s_waitcnt lgkmcnt(8)
	v_mfma_f32_16x16x32_f16 v[104:107], v[156:159], v[148:151], v[104:107]
	v_mfma_f32_16x16x32_f16 v[108:111], v[160:163], v[148:151], v[108:111]
	v_mfma_f32_16x16x32_f16 v[112:115], v[164:167], v[148:151], v[112:115]
	v_mfma_f32_16x16x32_f16 v[116:119], v[168:171], v[148:151], v[116:119]
	s_waitcnt vmcnt(6) lgkmcnt(0)
	s_barrier
	s_waitcnt lgkmcnt(7)
	ds_read_b128 v[136:139], v19
	ds_read_b128 v[156:159], v21
	ds_read_b128 v[160:163], v21 offset:2048
	ds_read_b128 v[164:167], v21 offset:4096
	ds_read_b128 v[168:171], v21 offset:6144
	ds_read_b128 v[140:143], v19 offset:2048
	ds_read_b128 v[144:147], v19 offset:4096
	ds_read_b128 v[148:151], v19 offset:6144
	s_waitcnt lgkmcnt(14)
	v_mfma_f32_16x16x32_f16 v[56:59], v[192:195], v[172:175], v[56:59]
	s_waitcnt lgkmcnt(13)
	v_mfma_f32_16x16x32_f16 v[60:63], v[196:199], v[172:175], v[60:63]
	s_waitcnt lgkmcnt(12)
	v_mfma_f32_16x16x32_f16 v[64:67], v[200:203], v[172:175], v[64:67]
	s_waitcnt lgkmcnt(11)
	v_mfma_f32_16x16x32_f16 v[68:71], v[204:207], v[172:175], v[68:71]
	s_waitcnt lgkmcnt(10)
	v_mfma_f32_16x16x32_f16 v[72:75], v[192:195], v[176:179], v[72:75]
	v_mfma_f32_16x16x32_f16 v[76:79], v[196:199], v[176:179], v[76:79]
	v_mfma_f32_16x16x32_f16 v[80:83], v[200:203], v[176:179], v[80:83]
	v_mfma_f32_16x16x32_f16 v[84:87], v[204:207], v[176:179], v[84:87]
	s_waitcnt lgkmcnt(9)
	v_mfma_f32_16x16x32_f16 v[88:91], v[192:195], v[180:183], v[88:91]
	v_mfma_f32_16x16x32_f16 v[92:95], v[196:199], v[180:183], v[92:95]
	v_mfma_f32_16x16x32_f16 v[96:99], v[200:203], v[180:183], v[96:99]
	v_mfma_f32_16x16x32_f16 v[100:103], v[204:207], v[180:183], v[100:103]
	s_waitcnt lgkmcnt(8)
	v_mfma_f32_16x16x32_f16 v[104:107], v[192:195], v[184:187], v[104:107]
	v_mfma_f32_16x16x32_f16 v[108:111], v[196:199], v[184:187], v[108:111]
	v_mfma_f32_16x16x32_f16 v[112:115], v[200:203], v[184:187], v[112:115]
	v_mfma_f32_16x16x32_f16 v[116:119], v[204:207], v[184:187], v[116:119]
	s_waitcnt lgkmcnt(7)
	ds_read_b128 v[172:175], v20
	ds_read_b128 v[192:195], v22
	ds_read_b128 v[196:199], v22 offset:2048
	ds_read_b128 v[200:203], v22 offset:4096
	ds_read_b128 v[204:207], v22 offset:6144
	ds_read_b128 v[176:179], v20 offset:2048
	ds_read_b128 v[180:183], v20 offset:4096
	ds_read_b128 v[184:187], v20 offset:6144
	s_waitcnt lgkmcnt(14)
	v_mfma_f32_16x16x32_f16 v[56:59], v[156:159], v[136:139], v[56:59]
	s_waitcnt lgkmcnt(13)
	v_mfma_f32_16x16x32_f16 v[60:63], v[160:163], v[136:139], v[60:63]
	s_waitcnt lgkmcnt(12)
	v_mfma_f32_16x16x32_f16 v[64:67], v[164:167], v[136:139], v[64:67]
	s_waitcnt lgkmcnt(11)
	v_mfma_f32_16x16x32_f16 v[68:71], v[168:171], v[136:139], v[68:71]
	s_waitcnt lgkmcnt(10)
	v_mfma_f32_16x16x32_f16 v[72:75], v[156:159], v[140:143], v[72:75]
	v_mfma_f32_16x16x32_f16 v[76:79], v[160:163], v[140:143], v[76:79]
	v_mfma_f32_16x16x32_f16 v[80:83], v[164:167], v[140:143], v[80:83]
	v_mfma_f32_16x16x32_f16 v[84:87], v[168:171], v[140:143], v[84:87]
	s_waitcnt lgkmcnt(9)
	v_mfma_f32_16x16x32_f16 v[88:91], v[156:159], v[144:147], v[88:91]
	v_mfma_f32_16x16x32_f16 v[92:95], v[160:163], v[144:147], v[92:95]
	v_mfma_f32_16x16x32_f16 v[96:99], v[164:167], v[144:147], v[96:99]
	v_mfma_f32_16x16x32_f16 v[100:103], v[168:171], v[144:147], v[100:103]
	s_waitcnt lgkmcnt(8)
	v_mfma_f32_16x16x32_f16 v[104:107], v[156:159], v[148:151], v[104:107]
	v_mfma_f32_16x16x32_f16 v[108:111], v[160:163], v[148:151], v[108:111]
	v_mfma_f32_16x16x32_f16 v[112:115], v[164:167], v[148:151], v[112:115]
	v_mfma_f32_16x16x32_f16 v[116:119], v[168:171], v[148:151], v[116:119]
	s_waitcnt vmcnt(0) lgkmcnt(0)
	s_barrier
	s_waitcnt lgkmcnt(7)
	ds_read_b128 v[136:139], v15
	ds_read_b128 v[156:159], v17
	ds_read_b128 v[160:163], v17 offset:2048
	ds_read_b128 v[164:167], v17 offset:4096
	ds_read_b128 v[168:171], v17 offset:6144
	ds_read_b128 v[140:143], v15 offset:2048
	ds_read_b128 v[144:147], v15 offset:4096
	ds_read_b128 v[148:151], v15 offset:6144
	s_waitcnt lgkmcnt(14)
	v_mfma_f32_16x16x32_f16 v[56:59], v[192:195], v[172:175], v[56:59]
	s_waitcnt lgkmcnt(13)
	v_mfma_f32_16x16x32_f16 v[60:63], v[196:199], v[172:175], v[60:63]
	s_waitcnt lgkmcnt(12)
	v_mfma_f32_16x16x32_f16 v[64:67], v[200:203], v[172:175], v[64:67]
	s_waitcnt lgkmcnt(11)
	v_mfma_f32_16x16x32_f16 v[68:71], v[204:207], v[172:175], v[68:71]
	s_waitcnt lgkmcnt(10)
	v_mfma_f32_16x16x32_f16 v[72:75], v[192:195], v[176:179], v[72:75]
	v_mfma_f32_16x16x32_f16 v[76:79], v[196:199], v[176:179], v[76:79]
	v_mfma_f32_16x16x32_f16 v[80:83], v[200:203], v[176:179], v[80:83]
	v_mfma_f32_16x16x32_f16 v[84:87], v[204:207], v[176:179], v[84:87]
	s_waitcnt lgkmcnt(9)
	v_mfma_f32_16x16x32_f16 v[88:91], v[192:195], v[180:183], v[88:91]
	v_mfma_f32_16x16x32_f16 v[92:95], v[196:199], v[180:183], v[92:95]
	v_mfma_f32_16x16x32_f16 v[96:99], v[200:203], v[180:183], v[96:99]
	v_mfma_f32_16x16x32_f16 v[100:103], v[204:207], v[180:183], v[100:103]
	s_waitcnt lgkmcnt(8)
	v_mfma_f32_16x16x32_f16 v[104:107], v[192:195], v[184:187], v[104:107]
	v_mfma_f32_16x16x32_f16 v[108:111], v[196:199], v[184:187], v[108:111]
	v_mfma_f32_16x16x32_f16 v[112:115], v[200:203], v[184:187], v[112:115]
	v_mfma_f32_16x16x32_f16 v[116:119], v[204:207], v[184:187], v[116:119]
	s_waitcnt lgkmcnt(7)
	ds_read_b128 v[172:175], v16
	ds_read_b128 v[192:195], v18
	ds_read_b128 v[196:199], v18 offset:2048
	ds_read_b128 v[200:203], v18 offset:4096
	ds_read_b128 v[204:207], v18 offset:6144
	ds_read_b128 v[176:179], v16 offset:2048
	ds_read_b128 v[180:183], v16 offset:4096
	ds_read_b128 v[184:187], v16 offset:6144
	s_waitcnt lgkmcnt(14)
	v_mfma_f32_16x16x32_f16 v[56:59], v[156:159], v[136:139], v[56:59]
	s_waitcnt lgkmcnt(13)
	v_mfma_f32_16x16x32_f16 v[60:63], v[160:163], v[136:139], v[60:63]
	s_waitcnt lgkmcnt(12)
	v_mfma_f32_16x16x32_f16 v[64:67], v[164:167], v[136:139], v[64:67]
	s_waitcnt lgkmcnt(11)
	v_mfma_f32_16x16x32_f16 v[68:71], v[168:171], v[136:139], v[68:71]
	s_waitcnt lgkmcnt(10)
	v_mfma_f32_16x16x32_f16 v[72:75], v[156:159], v[140:143], v[72:75]
	v_mfma_f32_16x16x32_f16 v[76:79], v[160:163], v[140:143], v[76:79]
	v_mfma_f32_16x16x32_f16 v[80:83], v[164:167], v[140:143], v[80:83]
	v_mfma_f32_16x16x32_f16 v[84:87], v[168:171], v[140:143], v[84:87]
	s_waitcnt lgkmcnt(9)
	v_mfma_f32_16x16x32_f16 v[88:91], v[156:159], v[144:147], v[88:91]
	v_mfma_f32_16x16x32_f16 v[92:95], v[160:163], v[144:147], v[92:95]
	v_mfma_f32_16x16x32_f16 v[96:99], v[164:167], v[144:147], v[96:99]
	v_mfma_f32_16x16x32_f16 v[100:103], v[168:171], v[144:147], v[100:103]
	s_waitcnt lgkmcnt(8)
	v_mfma_f32_16x16x32_f16 v[104:107], v[156:159], v[148:151], v[104:107]
	v_mfma_f32_16x16x32_f16 v[108:111], v[160:163], v[148:151], v[108:111]
	v_mfma_f32_16x16x32_f16 v[112:115], v[164:167], v[148:151], v[112:115]
	v_mfma_f32_16x16x32_f16 v[116:119], v[168:171], v[148:151], v[116:119]
	s_waitcnt lgkmcnt(6)
	v_mfma_f32_16x16x32_f16 v[56:59], v[192:195], v[172:175], v[56:59]
	s_waitcnt lgkmcnt(5)
	v_mfma_f32_16x16x32_f16 v[60:63], v[196:199], v[172:175], v[60:63]
	s_waitcnt lgkmcnt(4)
	v_mfma_f32_16x16x32_f16 v[64:67], v[200:203], v[172:175], v[64:67]
	s_waitcnt lgkmcnt(3)
	v_mfma_f32_16x16x32_f16 v[68:71], v[204:207], v[172:175], v[68:71]
	s_waitcnt lgkmcnt(2)
	v_mfma_f32_16x16x32_f16 v[72:75], v[192:195], v[176:179], v[72:75]
	v_mfma_f32_16x16x32_f16 v[76:79], v[196:199], v[176:179], v[76:79]
	v_mfma_f32_16x16x32_f16 v[80:83], v[200:203], v[176:179], v[80:83]
	v_mfma_f32_16x16x32_f16 v[84:87], v[204:207], v[176:179], v[84:87]
	s_waitcnt lgkmcnt(1)
	v_mfma_f32_16x16x32_f16 v[88:91], v[192:195], v[180:183], v[88:91]
	v_mfma_f32_16x16x32_f16 v[92:95], v[196:199], v[180:183], v[92:95]
	v_mfma_f32_16x16x32_f16 v[96:99], v[200:203], v[180:183], v[96:99]
	v_mfma_f32_16x16x32_f16 v[100:103], v[204:207], v[180:183], v[100:103]
	s_waitcnt lgkmcnt(0)
	v_mfma_f32_16x16x32_f16 v[104:107], v[192:195], v[184:187], v[104:107]
	v_mfma_f32_16x16x32_f16 v[108:111], v[196:199], v[184:187], v[108:111]
	v_mfma_f32_16x16x32_f16 v[112:115], v[200:203], v[184:187], v[112:115]
	v_mfma_f32_16x16x32_f16 v[116:119], v[204:207], v[184:187], v[116:119]
	s_nop 7
	s_nop 1
	v_mov_b32_e32 v213, s19
	v_pk_add_f32 v[56:57], v[56:57], v[24:25]
	v_pk_add_f32 v[58:59], v[58:59], v[26:27]
	v_pk_add_f32 v[60:61], v[60:61], v[28:29]
	v_pk_add_f32 v[62:63], v[62:63], v[30:31]
	v_pk_add_f32 v[64:65], v[64:65], v[32:33]
	v_pk_add_f32 v[66:67], v[66:67], v[34:35]
	v_pk_add_f32 v[68:69], v[68:69], v[36:37]
	v_pk_add_f32 v[70:71], v[70:71], v[38:39]
	v_pk_mul_f32 v[208:209], v[56:57], v[56:57]
	v_pk_fma_f32 v[208:209], v[58:59], v[58:59], v[208:209]
	v_pk_fma_f32 v[208:209], v[60:61], v[60:61], v[208:209]
	v_pk_fma_f32 v[208:209], v[62:63], v[62:63], v[208:209]
	v_pk_fma_f32 v[208:209], v[64:65], v[64:65], v[208:209]
	v_pk_fma_f32 v[208:209], v[66:67], v[66:67], v[208:209]
	v_pk_fma_f32 v[208:209], v[68:69], v[68:69], v[208:209]
	v_pk_fma_f32 v[208:209], v[70:71], v[70:71], v[208:209]
	v_add_f32_e32 v208, v208, v209
	v_mov_b32_e32 v209, v208
	s_nop 1
	v_permlane16_swap_b32_e32 v208, v209
	v_add_f32_e32 v208, v208, v209
	v_mov_b32_e32 v209, v208
	s_nop 1
	v_permlane32_swap_b32_e32 v208, v209
	v_add_f32_e32 v208, v208, v209
	v_mov_b32_e32 v210, 0x358637bd
	v_fmac_f32_e32 v210, 0x3c800000, v208
	v_rsq_f32_e32 v210, v210
	s_add_u32 s24, s29, 0
	s_lshr_b32 s8, s24, 1
	s_lshl_b32 s8, s8, 12
	s_and_b32 s24, s24, 1
	s_lshl_b32 s24, s24, 8
	s_add_u32 s8, s8, s24
	v_mul_f32_e32 v210, v213, v210
	v_add_u32_e32 v212, s8, v23
	v_pk_mul_f32 v[56:57], v[56:57], v[210:211] op_sel_hi:[1,0]
	v_pk_mul_f32 v[58:59], v[58:59], v[210:211] op_sel_hi:[1,0]
	v_pk_mul_f32 v[56:57], v[56:57], v[40:41]
	v_pk_mul_f32 v[58:59], v[58:59], v[42:43]
	v_cvt_pk_f16_f32 v56, v56, v57
	v_cvt_pk_f16_f32 v57, v58, v59
	global_store_dwordx2 v212, v[56:57], s[22:23] offset:0
	v_pk_mul_f32 v[60:61], v[60:61], v[210:211] op_sel_hi:[1,0]
	v_pk_mul_f32 v[62:63], v[62:63], v[210:211] op_sel_hi:[1,0]
	v_pk_mul_f32 v[60:61], v[60:61], v[44:45]
	v_pk_mul_f32 v[62:63], v[62:63], v[46:47]
	v_cvt_pk_f16_f32 v60, v60, v61
	v_cvt_pk_f16_f32 v61, v62, v63
	global_store_dwordx2 v212, v[60:61], s[22:23] offset:1024
	v_pk_mul_f32 v[64:65], v[64:65], v[210:211] op_sel_hi:[1,0]
	v_pk_mul_f32 v[66:67], v[66:67], v[210:211] op_sel_hi:[1,0]
	v_pk_mul_f32 v[64:65], v[64:65], v[48:49]
	v_pk_mul_f32 v[66:67], v[66:67], v[50:51]
	v_cvt_pk_f16_f32 v64, v64, v65
	v_cvt_pk_f16_f32 v65, v66, v67
	global_store_dwordx2 v212, v[64:65], s[22:23] offset:2048
	v_pk_mul_f32 v[68:69], v[68:69], v[210:211] op_sel_hi:[1,0]
	v_pk_mul_f32 v[70:71], v[70:71], v[210:211] op_sel_hi:[1,0]
	v_pk_mul_f32 v[68:69], v[68:69], v[52:53]
	v_pk_mul_f32 v[70:71], v[70:71], v[54:55]
	v_cvt_pk_f16_f32 v68, v68, v69
	v_cvt_pk_f16_f32 v69, v70, v71
	global_store_dwordx2 v212, v[68:69], s[22:23] offset:3072
	v_pk_add_f32 v[72:73], v[72:73], v[24:25]
	v_pk_add_f32 v[74:75], v[74:75], v[26:27]
	v_pk_add_f32 v[76:77], v[76:77], v[28:29]
	v_pk_add_f32 v[78:79], v[78:79], v[30:31]
	v_pk_add_f32 v[80:81], v[80:81], v[32:33]
	v_pk_add_f32 v[82:83], v[82:83], v[34:35]
	v_pk_add_f32 v[84:85], v[84:85], v[36:37]
	v_pk_add_f32 v[86:87], v[86:87], v[38:39]
	v_pk_mul_f32 v[208:209], v[72:73], v[72:73]
	v_pk_fma_f32 v[208:209], v[74:75], v[74:75], v[208:209]
	v_pk_fma_f32 v[208:209], v[76:77], v[76:77], v[208:209]
	v_pk_fma_f32 v[208:209], v[78:79], v[78:79], v[208:209]
	v_pk_fma_f32 v[208:209], v[80:81], v[80:81], v[208:209]
	v_pk_fma_f32 v[208:209], v[82:83], v[82:83], v[208:209]
	v_pk_fma_f32 v[208:209], v[84:85], v[84:85], v[208:209]
	v_pk_fma_f32 v[208:209], v[86:87], v[86:87], v[208:209]
	v_add_f32_e32 v208, v208, v209
	v_mov_b32_e32 v209, v208
	s_nop 1
	v_permlane16_swap_b32_e32 v208, v209
	v_add_f32_e32 v208, v208, v209
	v_mov_b32_e32 v209, v208
	s_nop 1
	v_permlane32_swap_b32_e32 v208, v209
	v_add_f32_e32 v208, v208, v209
	v_mov_b32_e32 v210, 0x358637bd
	v_fmac_f32_e32 v210, 0x3c800000, v208
	v_rsq_f32_e32 v210, v210
	s_add_u32 s24, s29, 1
	s_lshr_b32 s8, s24, 1
	s_lshl_b32 s8, s8, 12
	s_and_b32 s24, s24, 1
	s_lshl_b32 s24, s24, 8
	s_add_u32 s8, s8, s24
	v_mul_f32_e32 v210, v213, v210
	v_add_u32_e32 v212, s8, v23
	v_pk_mul_f32 v[72:73], v[72:73], v[210:211] op_sel_hi:[1,0]
	v_pk_mul_f32 v[74:75], v[74:75], v[210:211] op_sel_hi:[1,0]
	v_pk_mul_f32 v[72:73], v[72:73], v[40:41]
	v_pk_mul_f32 v[74:75], v[74:75], v[42:43]
	v_cvt_pk_f16_f32 v72, v72, v73
	v_cvt_pk_f16_f32 v73, v74, v75
	global_store_dwordx2 v212, v[72:73], s[22:23] offset:0
	v_pk_mul_f32 v[76:77], v[76:77], v[210:211] op_sel_hi:[1,0]
	v_pk_mul_f32 v[78:79], v[78:79], v[210:211] op_sel_hi:[1,0]
	v_pk_mul_f32 v[76:77], v[76:77], v[44:45]
	v_pk_mul_f32 v[78:79], v[78:79], v[46:47]
	v_cvt_pk_f16_f32 v76, v76, v77
	v_cvt_pk_f16_f32 v77, v78, v79
	global_store_dwordx2 v212, v[76:77], s[22:23] offset:1024
	v_pk_mul_f32 v[80:81], v[80:81], v[210:211] op_sel_hi:[1,0]
	v_pk_mul_f32 v[82:83], v[82:83], v[210:211] op_sel_hi:[1,0]
	v_pk_mul_f32 v[80:81], v[80:81], v[48:49]
	v_pk_mul_f32 v[82:83], v[82:83], v[50:51]
	v_cvt_pk_f16_f32 v80, v80, v81
	v_cvt_pk_f16_f32 v81, v82, v83
	global_store_dwordx2 v212, v[80:81], s[22:23] offset:2048
	v_pk_mul_f32 v[84:85], v[84:85], v[210:211] op_sel_hi:[1,0]
	v_pk_mul_f32 v[86:87], v[86:87], v[210:211] op_sel_hi:[1,0]
	v_pk_mul_f32 v[84:85], v[84:85], v[52:53]
	v_pk_mul_f32 v[86:87], v[86:87], v[54:55]
	v_cvt_pk_f16_f32 v84, v84, v85
	v_cvt_pk_f16_f32 v85, v86, v87
	global_store_dwordx2 v212, v[84:85], s[22:23] offset:3072
	v_pk_add_f32 v[88:89], v[88:89], v[24:25]
	v_pk_add_f32 v[90:91], v[90:91], v[26:27]
	v_pk_add_f32 v[92:93], v[92:93], v[28:29]
	v_pk_add_f32 v[94:95], v[94:95], v[30:31]
	v_pk_add_f32 v[96:97], v[96:97], v[32:33]
	v_pk_add_f32 v[98:99], v[98:99], v[34:35]
	v_pk_add_f32 v[100:101], v[100:101], v[36:37]
	v_pk_add_f32 v[102:103], v[102:103], v[38:39]
	v_pk_mul_f32 v[208:209], v[88:89], v[88:89]
	v_pk_fma_f32 v[208:209], v[90:91], v[90:91], v[208:209]
	v_pk_fma_f32 v[208:209], v[92:93], v[92:93], v[208:209]
	v_pk_fma_f32 v[208:209], v[94:95], v[94:95], v[208:209]
	v_pk_fma_f32 v[208:209], v[96:97], v[96:97], v[208:209]
	v_pk_fma_f32 v[208:209], v[98:99], v[98:99], v[208:209]
	v_pk_fma_f32 v[208:209], v[100:101], v[100:101], v[208:209]
	v_pk_fma_f32 v[208:209], v[102:103], v[102:103], v[208:209]
	v_add_f32_e32 v208, v208, v209
	v_mov_b32_e32 v209, v208
	s_nop 1
	v_permlane16_swap_b32_e32 v208, v209
	v_add_f32_e32 v208, v208, v209
	v_mov_b32_e32 v209, v208
	s_nop 1
	v_permlane32_swap_b32_e32 v208, v209
	v_add_f32_e32 v208, v208, v209
	v_mov_b32_e32 v210, 0x358637bd
	v_fmac_f32_e32 v210, 0x3c800000, v208
	v_rsq_f32_e32 v210, v210
	s_add_u32 s24, s29, 2
	s_lshr_b32 s8, s24, 1
	s_lshl_b32 s8, s8, 12
	s_and_b32 s24, s24, 1
	s_lshl_b32 s24, s24, 8
	s_add_u32 s8, s8, s24
	v_mul_f32_e32 v210, v213, v210
	v_add_u32_e32 v212, s8, v23
	v_pk_mul_f32 v[88:89], v[88:89], v[210:211] op_sel_hi:[1,0]
	v_pk_mul_f32 v[90:91], v[90:91], v[210:211] op_sel_hi:[1,0]
	v_pk_mul_f32 v[88:89], v[88:89], v[40:41]
	v_pk_mul_f32 v[90:91], v[90:91], v[42:43]
	v_cvt_pk_f16_f32 v88, v88, v89
	v_cvt_pk_f16_f32 v89, v90, v91
	global_store_dwordx2 v212, v[88:89], s[22:23] offset:0
	v_pk_mul_f32 v[92:93], v[92:93], v[210:211] op_sel_hi:[1,0]
	v_pk_mul_f32 v[94:95], v[94:95], v[210:211] op_sel_hi:[1,0]
	v_pk_mul_f32 v[92:93], v[92:93], v[44:45]
	v_pk_mul_f32 v[94:95], v[94:95], v[46:47]
	v_cvt_pk_f16_f32 v92, v92, v93
	v_cvt_pk_f16_f32 v93, v94, v95
	global_store_dwordx2 v212, v[92:93], s[22:23] offset:1024
	v_pk_mul_f32 v[96:97], v[96:97], v[210:211] op_sel_hi:[1,0]
	v_pk_mul_f32 v[98:99], v[98:99], v[210:211] op_sel_hi:[1,0]
	v_pk_mul_f32 v[96:97], v[96:97], v[48:49]
	v_pk_mul_f32 v[98:99], v[98:99], v[50:51]
	v_cvt_pk_f16_f32 v96, v96, v97
	v_cvt_pk_f16_f32 v97, v98, v99
	global_store_dwordx2 v212, v[96:97], s[22:23] offset:2048
	v_pk_mul_f32 v[100:101], v[100:101], v[210:211] op_sel_hi:[1,0]
	v_pk_mul_f32 v[102:103], v[102:103], v[210:211] op_sel_hi:[1,0]
	v_pk_mul_f32 v[100:101], v[100:101], v[52:53]
	v_pk_mul_f32 v[102:103], v[102:103], v[54:55]
	v_cvt_pk_f16_f32 v100, v100, v101
	v_cvt_pk_f16_f32 v101, v102, v103
	global_store_dwordx2 v212, v[100:101], s[22:23] offset:3072
	v_pk_add_f32 v[104:105], v[104:105], v[24:25]
	v_pk_add_f32 v[106:107], v[106:107], v[26:27]
	v_pk_add_f32 v[108:109], v[108:109], v[28:29]
	v_pk_add_f32 v[110:111], v[110:111], v[30:31]
	v_pk_add_f32 v[112:113], v[112:113], v[32:33]
	v_pk_add_f32 v[114:115], v[114:115], v[34:35]
	v_pk_add_f32 v[116:117], v[116:117], v[36:37]
	v_pk_add_f32 v[118:119], v[118:119], v[38:39]
	v_pk_mul_f32 v[208:209], v[104:105], v[104:105]
	v_pk_fma_f32 v[208:209], v[106:107], v[106:107], v[208:209]
	v_pk_fma_f32 v[208:209], v[108:109], v[108:109], v[208:209]
	v_pk_fma_f32 v[208:209], v[110:111], v[110:111], v[208:209]
	v_pk_fma_f32 v[208:209], v[112:113], v[112:113], v[208:209]
	v_pk_fma_f32 v[208:209], v[114:115], v[114:115], v[208:209]
	v_pk_fma_f32 v[208:209], v[116:117], v[116:117], v[208:209]
	v_pk_fma_f32 v[208:209], v[118:119], v[118:119], v[208:209]
	v_add_f32_e32 v208, v208, v209
	v_mov_b32_e32 v209, v208
	s_nop 1
	v_permlane16_swap_b32_e32 v208, v209
	v_add_f32_e32 v208, v208, v209
	v_mov_b32_e32 v209, v208
	s_nop 1
	v_permlane32_swap_b32_e32 v208, v209
	v_add_f32_e32 v208, v208, v209
	v_mov_b32_e32 v210, 0x358637bd
	v_fmac_f32_e32 v210, 0x3c800000, v208
	v_rsq_f32_e32 v210, v210
	s_add_u32 s24, s29, 3
	s_lshr_b32 s8, s24, 1
	s_lshl_b32 s8, s8, 12
	s_and_b32 s24, s24, 1
	s_lshl_b32 s24, s24, 8
	s_add_u32 s8, s8, s24
	v_mul_f32_e32 v210, v213, v210
	v_add_u32_e32 v212, s8, v23
	v_pk_mul_f32 v[104:105], v[104:105], v[210:211] op_sel_hi:[1,0]
	v_pk_mul_f32 v[106:107], v[106:107], v[210:211] op_sel_hi:[1,0]
	v_pk_mul_f32 v[104:105], v[104:105], v[40:41]
	v_pk_mul_f32 v[106:107], v[106:107], v[42:43]
	v_cvt_pk_f16_f32 v104, v104, v105
	v_cvt_pk_f16_f32 v105, v106, v107
	global_store_dwordx2 v212, v[104:105], s[22:23] offset:0
	v_pk_mul_f32 v[108:109], v[108:109], v[210:211] op_sel_hi:[1,0]
	v_pk_mul_f32 v[110:111], v[110:111], v[210:211] op_sel_hi:[1,0]
	v_pk_mul_f32 v[108:109], v[108:109], v[44:45]
	v_pk_mul_f32 v[110:111], v[110:111], v[46:47]
	v_cvt_pk_f16_f32 v108, v108, v109
	v_cvt_pk_f16_f32 v109, v110, v111
	global_store_dwordx2 v212, v[108:109], s[22:23] offset:1024
	v_pk_mul_f32 v[112:113], v[112:113], v[210:211] op_sel_hi:[1,0]
	v_pk_mul_f32 v[114:115], v[114:115], v[210:211] op_sel_hi:[1,0]
	v_pk_mul_f32 v[112:113], v[112:113], v[48:49]
	v_pk_mul_f32 v[114:115], v[114:115], v[50:51]
	v_cvt_pk_f16_f32 v112, v112, v113
	v_cvt_pk_f16_f32 v113, v114, v115
	global_store_dwordx2 v212, v[112:113], s[22:23] offset:2048
	v_pk_mul_f32 v[116:117], v[116:117], v[210:211] op_sel_hi:[1,0]
	v_pk_mul_f32 v[118:119], v[118:119], v[210:211] op_sel_hi:[1,0]
	v_pk_mul_f32 v[116:117], v[116:117], v[52:53]
	v_pk_mul_f32 v[118:119], v[118:119], v[54:55]
	v_cvt_pk_f16_f32 v116, v116, v117
	v_cvt_pk_f16_f32 v117, v118, v119
	global_store_dwordx2 v212, v[116:117], s[22:23] offset:3072
	s_branch .Lpf_done
.Lpf_vVA:
	s_mul_i32 s25, s25, 0x50
	s_add_u32 s29, s10, s25
	s_lshr_b32 s29, s29, 4
	v_add_u32_e32 v5, s25, v3
	v_lshlrev_b32_e32 v5, 7, v5
	v_add_u32_e32 v15, v5, v6
	v_add_u32_e32 v16, v5, v7
	v_add_u32_e32 v5, 0x9000, v9
	v_add_u32_e32 v17, v5, v6
	v_add_u32_e32 v18, v5, v7
	v_add_u32_e32 v19, 0x1a000, v15
	v_add_u32_e32 v20, 0x1a000, v16
	v_add_u32_e32 v21, 0x1a000, v17
	v_add_u32_e32 v22, 0x1a000, v18
	v_lshlrev_b32_e32 v5, 2, v3
	global_load_dword v24, v5, s[14:15] offset:0
	global_load_dword v26, v5, s[14:15] offset:64
	global_load_dword v28, v5, s[14:15] offset:128
	global_load_dword v30, v5, s[14:15] offset:192
	s_add_u32 m0, s28, 0x0
	s_nop 0
	global_load_lds_dwordx4 v10, s[4:5]
	s_add_u32 m0, s28, 0x2000
	s_nop 0
	global_load_lds_dwordx4 v11, s[4:5]
	s_add_u32 m0, s28, 0x4000
	s_nop 0
	global_load_lds_dwordx4 v12, s[4:5]
	s_add_u32 m0, s28, 0x6000
	s_nop 0
	global_load_lds_dwordx4 v13, s[4:5]
	s_add_u32 m0, s28, 0x8000
	s_nop 0
	global_load_lds_dwordx4 v14, s[4:5]
	s_add_u32 s4, s4, s20
	s_addc_u32 s5, s5, 0
	s_add_u32 m0, s28, 0x9000
	s_nop 0
	global_load_lds_dwordx4 v10, s[6:7]
	s_add_u32 m0, s28, 0xb000
	s_nop 0
	global_load_lds_dwordx4 v11, s[6:7]
	s_add_u32 s6, s6, s20
	s_addc_u32 s7, s7, 0
	s_add_u32 m0, s28, 0xd000
	s_nop 0
	global_load_lds_dwordx4 v10, s[4:5]
	s_add_u32 m0, s28, 0xf000
	s_nop 0
	global_load_lds_dwordx4 v11, s[4:5]
	s_add_u32 m0, s28, 0x11000
	s_nop 0
	global_load_lds_dwordx4 v12, s[4:5]
	s_add_u32 m0, s28, 0x13000
	s_nop 0
	global_load_lds_dwordx4 v13, s[4:5]
	s_add_u32 m0, s28, 0x15000
	s_nop 0
	global_load_lds_dwordx4 v14, s[4:5]
	s_add_u32 s4, s4, s20
	s_addc_u32 s5, s5, 0
	s_add_u32 m0, s28, 0x16000
	s_nop 0
	global_load_lds_dwordx4 v10, s[6:7]
	s_add_u32 m0, s28, 0x18000
	s_nop 0
	global_load_lds_dwordx4 v11, s[6:7]
	s_add_u32 s6, s6, s20
	s_addc_u32 s7, s7, 0
	s_add_u32 m0, s28, 0x1a000
	s_nop 0
	global_load_lds_dwordx4 v10, s[4:5]
	s_add_u32 m0, s28, 0x1c000
	s_nop 0
	global_load_lds_dwordx4 v11, s[4:5]
	s_add_u32 m0, s28, 0x1e000
	s_nop 0
	global_load_lds_dwordx4 v12, s[4:5]
	s_add_u32 m0, s28, 0x20000
	s_nop 0
	global_load_lds_dwordx4 v13, s[4:5]
	s_add_u32 m0, s28, 0x22000
	s_nop 0
	global_load_lds_dwordx4 v14, s[4:5]
	s_add_u32 s4, s4, s20
	s_addc_u32 s5, s5, 0
	s_add_u32 m0, s28, 0x23000
	s_nop 0
	global_load_lds_dwordx4 v10, s[6:7]
	s_add_u32 m0, s28, 0x25000
	s_nop 0
	global_load_lds_dwordx4 v11, s[6:7]
	s_add_u32 s6, s6, s20
	s_addc_u32 s7, s7, 0
	s_waitcnt vmcnt(14) lgkmcnt(0)
	s_barrier
	s_waitcnt lgkmcnt(6)
	ds_read_b128 v[136:139], v15
	ds_read_b128 v[156:159], v17
	ds_read_b128 v[160:163], v17 offset:2048
	ds_read_b128 v[164:167], v17 offset:4096
	ds_read_b128 v[168:171], v17 offset:6144
	ds_read_b128 v[140:143], v15 offset:2048
	ds_read_b128 v[144:147], v15 offset:4096
	ds_read_b128 v[148:151], v15 offset:6144
	ds_read_b128 v[152:155], v15 offset:8192
	s_waitcnt lgkmcnt(6)
	ds_read_b128 v[172:175], v16
	ds_read_b128 v[192:195], v18
	ds_read_b128 v[196:199], v18 offset:2048
	ds_read_b128 v[200:203], v18 offset:4096
	ds_read_b128 v[204:207], v18 offset:6144
	ds_read_b128 v[176:179], v16 offset:2048
	ds_read_b128 v[180:183], v16 offset:4096
	ds_read_b128 v[184:187], v16 offset:6144
	ds_read_b128 v[188:191], v16 offset:8192
	v_mfma_f32_16x16x32_f16 v[56:59], v[136:139], v[156:159], 0
	s_waitcnt lgkmcnt(15)
	v_mfma_f32_16x16x32_f16 v[60:63], v[136:139], v[160:163], 0
	s_waitcnt lgkmcnt(14)
	v_mfma_f32_16x16x32_f16 v[64:67], v[136:139], v[164:167], 0
	s_waitcnt lgkmcnt(13)
	v_mfma_f32_16x16x32_f16 v[68:71], v[136:139], v[168:171], 0
	s_waitcnt lgkmcnt(12)
	v_mfma_f32_16x16x32_f16 v[72:75], v[140:143], v[156:159], 0
	v_mfma_f32_16x16x32_f16 v[76:79], v[140:143], v[160:163], 0
	v_mfma_f32_16x16x32_f16 v[80:83], v[140:143], v[164:167], 0
	v_mfma_f32_16x16x32_f16 v[84:87], v[140:143], v[168:171], 0
	s_waitcnt lgkmcnt(11)
	v_mfma_f32_16x16x32_f16 v[88:91], v[144:147], v[156:159], 0
	v_mfma_f32_16x16x32_f16 v[92:95], v[144:147], v[160:163], 0
	v_mfma_f32_16x16x32_f16 v[96:99], v[144:147], v[164:167], 0
	v_mfma_f32_16x16x32_f16 v[100:103], v[144:147], v[168:171], 0
	s_waitcnt lgkmcnt(10)
	v_mfma_f32_16x16x32_f16 v[104:107], v[148:151], v[156:159], 0
	v_mfma_f32_16x16x32_f16 v[108:111], v[148:151], v[160:163], 0
	v_mfma_f32_16x16x32_f16 v[112:115], v[148:151], v[164:167], 0
	v_mfma_f32_16x16x32_f16 v[116:119], v[148:151], v[168:171], 0
	s_waitcnt lgkmcnt(9)
	v_mfma_f32_16x16x32_f16 v[120:123], v[152:155], v[156:159], 0
	v_mfma_f32_16x16x32_f16 v[124:127], v[152:155], v[160:163], 0
	v_mfma_f32_16x16x32_f16 v[128:131], v[152:155], v[164:167], 0
	v_mfma_f32_16x16x32_f16 v[132:135], v[152:155], v[168:171], 0
	s_waitcnt vmcnt(7) lgkmcnt(0)
	s_barrier
	s_waitcnt lgkmcnt(6)
	ds_read_b128 v[136:139], v15 offset:53248
	ds_read_b128 v[156:159], v17 offset:53248
	ds_read_b128 v[160:163], v17 offset:55296
	ds_read_b128 v[164:167], v17 offset:57344
	ds_read_b128 v[168:171], v17 offset:59392
	ds_read_b128 v[140:143], v15 offset:55296
	ds_read_b128 v[144:147], v15 offset:57344
	ds_read_b128 v[148:151], v15 offset:59392
	ds_read_b128 v[152:155], v15 offset:61440
	v_mfma_f32_16x16x32_f16 v[56:59], v[172:175], v[192:195], v[56:59]
	s_add_u32 m0, s28, 0x0
	s_nop 0
	global_load_lds_dwordx4 v10, s[4:5]
	s_waitcnt lgkmcnt(15)
	v_mfma_f32_16x16x32_f16 v[60:63], v[172:175], v[196:199], v[60:63]
	s_waitcnt lgkmcnt(14)
	v_mfma_f32_16x16x32_f16 v[64:67], v[172:175], v[200:203], v[64:67]
	s_waitcnt lgkmcnt(13)
	v_mfma_f32_16x16x32_f16 v[68:71], v[172:175], v[204:207], v[68:71]
	s_waitcnt lgkmcnt(12)
	v_mfma_f32_16x16x32_f16 v[72:75], v[176:179], v[192:195], v[72:75]
	v_mfma_f32_16x16x32_f16 v[76:79], v[176:179], v[196:199], v[76:79]
	s_add_u32 m0, s28, 0x2000
	s_nop 0
	global_load_lds_dwordx4 v11, s[4:5]
	v_mfma_f32_16x16x32_f16 v[80:83], v[176:179], v[200:203], v[80:83]
	v_mfma_f32_16x16x32_f16 v[84:87], v[176:179], v[204:207], v[84:87]
	s_waitcnt lgkmcnt(11)
	v_mfma_f32_16x16x32_f16 v[88:91], v[180:183], v[192:195], v[88:91]
	v_mfma_f32_16x16x32_f16 v[92:95], v[180:183], v[196:199], v[92:95]
	v_mfma_f32_16x16x32_f16 v[96:99], v[180:183], v[200:203], v[96:99]
	s_add_u32 m0, s28, 0x4000
	s_nop 0
	global_load_lds_dwordx4 v12, s[4:5]
	v_mfma_f32_16x16x32_f16 v[100:103], v[180:183], v[204:207], v[100:103]
	s_waitcnt lgkmcnt(10)
	v_mfma_f32_16x16x32_f16 v[104:107], v[184:187], v[192:195], v[104:107]
	v_mfma_f32_16x16x32_f16 v[108:111], v[184:187], v[196:199], v[108:111]
	v_mfma_f32_16x16x32_f16 v[112:115], v[184:187], v[200:203], v[112:115]
	v_mfma_f32_16x16x32_f16 v[116:119], v[184:187], v[204:207], v[116:119]
	s_add_u32 m0, s28, 0x6000
	s_nop 0
	global_load_lds_dwordx4 v13, s[4:5]
	s_waitcnt lgkmcnt(9)
	v_mfma_f32_16x16x32_f16 v[120:123], v[188:191], v[192:195], v[120:123]
	v_mfma_f32_16x16x32_f16 v[124:127], v[188:191], v[196:199], v[124:127]
	v_mfma_f32_16x16x32_f16 v[128:131], v[188:191], v[200:203], v[128:131]
	v_mfma_f32_16x16x32_f16 v[132:135], v[188:191], v[204:207], v[132:135]
	s_waitcnt lgkmcnt(6)
	ds_read_b128 v[172:175], v16 offset:53248
	ds_read_b128 v[192:195], v18 offset:53248
	ds_read_b128 v[196:199], v18 offset:55296
	ds_read_b128 v[200:203], v18 offset:57344
	ds_read_b128 v[204:207], v18 offset:59392
	ds_read_b128 v[176:179], v16 offset:55296
	ds_read_b128 v[180:183], v16 offset:57344
	ds_read_b128 v[184:187], v16 offset:59392
	ds_read_b128 v[188:191], v16 offset:61440
	v_mfma_f32_16x16x32_f16 v[56:59], v[136:139], v[156:159], v[56:59]
	s_add_u32 m0, s28, 0x8000
	s_nop 0
	global_load_lds_dwordx4 v14, s[4:5]
	s_add_u32 s4, s4, s20
	s_addc_u32 s5, s5, 0
	s_waitcnt lgkmcnt(15)
	v_mfma_f32_16x16x32_f16 v[60:63], v[136:139], v[160:163], v[60:63]
	s_waitcnt lgkmcnt(14)
	v_mfma_f32_16x16x32_f16 v[64:67], v[136:139], v[164:167], v[64:67]
	s_waitcnt lgkmcnt(13)
	v_mfma_f32_16x16x32_f16 v[68:71], v[136:139], v[168:171], v[68:71]
	s_waitcnt lgkmcnt(12)
	v_mfma_f32_16x16x32_f16 v[72:75], v[140:143], v[156:159], v[72:75]
	v_mfma_f32_16x16x32_f16 v[76:79], v[140:143], v[160:163], v[76:79]
	v_mfma_f32_16x16x32_f16 v[80:83], v[140:143], v[164:167], v[80:83]
	s_add_u32 m0, s28, 0x9000
	s_nop 0
	global_load_lds_dwordx4 v10, s[6:7]
	v_mfma_f32_16x16x32_f16 v[84:87], v[140:143], v[168:171], v[84:87]
	s_waitcnt lgkmcnt(11)
	v_mfma_f32_16x16x32_f16 v[88:91], v[144:147], v[156:159], v[88:91]
	v_mfma_f32_16x16x32_f16 v[92:95], v[144:147], v[160:163], v[92:95]
	v_mfma_f32_16x16x32_f16 v[96:99], v[144:147], v[164:167], v[96:99]
	v_mfma_f32_16x16x32_f16 v[100:103], v[144:147], v[168:171], v[100:103]
	s_waitcnt lgkmcnt(10)
	v_mfma_f32_16x16x32_f16 v[104:107], v[148:151], v[156:159], v[104:107]
	v_mfma_f32_16x16x32_f16 v[108:111], v[148:151], v[160:163], v[108:111]
	s_add_u32 m0, s28, 0xb000
	s_nop 0
	global_load_lds_dwordx4 v11, s[6:7]
	s_add_u32 s6, s6, s20
	s_addc_u32 s7, s7, 0
	v_mfma_f32_16x16x32_f16 v[112:115], v[148:151], v[164:167], v[112:115]
	v_mfma_f32_16x16x32_f16 v[116:119], v[148:151], v[168:171], v[116:119]
	s_waitcnt lgkmcnt(9)
	v_mfma_f32_16x16x32_f16 v[120:123], v[152:155], v[156:159], v[120:123]
	v_mfma_f32_16x16x32_f16 v[124:127], v[152:155], v[160:163], v[124:127]
	v_mfma_f32_16x16x32_f16 v[128:131], v[152:155], v[164:167], v[128:131]
	v_mfma_f32_16x16x32_f16 v[132:135], v[152:155], v[168:171], v[132:135]
	s_waitcnt vmcnt(7) lgkmcnt(0)
	s_barrier
	s_waitcnt lgkmcnt(6)
	ds_read_b128 v[136:139], v19
	ds_read_b128 v[156:159], v21
	ds_read_b128 v[160:163], v21 offset:2048
	ds_read_b128 v[164:167], v21 offset:4096
	ds_read_b128 v[168:171], v21 offset:6144
	ds_read_b128 v[140:143], v19 offset:2048
	ds_read_b128 v[144:147], v19 offset:4096
	ds_read_b128 v[148:151], v19 offset:6144
	ds_read_b128 v[152:155], v19 offset:8192
	v_mfma_f32_16x16x32_f16 v[56:59], v[172:175], v[192:195], v[56:59]
	s_add_u32 m0, s28, 0xd000
	s_nop 0
	global_load_lds_dwordx4 v10, s[4:5]
	s_waitcnt lgkmcnt(15)
	v_mfma_f32_16x16x32_f16 v[60:63], v[172:175], v[196:199], v[60:63]
	s_waitcnt lgkmcnt(14)
	v_mfma_f32_16x16x32_f16 v[64:67], v[172:175], v[200:203], v[64:67]
	s_waitcnt lgkmcnt(13)
	v_mfma_f32_16x16x32_f16 v[68:71], v[172:175], v[204:207], v[68:71]
	s_waitcnt lgkmcnt(12)
	v_mfma_f32_16x16x32_f16 v[72:75], v[176:179], v[192:195], v[72:75]
	v_mfma_f32_16x16x32_f16 v[76:79], v[176:179], v[196:199], v[76:79]
	s_add_u32 m0, s28, 0xf000
	s_nop 0
	global_load_lds_dwordx4 v11, s[4:5]
	v_mfma_f32_16x16x32_f16 v[80:83], v[176:179], v[200:203], v[80:83]
	v_mfma_f32_16x16x32_f16 v[84:87], v[176:179], v[204:207], v[84:87]
	s_waitcnt lgkmcnt(11)
	v_mfma_f32_16x16x32_f16 v[88:91], v[180:183], v[192:195], v[88:91]
	v_mfma_f32_16x16x32_f16 v[92:95], v[180:183], v[196:199], v[92:95]
	v_mfma_f32_16x16x32_f16 v[96:99], v[180:183], v[200:203], v[96:99]
	s_add_u32 m0, s28, 0x11000
	s_nop 0
	global_load_lds_dwordx4 v12, s[4:5]
	v_mfma_f32_16x16x32_f16 v[100:103], v[180:183], v[204:207], v[100:103]
	s_waitcnt lgkmcnt(10)
	v_mfma_f32_16x16x32_f16 v[104:107], v[184:187], v[192:195], v[104:107]
	v_mfma_f32_16x16x32_f16 v[108:111], v[184:187], v[196:199], v[108:111]
	v_mfma_f32_16x16x32_f16 v[112:115], v[184:187], v[200:203], v[112:115]
	v_mfma_f32_16x16x32_f16 v[116:119], v[184:187], v[204:207], v[116:119]
	s_add_u32 m0, s28, 0x13000
	s_nop 0
	global_load_lds_dwordx4 v13, s[4:5]
	s_waitcnt lgkmcnt(9)
	v_mfma_f32_16x16x32_f16 v[120:123], v[188:191], v[192:195], v[120:123]
	v_mfma_f32_16x16x32_f16 v[124:127], v[188:191], v[196:199], v[124:127]
	v_mfma_f32_16x16x32_f16 v[128:131], v[188:191], v[200:203], v[128:131]
	v_mfma_f32_16x16x32_f16 v[132:135], v[188:191], v[204:207], v[132:135]
	s_waitcnt lgkmcnt(6)
	ds_read_b128 v[172:175], v20
	ds_read_b128 v[192:195], v22
	ds_read_b128 v[196:199], v22 offset:2048
	ds_read_b128 v[200:203], v22 offset:4096
	ds_read_b128 v[204:207], v22 offset:6144
	ds_read_b128 v[176:179], v20 offset:2048
	ds_read_b128 v[180:183], v20 offset:4096
	ds_read_b128 v[184:187], v20 offset:6144
	ds_read_b128 v[188:191], v20 offset:8192
	v_mfma_f32_16x16x32_f16 v[56:59], v[136:139], v[156:159], v[56:59]
	s_add_u32 m0, s28, 0x15000
	s_nop 0
	global_load_lds_dwordx4 v14, s[4:5]
	s_add_u32 s4, s4, s20
	s_addc_u32 s5, s5, 0
	s_waitcnt lgkmcnt(15)
	v_mfma_f32_16x16x32_f16 v[60:63], v[136:139], v[160:163], v[60:63]
	s_waitcnt lgkmcnt(14)
	v_mfma_f32_16x16x32_f16 v[64:67], v[136:139], v[164:167], v[64:67]
	s_waitcnt lgkmcnt(13)
	v_mfma_f32_16x16x32_f16 v[68:71], v[136:139], v[168:171], v[68:71]
	s_waitcnt lgkmcnt(12)
	v_mfma_f32_16x16x32_f16 v[72:75], v[140:143], v[156:159], v[72:75]
	v_mfma_f32_16x16x32_f16 v[76:79], v[140:143], v[160:163], v[76:79]
	v_mfma_f32_16x16x32_f16 v[80:83], v[140:143], v[164:167], v[80:83]
	s_add_u32 m0, s28, 0x16000
	s_nop 0
	global_load_lds_dwordx4 v10, s[6:7]
	v_mfma_f32_16x16x32_f16 v[84:87], v[140:143], v[168:171], v[84:87]
	s_waitcnt lgkmcnt(11)
	v_mfma_f32_16x16x32_f16 v[88:91], v[144:147], v[156:159], v[88:91]
	v_mfma_f32_16x16x32_f16 v[92:95], v[144:147], v[160:163], v[92:95]
	v_mfma_f32_16x16x32_f16 v[96:99], v[144:147], v[164:167], v[96:99]
	v_mfma_f32_16x16x32_f16 v[100:103], v[144:147], v[168:171], v[100:103]
	s_waitcnt lgkmcnt(10)
	v_mfma_f32_16x16x32_f16 v[104:107], v[148:151], v[156:159], v[104:107]
	v_mfma_f32_16x16x32_f16 v[108:111], v[148:151], v[160:163], v[108:111]
	s_add_u32 m0, s28, 0x18000
	s_nop 0
	global_load_lds_dwordx4 v11, s[6:7]
	s_add_u32 s6, s6, s20
	s_addc_u32 s7, s7, 0
	v_mfma_f32_16x16x32_f16 v[112:115], v[148:151], v[164:167], v[112:115]
	v_mfma_f32_16x16x32_f16 v[116:119], v[148:151], v[168:171], v[116:119]
	s_waitcnt lgkmcnt(9)
	v_mfma_f32_16x16x32_f16 v[120:123], v[152:155], v[156:159], v[120:123]
	v_mfma_f32_16x16x32_f16 v[124:127], v[152:155], v[160:163], v[124:127]
	v_mfma_f32_16x16x32_f16 v[128:131], v[152:155], v[164:167], v[128:131]
	v_mfma_f32_16x16x32_f16 v[132:135], v[152:155], v[168:171], v[132:135]
	s_waitcnt vmcnt(7) lgkmcnt(0)
	s_barrier
	s_waitcnt lgkmcnt(6)
	ds_read_b128 v[136:139], v15
	ds_read_b128 v[156:159], v17
	ds_read_b128 v[160:163], v17 offset:2048
	ds_read_b128 v[164:167], v17 offset:4096
	ds_read_b128 v[168:171], v17 offset:6144
	ds_read_b128 v[140:143], v15 offset:2048
	ds_read_b128 v[144:147], v15 offset:4096
	ds_read_b128 v[148:151], v15 offset:6144
	ds_read_b128 v[152:155], v15 offset:8192
	v_mfma_f32_16x16x32_f16 v[56:59], v[172:175], v[192:195], v[56:59]
	s_add_u32 m0, s28, 0x1a000
	s_nop 0
	global_load_lds_dwordx4 v10, s[4:5]
	s_waitcnt lgkmcnt(15)
	v_mfma_f32_16x16x32_f16 v[60:63], v[172:175], v[196:199], v[60:63]
	s_waitcnt lgkmcnt(14)
	v_mfma_f32_16x16x32_f16 v[64:67], v[172:175], v[200:203], v[64:67]
	s_waitcnt lgkmcnt(13)
	v_mfma_f32_16x16x32_f16 v[68:71], v[172:175], v[204:207], v[68:71]
	s_waitcnt lgkmcnt(12)
	v_mfma_f32_16x16x32_f16 v[72:75], v[176:179], v[192:195], v[72:75]
	v_mfma_f32_16x16x32_f16 v[76:79], v[176:179], v[196:199], v[76:79]
	s_add_u32 m0, s28, 0x1c000
	s_nop 0
	global_load_lds_dwordx4 v11, s[4:5]
	v_mfma_f32_16x16x32_f16 v[80:83], v[176:179], v[200:203], v[80:83]
	v_mfma_f32_16x16x32_f16 v[84:87], v[176:179], v[204:207], v[84:87]
	s_waitcnt lgkmcnt(11)
	v_mfma_f32_16x16x32_f16 v[88:91], v[180:183], v[192:195], v[88:91]
	v_mfma_f32_16x16x32_f16 v[92:95], v[180:183], v[196:199], v[92:95]
	v_mfma_f32_16x16x32_f16 v[96:99], v[180:183], v[200:203], v[96:99]
	s_add_u32 m0, s28, 0x1e000
	s_nop 0
	global_load_lds_dwordx4 v12, s[4:5]
	v_mfma_f32_16x16x32_f16 v[100:103], v[180:183], v[204:207], v[100:103]
	s_waitcnt lgkmcnt(10)
	v_mfma_f32_16x16x32_f16 v[104:107], v[184:187], v[192:195], v[104:107]
	v_mfma_f32_16x16x32_f16 v[108:111], v[184:187], v[196:199], v[108:111]
	v_mfma_f32_16x16x32_f16 v[112:115], v[184:187], v[200:203], v[112:115]
	v_mfma_f32_16x16x32_f16 v[116:119], v[184:187], v[204:207], v[116:119]
	s_add_u32 m0, s28, 0x20000
	s_nop 0
	global_load_lds_dwordx4 v13, s[4:5]
	s_waitcnt lgkmcnt(9)
	v_mfma_f32_16x16x32_f16 v[120:123], v[188:191], v[192:195], v[120:123]
	v_mfma_f32_16x16x32_f16 v[124:127], v[188:191], v[196:199], v[124:127]
	v_mfma_f32_16x16x32_f16 v[128:131], v[188:191], v[200:203], v[128:131]
	v_mfma_f32_16x16x32_f16 v[132:135], v[188:191], v[204:207], v[132:135]
	s_waitcnt lgkmcnt(6)
	ds_read_b128 v[172:175], v16
	ds_read_b128 v[192:195], v18
	ds_read_b128 v[196:199], v18 offset:2048
	ds_read_b128 v[200:203], v18 offset:4096
	ds_read_b128 v[204:207], v18 offset:6144
	ds_read_b128 v[176:179], v16 offset:2048
	ds_read_b128 v[180:183], v16 offset:4096
	ds_read_b128 v[184:187], v16 offset:6144
	ds_read_b128 v[188:191], v16 offset:8192
	v_mfma_f32_16x16x32_f16 v[56:59], v[136:139], v[156:159], v[56:59]
	s_add_u32 m0, s28, 0x22000
	s_nop 0
	global_load_lds_dwordx4 v14, s[4:5]
	s_add_u32 s4, s4, s20
	s_addc_u32 s5, s5, 0
	s_waitcnt lgkmcnt(15)
	v_mfma_f32_16x16x32_f16 v[60:63], v[136:139], v[160:163], v[60:63]
	s_waitcnt lgkmcnt(14)
	v_mfma_f32_16x16x32_f16 v[64:67], v[136:139], v[164:167], v[64:67]
	s_waitcnt lgkmcnt(13)
	v_mfma_f32_16x16x32_f16 v[68:71], v[136:139], v[168:171], v[68:71]
	s_waitcnt lgkmcnt(12)
	v_mfma_f32_16x16x32_f16 v[72:75], v[140:143], v[156:159], v[72:75]
	v_mfma_f32_16x16x32_f16 v[76:79], v[140:143], v[160:163], v[76:79]
	v_mfma_f32_16x16x32_f16 v[80:83], v[140:143], v[164:167], v[80:83]
	s_add_u32 m0, s28, 0x23000
	s_nop 0
	global_load_lds_dwordx4 v10, s[6:7]
	v_mfma_f32_16x16x32_f16 v[84:87], v[140:143], v[168:171], v[84:87]
	s_waitcnt lgkmcnt(11)
	v_mfma_f32_16x16x32_f16 v[88:91], v[144:147], v[156:159], v[88:91]
	v_mfma_f32_16x16x32_f16 v[92:95], v[144:147], v[160:163], v[92:95]
	v_mfma_f32_16x16x32_f16 v[96:99], v[144:147], v[164:167], v[96:99]
	v_mfma_f32_16x16x32_f16 v[100:103], v[144:147], v[168:171], v[100:103]
	s_waitcnt lgkmcnt(10)
	v_mfma_f32_16x16x32_f16 v[104:107], v[148:151], v[156:159], v[104:107]
	v_mfma_f32_16x16x32_f16 v[108:111], v[148:151], v[160:163], v[108:111]
	s_add_u32 m0, s28, 0x25000
	s_nop 0
	global_load_lds_dwordx4 v11, s[6:7]
	s_add_u32 s6, s6, s20
	s_addc_u32 s7, s7, 0
	v_mfma_f32_16x16x32_f16 v[112:115], v[148:151], v[164:167], v[112:115]
	v_mfma_f32_16x16x32_f16 v[116:119], v[148:151], v[168:171], v[116:119]
	s_waitcnt lgkmcnt(9)
	v_mfma_f32_16x16x32_f16 v[120:123], v[152:155], v[156:159], v[120:123]
	v_mfma_f32_16x16x32_f16 v[124:127], v[152:155], v[160:163], v[124:127]
	v_mfma_f32_16x16x32_f16 v[128:131], v[152:155], v[164:167], v[128:131]
	v_mfma_f32_16x16x32_f16 v[132:135], v[152:155], v[168:171], v[132:135]
	s_waitcnt vmcnt(7) lgkmcnt(0)
	s_barrier
	s_waitcnt lgkmcnt(6)
	ds_read_b128 v[136:139], v15 offset:53248
	ds_read_b128 v[156:159], v17 offset:53248
	ds_read_b128 v[160:163], v17 offset:55296
	ds_read_b128 v[164:167], v17 offset:57344
	ds_read_b128 v[168:171], v17 offset:59392
	ds_read_b128 v[140:143], v15 offset:55296
	ds_read_b128 v[144:147], v15 offset:57344
	ds_read_b128 v[148:151], v15 offset:59392
	ds_read_b128 v[152:155], v15 offset:61440
	v_mfma_f32_16x16x32_f16 v[56:59], v[172:175], v[192:195], v[56:59]
	s_add_u32 m0, s28, 0x0
	s_nop 0
	global_load_lds_dwordx4 v10, s[4:5]
	s_waitcnt lgkmcnt(15)
	v_mfma_f32_16x16x32_f16 v[60:63], v[172:175], v[196:199], v[60:63]
	s_waitcnt lgkmcnt(14)
	v_mfma_f32_16x16x32_f16 v[64:67], v[172:175], v[200:203], v[64:67]
	s_waitcnt lgkmcnt(13)
	v_mfma_f32_16x16x32_f16 v[68:71], v[172:175], v[204:207], v[68:71]
	s_waitcnt lgkmcnt(12)
	v_mfma_f32_16x16x32_f16 v[72:75], v[176:179], v[192:195], v[72:75]
	v_mfma_f32_16x16x32_f16 v[76:79], v[176:179], v[196:199], v[76:79]
	s_add_u32 m0, s28, 0x2000
	s_nop 0
	global_load_lds_dwordx4 v11, s[4:5]
	v_mfma_f32_16x16x32_f16 v[80:83], v[176:179], v[200:203], v[80:83]
	v_mfma_f32_16x16x32_f16 v[84:87], v[176:179], v[204:207], v[84:87]
	s_waitcnt lgkmcnt(11)
	v_mfma_f32_16x16x32_f16 v[88:91], v[180:183], v[192:195], v[88:91]
	v_mfma_f32_16x16x32_f16 v[92:95], v[180:183], v[196:199], v[92:95]
	v_mfma_f32_16x16x32_f16 v[96:99], v[180:183], v[200:203], v[96:99]
	s_add_u32 m0, s28, 0x4000
	s_nop 0
	global_load_lds_dwordx4 v12, s[4:5]
	v_mfma_f32_16x16x32_f16 v[100:103], v[180:183], v[204:207], v[100:103]
	s_waitcnt lgkmcnt(10)
	v_mfma_f32_16x16x32_f16 v[104:107], v[184:187], v[192:195], v[104:107]
	v_mfma_f32_16x16x32_f16 v[108:111], v[184:187], v[196:199], v[108:111]
	v_mfma_f32_16x16x32_f16 v[112:115], v[184:187], v[200:203], v[112:115]
	v_mfma_f32_16x16x32_f16 v[116:119], v[184:187], v[204:207], v[116:119]
	s_add_u32 m0, s28, 0x6000
	s_nop 0
	global_load_lds_dwordx4 v13, s[4:5]
	s_waitcnt lgkmcnt(9)
	v_mfma_f32_16x16x32_f16 v[120:123], v[188:191], v[192:195], v[120:123]
	v_mfma_f32_16x16x32_f16 v[124:127], v[188:191], v[196:199], v[124:127]
	v_mfma_f32_16x16x32_f16 v[128:131], v[188:191], v[200:203], v[128:131]
	v_mfma_f32_16x16x32_f16 v[132:135], v[188:191], v[204:207], v[132:135]
	s_waitcnt lgkmcnt(6)
	ds_read_b128 v[172:175], v16 offset:53248
	ds_read_b128 v[192:195], v18 offset:53248
	ds_read_b128 v[196:199], v18 offset:55296
	ds_read_b128 v[200:203], v18 offset:57344
	ds_read_b128 v[204:207], v18 offset:59392
	ds_read_b128 v[176:179], v16 offset:55296
	ds_read_b128 v[180:183], v16 offset:57344
	ds_read_b128 v[184:187], v16 offset:59392
	ds_read_b128 v[188:191], v16 offset:61440
	v_mfma_f32_16x16x32_f16 v[56:59], v[136:139], v[156:159], v[56:59]
	s_add_u32 m0, s28, 0x8000
	s_nop 0
	global_load_lds_dwordx4 v14, s[4:5]
	s_add_u32 s4, s4, s20
	s_addc_u32 s5, s5, 0
	s_waitcnt lgkmcnt(15)
	v_mfma_f32_16x16x32_f16 v[60:63], v[136:139], v[160:163], v[60:63]
	s_waitcnt lgkmcnt(14)
	v_mfma_f32_16x16x32_f16 v[64:67], v[136:139], v[164:167], v[64:67]
	s_waitcnt lgkmcnt(13)
	v_mfma_f32_16x16x32_f16 v[68:71], v[136:139], v[168:171], v[68:71]
	s_waitcnt lgkmcnt(12)
	v_mfma_f32_16x16x32_f16 v[72:75], v[140:143], v[156:159], v[72:75]
	v_mfma_f32_16x16x32_f16 v[76:79], v[140:143], v[160:163], v[76:79]
	v_mfma_f32_16x16x32_f16 v[80:83], v[140:143], v[164:167], v[80:83]
	s_add_u32 m0, s28, 0x9000
	s_nop 0
	global_load_lds_dwordx4 v10, s[6:7]
	v_mfma_f32_16x16x32_f16 v[84:87], v[140:143], v[168:171], v[84:87]
	s_waitcnt lgkmcnt(11)
	v_mfma_f32_16x16x32_f16 v[88:91], v[144:147], v[156:159], v[88:91]
	v_mfma_f32_16x16x32_f16 v[92:95], v[144:147], v[160:163], v[92:95]
	v_mfma_f32_16x16x32_f16 v[96:99], v[144:147], v[164:167], v[96:99]
	v_mfma_f32_16x16x32_f16 v[100:103], v[144:147], v[168:171], v[100:103]
	s_waitcnt lgkmcnt(10)
	v_mfma_f32_16x16x32_f16 v[104:107], v[148:151], v[156:159], v[104:107]
	v_mfma_f32_16x16x32_f16 v[108:111], v[148:151], v[160:163], v[108:111]
	s_add_u32 m0, s28, 0xb000
	s_nop 0
	global_load_lds_dwordx4 v11, s[6:7]
	s_add_u32 s6, s6, s20
	s_addc_u32 s7, s7, 0
	v_mfma_f32_16x16x32_f16 v[112:115], v[148:151], v[164:167], v[112:115]
	v_mfma_f32_16x16x32_f16 v[116:119], v[148:151], v[168:171], v[116:119]
	s_waitcnt lgkmcnt(9)
	v_mfma_f32_16x16x32_f16 v[120:123], v[152:155], v[156:159], v[120:123]
	v_mfma_f32_16x16x32_f16 v[124:127], v[152:155], v[160:163], v[124:127]
	v_mfma_f32_16x16x32_f16 v[128:131], v[152:155], v[164:167], v[128:131]
	v_mfma_f32_16x16x32_f16 v[132:135], v[152:155], v[168:171], v[132:135]
	s_waitcnt vmcnt(7) lgkmcnt(0)
	s_barrier
	s_waitcnt lgkmcnt(6)
	ds_read_b128 v[136:139], v19
	ds_read_b128 v[156:159], v21
	ds_read_b128 v[160:163], v21 offset:2048
	ds_read_b128 v[164:167], v21 offset:4096
	ds_read_b128 v[168:171], v21 offset:6144
	ds_read_b128 v[140:143], v19 offset:2048
	ds_read_b128 v[144:147], v19 offset:4096
	ds_read_b128 v[148:151], v19 offset:6144
	ds_read_b128 v[152:155], v19 offset:8192
	v_mfma_f32_16x16x32_f16 v[56:59], v[172:175], v[192:195], v[56:59]
	s_add_u32 m0, s28, 0xd000
	s_nop 0
	global_load_lds_dwordx4 v10, s[4:5]
	s_waitcnt lgkmcnt(15)
	v_mfma_f32_16x16x32_f16 v[60:63], v[172:175], v[196:199], v[60:63]
	s_waitcnt lgkmcnt(14)
	v_mfma_f32_16x16x32_f16 v[64:67], v[172:175], v[200:203], v[64:67]
	s_waitcnt lgkmcnt(13)
	v_mfma_f32_16x16x32_f16 v[68:71], v[172:175], v[204:207], v[68:71]
	s_waitcnt lgkmcnt(12)
	v_mfma_f32_16x16x32_f16 v[72:75], v[176:179], v[192:195], v[72:75]
	v_mfma_f32_16x16x32_f16 v[76:79], v[176:179], v[196:199], v[76:79]
	s_add_u32 m0, s28, 0xf000
	s_nop 0
	global_load_lds_dwordx4 v11, s[4:5]
	v_mfma_f32_16x16x32_f16 v[80:83], v[176:179], v[200:203], v[80:83]
	v_mfma_f32_16x16x32_f16 v[84:87], v[176:179], v[204:207], v[84:87]
	s_waitcnt lgkmcnt(11)
	v_mfma_f32_16x16x32_f16 v[88:91], v[180:183], v[192:195], v[88:91]
	v_mfma_f32_16x16x32_f16 v[92:95], v[180:183], v[196:199], v[92:95]
	v_mfma_f32_16x16x32_f16 v[96:99], v[180:183], v[200:203], v[96:99]
	s_add_u32 m0, s28, 0x11000
	s_nop 0
	global_load_lds_dwordx4 v12, s[4:5]
	v_mfma_f32_16x16x32_f16 v[100:103], v[180:183], v[204:207], v[100:103]
	s_waitcnt lgkmcnt(10)
	v_mfma_f32_16x16x32_f16 v[104:107], v[184:187], v[192:195], v[104:107]
	v_mfma_f32_16x16x32_f16 v[108:111], v[184:187], v[196:199], v[108:111]
	v_mfma_f32_16x16x32_f16 v[112:115], v[184:187], v[200:203], v[112:115]
	v_mfma_f32_16x16x32_f16 v[116:119], v[184:187], v[204:207], v[116:119]
	s_add_u32 m0, s28, 0x13000
	s_nop 0
	global_load_lds_dwordx4 v13, s[4:5]
	s_waitcnt lgkmcnt(9)
	v_mfma_f32_16x16x32_f16 v[120:123], v[188:191], v[192:195], v[120:123]
	v_mfma_f32_16x16x32_f16 v[124:127], v[188:191], v[196:199], v[124:127]
	v_mfma_f32_16x16x32_f16 v[128:131], v[188:191], v[200:203], v[128:131]
	v_mfma_f32_16x16x32_f16 v[132:135], v[188:191], v[204:207], v[132:135]
	s_waitcnt lgkmcnt(6)
	ds_read_b128 v[172:175], v20
	ds_read_b128 v[192:195], v22
	ds_read_b128 v[196:199], v22 offset:2048
	ds_read_b128 v[200:203], v22 offset:4096
	ds_read_b128 v[204:207], v22 offset:6144
	ds_read_b128 v[176:179], v20 offset:2048
	ds_read_b128 v[180:183], v20 offset:4096
	ds_read_b128 v[184:187], v20 offset:6144
	ds_read_b128 v[188:191], v20 offset:8192
	v_mfma_f32_16x16x32_f16 v[56:59], v[136:139], v[156:159], v[56:59]
	s_add_u32 m0, s28, 0x15000
	s_nop 0
	global_load_lds_dwordx4 v14, s[4:5]
	s_add_u32 s4, s4, s20
	s_addc_u32 s5, s5, 0
	s_waitcnt lgkmcnt(15)
	v_mfma_f32_16x16x32_f16 v[60:63], v[136:139], v[160:163], v[60:63]
	s_waitcnt lgkmcnt(14)
	v_mfma_f32_16x16x32_f16 v[64:67], v[136:139], v[164:167], v[64:67]
	s_waitcnt lgkmcnt(13)
	v_mfma_f32_16x16x32_f16 v[68:71], v[136:139], v[168:171], v[68:71]
	s_waitcnt lgkmcnt(12)
	v_mfma_f32_16x16x32_f16 v[72:75], v[140:143], v[156:159], v[72:75]
	v_mfma_f32_16x16x32_f16 v[76:79], v[140:143], v[160:163], v[76:79]
	v_mfma_f32_16x16x32_f16 v[80:83], v[140:143], v[164:167], v[80:83]
	s_add_u32 m0, s28, 0x16000
	s_nop 0
	global_load_lds_dwordx4 v10, s[6:7]
	v_mfma_f32_16x16x32_f16 v[84:87], v[140:143], v[168:171], v[84:87]
	s_waitcnt lgkmcnt(11)
	v_mfma_f32_16x16x32_f16 v[88:91], v[144:147], v[156:159], v[88:91]
	v_mfma_f32_16x16x32_f16 v[92:95], v[144:147], v[160:163], v[92:95]
	v_mfma_f32_16x16x32_f16 v[96:99], v[144:147], v[164:167], v[96:99]
	v_mfma_f32_16x16x32_f16 v[100:103], v[144:147], v[168:171], v[100:103]
	s_waitcnt lgkmcnt(10)
	v_mfma_f32_16x16x32_f16 v[104:107], v[148:151], v[156:159], v[104:107]
	v_mfma_f32_16x16x32_f16 v[108:111], v[148:151], v[160:163], v[108:111]
	s_add_u32 m0, s28, 0x18000
	s_nop 0
	global_load_lds_dwordx4 v11, s[6:7]
	s_add_u32 s6, s6, s20
	s_addc_u32 s7, s7, 0
	v_mfma_f32_16x16x32_f16 v[112:115], v[148:151], v[164:167], v[112:115]
	v_mfma_f32_16x16x32_f16 v[116:119], v[148:151], v[168:171], v[116:119]
	s_waitcnt lgkmcnt(9)
	v_mfma_f32_16x16x32_f16 v[120:123], v[152:155], v[156:159], v[120:123]
	v_mfma_f32_16x16x32_f16 v[124:127], v[152:155], v[160:163], v[124:127]
	v_mfma_f32_16x16x32_f16 v[128:131], v[152:155], v[164:167], v[128:131]
	v_mfma_f32_16x16x32_f16 v[132:135], v[152:155], v[168:171], v[132:135]
	s_waitcnt vmcnt(7) lgkmcnt(0)
	s_barrier
	s_waitcnt lgkmcnt(6)
	ds_read_b128 v[136:139], v15
	ds_read_b128 v[156:159], v17
	ds_read_b128 v[160:163], v17 offset:2048
	ds_read_b128 v[164:167], v17 offset:4096
	ds_read_b128 v[168:171], v17 offset:6144
	ds_read_b128 v[140:143], v15 offset:2048
	ds_read_b128 v[144:147], v15 offset:4096
	ds_read_b128 v[148:151], v15 offset:6144
	ds_read_b128 v[152:155], v15 offset:8192
	v_mfma_f32_16x16x32_f16 v[56:59], v[172:175], v[192:195], v[56:59]
	s_add_u32 m0, s28, 0x1a000
	s_nop 0
	global_load_lds_dwordx4 v10, s[4:5]
	s_waitcnt lgkmcnt(15)
	v_mfma_f32_16x16x32_f16 v[60:63], v[172:175], v[196:199], v[60:63]
	s_waitcnt lgkmcnt(14)
	v_mfma_f32_16x16x32_f16 v[64:67], v[172:175], v[200:203], v[64:67]
	s_waitcnt lgkmcnt(13)
	v_mfma_f32_16x16x32_f16 v[68:71], v[172:175], v[204:207], v[68:71]
	s_waitcnt lgkmcnt(12)
	v_mfma_f32_16x16x32_f16 v[72:75], v[176:179], v[192:195], v[72:75]
	v_mfma_f32_16x16x32_f16 v[76:79], v[176:179], v[196:199], v[76:79]
	s_add_u32 m0, s28, 0x1c000
	s_nop 0
	global_load_lds_dwordx4 v11, s[4:5]
	v_mfma_f32_16x16x32_f16 v[80:83], v[176:179], v[200:203], v[80:83]
	v_mfma_f32_16x16x32_f16 v[84:87], v[176:179], v[204:207], v[84:87]
	s_waitcnt lgkmcnt(11)
	v_mfma_f32_16x16x32_f16 v[88:91], v[180:183], v[192:195], v[88:91]
	v_mfma_f32_16x16x32_f16 v[92:95], v[180:183], v[196:199], v[92:95]
	v_mfma_f32_16x16x32_f16 v[96:99], v[180:183], v[200:203], v[96:99]
	s_add_u32 m0, s28, 0x1e000
	s_nop 0
	global_load_lds_dwordx4 v12, s[4:5]
	v_mfma_f32_16x16x32_f16 v[100:103], v[180:183], v[204:207], v[100:103]
	s_waitcnt lgkmcnt(10)
	v_mfma_f32_16x16x32_f16 v[104:107], v[184:187], v[192:195], v[104:107]
	v_mfma_f32_16x16x32_f16 v[108:111], v[184:187], v[196:199], v[108:111]
	v_mfma_f32_16x16x32_f16 v[112:115], v[184:187], v[200:203], v[112:115]
	v_mfma_f32_16x16x32_f16 v[116:119], v[184:187], v[204:207], v[116:119]
	s_add_u32 m0, s28, 0x20000
	s_nop 0
	global_load_lds_dwordx4 v13, s[4:5]
	s_waitcnt lgkmcnt(9)
	v_mfma_f32_16x16x32_f16 v[120:123], v[188:191], v[192:195], v[120:123]
	v_mfma_f32_16x16x32_f16 v[124:127], v[188:191], v[196:199], v[124:127]
	v_mfma_f32_16x16x32_f16 v[128:131], v[188:191], v[200:203], v[128:131]
	v_mfma_f32_16x16x32_f16 v[132:135], v[188:191], v[204:207], v[132:135]
	s_waitcnt lgkmcnt(6)
	ds_read_b128 v[172:175], v16
	ds_read_b128 v[192:195], v18
	ds_read_b128 v[196:199], v18 offset:2048
	ds_read_b128 v[200:203], v18 offset:4096
	ds_read_b128 v[204:207], v18 offset:6144
	ds_read_b128 v[176:179], v16 offset:2048
	ds_read_b128 v[180:183], v16 offset:4096
	ds_read_b128 v[184:187], v16 offset:6144
	ds_read_b128 v[188:191], v16 offset:8192
	v_mfma_f32_16x16x32_f16 v[56:59], v[136:139], v[156:159], v[56:59]
	s_add_u32 m0, s28, 0x22000
	s_nop 0
	global_load_lds_dwordx4 v14, s[4:5]
	s_add_u32 s4, s4, s20
	s_addc_u32 s5, s5, 0
	s_waitcnt lgkmcnt(15)
	v_mfma_f32_16x16x32_f16 v[60:63], v[136:139], v[160:163], v[60:63]
	s_waitcnt lgkmcnt(14)
	v_mfma_f32_16x16x32_f16 v[64:67], v[136:139], v[164:167], v[64:67]
	s_waitcnt lgkmcnt(13)
	v_mfma_f32_16x16x32_f16 v[68:71], v[136:139], v[168:171], v[68:71]
	s_waitcnt lgkmcnt(12)
	v_mfma_f32_16x16x32_f16 v[72:75], v[140:143], v[156:159], v[72:75]
	v_mfma_f32_16x16x32_f16 v[76:79], v[140:143], v[160:163], v[76:79]
	v_mfma_f32_16x16x32_f16 v[80:83], v[140:143], v[164:167], v[80:83]
	s_add_u32 m0, s28, 0x23000
	s_nop 0
	global_load_lds_dwordx4 v10, s[6:7]
	v_mfma_f32_16x16x32_f16 v[84:87], v[140:143], v[168:171], v[84:87]
	s_waitcnt lgkmcnt(11)
	v_mfma_f32_16x16x32_f16 v[88:91], v[144:147], v[156:159], v[88:91]
	v_mfma_f32_16x16x32_f16 v[92:95], v[144:147], v[160:163], v[92:95]
	v_mfma_f32_16x16x32_f16 v[96:99], v[144:147], v[164:167], v[96:99]
	v_mfma_f32_16x16x32_f16 v[100:103], v[144:147], v[168:171], v[100:103]
	s_waitcnt lgkmcnt(10)
	v_mfma_f32_16x16x32_f16 v[104:107], v[148:151], v[156:159], v[104:107]
	v_mfma_f32_16x16x32_f16 v[108:111], v[148:151], v[160:163], v[108:111]
	s_add_u32 m0, s28, 0x25000
	s_nop 0
	global_load_lds_dwordx4 v11, s[6:7]
	s_add_u32 s6, s6, s20
	s_addc_u32 s7, s7, 0
	v_mfma_f32_16x16x32_f16 v[112:115], v[148:151], v[164:167], v[112:115]
	v_mfma_f32_16x16x32_f16 v[116:119], v[148:151], v[168:171], v[116:119]
	s_waitcnt lgkmcnt(9)
	v_mfma_f32_16x16x32_f16 v[120:123], v[152:155], v[156:159], v[120:123]
	v_mfma_f32_16x16x32_f16 v[124:127], v[152:155], v[160:163], v[124:127]
	v_mfma_f32_16x16x32_f16 v[128:131], v[152:155], v[164:167], v[128:131]
	v_mfma_f32_16x16x32_f16 v[132:135], v[152:155], v[168:171], v[132:135]
	s_waitcnt vmcnt(7) lgkmcnt(0)
	s_barrier
	s_waitcnt lgkmcnt(6)
	ds_read_b128 v[136:139], v15 offset:53248
	ds_read_b128 v[156:159], v17 offset:53248
	ds_read_b128 v[160:163], v17 offset:55296
	ds_read_b128 v[164:167], v17 offset:57344
	ds_read_b128 v[168:171], v17 offset:59392
	ds_read_b128 v[140:143], v15 offset:55296
	ds_read_b128 v[144:147], v15 offset:57344
	ds_read_b128 v[148:151], v15 offset:59392
	ds_read_b128 v[152:155], v15 offset:61440
	v_mfma_f32_16x16x32_f16 v[56:59], v[172:175], v[192:195], v[56:59]
	s_add_u32 m0, s28, 0x0
	s_nop 0
	global_load_lds_dwordx4 v10, s[4:5]
	s_waitcnt lgkmcnt(15)
	v_mfma_f32_16x16x32_f16 v[60:63], v[172:175], v[196:199], v[60:63]
	s_waitcnt lgkmcnt(14)
	v_mfma_f32_16x16x32_f16 v[64:67], v[172:175], v[200:203], v[64:67]
	s_waitcnt lgkmcnt(13)
	v_mfma_f32_16x16x32_f16 v[68:71], v[172:175], v[204:207], v[68:71]
	s_waitcnt lgkmcnt(12)
	v_mfma_f32_16x16x32_f16 v[72:75], v[176:179], v[192:195], v[72:75]
	v_mfma_f32_16x16x32_f16 v[76:79], v[176:179], v[196:199], v[76:79]
	s_add_u32 m0, s28, 0x2000
	s_nop 0
	global_load_lds_dwordx4 v11, s[4:5]
	v_mfma_f32_16x16x32_f16 v[80:83], v[176:179], v[200:203], v[80:83]
	v_mfma_f32_16x16x32_f16 v[84:87], v[176:179], v[204:207], v[84:87]
	s_waitcnt lgkmcnt(11)
	v_mfma_f32_16x16x32_f16 v[88:91], v[180:183], v[192:195], v[88:91]
	v_mfma_f32_16x16x32_f16 v[92:95], v[180:183], v[196:199], v[92:95]
	v_mfma_f32_16x16x32_f16 v[96:99], v[180:183], v[200:203], v[96:99]
	s_add_u32 m0, s28, 0x4000
	s_nop 0
	global_load_lds_dwordx4 v12, s[4:5]
	v_mfma_f32_16x16x32_f16 v[100:103], v[180:183], v[204:207], v[100:103]
	s_waitcnt lgkmcnt(10)
	v_mfma_f32_16x16x32_f16 v[104:107], v[184:187], v[192:195], v[104:107]
	v_mfma_f32_16x16x32_f16 v[108:111], v[184:187], v[196:199], v[108:111]
	v_mfma_f32_16x16x32_f16 v[112:115], v[184:187], v[200:203], v[112:115]
	v_mfma_f32_16x16x32_f16 v[116:119], v[184:187], v[204:207], v[116:119]
	s_add_u32 m0, s28, 0x6000
	s_nop 0
	global_load_lds_dwordx4 v13, s[4:5]
	s_waitcnt lgkmcnt(9)
	v_mfma_f32_16x16x32_f16 v[120:123], v[188:191], v[192:195], v[120:123]
	v_mfma_f32_16x16x32_f16 v[124:127], v[188:191], v[196:199], v[124:127]
	v_mfma_f32_16x16x32_f16 v[128:131], v[188:191], v[200:203], v[128:131]
	v_mfma_f32_16x16x32_f16 v[132:135], v[188:191], v[204:207], v[132:135]
	s_waitcnt lgkmcnt(6)
	ds_read_b128 v[172:175], v16 offset:53248
	ds_read_b128 v[192:195], v18 offset:53248
	ds_read_b128 v[196:199], v18 offset:55296
	ds_read_b128 v[200:203], v18 offset:57344
	ds_read_b128 v[204:207], v18 offset:59392
	ds_read_b128 v[176:179], v16 offset:55296
	ds_read_b128 v[180:183], v16 offset:57344
	ds_read_b128 v[184:187], v16 offset:59392
	ds_read_b128 v[188:191], v16 offset:61440
	v_mfma_f32_16x16x32_f16 v[56:59], v[136:139], v[156:159], v[56:59]
	s_add_u32 m0, s28, 0x8000
	s_nop 0
	global_load_lds_dwordx4 v14, s[4:5]
	s_add_u32 s4, s4, s20
	s_addc_u32 s5, s5, 0
	s_waitcnt lgkmcnt(15)
	v_mfma_f32_16x16x32_f16 v[60:63], v[136:139], v[160:163], v[60:63]
	s_waitcnt lgkmcnt(14)
	v_mfma_f32_16x16x32_f16 v[64:67], v[136:139], v[164:167], v[64:67]
	s_waitcnt lgkmcnt(13)
	v_mfma_f32_16x16x32_f16 v[68:71], v[136:139], v[168:171], v[68:71]
	s_waitcnt lgkmcnt(12)
	v_mfma_f32_16x16x32_f16 v[72:75], v[140:143], v[156:159], v[72:75]
	v_mfma_f32_16x16x32_f16 v[76:79], v[140:143], v[160:163], v[76:79]
	v_mfma_f32_16x16x32_f16 v[80:83], v[140:143], v[164:167], v[80:83]
	s_add_u32 m0, s28, 0x9000
	s_nop 0
	global_load_lds_dwordx4 v10, s[6:7]
	v_mfma_f32_16x16x32_f16 v[84:87], v[140:143], v[168:171], v[84:87]
	s_waitcnt lgkmcnt(11)
	v_mfma_f32_16x16x32_f16 v[88:91], v[144:147], v[156:159], v[88:91]
	v_mfma_f32_16x16x32_f16 v[92:95], v[144:147], v[160:163], v[92:95]
	v_mfma_f32_16x16x32_f16 v[96:99], v[144:147], v[164:167], v[96:99]
	v_mfma_f32_16x16x32_f16 v[100:103], v[144:147], v[168:171], v[100:103]
	s_waitcnt lgkmcnt(10)
	v_mfma_f32_16x16x32_f16 v[104:107], v[148:151], v[156:159], v[104:107]
	v_mfma_f32_16x16x32_f16 v[108:111], v[148:151], v[160:163], v[108:111]
	s_add_u32 m0, s28, 0xb000
	s_nop 0
	global_load_lds_dwordx4 v11, s[6:7]
	s_add_u32 s6, s6, s20
	s_addc_u32 s7, s7, 0
	v_mfma_f32_16x16x32_f16 v[112:115], v[148:151], v[164:167], v[112:115]
	v_mfma_f32_16x16x32_f16 v[116:119], v[148:151], v[168:171], v[116:119]
	s_waitcnt lgkmcnt(9)
	v_mfma_f32_16x16x32_f16 v[120:123], v[152:155], v[156:159], v[120:123]
	v_mfma_f32_16x16x32_f16 v[124:127], v[152:155], v[160:163], v[124:127]
	v_mfma_f32_16x16x32_f16 v[128:131], v[152:155], v[164:167], v[128:131]
	v_mfma_f32_16x16x32_f16 v[132:135], v[152:155], v[168:171], v[132:135]
	s_waitcnt vmcnt(7) lgkmcnt(0)
	s_barrier
	s_waitcnt lgkmcnt(6)
	ds_read_b128 v[136:139], v19
	ds_read_b128 v[156:159], v21
	ds_read_b128 v[160:163], v21 offset:2048
	ds_read_b128 v[164:167], v21 offset:4096
	ds_read_b128 v[168:171], v21 offset:6144
	ds_read_b128 v[140:143], v19 offset:2048
	ds_read_b128 v[144:147], v19 offset:4096
	ds_read_b128 v[148:151], v19 offset:6144
	ds_read_b128 v[152:155], v19 offset:8192
	v_mfma_f32_16x16x32_f16 v[56:59], v[172:175], v[192:195], v[56:59]
	s_add_u32 m0, s28, 0xd000
	s_nop 0
	global_load_lds_dwordx4 v10, s[4:5]
	s_waitcnt lgkmcnt(15)
	v_mfma_f32_16x16x32_f16 v[60:63], v[172:175], v[196:199], v[60:63]
	s_waitcnt lgkmcnt(14)
	v_mfma_f32_16x16x32_f16 v[64:67], v[172:175], v[200:203], v[64:67]
	s_waitcnt lgkmcnt(13)
	v_mfma_f32_16x16x32_f16 v[68:71], v[172:175], v[204:207], v[68:71]
	s_waitcnt lgkmcnt(12)
	v_mfma_f32_16x16x32_f16 v[72:75], v[176:179], v[192:195], v[72:75]
	v_mfma_f32_16x16x32_f16 v[76:79], v[176:179], v[196:199], v[76:79]
	s_add_u32 m0, s28, 0xf000
	s_nop 0
	global_load_lds_dwordx4 v11, s[4:5]
	v_mfma_f32_16x16x32_f16 v[80:83], v[176:179], v[200:203], v[80:83]
	v_mfma_f32_16x16x32_f16 v[84:87], v[176:179], v[204:207], v[84:87]
	s_waitcnt lgkmcnt(11)
	v_mfma_f32_16x16x32_f16 v[88:91], v[180:183], v[192:195], v[88:91]
	v_mfma_f32_16x16x32_f16 v[92:95], v[180:183], v[196:199], v[92:95]
	v_mfma_f32_16x16x32_f16 v[96:99], v[180:183], v[200:203], v[96:99]
	s_add_u32 m0, s28, 0x11000
	s_nop 0
	global_load_lds_dwordx4 v12, s[4:5]
	v_mfma_f32_16x16x32_f16 v[100:103], v[180:183], v[204:207], v[100:103]
	s_waitcnt lgkmcnt(10)
	v_mfma_f32_16x16x32_f16 v[104:107], v[184:187], v[192:195], v[104:107]
	v_mfma_f32_16x16x32_f16 v[108:111], v[184:187], v[196:199], v[108:111]
	v_mfma_f32_16x16x32_f16 v[112:115], v[184:187], v[200:203], v[112:115]
	v_mfma_f32_16x16x32_f16 v[116:119], v[184:187], v[204:207], v[116:119]
	s_add_u32 m0, s28, 0x13000
	s_nop 0
	global_load_lds_dwordx4 v13, s[4:5]
	s_waitcnt lgkmcnt(9)
	v_mfma_f32_16x16x32_f16 v[120:123], v[188:191], v[192:195], v[120:123]
	v_mfma_f32_16x16x32_f16 v[124:127], v[188:191], v[196:199], v[124:127]
	v_mfma_f32_16x16x32_f16 v[128:131], v[188:191], v[200:203], v[128:131]
	v_mfma_f32_16x16x32_f16 v[132:135], v[188:191], v[204:207], v[132:135]
	s_waitcnt lgkmcnt(6)
	ds_read_b128 v[172:175], v20
	ds_read_b128 v[192:195], v22
	ds_read_b128 v[196:199], v22 offset:2048
	ds_read_b128 v[200:203], v22 offset:4096
	ds_read_b128 v[204:207], v22 offset:6144
	ds_read_b128 v[176:179], v20 offset:2048
	ds_read_b128 v[180:183], v20 offset:4096
	ds_read_b128 v[184:187], v20 offset:6144
	ds_read_b128 v[188:191], v20 offset:8192
	v_mfma_f32_16x16x32_f16 v[56:59], v[136:139], v[156:159], v[56:59]
	s_add_u32 m0, s28, 0x15000
	s_nop 0
	global_load_lds_dwordx4 v14, s[4:5]
	s_add_u32 s4, s4, s20
	s_addc_u32 s5, s5, 0
	s_waitcnt lgkmcnt(15)
	v_mfma_f32_16x16x32_f16 v[60:63], v[136:139], v[160:163], v[60:63]
	s_waitcnt lgkmcnt(14)
	v_mfma_f32_16x16x32_f16 v[64:67], v[136:139], v[164:167], v[64:67]
	s_waitcnt lgkmcnt(13)
	v_mfma_f32_16x16x32_f16 v[68:71], v[136:139], v[168:171], v[68:71]
	s_waitcnt lgkmcnt(12)
	v_mfma_f32_16x16x32_f16 v[72:75], v[140:143], v[156:159], v[72:75]
	v_mfma_f32_16x16x32_f16 v[76:79], v[140:143], v[160:163], v[76:79]
	v_mfma_f32_16x16x32_f16 v[80:83], v[140:143], v[164:167], v[80:83]
	s_add_u32 m0, s28, 0x16000
	s_nop 0
	global_load_lds_dwordx4 v10, s[6:7]
	v_mfma_f32_16x16x32_f16 v[84:87], v[140:143], v[168:171], v[84:87]
	s_waitcnt lgkmcnt(11)
	v_mfma_f32_16x16x32_f16 v[88:91], v[144:147], v[156:159], v[88:91]
	v_mfma_f32_16x16x32_f16 v[92:95], v[144:147], v[160:163], v[92:95]
	v_mfma_f32_16x16x32_f16 v[96:99], v[144:147], v[164:167], v[96:99]
	v_mfma_f32_16x16x32_f16 v[100:103], v[144:147], v[168:171], v[100:103]
	s_waitcnt lgkmcnt(10)
	v_mfma_f32_16x16x32_f16 v[104:107], v[148:151], v[156:159], v[104:107]
	v_mfma_f32_16x16x32_f16 v[108:111], v[148:151], v[160:163], v[108:111]
	s_add_u32 m0, s28, 0x18000
	s_nop 0
	global_load_lds_dwordx4 v11, s[6:7]
	s_add_u32 s6, s6, s20
	s_addc_u32 s7, s7, 0
	v_mfma_f32_16x16x32_f16 v[112:115], v[148:151], v[164:167], v[112:115]
	v_mfma_f32_16x16x32_f16 v[116:119], v[148:151], v[168:171], v[116:119]
	s_waitcnt lgkmcnt(9)
	v_mfma_f32_16x16x32_f16 v[120:123], v[152:155], v[156:159], v[120:123]
	v_mfma_f32_16x16x32_f16 v[124:127], v[152:155], v[160:163], v[124:127]
	v_mfma_f32_16x16x32_f16 v[128:131], v[152:155], v[164:167], v[128:131]
	v_mfma_f32_16x16x32_f16 v[132:135], v[152:155], v[168:171], v[132:135]
	s_waitcnt vmcnt(7) lgkmcnt(0)
	s_barrier
	s_waitcnt lgkmcnt(6)
	ds_read_b128 v[136:139], v15
	ds_read_b128 v[156:159], v17
	ds_read_b128 v[160:163], v17 offset:2048
	ds_read_b128 v[164:167], v17 offset:4096
	ds_read_b128 v[168:171], v17 offset:6144
	ds_read_b128 v[140:143], v15 offset:2048
	ds_read_b128 v[144:147], v15 offset:4096
	ds_read_b128 v[148:151], v15 offset:6144
	ds_read_b128 v[152:155], v15 offset:8192
	v_mfma_f32_16x16x32_f16 v[56:59], v[172:175], v[192:195], v[56:59]
	s_add_u32 m0, s28, 0x1a000
	s_nop 0
	global_load_lds_dwordx4 v10, s[4:5]
	s_waitcnt lgkmcnt(15)
	v_mfma_f32_16x16x32_f16 v[60:63], v[172:175], v[196:199], v[60:63]
	s_waitcnt lgkmcnt(14)
	v_mfma_f32_16x16x32_f16 v[64:67], v[172:175], v[200:203], v[64:67]
	s_waitcnt lgkmcnt(13)
	v_mfma_f32_16x16x32_f16 v[68:71], v[172:175], v[204:207], v[68:71]
	s_waitcnt lgkmcnt(12)
	v_mfma_f32_16x16x32_f16 v[72:75], v[176:179], v[192:195], v[72:75]
	v_mfma_f32_16x16x32_f16 v[76:79], v[176:179], v[196:199], v[76:79]
	s_add_u32 m0, s28, 0x1c000
	s_nop 0
	global_load_lds_dwordx4 v11, s[4:5]
	v_mfma_f32_16x16x32_f16 v[80:83], v[176:179], v[200:203], v[80:83]
	v_mfma_f32_16x16x32_f16 v[84:87], v[176:179], v[204:207], v[84:87]
	s_waitcnt lgkmcnt(11)
	v_mfma_f32_16x16x32_f16 v[88:91], v[180:183], v[192:195], v[88:91]
	v_mfma_f32_16x16x32_f16 v[92:95], v[180:183], v[196:199], v[92:95]
	v_mfma_f32_16x16x32_f16 v[96:99], v[180:183], v[200:203], v[96:99]
	s_add_u32 m0, s28, 0x1e000
	s_nop 0
	global_load_lds_dwordx4 v12, s[4:5]
	v_mfma_f32_16x16x32_f16 v[100:103], v[180:183], v[204:207], v[100:103]
	s_waitcnt lgkmcnt(10)
	v_mfma_f32_16x16x32_f16 v[104:107], v[184:187], v[192:195], v[104:107]
	v_mfma_f32_16x16x32_f16 v[108:111], v[184:187], v[196:199], v[108:111]
	v_mfma_f32_16x16x32_f16 v[112:115], v[184:187], v[200:203], v[112:115]
	v_mfma_f32_16x16x32_f16 v[116:119], v[184:187], v[204:207], v[116:119]
	s_add_u32 m0, s28, 0x20000
	s_nop 0
	global_load_lds_dwordx4 v13, s[4:5]
	s_waitcnt lgkmcnt(9)
	v_mfma_f32_16x16x32_f16 v[120:123], v[188:191], v[192:195], v[120:123]
	v_mfma_f32_16x16x32_f16 v[124:127], v[188:191], v[196:199], v[124:127]
	v_mfma_f32_16x16x32_f16 v[128:131], v[188:191], v[200:203], v[128:131]
	v_mfma_f32_16x16x32_f16 v[132:135], v[188:191], v[204:207], v[132:135]
	s_waitcnt lgkmcnt(6)
	ds_read_b128 v[172:175], v16
	ds_read_b128 v[192:195], v18
	ds_read_b128 v[196:199], v18 offset:2048
	ds_read_b128 v[200:203], v18 offset:4096
	ds_read_b128 v[204:207], v18 offset:6144
	ds_read_b128 v[176:179], v16 offset:2048
	ds_read_b128 v[180:183], v16 offset:4096
	ds_read_b128 v[184:187], v16 offset:6144
	ds_read_b128 v[188:191], v16 offset:8192
	v_mfma_f32_16x16x32_f16 v[56:59], v[136:139], v[156:159], v[56:59]
	s_add_u32 m0, s28, 0x22000
	s_nop 0
	global_load_lds_dwordx4 v14, s[4:5]
	s_add_u32 s4, s4, s20
	s_addc_u32 s5, s5, 0
	s_waitcnt lgkmcnt(15)
	v_mfma_f32_16x16x32_f16 v[60:63], v[136:139], v[160:163], v[60:63]
	s_waitcnt lgkmcnt(14)
	v_mfma_f32_16x16x32_f16 v[64:67], v[136:139], v[164:167], v[64:67]
	s_waitcnt lgkmcnt(13)
	v_mfma_f32_16x16x32_f16 v[68:71], v[136:139], v[168:171], v[68:71]
	s_waitcnt lgkmcnt(12)
	v_mfma_f32_16x16x32_f16 v[72:75], v[140:143], v[156:159], v[72:75]
	v_mfma_f32_16x16x32_f16 v[76:79], v[140:143], v[160:163], v[76:79]
	v_mfma_f32_16x16x32_f16 v[80:83], v[140:143], v[164:167], v[80:83]
	s_add_u32 m0, s28, 0x23000
	s_nop 0
	global_load_lds_dwordx4 v10, s[6:7]
	v_mfma_f32_16x16x32_f16 v[84:87], v[140:143], v[168:171], v[84:87]
	s_waitcnt lgkmcnt(11)
	v_mfma_f32_16x16x32_f16 v[88:91], v[144:147], v[156:159], v[88:91]
	v_mfma_f32_16x16x32_f16 v[92:95], v[144:147], v[160:163], v[92:95]
	v_mfma_f32_16x16x32_f16 v[96:99], v[144:147], v[164:167], v[96:99]
	v_mfma_f32_16x16x32_f16 v[100:103], v[144:147], v[168:171], v[100:103]
	s_waitcnt lgkmcnt(10)
	v_mfma_f32_16x16x32_f16 v[104:107], v[148:151], v[156:159], v[104:107]
	v_mfma_f32_16x16x32_f16 v[108:111], v[148:151], v[160:163], v[108:111]
	s_add_u32 m0, s28, 0x25000
	s_nop 0
	global_load_lds_dwordx4 v11, s[6:7]
	s_add_u32 s6, s6, s20
	s_addc_u32 s7, s7, 0
	v_mfma_f32_16x16x32_f16 v[112:115], v[148:151], v[164:167], v[112:115]
	v_mfma_f32_16x16x32_f16 v[116:119], v[148:151], v[168:171], v[116:119]
	s_waitcnt lgkmcnt(9)
	v_mfma_f32_16x16x32_f16 v[120:123], v[152:155], v[156:159], v[120:123]
	v_mfma_f32_16x16x32_f16 v[124:127], v[152:155], v[160:163], v[124:127]
	v_mfma_f32_16x16x32_f16 v[128:131], v[152:155], v[164:167], v[128:131]
	v_mfma_f32_16x16x32_f16 v[132:135], v[152:155], v[168:171], v[132:135]
	s_waitcnt vmcnt(7) lgkmcnt(0)
	s_barrier
	s_waitcnt lgkmcnt(6)
	ds_read_b128 v[136:139], v15 offset:53248
	ds_read_b128 v[156:159], v17 offset:53248
	ds_read_b128 v[160:163], v17 offset:55296
	ds_read_b128 v[164:167], v17 offset:57344
	ds_read_b128 v[168:171], v17 offset:59392
	ds_read_b128 v[140:143], v15 offset:55296
	ds_read_b128 v[144:147], v15 offset:57344
	ds_read_b128 v[148:151], v15 offset:59392
	ds_read_b128 v[152:155], v15 offset:61440
	v_mfma_f32_16x16x32_f16 v[56:59], v[172:175], v[192:195], v[56:59]
	s_add_u32 m0, s28, 0x0
	s_nop 0
	global_load_lds_dwordx4 v10, s[4:5]
	s_waitcnt lgkmcnt(15)
	v_mfma_f32_16x16x32_f16 v[60:63], v[172:175], v[196:199], v[60:63]
	s_waitcnt lgkmcnt(14)
	v_mfma_f32_16x16x32_f16 v[64:67], v[172:175], v[200:203], v[64:67]
	s_waitcnt lgkmcnt(13)
	v_mfma_f32_16x16x32_f16 v[68:71], v[172:175], v[204:207], v[68:71]
	s_waitcnt lgkmcnt(12)
	v_mfma_f32_16x16x32_f16 v[72:75], v[176:179], v[192:195], v[72:75]
	v_mfma_f32_16x16x32_f16 v[76:79], v[176:179], v[196:199], v[76:79]
	s_add_u32 m0, s28, 0x2000
	s_nop 0
	global_load_lds_dwordx4 v11, s[4:5]
	v_mfma_f32_16x16x32_f16 v[80:83], v[176:179], v[200:203], v[80:83]
	v_mfma_f32_16x16x32_f16 v[84:87], v[176:179], v[204:207], v[84:87]
	s_waitcnt lgkmcnt(11)
	v_mfma_f32_16x16x32_f16 v[88:91], v[180:183], v[192:195], v[88:91]
	v_mfma_f32_16x16x32_f16 v[92:95], v[180:183], v[196:199], v[92:95]
	v_mfma_f32_16x16x32_f16 v[96:99], v[180:183], v[200:203], v[96:99]
	s_add_u32 m0, s28, 0x4000
	s_nop 0
	global_load_lds_dwordx4 v12, s[4:5]
	v_mfma_f32_16x16x32_f16 v[100:103], v[180:183], v[204:207], v[100:103]
	s_waitcnt lgkmcnt(10)
	v_mfma_f32_16x16x32_f16 v[104:107], v[184:187], v[192:195], v[104:107]
	v_mfma_f32_16x16x32_f16 v[108:111], v[184:187], v[196:199], v[108:111]
	v_mfma_f32_16x16x32_f16 v[112:115], v[184:187], v[200:203], v[112:115]
	v_mfma_f32_16x16x32_f16 v[116:119], v[184:187], v[204:207], v[116:119]
	s_add_u32 m0, s28, 0x6000
	s_nop 0
	global_load_lds_dwordx4 v13, s[4:5]
	s_waitcnt lgkmcnt(9)
	v_mfma_f32_16x16x32_f16 v[120:123], v[188:191], v[192:195], v[120:123]
	v_mfma_f32_16x16x32_f16 v[124:127], v[188:191], v[196:199], v[124:127]
	v_mfma_f32_16x16x32_f16 v[128:131], v[188:191], v[200:203], v[128:131]
	v_mfma_f32_16x16x32_f16 v[132:135], v[188:191], v[204:207], v[132:135]
	s_waitcnt lgkmcnt(6)
	ds_read_b128 v[172:175], v16 offset:53248
	ds_read_b128 v[192:195], v18 offset:53248
	ds_read_b128 v[196:199], v18 offset:55296
	ds_read_b128 v[200:203], v18 offset:57344
	ds_read_b128 v[204:207], v18 offset:59392
	ds_read_b128 v[176:179], v16 offset:55296
	ds_read_b128 v[180:183], v16 offset:57344
	ds_read_b128 v[184:187], v16 offset:59392
	ds_read_b128 v[188:191], v16 offset:61440
	v_mfma_f32_16x16x32_f16 v[56:59], v[136:139], v[156:159], v[56:59]
	s_add_u32 m0, s28, 0x8000
	s_nop 0
	global_load_lds_dwordx4 v14, s[4:5]
	s_add_u32 s4, s4, s20
	s_addc_u32 s5, s5, 0
	s_waitcnt lgkmcnt(15)
	v_mfma_f32_16x16x32_f16 v[60:63], v[136:139], v[160:163], v[60:63]
	s_waitcnt lgkmcnt(14)
	v_mfma_f32_16x16x32_f16 v[64:67], v[136:139], v[164:167], v[64:67]
	s_waitcnt lgkmcnt(13)
	v_mfma_f32_16x16x32_f16 v[68:71], v[136:139], v[168:171], v[68:71]
	s_waitcnt lgkmcnt(12)
	v_mfma_f32_16x16x32_f16 v[72:75], v[140:143], v[156:159], v[72:75]
	v_mfma_f32_16x16x32_f16 v[76:79], v[140:143], v[160:163], v[76:79]
	v_mfma_f32_16x16x32_f16 v[80:83], v[140:143], v[164:167], v[80:83]
	s_add_u32 m0, s28, 0x9000
	s_nop 0
	global_load_lds_dwordx4 v10, s[6:7]
	v_mfma_f32_16x16x32_f16 v[84:87], v[140:143], v[168:171], v[84:87]
	s_waitcnt lgkmcnt(11)
	v_mfma_f32_16x16x32_f16 v[88:91], v[144:147], v[156:159], v[88:91]
	v_mfma_f32_16x16x32_f16 v[92:95], v[144:147], v[160:163], v[92:95]
	v_mfma_f32_16x16x32_f16 v[96:99], v[144:147], v[164:167], v[96:99]
	v_mfma_f32_16x16x32_f16 v[100:103], v[144:147], v[168:171], v[100:103]
	s_waitcnt lgkmcnt(10)
	v_mfma_f32_16x16x32_f16 v[104:107], v[148:151], v[156:159], v[104:107]
	v_mfma_f32_16x16x32_f16 v[108:111], v[148:151], v[160:163], v[108:111]
	s_add_u32 m0, s28, 0xb000
	s_nop 0
	global_load_lds_dwordx4 v11, s[6:7]
	s_add_u32 s6, s6, s20
	s_addc_u32 s7, s7, 0
	v_mfma_f32_16x16x32_f16 v[112:115], v[148:151], v[164:167], v[112:115]
	v_mfma_f32_16x16x32_f16 v[116:119], v[148:151], v[168:171], v[116:119]
	s_waitcnt lgkmcnt(9)
	v_mfma_f32_16x16x32_f16 v[120:123], v[152:155], v[156:159], v[120:123]
	v_mfma_f32_16x16x32_f16 v[124:127], v[152:155], v[160:163], v[124:127]
	v_mfma_f32_16x16x32_f16 v[128:131], v[152:155], v[164:167], v[128:131]
	v_mfma_f32_16x16x32_f16 v[132:135], v[152:155], v[168:171], v[132:135]
	s_waitcnt vmcnt(7) lgkmcnt(0)
	s_barrier
	s_waitcnt lgkmcnt(6)
	ds_read_b128 v[136:139], v19
	ds_read_b128 v[156:159], v21
	ds_read_b128 v[160:163], v21 offset:2048
	ds_read_b128 v[164:167], v21 offset:4096
	ds_read_b128 v[168:171], v21 offset:6144
	ds_read_b128 v[140:143], v19 offset:2048
	ds_read_b128 v[144:147], v19 offset:4096
	ds_read_b128 v[148:151], v19 offset:6144
	ds_read_b128 v[152:155], v19 offset:8192
	v_mfma_f32_16x16x32_f16 v[56:59], v[172:175], v[192:195], v[56:59]
	s_add_u32 m0, s28, 0xd000
	s_nop 0
	global_load_lds_dwordx4 v10, s[4:5]
	s_waitcnt lgkmcnt(15)
	v_mfma_f32_16x16x32_f16 v[60:63], v[172:175], v[196:199], v[60:63]
	s_waitcnt lgkmcnt(14)
	v_mfma_f32_16x16x32_f16 v[64:67], v[172:175], v[200:203], v[64:67]
	s_waitcnt lgkmcnt(13)
	v_mfma_f32_16x16x32_f16 v[68:71], v[172:175], v[204:207], v[68:71]
	s_waitcnt lgkmcnt(12)
	v_mfma_f32_16x16x32_f16 v[72:75], v[176:179], v[192:195], v[72:75]
	v_mfma_f32_16x16x32_f16 v[76:79], v[176:179], v[196:199], v[76:79]
	s_add_u32 m0, s28, 0xf000
	s_nop 0
	global_load_lds_dwordx4 v11, s[4:5]
	v_mfma_f32_16x16x32_f16 v[80:83], v[176:179], v[200:203], v[80:83]
	v_mfma_f32_16x16x32_f16 v[84:87], v[176:179], v[204:207], v[84:87]
	s_waitcnt lgkmcnt(11)
	v_mfma_f32_16x16x32_f16 v[88:91], v[180:183], v[192:195], v[88:91]
	v_mfma_f32_16x16x32_f16 v[92:95], v[180:183], v[196:199], v[92:95]
	v_mfma_f32_16x16x32_f16 v[96:99], v[180:183], v[200:203], v[96:99]
	s_add_u32 m0, s28, 0x11000
	s_nop 0
	global_load_lds_dwordx4 v12, s[4:5]
	v_mfma_f32_16x16x32_f16 v[100:103], v[180:183], v[204:207], v[100:103]
	s_waitcnt lgkmcnt(10)
	v_mfma_f32_16x16x32_f16 v[104:107], v[184:187], v[192:195], v[104:107]
	v_mfma_f32_16x16x32_f16 v[108:111], v[184:187], v[196:199], v[108:111]
	v_mfma_f32_16x16x32_f16 v[112:115], v[184:187], v[200:203], v[112:115]
	v_mfma_f32_16x16x32_f16 v[116:119], v[184:187], v[204:207], v[116:119]
	s_add_u32 m0, s28, 0x13000
	s_nop 0
	global_load_lds_dwordx4 v13, s[4:5]
	s_waitcnt lgkmcnt(9)
	v_mfma_f32_16x16x32_f16 v[120:123], v[188:191], v[192:195], v[120:123]
	v_mfma_f32_16x16x32_f16 v[124:127], v[188:191], v[196:199], v[124:127]
	v_mfma_f32_16x16x32_f16 v[128:131], v[188:191], v[200:203], v[128:131]
	v_mfma_f32_16x16x32_f16 v[132:135], v[188:191], v[204:207], v[132:135]
	s_waitcnt lgkmcnt(6)
	ds_read_b128 v[172:175], v20
	ds_read_b128 v[192:195], v22
	ds_read_b128 v[196:199], v22 offset:2048
	ds_read_b128 v[200:203], v22 offset:4096
	ds_read_b128 v[204:207], v22 offset:6144
	ds_read_b128 v[176:179], v20 offset:2048
	ds_read_b128 v[180:183], v20 offset:4096
	ds_read_b128 v[184:187], v20 offset:6144
	ds_read_b128 v[188:191], v20 offset:8192
	v_mfma_f32_16x16x32_f16 v[56:59], v[136:139], v[156:159], v[56:59]
	s_add_u32 m0, s28, 0x15000
	s_nop 0
	global_load_lds_dwordx4 v14, s[4:5]
	s_add_u32 s4, s4, s20
	s_addc_u32 s5, s5, 0
	s_waitcnt lgkmcnt(15)
	v_mfma_f32_16x16x32_f16 v[60:63], v[136:139], v[160:163], v[60:63]
	s_waitcnt lgkmcnt(14)
	v_mfma_f32_16x16x32_f16 v[64:67], v[136:139], v[164:167], v[64:67]
	s_waitcnt lgkmcnt(13)
	v_mfma_f32_16x16x32_f16 v[68:71], v[136:139], v[168:171], v[68:71]
	s_waitcnt lgkmcnt(12)
	v_mfma_f32_16x16x32_f16 v[72:75], v[140:143], v[156:159], v[72:75]
	v_mfma_f32_16x16x32_f16 v[76:79], v[140:143], v[160:163], v[76:79]
	v_mfma_f32_16x16x32_f16 v[80:83], v[140:143], v[164:167], v[80:83]
	s_add_u32 m0, s28, 0x16000
	s_nop 0
	global_load_lds_dwordx4 v10, s[6:7]
	v_mfma_f32_16x16x32_f16 v[84:87], v[140:143], v[168:171], v[84:87]
	s_waitcnt lgkmcnt(11)
	v_mfma_f32_16x16x32_f16 v[88:91], v[144:147], v[156:159], v[88:91]
	v_mfma_f32_16x16x32_f16 v[92:95], v[144:147], v[160:163], v[92:95]
	v_mfma_f32_16x16x32_f16 v[96:99], v[144:147], v[164:167], v[96:99]
	v_mfma_f32_16x16x32_f16 v[100:103], v[144:147], v[168:171], v[100:103]
	s_waitcnt lgkmcnt(10)
	v_mfma_f32_16x16x32_f16 v[104:107], v[148:151], v[156:159], v[104:107]
	v_mfma_f32_16x16x32_f16 v[108:111], v[148:151], v[160:163], v[108:111]
	s_add_u32 m0, s28, 0x18000
	s_nop 0
	global_load_lds_dwordx4 v11, s[6:7]
	s_add_u32 s6, s6, s20
	s_addc_u32 s7, s7, 0
	v_mfma_f32_16x16x32_f16 v[112:115], v[148:151], v[164:167], v[112:115]
	v_mfma_f32_16x16x32_f16 v[116:119], v[148:151], v[168:171], v[116:119]
	s_waitcnt lgkmcnt(9)
	v_mfma_f32_16x16x32_f16 v[120:123], v[152:155], v[156:159], v[120:123]
	v_mfma_f32_16x16x32_f16 v[124:127], v[152:155], v[160:163], v[124:127]
	v_mfma_f32_16x16x32_f16 v[128:131], v[152:155], v[164:167], v[128:131]
	v_mfma_f32_16x16x32_f16 v[132:135], v[152:155], v[168:171], v[132:135]
	s_waitcnt vmcnt(7) lgkmcnt(0)
	s_barrier
	s_waitcnt lgkmcnt(6)
	ds_read_b128 v[136:139], v15
	ds_read_b128 v[156:159], v17
	ds_read_b128 v[160:163], v17 offset:2048
	ds_read_b128 v[164:167], v17 offset:4096
	ds_read_b128 v[168:171], v17 offset:6144
	ds_read_b128 v[140:143], v15 offset:2048
	ds_read_b128 v[144:147], v15 offset:4096
	ds_read_b128 v[148:151], v15 offset:6144
	ds_read_b128 v[152:155], v15 offset:8192
	v_mfma_f32_16x16x32_f16 v[56:59], v[172:175], v[192:195], v[56:59]
	s_add_u32 m0, s28, 0x1a000
	s_nop 0
	global_load_lds_dwordx4 v10, s[4:5]
	s_waitcnt lgkmcnt(15)
	v_mfma_f32_16x16x32_f16 v[60:63], v[172:175], v[196:199], v[60:63]
	s_waitcnt lgkmcnt(14)
	v_mfma_f32_16x16x32_f16 v[64:67], v[172:175], v[200:203], v[64:67]
	s_waitcnt lgkmcnt(13)
	v_mfma_f32_16x16x32_f16 v[68:71], v[172:175], v[204:207], v[68:71]
	s_waitcnt lgkmcnt(12)
	v_mfma_f32_16x16x32_f16 v[72:75], v[176:179], v[192:195], v[72:75]
	v_mfma_f32_16x16x32_f16 v[76:79], v[176:179], v[196:199], v[76:79]
	s_add_u32 m0, s28, 0x1c000
	s_nop 0
	global_load_lds_dwordx4 v11, s[4:5]
	v_mfma_f32_16x16x32_f16 v[80:83], v[176:179], v[200:203], v[80:83]
	v_mfma_f32_16x16x32_f16 v[84:87], v[176:179], v[204:207], v[84:87]
	s_waitcnt lgkmcnt(11)
	v_mfma_f32_16x16x32_f16 v[88:91], v[180:183], v[192:195], v[88:91]
	v_mfma_f32_16x16x32_f16 v[92:95], v[180:183], v[196:199], v[92:95]
	v_mfma_f32_16x16x32_f16 v[96:99], v[180:183], v[200:203], v[96:99]
	s_add_u32 m0, s28, 0x1e000
	s_nop 0
	global_load_lds_dwordx4 v12, s[4:5]
	v_mfma_f32_16x16x32_f16 v[100:103], v[180:183], v[204:207], v[100:103]
	s_waitcnt lgkmcnt(10)
	v_mfma_f32_16x16x32_f16 v[104:107], v[184:187], v[192:195], v[104:107]
	v_mfma_f32_16x16x32_f16 v[108:111], v[184:187], v[196:199], v[108:111]
	v_mfma_f32_16x16x32_f16 v[112:115], v[184:187], v[200:203], v[112:115]
	v_mfma_f32_16x16x32_f16 v[116:119], v[184:187], v[204:207], v[116:119]
	s_add_u32 m0, s28, 0x20000
	s_nop 0
	global_load_lds_dwordx4 v13, s[4:5]
	s_waitcnt lgkmcnt(9)
	v_mfma_f32_16x16x32_f16 v[120:123], v[188:191], v[192:195], v[120:123]
	v_mfma_f32_16x16x32_f16 v[124:127], v[188:191], v[196:199], v[124:127]
	v_mfma_f32_16x16x32_f16 v[128:131], v[188:191], v[200:203], v[128:131]
	v_mfma_f32_16x16x32_f16 v[132:135], v[188:191], v[204:207], v[132:135]
	s_waitcnt lgkmcnt(6)
	ds_read_b128 v[172:175], v16
	ds_read_b128 v[192:195], v18
	ds_read_b128 v[196:199], v18 offset:2048
	ds_read_b128 v[200:203], v18 offset:4096
	ds_read_b128 v[204:207], v18 offset:6144
	ds_read_b128 v[176:179], v16 offset:2048
	ds_read_b128 v[180:183], v16 offset:4096
	ds_read_b128 v[184:187], v16 offset:6144
	ds_read_b128 v[188:191], v16 offset:8192
	v_mfma_f32_16x16x32_f16 v[56:59], v[136:139], v[156:159], v[56:59]
	s_add_u32 m0, s28, 0x22000
	s_nop 0
	global_load_lds_dwordx4 v14, s[4:5]
	s_add_u32 s4, s4, s20
	s_addc_u32 s5, s5, 0
	s_waitcnt lgkmcnt(15)
	v_mfma_f32_16x16x32_f16 v[60:63], v[136:139], v[160:163], v[60:63]
	s_waitcnt lgkmcnt(14)
	v_mfma_f32_16x16x32_f16 v[64:67], v[136:139], v[164:167], v[64:67]
	s_waitcnt lgkmcnt(13)
	v_mfma_f32_16x16x32_f16 v[68:71], v[136:139], v[168:171], v[68:71]
	s_waitcnt lgkmcnt(12)
	v_mfma_f32_16x16x32_f16 v[72:75], v[140:143], v[156:159], v[72:75]
	v_mfma_f32_16x16x32_f16 v[76:79], v[140:143], v[160:163], v[76:79]
	v_mfma_f32_16x16x32_f16 v[80:83], v[140:143], v[164:167], v[80:83]
	s_add_u32 m0, s28, 0x23000
	s_nop 0
	global_load_lds_dwordx4 v10, s[6:7]
	v_mfma_f32_16x16x32_f16 v[84:87], v[140:143], v[168:171], v[84:87]
	s_waitcnt lgkmcnt(11)
	v_mfma_f32_16x16x32_f16 v[88:91], v[144:147], v[156:159], v[88:91]
	v_mfma_f32_16x16x32_f16 v[92:95], v[144:147], v[160:163], v[92:95]
	v_mfma_f32_16x16x32_f16 v[96:99], v[144:147], v[164:167], v[96:99]
	v_mfma_f32_16x16x32_f16 v[100:103], v[144:147], v[168:171], v[100:103]
	s_waitcnt lgkmcnt(10)
	v_mfma_f32_16x16x32_f16 v[104:107], v[148:151], v[156:159], v[104:107]
	v_mfma_f32_16x16x32_f16 v[108:111], v[148:151], v[160:163], v[108:111]
	s_add_u32 m0, s28, 0x25000
	s_nop 0
	global_load_lds_dwordx4 v11, s[6:7]
	s_add_u32 s6, s6, s20
	s_addc_u32 s7, s7, 0
	v_mfma_f32_16x16x32_f16 v[112:115], v[148:151], v[164:167], v[112:115]
	v_mfma_f32_16x16x32_f16 v[116:119], v[148:151], v[168:171], v[116:119]
	s_waitcnt lgkmcnt(9)
	v_mfma_f32_16x16x32_f16 v[120:123], v[152:155], v[156:159], v[120:123]
	v_mfma_f32_16x16x32_f16 v[124:127], v[152:155], v[160:163], v[124:127]
	v_mfma_f32_16x16x32_f16 v[128:131], v[152:155], v[164:167], v[128:131]
	v_mfma_f32_16x16x32_f16 v[132:135], v[152:155], v[168:171], v[132:135]
	s_waitcnt vmcnt(7) lgkmcnt(0)
	s_barrier
	s_waitcnt lgkmcnt(6)
	ds_read_b128 v[136:139], v15 offset:53248
	ds_read_b128 v[156:159], v17 offset:53248
	ds_read_b128 v[160:163], v17 offset:55296
	ds_read_b128 v[164:167], v17 offset:57344
	ds_read_b128 v[168:171], v17 offset:59392
	ds_read_b128 v[140:143], v15 offset:55296
	ds_read_b128 v[144:147], v15 offset:57344
	ds_read_b128 v[148:151], v15 offset:59392
	ds_read_b128 v[152:155], v15 offset:61440
	v_mfma_f32_16x16x32_f16 v[56:59], v[172:175], v[192:195], v[56:59]
	s_add_u32 m0, s28, 0x0
	s_nop 0
	global_load_lds_dwordx4 v10, s[4:5]
	s_waitcnt lgkmcnt(15)
	v_mfma_f32_16x16x32_f16 v[60:63], v[172:175], v[196:199], v[60:63]
	s_waitcnt lgkmcnt(14)
	v_mfma_f32_16x16x32_f16 v[64:67], v[172:175], v[200:203], v[64:67]
	s_waitcnt lgkmcnt(13)
	v_mfma_f32_16x16x32_f16 v[68:71], v[172:175], v[204:207], v[68:71]
	s_waitcnt lgkmcnt(12)
	v_mfma_f32_16x16x32_f16 v[72:75], v[176:179], v[192:195], v[72:75]
	v_mfma_f32_16x16x32_f16 v[76:79], v[176:179], v[196:199], v[76:79]
	s_add_u32 m0, s28, 0x2000
	s_nop 0
	global_load_lds_dwordx4 v11, s[4:5]
	v_mfma_f32_16x16x32_f16 v[80:83], v[176:179], v[200:203], v[80:83]
	v_mfma_f32_16x16x32_f16 v[84:87], v[176:179], v[204:207], v[84:87]
	s_waitcnt lgkmcnt(11)
	v_mfma_f32_16x16x32_f16 v[88:91], v[180:183], v[192:195], v[88:91]
	v_mfma_f32_16x16x32_f16 v[92:95], v[180:183], v[196:199], v[92:95]
	v_mfma_f32_16x16x32_f16 v[96:99], v[180:183], v[200:203], v[96:99]
	s_add_u32 m0, s28, 0x4000
	s_nop 0
	global_load_lds_dwordx4 v12, s[4:5]
	v_mfma_f32_16x16x32_f16 v[100:103], v[180:183], v[204:207], v[100:103]
	s_waitcnt lgkmcnt(10)
	v_mfma_f32_16x16x32_f16 v[104:107], v[184:187], v[192:195], v[104:107]
	v_mfma_f32_16x16x32_f16 v[108:111], v[184:187], v[196:199], v[108:111]
	v_mfma_f32_16x16x32_f16 v[112:115], v[184:187], v[200:203], v[112:115]
	v_mfma_f32_16x16x32_f16 v[116:119], v[184:187], v[204:207], v[116:119]
	s_add_u32 m0, s28, 0x6000
	s_nop 0
	global_load_lds_dwordx4 v13, s[4:5]
	s_waitcnt lgkmcnt(9)
	v_mfma_f32_16x16x32_f16 v[120:123], v[188:191], v[192:195], v[120:123]
	v_mfma_f32_16x16x32_f16 v[124:127], v[188:191], v[196:199], v[124:127]
	v_mfma_f32_16x16x32_f16 v[128:131], v[188:191], v[200:203], v[128:131]
	v_mfma_f32_16x16x32_f16 v[132:135], v[188:191], v[204:207], v[132:135]
	s_waitcnt lgkmcnt(6)
	ds_read_b128 v[172:175], v16 offset:53248
	ds_read_b128 v[192:195], v18 offset:53248
	ds_read_b128 v[196:199], v18 offset:55296
	ds_read_b128 v[200:203], v18 offset:57344
	ds_read_b128 v[204:207], v18 offset:59392
	ds_read_b128 v[176:179], v16 offset:55296
	ds_read_b128 v[180:183], v16 offset:57344
	ds_read_b128 v[184:187], v16 offset:59392
	ds_read_b128 v[188:191], v16 offset:61440
	v_mfma_f32_16x16x32_f16 v[56:59], v[136:139], v[156:159], v[56:59]
	s_add_u32 m0, s28, 0x8000
	s_nop 0
	global_load_lds_dwordx4 v14, s[4:5]
	s_add_u32 s4, s4, s20
	s_addc_u32 s5, s5, 0
	s_waitcnt lgkmcnt(15)
	v_mfma_f32_16x16x32_f16 v[60:63], v[136:139], v[160:163], v[60:63]
	s_waitcnt lgkmcnt(14)
	v_mfma_f32_16x16x32_f16 v[64:67], v[136:139], v[164:167], v[64:67]
	s_waitcnt lgkmcnt(13)
	v_mfma_f32_16x16x32_f16 v[68:71], v[136:139], v[168:171], v[68:71]
	s_waitcnt lgkmcnt(12)
	v_mfma_f32_16x16x32_f16 v[72:75], v[140:143], v[156:159], v[72:75]
	v_mfma_f32_16x16x32_f16 v[76:79], v[140:143], v[160:163], v[76:79]
	v_mfma_f32_16x16x32_f16 v[80:83], v[140:143], v[164:167], v[80:83]
	s_add_u32 m0, s28, 0x9000
	s_nop 0
	global_load_lds_dwordx4 v10, s[6:7]
	v_mfma_f32_16x16x32_f16 v[84:87], v[140:143], v[168:171], v[84:87]
	s_waitcnt lgkmcnt(11)
	v_mfma_f32_16x16x32_f16 v[88:91], v[144:147], v[156:159], v[88:91]
	v_mfma_f32_16x16x32_f16 v[92:95], v[144:147], v[160:163], v[92:95]
	v_mfma_f32_16x16x32_f16 v[96:99], v[144:147], v[164:167], v[96:99]
	v_mfma_f32_16x16x32_f16 v[100:103], v[144:147], v[168:171], v[100:103]
	s_waitcnt lgkmcnt(10)
	v_mfma_f32_16x16x32_f16 v[104:107], v[148:151], v[156:159], v[104:107]
	v_mfma_f32_16x16x32_f16 v[108:111], v[148:151], v[160:163], v[108:111]
	s_add_u32 m0, s28, 0xb000
	s_nop 0
	global_load_lds_dwordx4 v11, s[6:7]
	s_add_u32 s6, s6, s20
	s_addc_u32 s7, s7, 0
	v_mfma_f32_16x16x32_f16 v[112:115], v[148:151], v[164:167], v[112:115]
	v_mfma_f32_16x16x32_f16 v[116:119], v[148:151], v[168:171], v[116:119]
	s_waitcnt lgkmcnt(9)
	v_mfma_f32_16x16x32_f16 v[120:123], v[152:155], v[156:159], v[120:123]
	v_mfma_f32_16x16x32_f16 v[124:127], v[152:155], v[160:163], v[124:127]
	v_mfma_f32_16x16x32_f16 v[128:131], v[152:155], v[164:167], v[128:131]
	v_mfma_f32_16x16x32_f16 v[132:135], v[152:155], v[168:171], v[132:135]
	s_waitcnt vmcnt(7) lgkmcnt(0)
	s_barrier
	s_waitcnt lgkmcnt(6)
	ds_read_b128 v[136:139], v19
	ds_read_b128 v[156:159], v21
	ds_read_b128 v[160:163], v21 offset:2048
	ds_read_b128 v[164:167], v21 offset:4096
	ds_read_b128 v[168:171], v21 offset:6144
	ds_read_b128 v[140:143], v19 offset:2048
	ds_read_b128 v[144:147], v19 offset:4096
	ds_read_b128 v[148:151], v19 offset:6144
	ds_read_b128 v[152:155], v19 offset:8192
	v_mfma_f32_16x16x32_f16 v[56:59], v[172:175], v[192:195], v[56:59]
	s_waitcnt lgkmcnt(15)
	v_mfma_f32_16x16x32_f16 v[60:63], v[172:175], v[196:199], v[60:63]
	s_waitcnt lgkmcnt(14)
	v_mfma_f32_16x16x32_f16 v[64:67], v[172:175], v[200:203], v[64:67]
	s_waitcnt lgkmcnt(13)
	v_mfma_f32_16x16x32_f16 v[68:71], v[172:175], v[204:207], v[68:71]
	s_waitcnt lgkmcnt(12)
	v_mfma_f32_16x16x32_f16 v[72:75], v[176:179], v[192:195], v[72:75]
	v_mfma_f32_16x16x32_f16 v[76:79], v[176:179], v[196:199], v[76:79]
	v_mfma_f32_16x16x32_f16 v[80:83], v[176:179], v[200:203], v[80:83]
	v_mfma_f32_16x16x32_f16 v[84:87], v[176:179], v[204:207], v[84:87]
	s_waitcnt lgkmcnt(11)
	v_mfma_f32_16x16x32_f16 v[88:91], v[180:183], v[192:195], v[88:91]
	v_mfma_f32_16x16x32_f16 v[92:95], v[180:183], v[196:199], v[92:95]
	v_mfma_f32_16x16x32_f16 v[96:99], v[180:183], v[200:203], v[96:99]
	v_mfma_f32_16x16x32_f16 v[100:103], v[180:183], v[204:207], v[100:103]
	s_waitcnt lgkmcnt(10)
	v_mfma_f32_16x16x32_f16 v[104:107], v[184:187], v[192:195], v[104:107]
	v_mfma_f32_16x16x32_f16 v[108:111], v[184:187], v[196:199], v[108:111]
	v_mfma_f32_16x16x32_f16 v[112:115], v[184:187], v[200:203], v[112:115]
	v_mfma_f32_16x16x32_f16 v[116:119], v[184:187], v[204:207], v[116:119]
	s_waitcnt lgkmcnt(9)
	v_mfma_f32_16x16x32_f16 v[120:123], v[188:191], v[192:195], v[120:123]
	v_mfma_f32_16x16x32_f16 v[124:127], v[188:191], v[196:199], v[124:127]
	v_mfma_f32_16x16x32_f16 v[128:131], v[188:191], v[200:203], v[128:131]
	v_mfma_f32_16x16x32_f16 v[132:135], v[188:191], v[204:207], v[132:135]
	s_waitcnt lgkmcnt(6)
	ds_read_b128 v[172:175], v20
	ds_read_b128 v[192:195], v22
	ds_read_b128 v[196:199], v22 offset:2048
	ds_read_b128 v[200:203], v22 offset:4096
	ds_read_b128 v[204:207], v22 offset:6144
	ds_read_b128 v[176:179], v20 offset:2048
	ds_read_b128 v[180:183], v20 offset:4096
	ds_read_b128 v[184:187], v20 offset:6144
	ds_read_b128 v[188:191], v20 offset:8192
	v_mfma_f32_16x16x32_f16 v[56:59], v[136:139], v[156:159], v[56:59]
	s_waitcnt lgkmcnt(15)
	v_mfma_f32_16x16x32_f16 v[60:63], v[136:139], v[160:163], v[60:63]
	s_waitcnt lgkmcnt(14)
	v_mfma_f32_16x16x32_f16 v[64:67], v[136:139], v[164:167], v[64:67]
	s_waitcnt lgkmcnt(13)
	v_mfma_f32_16x16x32_f16 v[68:71], v[136:139], v[168:171], v[68:71]
	s_waitcnt lgkmcnt(12)
	v_mfma_f32_16x16x32_f16 v[72:75], v[140:143], v[156:159], v[72:75]
	v_mfma_f32_16x16x32_f16 v[76:79], v[140:143], v[160:163], v[76:79]
	v_mfma_f32_16x16x32_f16 v[80:83], v[140:143], v[164:167], v[80:83]
	v_mfma_f32_16x16x32_f16 v[84:87], v[140:143], v[168:171], v[84:87]
	s_waitcnt lgkmcnt(11)
	v_mfma_f32_16x16x32_f16 v[88:91], v[144:147], v[156:159], v[88:91]
	v_mfma_f32_16x16x32_f16 v[92:95], v[144:147], v[160:163], v[92:95]
	v_mfma_f32_16x16x32_f16 v[96:99], v[144:147], v[164:167], v[96:99]
	v_mfma_f32_16x16x32_f16 v[100:103], v[144:147], v[168:171], v[100:103]
	s_waitcnt lgkmcnt(10)
	v_mfma_f32_16x16x32_f16 v[104:107], v[148:151], v[156:159], v[104:107]
	v_mfma_f32_16x16x32_f16 v[108:111], v[148:151], v[160:163], v[108:111]
	v_mfma_f32_16x16x32_f16 v[112:115], v[148:151], v[164:167], v[112:115]
	v_mfma_f32_16x16x32_f16 v[116:119], v[148:151], v[168:171], v[116:119]
	s_waitcnt lgkmcnt(9)
	v_mfma_f32_16x16x32_f16 v[120:123], v[152:155], v[156:159], v[120:123]
	v_mfma_f32_16x16x32_f16 v[124:127], v[152:155], v[160:163], v[124:127]
	v_mfma_f32_16x16x32_f16 v[128:131], v[152:155], v[164:167], v[128:131]
	v_mfma_f32_16x16x32_f16 v[132:135], v[152:155], v[168:171], v[132:135]
	s_waitcnt vmcnt(0) lgkmcnt(0)
	s_barrier
	s_waitcnt lgkmcnt(6)
	ds_read_b128 v[136:139], v15
	ds_read_b128 v[156:159], v17
	ds_read_b128 v[160:163], v17 offset:2048
	ds_read_b128 v[164:167], v17 offset:4096
	ds_read_b128 v[168:171], v17 offset:6144
	ds_read_b128 v[140:143], v15 offset:2048
	ds_read_b128 v[144:147], v15 offset:4096
	ds_read_b128 v[148:151], v15 offset:6144
	ds_read_b128 v[152:155], v15 offset:8192
	v_mfma_f32_16x16x32_f16 v[56:59], v[172:175], v[192:195], v[56:59]
	s_waitcnt lgkmcnt(15)
	v_mfma_f32_16x16x32_f16 v[60:63], v[172:175], v[196:199], v[60:63]
	s_waitcnt lgkmcnt(14)
	v_mfma_f32_16x16x32_f16 v[64:67], v[172:175], v[200:203], v[64:67]
	s_waitcnt lgkmcnt(13)
	v_mfma_f32_16x16x32_f16 v[68:71], v[172:175], v[204:207], v[68:71]
	s_waitcnt lgkmcnt(12)
	v_mfma_f32_16x16x32_f16 v[72:75], v[176:179], v[192:195], v[72:75]
	v_mfma_f32_16x16x32_f16 v[76:79], v[176:179], v[196:199], v[76:79]
	v_mfma_f32_16x16x32_f16 v[80:83], v[176:179], v[200:203], v[80:83]
	v_mfma_f32_16x16x32_f16 v[84:87], v[176:179], v[204:207], v[84:87]
	s_waitcnt lgkmcnt(11)
	v_mfma_f32_16x16x32_f16 v[88:91], v[180:183], v[192:195], v[88:91]
	v_mfma_f32_16x16x32_f16 v[92:95], v[180:183], v[196:199], v[92:95]
	v_mfma_f32_16x16x32_f16 v[96:99], v[180:183], v[200:203], v[96:99]
	v_mfma_f32_16x16x32_f16 v[100:103], v[180:183], v[204:207], v[100:103]
	s_waitcnt lgkmcnt(10)
	v_mfma_f32_16x16x32_f16 v[104:107], v[184:187], v[192:195], v[104:107]
	v_mfma_f32_16x16x32_f16 v[108:111], v[184:187], v[196:199], v[108:111]
	v_mfma_f32_16x16x32_f16 v[112:115], v[184:187], v[200:203], v[112:115]
	v_mfma_f32_16x16x32_f16 v[116:119], v[184:187], v[204:207], v[116:119]
	s_waitcnt lgkmcnt(9)
	v_mfma_f32_16x16x32_f16 v[120:123], v[188:191], v[192:195], v[120:123]
	v_mfma_f32_16x16x32_f16 v[124:127], v[188:191], v[196:199], v[124:127]
	v_mfma_f32_16x16x32_f16 v[128:131], v[188:191], v[200:203], v[128:131]
	v_mfma_f32_16x16x32_f16 v[132:135], v[188:191], v[204:207], v[132:135]
	s_waitcnt lgkmcnt(6)
	ds_read_b128 v[172:175], v16
	ds_read_b128 v[192:195], v18
	ds_read_b128 v[196:199], v18 offset:2048
	ds_read_b128 v[200:203], v18 offset:4096
	ds_read_b128 v[204:207], v18 offset:6144
	ds_read_b128 v[176:179], v16 offset:2048
	ds_read_b128 v[180:183], v16 offset:4096
	ds_read_b128 v[184:187], v16 offset:6144
	ds_read_b128 v[188:191], v16 offset:8192
	v_mfma_f32_16x16x32_f16 v[56:59], v[136:139], v[156:159], v[56:59]
	s_waitcnt lgkmcnt(15)
	v_mfma_f32_16x16x32_f16 v[60:63], v[136:139], v[160:163], v[60:63]
	s_waitcnt lgkmcnt(14)
	v_mfma_f32_16x16x32_f16 v[64:67], v[136:139], v[164:167], v[64:67]
	s_waitcnt lgkmcnt(13)
	v_mfma_f32_16x16x32_f16 v[68:71], v[136:139], v[168:171], v[68:71]
	s_waitcnt lgkmcnt(12)
	v_mfma_f32_16x16x32_f16 v[72:75], v[140:143], v[156:159], v[72:75]
	v_mfma_f32_16x16x32_f16 v[76:79], v[140:143], v[160:163], v[76:79]
	v_mfma_f32_16x16x32_f16 v[80:83], v[140:143], v[164:167], v[80:83]
	v_mfma_f32_16x16x32_f16 v[84:87], v[140:143], v[168:171], v[84:87]
	s_waitcnt lgkmcnt(11)
	v_mfma_f32_16x16x32_f16 v[88:91], v[144:147], v[156:159], v[88:91]
	v_mfma_f32_16x16x32_f16 v[92:95], v[144:147], v[160:163], v[92:95]
	v_mfma_f32_16x16x32_f16 v[96:99], v[144:147], v[164:167], v[96:99]
	v_mfma_f32_16x16x32_f16 v[100:103], v[144:147], v[168:171], v[100:103]
	s_waitcnt lgkmcnt(10)
	v_mfma_f32_16x16x32_f16 v[104:107], v[148:151], v[156:159], v[104:107]
	v_mfma_f32_16x16x32_f16 v[108:111], v[148:151], v[160:163], v[108:111]
	v_mfma_f32_16x16x32_f16 v[112:115], v[148:151], v[164:167], v[112:115]
	v_mfma_f32_16x16x32_f16 v[116:119], v[148:151], v[168:171], v[116:119]
	s_waitcnt lgkmcnt(9)
	v_mfma_f32_16x16x32_f16 v[120:123], v[152:155], v[156:159], v[120:123]
	v_mfma_f32_16x16x32_f16 v[124:127], v[152:155], v[160:163], v[124:127]
	v_mfma_f32_16x16x32_f16 v[128:131], v[152:155], v[164:167], v[128:131]
	v_mfma_f32_16x16x32_f16 v[132:135], v[152:155], v[168:171], v[132:135]
	s_waitcnt lgkmcnt(7)
	v_mfma_f32_16x16x32_f16 v[56:59], v[172:175], v[192:195], v[56:59]
	s_waitcnt lgkmcnt(6)
	v_mfma_f32_16x16x32_f16 v[60:63], v[172:175], v[196:199], v[60:63]
	s_waitcnt lgkmcnt(5)
	v_mfma_f32_16x16x32_f16 v[64:67], v[172:175], v[200:203], v[64:67]
	s_waitcnt lgkmcnt(4)
	v_mfma_f32_16x16x32_f16 v[68:71], v[172:175], v[204:207], v[68:71]
	s_waitcnt lgkmcnt(3)
	v_mfma_f32_16x16x32_f16 v[72:75], v[176:179], v[192:195], v[72:75]
	v_mfma_f32_16x16x32_f16 v[76:79], v[176:179], v[196:199], v[76:79]
	v_mfma_f32_16x16x32_f16 v[80:83], v[176:179], v[200:203], v[80:83]
	v_mfma_f32_16x16x32_f16 v[84:87], v[176:179], v[204:207], v[84:87]
	s_waitcnt lgkmcnt(2)
	v_mfma_f32_16x16x32_f16 v[88:91], v[180:183], v[192:195], v[88:91]
	v_mfma_f32_16x16x32_f16 v[92:95], v[180:183], v[196:199], v[92:95]
	v_mfma_f32_16x16x32_f16 v[96:99], v[180:183], v[200:203], v[96:99]
	v_mfma_f32_16x16x32_f16 v[100:103], v[180:183], v[204:207], v[100:103]
	s_waitcnt lgkmcnt(1)
	v_mfma_f32_16x16x32_f16 v[104:107], v[184:187], v[192:195], v[104:107]
	v_mfma_f32_16x16x32_f16 v[108:111], v[184:187], v[196:199], v[108:111]
	v_mfma_f32_16x16x32_f16 v[112:115], v[184:187], v[200:203], v[112:115]
	v_mfma_f32_16x16x32_f16 v[116:119], v[184:187], v[204:207], v[116:119]
	s_waitcnt lgkmcnt(0)
	v_mfma_f32_16x16x32_f16 v[120:123], v[188:191], v[192:195], v[120:123]
	v_mfma_f32_16x16x32_f16 v[124:127], v[188:191], v[196:199], v[124:127]
	v_mfma_f32_16x16x32_f16 v[128:131], v[188:191], v[200:203], v[128:131]
	v_mfma_f32_16x16x32_f16 v[132:135], v[188:191], v[204:207], v[132:135]
	s_nop 7
	s_nop 1
	s_add_u32 s24, s29, 0
	s_lshl_b32 s8, s24, 11
	v_add_u32_e32 v212, s8, v23
	v_pk_add_f32 v[56:57], v[56:57], v[24:25] op_sel_hi:[1,0]
	v_pk_add_f32 v[58:59], v[58:59], v[24:25] op_sel_hi:[1,0]
	v_cvt_pk_f16_f32 v56, v56, v57
	v_cvt_pk_f16_f32 v57, v58, v59
	global_store_dwordx2 v212, v[56:57], s[22:23] offset:0
	v_pk_add_f32 v[60:61], v[60:61], v[26:27] op_sel_hi:[1,0]
	v_pk_add_f32 v[62:63], v[62:63], v[26:27] op_sel_hi:[1,0]
	v_cvt_pk_f16_f32 v60, v60, v61
	v_cvt_pk_f16_f32 v61, v62, v63
	global_store_dwordx2 v212, v[60:61], s[22:23] offset:256
	v_pk_add_f32 v[64:65], v[64:65], v[28:29] op_sel_hi:[1,0]
	v_pk_add_f32 v[66:67], v[66:67], v[28:29] op_sel_hi:[1,0]
	v_cvt_pk_f16_f32 v64, v64, v65
	v_cvt_pk_f16_f32 v65, v66, v67
	global_store_dwordx2 v212, v[64:65], s[22:23] offset:1024
	v_pk_add_f32 v[68:69], v[68:69], v[30:31] op_sel_hi:[1,0]
	v_pk_add_f32 v[70:71], v[70:71], v[30:31] op_sel_hi:[1,0]
	v_cvt_pk_f16_f32 v68, v68, v69
	v_cvt_pk_f16_f32 v69, v70, v71
	global_store_dwordx2 v212, v[68:69], s[22:23] offset:1280
	s_add_u32 s24, s29, 1
	s_lshl_b32 s8, s24, 11
	v_add_u32_e32 v212, s8, v23
	v_pk_add_f32 v[72:73], v[72:73], v[24:25] op_sel_hi:[1,0]
	v_pk_add_f32 v[74:75], v[74:75], v[24:25] op_sel_hi:[1,0]
	v_cvt_pk_f16_f32 v72, v72, v73
	v_cvt_pk_f16_f32 v73, v74, v75
	global_store_dwordx2 v212, v[72:73], s[22:23] offset:0
	v_pk_add_f32 v[76:77], v[76:77], v[26:27] op_sel_hi:[1,0]
	v_pk_add_f32 v[78:79], v[78:79], v[26:27] op_sel_hi:[1,0]
	v_cvt_pk_f16_f32 v76, v76, v77
	v_cvt_pk_f16_f32 v77, v78, v79
	global_store_dwordx2 v212, v[76:77], s[22:23] offset:256
	v_pk_add_f32 v[80:81], v[80:81], v[28:29] op_sel_hi:[1,0]
	v_pk_add_f32 v[82:83], v[82:83], v[28:29] op_sel_hi:[1,0]
	v_cvt_pk_f16_f32 v80, v80, v81
	v_cvt_pk_f16_f32 v81, v82, v83
	global_store_dwordx2 v212, v[80:81], s[22:23] offset:1024
	v_pk_add_f32 v[84:85], v[84:85], v[30:31] op_sel_hi:[1,0]
	v_pk_add_f32 v[86:87], v[86:87], v[30:31] op_sel_hi:[1,0]
	v_cvt_pk_f16_f32 v84, v84, v85
	v_cvt_pk_f16_f32 v85, v86, v87
	global_store_dwordx2 v212, v[84:85], s[22:23] offset:1280
	s_add_u32 s24, s29, 2
	s_lshl_b32 s8, s24, 11
	v_add_u32_e32 v212, s8, v23
	v_pk_add_f32 v[88:89], v[88:89], v[24:25] op_sel_hi:[1,0]
	v_pk_add_f32 v[90:91], v[90:91], v[24:25] op_sel_hi:[1,0]
	v_cvt_pk_f16_f32 v88, v88, v89
	v_cvt_pk_f16_f32 v89, v90, v91
	global_store_dwordx2 v212, v[88:89], s[22:23] offset:0
	v_pk_add_f32 v[92:93], v[92:93], v[26:27] op_sel_hi:[1,0]
	v_pk_add_f32 v[94:95], v[94:95], v[26:27] op_sel_hi:[1,0]
	v_cvt_pk_f16_f32 v92, v92, v93
	v_cvt_pk_f16_f32 v93, v94, v95
	global_store_dwordx2 v212, v[92:93], s[22:23] offset:256
	v_pk_add_f32 v[96:97], v[96:97], v[28:29] op_sel_hi:[1,0]
	v_pk_add_f32 v[98:99], v[98:99], v[28:29] op_sel_hi:[1,0]
	v_cvt_pk_f16_f32 v96, v96, v97
	v_cvt_pk_f16_f32 v97, v98, v99
	global_store_dwordx2 v212, v[96:97], s[22:23] offset:1024
	v_pk_add_f32 v[100:101], v[100:101], v[30:31] op_sel_hi:[1,0]
	v_pk_add_f32 v[102:103], v[102:103], v[30:31] op_sel_hi:[1,0]
	v_cvt_pk_f16_f32 v100, v100, v101
	v_cvt_pk_f16_f32 v101, v102, v103
	global_store_dwordx2 v212, v[100:101], s[22:23] offset:1280
	s_add_u32 s24, s29, 3
	s_lshl_b32 s8, s24, 11
	v_add_u32_e32 v212, s8, v23
	v_pk_add_f32 v[104:105], v[104:105], v[24:25] op_sel_hi:[1,0]
	v_pk_add_f32 v[106:107], v[106:107], v[24:25] op_sel_hi:[1,0]
	v_cvt_pk_f16_f32 v104, v104, v105
	v_cvt_pk_f16_f32 v105, v106, v107
	global_store_dwordx2 v212, v[104:105], s[22:23] offset:0
	v_pk_add_f32 v[108:109], v[108:109], v[26:27] op_sel_hi:[1,0]
	v_pk_add_f32 v[110:111], v[110:111], v[26:27] op_sel_hi:[1,0]
	v_cvt_pk_f16_f32 v108, v108, v109
	v_cvt_pk_f16_f32 v109, v110, v111
	global_store_dwordx2 v212, v[108:109], s[22:23] offset:256
	v_pk_add_f32 v[112:113], v[112:113], v[28:29] op_sel_hi:[1,0]
	v_pk_add_f32 v[114:115], v[114:115], v[28:29] op_sel_hi:[1,0]
	v_cvt_pk_f16_f32 v112, v112, v113
	v_cvt_pk_f16_f32 v113, v114, v115
	global_store_dwordx2 v212, v[112:113], s[22:23] offset:1024
	v_pk_add_f32 v[116:117], v[116:117], v[30:31] op_sel_hi:[1,0]
	v_pk_add_f32 v[118:119], v[118:119], v[30:31] op_sel_hi:[1,0]
	v_cvt_pk_f16_f32 v116, v116, v117
	v_cvt_pk_f16_f32 v117, v118, v119
	global_store_dwordx2 v212, v[116:117], s[22:23] offset:1280
	s_add_u32 s24, s29, 4
	s_lshl_b32 s8, s24, 11
	v_add_u32_e32 v212, s8, v23
	v_pk_add_f32 v[120:121], v[120:121], v[24:25] op_sel_hi:[1,0]
	v_pk_add_f32 v[122:123], v[122:123], v[24:25] op_sel_hi:[1,0]
	v_cvt_pk_f16_f32 v120, v120, v121
	v_cvt_pk_f16_f32 v121, v122, v123
	global_store_dwordx2 v212, v[120:121], s[22:23] offset:0
	v_pk_add_f32 v[124:125], v[124:125], v[26:27] op_sel_hi:[1,0]
	v_pk_add_f32 v[126:127], v[126:127], v[26:27] op_sel_hi:[1,0]
	v_cvt_pk_f16_f32 v124, v124, v125
	v_cvt_pk_f16_f32 v125, v126, v127
	global_store_dwordx2 v212, v[124:125], s[22:23] offset:256
	v_pk_add_f32 v[128:129], v[128:129], v[28:29] op_sel_hi:[1,0]
	v_pk_add_f32 v[130:131], v[130:131], v[28:29] op_sel_hi:[1,0]
	v_cvt_pk_f16_f32 v128, v128, v129
	v_cvt_pk_f16_f32 v129, v130, v131
	global_store_dwordx2 v212, v[128:129], s[22:23] offset:1024
	v_pk_add_f32 v[132:133], v[132:133], v[30:31] op_sel_hi:[1,0]
	v_pk_add_f32 v[134:135], v[134:135], v[30:31] op_sel_hi:[1,0]
	v_cvt_pk_f16_f32 v132, v132, v133
	v_cvt_pk_f16_f32 v133, v134, v135
	global_store_dwordx2 v212, v[132:133], s[22:23] offset:1280
	s_branch .Lpf_done
.Lpf_vVB:
	s_lshl_b32 s25, s25, 6
	s_add_u32 s25, s25, 32
	s_add_u32 s29, s10, s25
	s_lshr_b32 s29, s29, 4
	v_add_u32_e32 v5, s25, v3
	v_lshlrev_b32_e32 v5, 7, v5
	v_add_u32_e32 v15, v5, v6
	v_add_u32_e32 v16, v5, v7
	v_add_u32_e32 v5, 0x9000, v9
	v_add_u32_e32 v17, v5, v6
	v_add_u32_e32 v18, v5, v7
	v_add_u32_e32 v19, 0x1a000, v15
	v_add_u32_e32 v20, 0x1a000, v16
	v_add_u32_e32 v21, 0x1a000, v17
	v_add_u32_e32 v22, 0x1a000, v18
	v_lshlrev_b32_e32 v5, 2, v3
	global_load_dword v24, v5, s[14:15] offset:0
	global_load_dword v26, v5, s[14:15] offset:64
	global_load_dword v28, v5, s[14:15] offset:128
	global_load_dword v30, v5, s[14:15] offset:192
	s_add_u32 m0, s28, 0x0
	s_nop 0
	global_load_lds_dwordx4 v10, s[4:5]
	s_add_u32 m0, s28, 0x2000
	s_nop 0
	global_load_lds_dwordx4 v11, s[4:5]
	s_add_u32 m0, s28, 0x4000
	s_nop 0
	global_load_lds_dwordx4 v12, s[4:5]
	s_add_u32 m0, s28, 0x6000
	s_nop 0
	global_load_lds_dwordx4 v13, s[4:5]
	s_add_u32 s4, s4, s20
	s_addc_u32 s5, s5, 0
	s_add_u32 m0, s28, 0x9000
	s_nop 0
	global_load_lds_dwordx4 v10, s[6:7]
	s_add_u32 m0, s28, 0xb000
	s_nop 0
	global_load_lds_dwordx4 v11, s[6:7]
	s_add_u32 s6, s6, s20
	s_addc_u32 s7, s7, 0
	s_add_u32 m0, s28, 0xd000
	s_nop 0
	global_load_lds_dwordx4 v10, s[4:5]
	s_add_u32 m0, s28, 0xf000
	s_nop 0
	global_load_lds_dwordx4 v11, s[4:5]
	s_add_u32 m0, s28, 0x11000
	s_nop 0
	global_load_lds_dwordx4 v12, s[4:5]
	s_add_u32 m0, s28, 0x13000
	s_nop 0
	global_load_lds_dwordx4 v13, s[4:5]
	s_add_u32 s4, s4, s20
	s_addc_u32 s5, s5, 0
	s_add_u32 m0, s28, 0x16000
	s_nop 0
	global_load_lds_dwordx4 v10, s[6:7]
	s_add_u32 m0, s28, 0x18000
	s_nop 0
	global_load_lds_dwordx4 v11, s[6:7]
	s_add_u32 s6, s6, s20
	s_addc_u32 s7, s7, 0
	s_add_u32 m0, s28, 0x1a000
	s_nop 0
	global_load_lds_dwordx4 v10, s[4:5]
	s_add_u32 m0, s28, 0x1c000
	s_nop 0
	global_load_lds_dwordx4 v11, s[4:5]
	s_add_u32 m0, s28, 0x1e000
	s_nop 0
	global_load_lds_dwordx4 v12, s[4:5]
	s_add_u32 m0, s28, 0x20000
	s_nop 0
	global_load_lds_dwordx4 v13, s[4:5]
	s_add_u32 s4, s4, s20
	s_addc_u32 s5, s5, 0
	s_add_u32 m0, s28, 0x23000
	s_nop 0
	global_load_lds_dwordx4 v10, s[6:7]
	s_add_u32 m0, s28, 0x25000
	s_nop 0
	global_load_lds_dwordx4 v11, s[6:7]
	s_add_u32 s6, s6, s20
	s_addc_u32 s7, s7, 0
	s_waitcnt vmcnt(12) lgkmcnt(0)
	s_barrier
	s_waitcnt lgkmcnt(7)
	ds_read_b128 v[136:139], v15
	ds_read_b128 v[156:159], v17
	ds_read_b128 v[160:163], v17 offset:2048
	ds_read_b128 v[164:167], v17 offset:4096
	ds_read_b128 v[168:171], v17 offset:6144
	ds_read_b128 v[140:143], v15 offset:2048
	ds_read_b128 v[144:147], v15 offset:4096
	ds_read_b128 v[148:151], v15 offset:6144
	s_waitcnt lgkmcnt(7)
	ds_read_b128 v[172:175], v16
	ds_read_b128 v[192:195], v18
	ds_read_b128 v[196:199], v18 offset:2048
	ds_read_b128 v[200:203], v18 offset:4096
	ds_read_b128 v[204:207], v18 offset:6144
	ds_read_b128 v[176:179], v16 offset:2048
	ds_read_b128 v[180:183], v16 offset:4096
	ds_read_b128 v[184:187], v16 offset:6144
	s_waitcnt lgkmcnt(14)
	v_mfma_f32_16x16x32_f16 v[56:59], v[136:139], v[156:159], 0
	s_waitcnt lgkmcnt(13)
	v_mfma_f32_16x16x32_f16 v[60:63], v[136:139], v[160:163], 0
	s_waitcnt lgkmcnt(12)
	v_mfma_f32_16x16x32_f16 v[64:67], v[136:139], v[164:167], 0
	s_waitcnt lgkmcnt(11)
	v_mfma_f32_16x16x32_f16 v[68:71], v[136:139], v[168:171], 0
	s_waitcnt lgkmcnt(10)
	v_mfma_f32_16x16x32_f16 v[72:75], v[140:143], v[156:159], 0
	v_mfma_f32_16x16x32_f16 v[76:79], v[140:143], v[160:163], 0
	v_mfma_f32_16x16x32_f16 v[80:83], v[140:143], v[164:167], 0
	v_mfma_f32_16x16x32_f16 v[84:87], v[140:143], v[168:171], 0
	s_waitcnt lgkmcnt(9)
	v_mfma_f32_16x16x32_f16 v[88:91], v[144:147], v[156:159], 0
	v_mfma_f32_16x16x32_f16 v[92:95], v[144:147], v[160:163], 0
	v_mfma_f32_16x16x32_f16 v[96:99], v[144:147], v[164:167], 0
	v_mfma_f32_16x16x32_f16 v[100:103], v[144:147], v[168:171], 0
	s_waitcnt lgkmcnt(8)
	v_mfma_f32_16x16x32_f16 v[104:107], v[148:151], v[156:159], 0
	v_mfma_f32_16x16x32_f16 v[108:111], v[148:151], v[160:163], 0
	v_mfma_f32_16x16x32_f16 v[112:115], v[148:151], v[164:167], 0
	v_mfma_f32_16x16x32_f16 v[116:119], v[148:151], v[168:171], 0
	s_waitcnt vmcnt(6) lgkmcnt(0)
	s_barrier
	s_waitcnt lgkmcnt(7)
	ds_read_b128 v[136:139], v15 offset:53248
	ds_read_b128 v[156:159], v17 offset:53248
	ds_read_b128 v[160:163], v17 offset:55296
	ds_read_b128 v[164:167], v17 offset:57344
	ds_read_b128 v[168:171], v17 offset:59392
	ds_read_b128 v[140:143], v15 offset:55296
	ds_read_b128 v[144:147], v15 offset:57344
	ds_read_b128 v[148:151], v15 offset:59392
	s_waitcnt lgkmcnt(14)
	v_mfma_f32_16x16x32_f16 v[56:59], v[172:175], v[192:195], v[56:59]
	s_add_u32 m0, s28, 0x0
	s_nop 0
	global_load_lds_dwordx4 v10, s[4:5]
	s_waitcnt lgkmcnt(13)
	v_mfma_f32_16x16x32_f16 v[60:63], v[172:175], v[196:199], v[60:63]
	s_waitcnt lgkmcnt(12)
	v_mfma_f32_16x16x32_f16 v[64:67], v[172:175], v[200:203], v[64:67]
	s_waitcnt lgkmcnt(11)
	v_mfma_f32_16x16x32_f16 v[68:71], v[172:175], v[204:207], v[68:71]
	s_waitcnt lgkmcnt(10)
	v_mfma_f32_16x16x32_f16 v[72:75], v[176:179], v[192:195], v[72:75]
	v_mfma_f32_16x16x32_f16 v[76:79], v[176:179], v[196:199], v[76:79]
	s_add_u32 m0, s28, 0x2000
	s_nop 0
	global_load_lds_dwordx4 v11, s[4:5]
	v_mfma_f32_16x16x32_f16 v[80:83], v[176:179], v[200:203], v[80:83]
	v_mfma_f32_16x16x32_f16 v[84:87], v[176:179], v[204:207], v[84:87]
	s_waitcnt lgkmcnt(9)
	v_mfma_f32_16x16x32_f16 v[88:91], v[180:183], v[192:195], v[88:91]
	v_mfma_f32_16x16x32_f16 v[92:95], v[180:183], v[196:199], v[92:95]
	v_mfma_f32_16x16x32_f16 v[96:99], v[180:183], v[200:203], v[96:99]
	s_add_u32 m0, s28, 0x4000
	s_nop 0
	global_load_lds_dwordx4 v12, s[4:5]
	v_mfma_f32_16x16x32_f16 v[100:103], v[180:183], v[204:207], v[100:103]
	s_waitcnt lgkmcnt(8)
	v_mfma_f32_16x16x32_f16 v[104:107], v[184:187], v[192:195], v[104:107]
	v_mfma_f32_16x16x32_f16 v[108:111], v[184:187], v[196:199], v[108:111]
	v_mfma_f32_16x16x32_f16 v[112:115], v[184:187], v[200:203], v[112:115]
	v_mfma_f32_16x16x32_f16 v[116:119], v[184:187], v[204:207], v[116:119]
	s_waitcnt lgkmcnt(7)
	ds_read_b128 v[172:175], v16 offset:53248
	ds_read_b128 v[192:195], v18 offset:53248
	ds_read_b128 v[196:199], v18 offset:55296
	ds_read_b128 v[200:203], v18 offset:57344
	ds_read_b128 v[204:207], v18 offset:59392
	ds_read_b128 v[176:179], v16 offset:55296
	ds_read_b128 v[180:183], v16 offset:57344
	ds_read_b128 v[184:187], v16 offset:59392
	s_waitcnt lgkmcnt(14)
	v_mfma_f32_16x16x32_f16 v[56:59], v[136:139], v[156:159], v[56:59]
	s_add_u32 m0, s28, 0x6000
	s_nop 0
	global_load_lds_dwordx4 v13, s[4:5]
	s_add_u32 s4, s4, s20
	s_addc_u32 s5, s5, 0
	s_waitcnt lgkmcnt(13)
	v_mfma_f32_16x16x32_f16 v[60:63], v[136:139], v[160:163], v[60:63]
	s_waitcnt lgkmcnt(12)
	v_mfma_f32_16x16x32_f16 v[64:67], v[136:139], v[164:167], v[64:67]
	s_waitcnt lgkmcnt(11)
	v_mfma_f32_16x16x32_f16 v[68:71], v[136:139], v[168:171], v[68:71]
	s_waitcnt lgkmcnt(10)
	v_mfma_f32_16x16x32_f16 v[72:75], v[140:143], v[156:159], v[72:75]
	v_mfma_f32_16x16x32_f16 v[76:79], v[140:143], v[160:163], v[76:79]
	s_add_u32 m0, s28, 0x9000
	s_nop 0
	global_load_lds_dwordx4 v10, s[6:7]
	v_mfma_f32_16x16x32_f16 v[80:83], v[140:143], v[164:167], v[80:83]
	v_mfma_f32_16x16x32_f16 v[84:87], v[140:143], v[168:171], v[84:87]
	s_waitcnt lgkmcnt(9)
	v_mfma_f32_16x16x32_f16 v[88:91], v[144:147], v[156:159], v[88:91]
	v_mfma_f32_16x16x32_f16 v[92:95], v[144:147], v[160:163], v[92:95]
	v_mfma_f32_16x16x32_f16 v[96:99], v[144:147], v[164:167], v[96:99]
	s_add_u32 m0, s28, 0xb000
	s_nop 0
	global_load_lds_dwordx4 v11, s[6:7]
	s_add_u32 s6, s6, s20
	s_addc_u32 s7, s7, 0
	v_mfma_f32_16x16x32_f16 v[100:103], v[144:147], v[168:171], v[100:103]
	s_waitcnt lgkmcnt(8)
	v_mfma_f32_16x16x32_f16 v[104:107], v[148:151], v[156:159], v[104:107]
	v_mfma_f32_16x16x32_f16 v[108:111], v[148:151], v[160:163], v[108:111]
	v_mfma_f32_16x16x32_f16 v[112:115], v[148:151], v[164:167], v[112:115]
	v_mfma_f32_16x16x32_f16 v[116:119], v[148:151], v[168:171], v[116:119]
	s_waitcnt vmcnt(6) lgkmcnt(0)
	s_barrier
	s_waitcnt lgkmcnt(7)
	ds_read_b128 v[136:139], v19
	ds_read_b128 v[156:159], v21
	ds_read_b128 v[160:163], v21 offset:2048
	ds_read_b128 v[164:167], v21 offset:4096
	ds_read_b128 v[168:171], v21 offset:6144
	ds_read_b128 v[140:143], v19 offset:2048
	ds_read_b128 v[144:147], v19 offset:4096
	ds_read_b128 v[148:151], v19 offset:6144
	s_waitcnt lgkmcnt(14)
	v_mfma_f32_16x16x32_f16 v[56:59], v[172:175], v[192:195], v[56:59]
	s_add_u32 m0, s28, 0xd000
	s_nop 0
	global_load_lds_dwordx4 v10, s[4:5]
	s_waitcnt lgkmcnt(13)
	v_mfma_f32_16x16x32_f16 v[60:63], v[172:175], v[196:199], v[60:63]
	s_waitcnt lgkmcnt(12)
	v_mfma_f32_16x16x32_f16 v[64:67], v[172:175], v[200:203], v[64:67]
	s_waitcnt lgkmcnt(11)
	v_mfma_f32_16x16x32_f16 v[68:71], v[172:175], v[204:207], v[68:71]
	s_waitcnt lgkmcnt(10)
	v_mfma_f32_16x16x32_f16 v[72:75], v[176:179], v[192:195], v[72:75]
	v_mfma_f32_16x16x32_f16 v[76:79], v[176:179], v[196:199], v[76:79]
	s_add_u32 m0, s28, 0xf000
	s_nop 0
	global_load_lds_dwordx4 v11, s[4:5]
	v_mfma_f32_16x16x32_f16 v[80:83], v[176:179], v[200:203], v[80:83]
	v_mfma_f32_16x16x32_f16 v[84:87], v[176:179], v[204:207], v[84:87]
	s_waitcnt lgkmcnt(9)
	v_mfma_f32_16x16x32_f16 v[88:91], v[180:183], v[192:195], v[88:91]
	v_mfma_f32_16x16x32_f16 v[92:95], v[180:183], v[196:199], v[92:95]
	v_mfma_f32_16x16x32_f16 v[96:99], v[180:183], v[200:203], v[96:99]
	s_add_u32 m0, s28, 0x11000
	s_nop 0
	global_load_lds_dwordx4 v12, s[4:5]
	v_mfma_f32_16x16x32_f16 v[100:103], v[180:183], v[204:207], v[100:103]
	s_waitcnt lgkmcnt(8)
	v_mfma_f32_16x16x32_f16 v[104:107], v[184:187], v[192:195], v[104:107]
	v_mfma_f32_16x16x32_f16 v[108:111], v[184:187], v[196:199], v[108:111]
	v_mfma_f32_16x16x32_f16 v[112:115], v[184:187], v[200:203], v[112:115]
	v_mfma_f32_16x16x32_f16 v[116:119], v[184:187], v[204:207], v[116:119]
	s_waitcnt lgkmcnt(7)
	ds_read_b128 v[172:175], v20
	ds_read_b128 v[192:195], v22
	ds_read_b128 v[196:199], v22 offset:2048
	ds_read_b128 v[200:203], v22 offset:4096
	ds_read_b128 v[204:207], v22 offset:6144
	ds_read_b128 v[176:179], v20 offset:2048
	ds_read_b128 v[180:183], v20 offset:4096
	ds_read_b128 v[184:187], v20 offset:6144
	s_waitcnt lgkmcnt(14)
	v_mfma_f32_16x16x32_f16 v[56:59], v[136:139], v[156:159], v[56:59]
	s_add_u32 m0, s28, 0x13000
	s_nop 0
	global_load_lds_dwordx4 v13, s[4:5]
	s_add_u32 s4, s4, s20
	s_addc_u32 s5, s5, 0
	s_waitcnt lgkmcnt(13)
	v_mfma_f32_16x16x32_f16 v[60:63], v[136:139], v[160:163], v[60:63]
	s_waitcnt lgkmcnt(12)
	v_mfma_f32_16x16x32_f16 v[64:67], v[136:139], v[164:167], v[64:67]
	s_waitcnt lgkmcnt(11)
	v_mfma_f32_16x16x32_f16 v[68:71], v[136:139], v[168:171], v[68:71]
	s_waitcnt lgkmcnt(10)
	v_mfma_f32_16x16x32_f16 v[72:75], v[140:143], v[156:159], v[72:75]
	v_mfma_f32_16x16x32_f16 v[76:79], v[140:143], v[160:163], v[76:79]
	s_add_u32 m0, s28, 0x16000
	s_nop 0
	global_load_lds_dwordx4 v10, s[6:7]
	v_mfma_f32_16x16x32_f16 v[80:83], v[140:143], v[164:167], v[80:83]
	v_mfma_f32_16x16x32_f16 v[84:87], v[140:143], v[168:171], v[84:87]
	s_waitcnt lgkmcnt(9)
	v_mfma_f32_16x16x32_f16 v[88:91], v[144:147], v[156:159], v[88:91]
	v_mfma_f32_16x16x32_f16 v[92:95], v[144:147], v[160:163], v[92:95]
	v_mfma_f32_16x16x32_f16 v[96:99], v[144:147], v[164:167], v[96:99]
	s_add_u32 m0, s28, 0x18000
	s_nop 0
	global_load_lds_dwordx4 v11, s[6:7]
	s_add_u32 s6, s6, s20
	s_addc_u32 s7, s7, 0
	v_mfma_f32_16x16x32_f16 v[100:103], v[144:147], v[168:171], v[100:103]
	s_waitcnt lgkmcnt(8)
	v_mfma_f32_16x16x32_f16 v[104:107], v[148:151], v[156:159], v[104:107]
	v_mfma_f32_16x16x32_f16 v[108:111], v[148:151], v[160:163], v[108:111]
	v_mfma_f32_16x16x32_f16 v[112:115], v[148:151], v[164:167], v[112:115]
	v_mfma_f32_16x16x32_f16 v[116:119], v[148:151], v[168:171], v[116:119]
	s_waitcnt vmcnt(6) lgkmcnt(0)
	s_barrier
	s_waitcnt lgkmcnt(7)
	ds_read_b128 v[136:139], v15
	ds_read_b128 v[156:159], v17
	ds_read_b128 v[160:163], v17 offset:2048
	ds_read_b128 v[164:167], v17 offset:4096
	ds_read_b128 v[168:171], v17 offset:6144
	ds_read_b128 v[140:143], v15 offset:2048
	ds_read_b128 v[144:147], v15 offset:4096
	ds_read_b128 v[148:151], v15 offset:6144
	s_waitcnt lgkmcnt(14)
	v_mfma_f32_16x16x32_f16 v[56:59], v[172:175], v[192:195], v[56:59]
	s_add_u32 m0, s28, 0x1a000
	s_nop 0
	global_load_lds_dwordx4 v10, s[4:5]
	s_waitcnt lgkmcnt(13)
	v_mfma_f32_16x16x32_f16 v[60:63], v[172:175], v[196:199], v[60:63]
	s_waitcnt lgkmcnt(12)
	v_mfma_f32_16x16x32_f16 v[64:67], v[172:175], v[200:203], v[64:67]
	s_waitcnt lgkmcnt(11)
	v_mfma_f32_16x16x32_f16 v[68:71], v[172:175], v[204:207], v[68:71]
	s_waitcnt lgkmcnt(10)
	v_mfma_f32_16x16x32_f16 v[72:75], v[176:179], v[192:195], v[72:75]
	v_mfma_f32_16x16x32_f16 v[76:79], v[176:179], v[196:199], v[76:79]
	s_add_u32 m0, s28, 0x1c000
	s_nop 0
	global_load_lds_dwordx4 v11, s[4:5]
	v_mfma_f32_16x16x32_f16 v[80:83], v[176:179], v[200:203], v[80:83]
	v_mfma_f32_16x16x32_f16 v[84:87], v[176:179], v[204:207], v[84:87]
	s_waitcnt lgkmcnt(9)
	v_mfma_f32_16x16x32_f16 v[88:91], v[180:183], v[192:195], v[88:91]
	v_mfma_f32_16x16x32_f16 v[92:95], v[180:183], v[196:199], v[92:95]
	v_mfma_f32_16x16x32_f16 v[96:99], v[180:183], v[200:203], v[96:99]
	s_add_u32 m0, s28, 0x1e000
	s_nop 0
	global_load_lds_dwordx4 v12, s[4:5]
	v_mfma_f32_16x16x32_f16 v[100:103], v[180:183], v[204:207], v[100:103]
	s_waitcnt lgkmcnt(8)
	v_mfma_f32_16x16x32_f16 v[104:107], v[184:187], v[192:195], v[104:107]
	v_mfma_f32_16x16x32_f16 v[108:111], v[184:187], v[196:199], v[108:111]
	v_mfma_f32_16x16x32_f16 v[112:115], v[184:187], v[200:203], v[112:115]
	v_mfma_f32_16x16x32_f16 v[116:119], v[184:187], v[204:207], v[116:119]
	s_waitcnt lgkmcnt(7)
	ds_read_b128 v[172:175], v16
	ds_read_b128 v[192:195], v18
	ds_read_b128 v[196:199], v18 offset:2048
	ds_read_b128 v[200:203], v18 offset:4096
	ds_read_b128 v[204:207], v18 offset:6144
	ds_read_b128 v[176:179], v16 offset:2048
	ds_read_b128 v[180:183], v16 offset:4096
	ds_read_b128 v[184:187], v16 offset:6144
	s_waitcnt lgkmcnt(14)
	v_mfma_f32_16x16x32_f16 v[56:59], v[136:139], v[156:159], v[56:59]
	s_add_u32 m0, s28, 0x20000
	s_nop 0
	global_load_lds_dwordx4 v13, s[4:5]
	s_add_u32 s4, s4, s20
	s_addc_u32 s5, s5, 0
	s_waitcnt lgkmcnt(13)
	v_mfma_f32_16x16x32_f16 v[60:63], v[136:139], v[160:163], v[60:63]
	s_waitcnt lgkmcnt(12)
	v_mfma_f32_16x16x32_f16 v[64:67], v[136:139], v[164:167], v[64:67]
	s_waitcnt lgkmcnt(11)
	v_mfma_f32_16x16x32_f16 v[68:71], v[136:139], v[168:171], v[68:71]
	s_waitcnt lgkmcnt(10)
	v_mfma_f32_16x16x32_f16 v[72:75], v[140:143], v[156:159], v[72:75]
	v_mfma_f32_16x16x32_f16 v[76:79], v[140:143], v[160:163], v[76:79]
	s_add_u32 m0, s28, 0x23000
	s_nop 0
	global_load_lds_dwordx4 v10, s[6:7]
	v_mfma_f32_16x16x32_f16 v[80:83], v[140:143], v[164:167], v[80:83]
	v_mfma_f32_16x16x32_f16 v[84:87], v[140:143], v[168:171], v[84:87]
	s_waitcnt lgkmcnt(9)
	v_mfma_f32_16x16x32_f16 v[88:91], v[144:147], v[156:159], v[88:91]
	v_mfma_f32_16x16x32_f16 v[92:95], v[144:147], v[160:163], v[92:95]
	v_mfma_f32_16x16x32_f16 v[96:99], v[144:147], v[164:167], v[96:99]
	s_add_u32 m0, s28, 0x25000
	s_nop 0
	global_load_lds_dwordx4 v11, s[6:7]
	s_add_u32 s6, s6, s20
	s_addc_u32 s7, s7, 0
	v_mfma_f32_16x16x32_f16 v[100:103], v[144:147], v[168:171], v[100:103]
	s_waitcnt lgkmcnt(8)
	v_mfma_f32_16x16x32_f16 v[104:107], v[148:151], v[156:159], v[104:107]
	v_mfma_f32_16x16x32_f16 v[108:111], v[148:151], v[160:163], v[108:111]
	v_mfma_f32_16x16x32_f16 v[112:115], v[148:151], v[164:167], v[112:115]
	v_mfma_f32_16x16x32_f16 v[116:119], v[148:151], v[168:171], v[116:119]
	s_waitcnt vmcnt(6) lgkmcnt(0)
	s_barrier
	s_waitcnt lgkmcnt(7)
	ds_read_b128 v[136:139], v15 offset:53248
	ds_read_b128 v[156:159], v17 offset:53248
	ds_read_b128 v[160:163], v17 offset:55296
	ds_read_b128 v[164:167], v17 offset:57344
	ds_read_b128 v[168:171], v17 offset:59392
	ds_read_b128 v[140:143], v15 offset:55296
	ds_read_b128 v[144:147], v15 offset:57344
	ds_read_b128 v[148:151], v15 offset:59392
	s_waitcnt lgkmcnt(14)
	v_mfma_f32_16x16x32_f16 v[56:59], v[172:175], v[192:195], v[56:59]
	s_add_u32 m0, s28, 0x0
	s_nop 0
	global_load_lds_dwordx4 v10, s[4:5]
	s_waitcnt lgkmcnt(13)
	v_mfma_f32_16x16x32_f16 v[60:63], v[172:175], v[196:199], v[60:63]
	s_waitcnt lgkmcnt(12)
	v_mfma_f32_16x16x32_f16 v[64:67], v[172:175], v[200:203], v[64:67]
	s_waitcnt lgkmcnt(11)
	v_mfma_f32_16x16x32_f16 v[68:71], v[172:175], v[204:207], v[68:71]
	s_waitcnt lgkmcnt(10)
	v_mfma_f32_16x16x32_f16 v[72:75], v[176:179], v[192:195], v[72:75]
	v_mfma_f32_16x16x32_f16 v[76:79], v[176:179], v[196:199], v[76:79]
	s_add_u32 m0, s28, 0x2000
	s_nop 0
	global_load_lds_dwordx4 v11, s[4:5]
	v_mfma_f32_16x16x32_f16 v[80:83], v[176:179], v[200:203], v[80:83]
	v_mfma_f32_16x16x32_f16 v[84:87], v[176:179], v[204:207], v[84:87]
	s_waitcnt lgkmcnt(9)
	v_mfma_f32_16x16x32_f16 v[88:91], v[180:183], v[192:195], v[88:91]
	v_mfma_f32_16x16x32_f16 v[92:95], v[180:183], v[196:199], v[92:95]
	v_mfma_f32_16x16x32_f16 v[96:99], v[180:183], v[200:203], v[96:99]
	s_add_u32 m0, s28, 0x4000
	s_nop 0
	global_load_lds_dwordx4 v12, s[4:5]
	v_mfma_f32_16x16x32_f16 v[100:103], v[180:183], v[204:207], v[100:103]
	s_waitcnt lgkmcnt(8)
	v_mfma_f32_16x16x32_f16 v[104:107], v[184:187], v[192:195], v[104:107]
	v_mfma_f32_16x16x32_f16 v[108:111], v[184:187], v[196:199], v[108:111]
	v_mfma_f32_16x16x32_f16 v[112:115], v[184:187], v[200:203], v[112:115]
	v_mfma_f32_16x16x32_f16 v[116:119], v[184:187], v[204:207], v[116:119]
	s_waitcnt lgkmcnt(7)
	ds_read_b128 v[172:175], v16 offset:53248
	ds_read_b128 v[192:195], v18 offset:53248
	ds_read_b128 v[196:199], v18 offset:55296
	ds_read_b128 v[200:203], v18 offset:57344
	ds_read_b128 v[204:207], v18 offset:59392
	ds_read_b128 v[176:179], v16 offset:55296
	ds_read_b128 v[180:183], v16 offset:57344
	ds_read_b128 v[184:187], v16 offset:59392
	s_waitcnt lgkmcnt(14)
	v_mfma_f32_16x16x32_f16 v[56:59], v[136:139], v[156:159], v[56:59]
	s_add_u32 m0, s28, 0x6000
	s_nop 0
	global_load_lds_dwordx4 v13, s[4:5]
	s_add_u32 s4, s4, s20
	s_addc_u32 s5, s5, 0
	s_waitcnt lgkmcnt(13)
	v_mfma_f32_16x16x32_f16 v[60:63], v[136:139], v[160:163], v[60:63]
	s_waitcnt lgkmcnt(12)
	v_mfma_f32_16x16x32_f16 v[64:67], v[136:139], v[164:167], v[64:67]
	s_waitcnt lgkmcnt(11)
	v_mfma_f32_16x16x32_f16 v[68:71], v[136:139], v[168:171], v[68:71]
	s_waitcnt lgkmcnt(10)
	v_mfma_f32_16x16x32_f16 v[72:75], v[140:143], v[156:159], v[72:75]
	v_mfma_f32_16x16x32_f16 v[76:79], v[140:143], v[160:163], v[76:79]
	s_add_u32 m0, s28, 0x9000
	s_nop 0
	global_load_lds_dwordx4 v10, s[6:7]
	v_mfma_f32_16x16x32_f16 v[80:83], v[140:143], v[164:167], v[80:83]
	v_mfma_f32_16x16x32_f16 v[84:87], v[140:143], v[168:171], v[84:87]
	s_waitcnt lgkmcnt(9)
	v_mfma_f32_16x16x32_f16 v[88:91], v[144:147], v[156:159], v[88:91]
	v_mfma_f32_16x16x32_f16 v[92:95], v[144:147], v[160:163], v[92:95]
	v_mfma_f32_16x16x32_f16 v[96:99], v[144:147], v[164:167], v[96:99]
	s_add_u32 m0, s28, 0xb000
	s_nop 0
	global_load_lds_dwordx4 v11, s[6:7]
	s_add_u32 s6, s6, s20
	s_addc_u32 s7, s7, 0
	v_mfma_f32_16x16x32_f16 v[100:103], v[144:147], v[168:171], v[100:103]
	s_waitcnt lgkmcnt(8)
	v_mfma_f32_16x16x32_f16 v[104:107], v[148:151], v[156:159], v[104:107]
	v_mfma_f32_16x16x32_f16 v[108:111], v[148:151], v[160:163], v[108:111]
	v_mfma_f32_16x16x32_f16 v[112:115], v[148:151], v[164:167], v[112:115]
	v_mfma_f32_16x16x32_f16 v[116:119], v[148:151], v[168:171], v[116:119]
	s_waitcnt vmcnt(6) lgkmcnt(0)
	s_barrier
	s_waitcnt lgkmcnt(7)
	ds_read_b128 v[136:139], v19
	ds_read_b128 v[156:159], v21
	ds_read_b128 v[160:163], v21 offset:2048
	ds_read_b128 v[164:167], v21 offset:4096
	ds_read_b128 v[168:171], v21 offset:6144
	ds_read_b128 v[140:143], v19 offset:2048
	ds_read_b128 v[144:147], v19 offset:4096
	ds_read_b128 v[148:151], v19 offset:6144
	s_waitcnt lgkmcnt(14)
	v_mfma_f32_16x16x32_f16 v[56:59], v[172:175], v[192:195], v[56:59]
	s_add_u32 m0, s28, 0xd000
	s_nop 0
	global_load_lds_dwordx4 v10, s[4:5]
	s_waitcnt lgkmcnt(13)
	v_mfma_f32_16x16x32_f16 v[60:63], v[172:175], v[196:199], v[60:63]
	s_waitcnt lgkmcnt(12)
	v_mfma_f32_16x16x32_f16 v[64:67], v[172:175], v[200:203], v[64:67]
	s_waitcnt lgkmcnt(11)
	v_mfma_f32_16x16x32_f16 v[68:71], v[172:175], v[204:207], v[68:71]
	s_waitcnt lgkmcnt(10)
	v_mfma_f32_16x16x32_f16 v[72:75], v[176:179], v[192:195], v[72:75]
	v_mfma_f32_16x16x32_f16 v[76:79], v[176:179], v[196:199], v[76:79]
	s_add_u32 m0, s28, 0xf000
	s_nop 0
	global_load_lds_dwordx4 v11, s[4:5]
	v_mfma_f32_16x16x32_f16 v[80:83], v[176:179], v[200:203], v[80:83]
	v_mfma_f32_16x16x32_f16 v[84:87], v[176:179], v[204:207], v[84:87]
	s_waitcnt lgkmcnt(9)
	v_mfma_f32_16x16x32_f16 v[88:91], v[180:183], v[192:195], v[88:91]
	v_mfma_f32_16x16x32_f16 v[92:95], v[180:183], v[196:199], v[92:95]
	v_mfma_f32_16x16x32_f16 v[96:99], v[180:183], v[200:203], v[96:99]
	s_add_u32 m0, s28, 0x11000
	s_nop 0
	global_load_lds_dwordx4 v12, s[4:5]
	v_mfma_f32_16x16x32_f16 v[100:103], v[180:183], v[204:207], v[100:103]
	s_waitcnt lgkmcnt(8)
	v_mfma_f32_16x16x32_f16 v[104:107], v[184:187], v[192:195], v[104:107]
	v_mfma_f32_16x16x32_f16 v[108:111], v[184:187], v[196:199], v[108:111]
	v_mfma_f32_16x16x32_f16 v[112:115], v[184:187], v[200:203], v[112:115]
	v_mfma_f32_16x16x32_f16 v[116:119], v[184:187], v[204:207], v[116:119]
	s_waitcnt lgkmcnt(7)
	ds_read_b128 v[172:175], v20
	ds_read_b128 v[192:195], v22
	ds_read_b128 v[196:199], v22 offset:2048
	ds_read_b128 v[200:203], v22 offset:4096
	ds_read_b128 v[204:207], v22 offset:6144
	ds_read_b128 v[176:179], v20 offset:2048
	ds_read_b128 v[180:183], v20 offset:4096
	ds_read_b128 v[184:187], v20 offset:6144
	s_waitcnt lgkmcnt(14)
	v_mfma_f32_16x16x32_f16 v[56:59], v[136:139], v[156:159], v[56:59]
	s_add_u32 m0, s28, 0x13000
	s_nop 0
	global_load_lds_dwordx4 v13, s[4:5]
	s_add_u32 s4, s4, s20
	s_addc_u32 s5, s5, 0
	s_waitcnt lgkmcnt(13)
	v_mfma_f32_16x16x32_f16 v[60:63], v[136:139], v[160:163], v[60:63]
	s_waitcnt lgkmcnt(12)
	v_mfma_f32_16x16x32_f16 v[64:67], v[136:139], v[164:167], v[64:67]
	s_waitcnt lgkmcnt(11)
	v_mfma_f32_16x16x32_f16 v[68:71], v[136:139], v[168:171], v[68:71]
	s_waitcnt lgkmcnt(10)
	v_mfma_f32_16x16x32_f16 v[72:75], v[140:143], v[156:159], v[72:75]
	v_mfma_f32_16x16x32_f16 v[76:79], v[140:143], v[160:163], v[76:79]
	s_add_u32 m0, s28, 0x16000
	s_nop 0
	global_load_lds_dwordx4 v10, s[6:7]
	v_mfma_f32_16x16x32_f16 v[80:83], v[140:143], v[164:167], v[80:83]
	v_mfma_f32_16x16x32_f16 v[84:87], v[140:143], v[168:171], v[84:87]
	s_waitcnt lgkmcnt(9)
	v_mfma_f32_16x16x32_f16 v[88:91], v[144:147], v[156:159], v[88:91]
	v_mfma_f32_16x16x32_f16 v[92:95], v[144:147], v[160:163], v[92:95]
	v_mfma_f32_16x16x32_f16 v[96:99], v[144:147], v[164:167], v[96:99]
	s_add_u32 m0, s28, 0x18000
	s_nop 0
	global_load_lds_dwordx4 v11, s[6:7]
	s_add_u32 s6, s6, s20
	s_addc_u32 s7, s7, 0
	v_mfma_f32_16x16x32_f16 v[100:103], v[144:147], v[168:171], v[100:103]
	s_waitcnt lgkmcnt(8)
	v_mfma_f32_16x16x32_f16 v[104:107], v[148:151], v[156:159], v[104:107]
	v_mfma_f32_16x16x32_f16 v[108:111], v[148:151], v[160:163], v[108:111]
	v_mfma_f32_16x16x32_f16 v[112:115], v[148:151], v[164:167], v[112:115]
	v_mfma_f32_16x16x32_f16 v[116:119], v[148:151], v[168:171], v[116:119]
	s_waitcnt vmcnt(6) lgkmcnt(0)
	s_barrier
	s_waitcnt lgkmcnt(7)
	ds_read_b128 v[136:139], v15
	ds_read_b128 v[156:159], v17
	ds_read_b128 v[160:163], v17 offset:2048
	ds_read_b128 v[164:167], v17 offset:4096
	ds_read_b128 v[168:171], v17 offset:6144
	ds_read_b128 v[140:143], v15 offset:2048
	ds_read_b128 v[144:147], v15 offset:4096
	ds_read_b128 v[148:151], v15 offset:6144
	s_waitcnt lgkmcnt(14)
	v_mfma_f32_16x16x32_f16 v[56:59], v[172:175], v[192:195], v[56:59]
	s_add_u32 m0, s28, 0x1a000
	s_nop 0
	global_load_lds_dwordx4 v10, s[4:5]
	s_waitcnt lgkmcnt(13)
	v_mfma_f32_16x16x32_f16 v[60:63], v[172:175], v[196:199], v[60:63]
	s_waitcnt lgkmcnt(12)
	v_mfma_f32_16x16x32_f16 v[64:67], v[172:175], v[200:203], v[64:67]
	s_waitcnt lgkmcnt(11)
	v_mfma_f32_16x16x32_f16 v[68:71], v[172:175], v[204:207], v[68:71]
	s_waitcnt lgkmcnt(10)
	v_mfma_f32_16x16x32_f16 v[72:75], v[176:179], v[192:195], v[72:75]
	v_mfma_f32_16x16x32_f16 v[76:79], v[176:179], v[196:199], v[76:79]
	s_add_u32 m0, s28, 0x1c000
	s_nop 0
	global_load_lds_dwordx4 v11, s[4:5]
	v_mfma_f32_16x16x32_f16 v[80:83], v[176:179], v[200:203], v[80:83]
	v_mfma_f32_16x16x32_f16 v[84:87], v[176:179], v[204:207], v[84:87]
	s_waitcnt lgkmcnt(9)
	v_mfma_f32_16x16x32_f16 v[88:91], v[180:183], v[192:195], v[88:91]
	v_mfma_f32_16x16x32_f16 v[92:95], v[180:183], v[196:199], v[92:95]
	v_mfma_f32_16x16x32_f16 v[96:99], v[180:183], v[200:203], v[96:99]
	s_add_u32 m0, s28, 0x1e000
	s_nop 0
	global_load_lds_dwordx4 v12, s[4:5]
	v_mfma_f32_16x16x32_f16 v[100:103], v[180:183], v[204:207], v[100:103]
	s_waitcnt lgkmcnt(8)
	v_mfma_f32_16x16x32_f16 v[104:107], v[184:187], v[192:195], v[104:107]
	v_mfma_f32_16x16x32_f16 v[108:111], v[184:187], v[196:199], v[108:111]
	v_mfma_f32_16x16x32_f16 v[112:115], v[184:187], v[200:203], v[112:115]
	v_mfma_f32_16x16x32_f16 v[116:119], v[184:187], v[204:207], v[116:119]
	s_waitcnt lgkmcnt(7)
	ds_read_b128 v[172:175], v16
	ds_read_b128 v[192:195], v18
	ds_read_b128 v[196:199], v18 offset:2048
	ds_read_b128 v[200:203], v18 offset:4096
	ds_read_b128 v[204:207], v18 offset:6144
	ds_read_b128 v[176:179], v16 offset:2048
	ds_read_b128 v[180:183], v16 offset:4096
	ds_read_b128 v[184:187], v16 offset:6144
	s_waitcnt lgkmcnt(14)
	v_mfma_f32_16x16x32_f16 v[56:59], v[136:139], v[156:159], v[56:59]
	s_add_u32 m0, s28, 0x20000
	s_nop 0
	global_load_lds_dwordx4 v13, s[4:5]
	s_add_u32 s4, s4, s20
	s_addc_u32 s5, s5, 0
	s_waitcnt lgkmcnt(13)
	v_mfma_f32_16x16x32_f16 v[60:63], v[136:139], v[160:163], v[60:63]
	s_waitcnt lgkmcnt(12)
	v_mfma_f32_16x16x32_f16 v[64:67], v[136:139], v[164:167], v[64:67]
	s_waitcnt lgkmcnt(11)
	v_mfma_f32_16x16x32_f16 v[68:71], v[136:139], v[168:171], v[68:71]
	s_waitcnt lgkmcnt(10)
	v_mfma_f32_16x16x32_f16 v[72:75], v[140:143], v[156:159], v[72:75]
	v_mfma_f32_16x16x32_f16 v[76:79], v[140:143], v[160:163], v[76:79]
	s_add_u32 m0, s28, 0x23000
	s_nop 0
	global_load_lds_dwordx4 v10, s[6:7]
	v_mfma_f32_16x16x32_f16 v[80:83], v[140:143], v[164:167], v[80:83]
	v_mfma_f32_16x16x32_f16 v[84:87], v[140:143], v[168:171], v[84:87]
	s_waitcnt lgkmcnt(9)
	v_mfma_f32_16x16x32_f16 v[88:91], v[144:147], v[156:159], v[88:91]
	v_mfma_f32_16x16x32_f16 v[92:95], v[144:147], v[160:163], v[92:95]
	v_mfma_f32_16x16x32_f16 v[96:99], v[144:147], v[164:167], v[96:99]
	s_add_u32 m0, s28, 0x25000
	s_nop 0
	global_load_lds_dwordx4 v11, s[6:7]
	s_add_u32 s6, s6, s20
	s_addc_u32 s7, s7, 0
	v_mfma_f32_16x16x32_f16 v[100:103], v[144:147], v[168:171], v[100:103]
	s_waitcnt lgkmcnt(8)
	v_mfma_f32_16x16x32_f16 v[104:107], v[148:151], v[156:159], v[104:107]
	v_mfma_f32_16x16x32_f16 v[108:111], v[148:151], v[160:163], v[108:111]
	v_mfma_f32_16x16x32_f16 v[112:115], v[148:151], v[164:167], v[112:115]
	v_mfma_f32_16x16x32_f16 v[116:119], v[148:151], v[168:171], v[116:119]
	s_waitcnt vmcnt(6) lgkmcnt(0)
	s_barrier
	s_waitcnt lgkmcnt(7)
	ds_read_b128 v[136:139], v15 offset:53248
	ds_read_b128 v[156:159], v17 offset:53248
	ds_read_b128 v[160:163], v17 offset:55296
	ds_read_b128 v[164:167], v17 offset:57344
	ds_read_b128 v[168:171], v17 offset:59392
	ds_read_b128 v[140:143], v15 offset:55296
	ds_read_b128 v[144:147], v15 offset:57344
	ds_read_b128 v[148:151], v15 offset:59392
	s_waitcnt lgkmcnt(14)
	v_mfma_f32_16x16x32_f16 v[56:59], v[172:175], v[192:195], v[56:59]
	s_add_u32 m0, s28, 0x0
	s_nop 0
	global_load_lds_dwordx4 v10, s[4:5]
	s_waitcnt lgkmcnt(13)
	v_mfma_f32_16x16x32_f16 v[60:63], v[172:175], v[196:199], v[60:63]
	s_waitcnt lgkmcnt(12)
	v_mfma_f32_16x16x32_f16 v[64:67], v[172:175], v[200:203], v[64:67]
	s_waitcnt lgkmcnt(11)
	v_mfma_f32_16x16x32_f16 v[68:71], v[172:175], v[204:207], v[68:71]
	s_waitcnt lgkmcnt(10)
	v_mfma_f32_16x16x32_f16 v[72:75], v[176:179], v[192:195], v[72:75]
	v_mfma_f32_16x16x32_f16 v[76:79], v[176:179], v[196:199], v[76:79]
	s_add_u32 m0, s28, 0x2000
	s_nop 0
	global_load_lds_dwordx4 v11, s[4:5]
	v_mfma_f32_16x16x32_f16 v[80:83], v[176:179], v[200:203], v[80:83]
	v_mfma_f32_16x16x32_f16 v[84:87], v[176:179], v[204:207], v[84:87]
	s_waitcnt lgkmcnt(9)
	v_mfma_f32_16x16x32_f16 v[88:91], v[180:183], v[192:195], v[88:91]
	v_mfma_f32_16x16x32_f16 v[92:95], v[180:183], v[196:199], v[92:95]
	v_mfma_f32_16x16x32_f16 v[96:99], v[180:183], v[200:203], v[96:99]
	s_add_u32 m0, s28, 0x4000
	s_nop 0
	global_load_lds_dwordx4 v12, s[4:5]
	v_mfma_f32_16x16x32_f16 v[100:103], v[180:183], v[204:207], v[100:103]
	s_waitcnt lgkmcnt(8)
	v_mfma_f32_16x16x32_f16 v[104:107], v[184:187], v[192:195], v[104:107]
	v_mfma_f32_16x16x32_f16 v[108:111], v[184:187], v[196:199], v[108:111]
	v_mfma_f32_16x16x32_f16 v[112:115], v[184:187], v[200:203], v[112:115]
	v_mfma_f32_16x16x32_f16 v[116:119], v[184:187], v[204:207], v[116:119]
	s_waitcnt lgkmcnt(7)
	ds_read_b128 v[172:175], v16 offset:53248
	ds_read_b128 v[192:195], v18 offset:53248
	ds_read_b128 v[196:199], v18 offset:55296
	ds_read_b128 v[200:203], v18 offset:57344
	ds_read_b128 v[204:207], v18 offset:59392
	ds_read_b128 v[176:179], v16 offset:55296
	ds_read_b128 v[180:183], v16 offset:57344
	ds_read_b128 v[184:187], v16 offset:59392
	s_waitcnt lgkmcnt(14)
	v_mfma_f32_16x16x32_f16 v[56:59], v[136:139], v[156:159], v[56:59]
	s_add_u32 m0, s28, 0x6000
	s_nop 0
	global_load_lds_dwordx4 v13, s[4:5]
	s_add_u32 s4, s4, s20
	s_addc_u32 s5, s5, 0
	s_waitcnt lgkmcnt(13)
	v_mfma_f32_16x16x32_f16 v[60:63], v[136:139], v[160:163], v[60:63]
	s_waitcnt lgkmcnt(12)
	v_mfma_f32_16x16x32_f16 v[64:67], v[136:139], v[164:167], v[64:67]
	s_waitcnt lgkmcnt(11)
	v_mfma_f32_16x16x32_f16 v[68:71], v[136:139], v[168:171], v[68:71]
	s_waitcnt lgkmcnt(10)
	v_mfma_f32_16x16x32_f16 v[72:75], v[140:143], v[156:159], v[72:75]
	v_mfma_f32_16x16x32_f16 v[76:79], v[140:143], v[160:163], v[76:79]
	s_add_u32 m0, s28, 0x9000
	s_nop 0
	global_load_lds_dwordx4 v10, s[6:7]
	v_mfma_f32_16x16x32_f16 v[80:83], v[140:143], v[164:167], v[80:83]
	v_mfma_f32_16x16x32_f16 v[84:87], v[140:143], v[168:171], v[84:87]
	s_waitcnt lgkmcnt(9)
	v_mfma_f32_16x16x32_f16 v[88:91], v[144:147], v[156:159], v[88:91]
	v_mfma_f32_16x16x32_f16 v[92:95], v[144:147], v[160:163], v[92:95]
	v_mfma_f32_16x16x32_f16 v[96:99], v[144:147], v[164:167], v[96:99]
	s_add_u32 m0, s28, 0xb000
	s_nop 0
	global_load_lds_dwordx4 v11, s[6:7]
	s_add_u32 s6, s6, s20
	s_addc_u32 s7, s7, 0
	v_mfma_f32_16x16x32_f16 v[100:103], v[144:147], v[168:171], v[100:103]
	s_waitcnt lgkmcnt(8)
	v_mfma_f32_16x16x32_f16 v[104:107], v[148:151], v[156:159], v[104:107]
	v_mfma_f32_16x16x32_f16 v[108:111], v[148:151], v[160:163], v[108:111]
	v_mfma_f32_16x16x32_f16 v[112:115], v[148:151], v[164:167], v[112:115]
	v_mfma_f32_16x16x32_f16 v[116:119], v[148:151], v[168:171], v[116:119]
	s_waitcnt vmcnt(6) lgkmcnt(0)
	s_barrier
	s_waitcnt lgkmcnt(7)
	ds_read_b128 v[136:139], v19
	ds_read_b128 v[156:159], v21
	ds_read_b128 v[160:163], v21 offset:2048
	ds_read_b128 v[164:167], v21 offset:4096
	ds_read_b128 v[168:171], v21 offset:6144
	ds_read_b128 v[140:143], v19 offset:2048
	ds_read_b128 v[144:147], v19 offset:4096
	ds_read_b128 v[148:151], v19 offset:6144
	s_waitcnt lgkmcnt(14)
	v_mfma_f32_16x16x32_f16 v[56:59], v[172:175], v[192:195], v[56:59]
	s_add_u32 m0, s28, 0xd000
	s_nop 0
	global_load_lds_dwordx4 v10, s[4:5]
	s_waitcnt lgkmcnt(13)
	v_mfma_f32_16x16x32_f16 v[60:63], v[172:175], v[196:199], v[60:63]
	s_waitcnt lgkmcnt(12)
	v_mfma_f32_16x16x32_f16 v[64:67], v[172:175], v[200:203], v[64:67]
	s_waitcnt lgkmcnt(11)
	v_mfma_f32_16x16x32_f16 v[68:71], v[172:175], v[204:207], v[68:71]
	s_waitcnt lgkmcnt(10)
	v_mfma_f32_16x16x32_f16 v[72:75], v[176:179], v[192:195], v[72:75]
	v_mfma_f32_16x16x32_f16 v[76:79], v[176:179], v[196:199], v[76:79]
	s_add_u32 m0, s28, 0xf000
	s_nop 0
	global_load_lds_dwordx4 v11, s[4:5]
	v_mfma_f32_16x16x32_f16 v[80:83], v[176:179], v[200:203], v[80:83]
	v_mfma_f32_16x16x32_f16 v[84:87], v[176:179], v[204:207], v[84:87]
	s_waitcnt lgkmcnt(9)
	v_mfma_f32_16x16x32_f16 v[88:91], v[180:183], v[192:195], v[88:91]
	v_mfma_f32_16x16x32_f16 v[92:95], v[180:183], v[196:199], v[92:95]
	v_mfma_f32_16x16x32_f16 v[96:99], v[180:183], v[200:203], v[96:99]
	s_add_u32 m0, s28, 0x11000
	s_nop 0
	global_load_lds_dwordx4 v12, s[4:5]
	v_mfma_f32_16x16x32_f16 v[100:103], v[180:183], v[204:207], v[100:103]
	s_waitcnt lgkmcnt(8)
	v_mfma_f32_16x16x32_f16 v[104:107], v[184:187], v[192:195], v[104:107]
	v_mfma_f32_16x16x32_f16 v[108:111], v[184:187], v[196:199], v[108:111]
	v_mfma_f32_16x16x32_f16 v[112:115], v[184:187], v[200:203], v[112:115]
	v_mfma_f32_16x16x32_f16 v[116:119], v[184:187], v[204:207], v[116:119]
	s_waitcnt lgkmcnt(7)
	ds_read_b128 v[172:175], v20
	ds_read_b128 v[192:195], v22
	ds_read_b128 v[196:199], v22 offset:2048
	ds_read_b128 v[200:203], v22 offset:4096
	ds_read_b128 v[204:207], v22 offset:6144
	ds_read_b128 v[176:179], v20 offset:2048
	ds_read_b128 v[180:183], v20 offset:4096
	ds_read_b128 v[184:187], v20 offset:6144
	s_waitcnt lgkmcnt(14)
	v_mfma_f32_16x16x32_f16 v[56:59], v[136:139], v[156:159], v[56:59]
	s_add_u32 m0, s28, 0x13000
	s_nop 0
	global_load_lds_dwordx4 v13, s[4:5]
	s_add_u32 s4, s4, s20
	s_addc_u32 s5, s5, 0
	s_waitcnt lgkmcnt(13)
	v_mfma_f32_16x16x32_f16 v[60:63], v[136:139], v[160:163], v[60:63]
	s_waitcnt lgkmcnt(12)
	v_mfma_f32_16x16x32_f16 v[64:67], v[136:139], v[164:167], v[64:67]
	s_waitcnt lgkmcnt(11)
	v_mfma_f32_16x16x32_f16 v[68:71], v[136:139], v[168:171], v[68:71]
	s_waitcnt lgkmcnt(10)
	v_mfma_f32_16x16x32_f16 v[72:75], v[140:143], v[156:159], v[72:75]
	v_mfma_f32_16x16x32_f16 v[76:79], v[140:143], v[160:163], v[76:79]
	s_add_u32 m0, s28, 0x16000
	s_nop 0
	global_load_lds_dwordx4 v10, s[6:7]
	v_mfma_f32_16x16x32_f16 v[80:83], v[140:143], v[164:167], v[80:83]
	v_mfma_f32_16x16x32_f16 v[84:87], v[140:143], v[168:171], v[84:87]
	s_waitcnt lgkmcnt(9)
	v_mfma_f32_16x16x32_f16 v[88:91], v[144:147], v[156:159], v[88:91]
	v_mfma_f32_16x16x32_f16 v[92:95], v[144:147], v[160:163], v[92:95]
	v_mfma_f32_16x16x32_f16 v[96:99], v[144:147], v[164:167], v[96:99]
	s_add_u32 m0, s28, 0x18000
	s_nop 0
	global_load_lds_dwordx4 v11, s[6:7]
	s_add_u32 s6, s6, s20
	s_addc_u32 s7, s7, 0
	v_mfma_f32_16x16x32_f16 v[100:103], v[144:147], v[168:171], v[100:103]
	s_waitcnt lgkmcnt(8)
	v_mfma_f32_16x16x32_f16 v[104:107], v[148:151], v[156:159], v[104:107]
	v_mfma_f32_16x16x32_f16 v[108:111], v[148:151], v[160:163], v[108:111]
	v_mfma_f32_16x16x32_f16 v[112:115], v[148:151], v[164:167], v[112:115]
	v_mfma_f32_16x16x32_f16 v[116:119], v[148:151], v[168:171], v[116:119]
	s_waitcnt vmcnt(6) lgkmcnt(0)
	s_barrier
	s_waitcnt lgkmcnt(7)
	ds_read_b128 v[136:139], v15
	ds_read_b128 v[156:159], v17
	ds_read_b128 v[160:163], v17 offset:2048
	ds_read_b128 v[164:167], v17 offset:4096
	ds_read_b128 v[168:171], v17 offset:6144
	ds_read_b128 v[140:143], v15 offset:2048
	ds_read_b128 v[144:147], v15 offset:4096
	ds_read_b128 v[148:151], v15 offset:6144
	s_waitcnt lgkmcnt(14)
	v_mfma_f32_16x16x32_f16 v[56:59], v[172:175], v[192:195], v[56:59]
	s_add_u32 m0, s28, 0x1a000
	s_nop 0
	global_load_lds_dwordx4 v10, s[4:5]
	s_waitcnt lgkmcnt(13)
	v_mfma_f32_16x16x32_f16 v[60:63], v[172:175], v[196:199], v[60:63]
	s_waitcnt lgkmcnt(12)
	v_mfma_f32_16x16x32_f16 v[64:67], v[172:175], v[200:203], v[64:67]
	s_waitcnt lgkmcnt(11)
	v_mfma_f32_16x16x32_f16 v[68:71], v[172:175], v[204:207], v[68:71]
	s_waitcnt lgkmcnt(10)
	v_mfma_f32_16x16x32_f16 v[72:75], v[176:179], v[192:195], v[72:75]
	v_mfma_f32_16x16x32_f16 v[76:79], v[176:179], v[196:199], v[76:79]
	s_add_u32 m0, s28, 0x1c000
	s_nop 0
	global_load_lds_dwordx4 v11, s[4:5]
	v_mfma_f32_16x16x32_f16 v[80:83], v[176:179], v[200:203], v[80:83]
	v_mfma_f32_16x16x32_f16 v[84:87], v[176:179], v[204:207], v[84:87]
	s_waitcnt lgkmcnt(9)
	v_mfma_f32_16x16x32_f16 v[88:91], v[180:183], v[192:195], v[88:91]
	v_mfma_f32_16x16x32_f16 v[92:95], v[180:183], v[196:199], v[92:95]
	v_mfma_f32_16x16x32_f16 v[96:99], v[180:183], v[200:203], v[96:99]
	s_add_u32 m0, s28, 0x1e000
	s_nop 0
	global_load_lds_dwordx4 v12, s[4:5]
	v_mfma_f32_16x16x32_f16 v[100:103], v[180:183], v[204:207], v[100:103]
	s_waitcnt lgkmcnt(8)
	v_mfma_f32_16x16x32_f16 v[104:107], v[184:187], v[192:195], v[104:107]
	v_mfma_f32_16x16x32_f16 v[108:111], v[184:187], v[196:199], v[108:111]
	v_mfma_f32_16x16x32_f16 v[112:115], v[184:187], v[200:203], v[112:115]
	v_mfma_f32_16x16x32_f16 v[116:119], v[184:187], v[204:207], v[116:119]
	s_waitcnt lgkmcnt(7)
	ds_read_b128 v[172:175], v16
	ds_read_b128 v[192:195], v18
	ds_read_b128 v[196:199], v18 offset:2048
	ds_read_b128 v[200:203], v18 offset:4096
	ds_read_b128 v[204:207], v18 offset:6144
	ds_read_b128 v[176:179], v16 offset:2048
	ds_read_b128 v[180:183], v16 offset:4096
	ds_read_b128 v[184:187], v16 offset:6144
	s_waitcnt lgkmcnt(14)
	v_mfma_f32_16x16x32_f16 v[56:59], v[136:139], v[156:159], v[56:59]
	s_add_u32 m0, s28, 0x20000
	s_nop 0
	global_load_lds_dwordx4 v13, s[4:5]
	s_add_u32 s4, s4, s20
	s_addc_u32 s5, s5, 0
	s_waitcnt lgkmcnt(13)
	v_mfma_f32_16x16x32_f16 v[60:63], v[136:139], v[160:163], v[60:63]
	s_waitcnt lgkmcnt(12)
	v_mfma_f32_16x16x32_f16 v[64:67], v[136:139], v[164:167], v[64:67]
	s_waitcnt lgkmcnt(11)
	v_mfma_f32_16x16x32_f16 v[68:71], v[136:139], v[168:171], v[68:71]
	s_waitcnt lgkmcnt(10)
	v_mfma_f32_16x16x32_f16 v[72:75], v[140:143], v[156:159], v[72:75]
	v_mfma_f32_16x16x32_f16 v[76:79], v[140:143], v[160:163], v[76:79]
	s_add_u32 m0, s28, 0x23000
	s_nop 0
	global_load_lds_dwordx4 v10, s[6:7]
	v_mfma_f32_16x16x32_f16 v[80:83], v[140:143], v[164:167], v[80:83]
	v_mfma_f32_16x16x32_f16 v[84:87], v[140:143], v[168:171], v[84:87]
	s_waitcnt lgkmcnt(9)
	v_mfma_f32_16x16x32_f16 v[88:91], v[144:147], v[156:159], v[88:91]
	v_mfma_f32_16x16x32_f16 v[92:95], v[144:147], v[160:163], v[92:95]
	v_mfma_f32_16x16x32_f16 v[96:99], v[144:147], v[164:167], v[96:99]
	s_add_u32 m0, s28, 0x25000
	s_nop 0
	global_load_lds_dwordx4 v11, s[6:7]
	s_add_u32 s6, s6, s20
	s_addc_u32 s7, s7, 0
	v_mfma_f32_16x16x32_f16 v[100:103], v[144:147], v[168:171], v[100:103]
	s_waitcnt lgkmcnt(8)
	v_mfma_f32_16x16x32_f16 v[104:107], v[148:151], v[156:159], v[104:107]
	v_mfma_f32_16x16x32_f16 v[108:111], v[148:151], v[160:163], v[108:111]
	v_mfma_f32_16x16x32_f16 v[112:115], v[148:151], v[164:167], v[112:115]
	v_mfma_f32_16x16x32_f16 v[116:119], v[148:151], v[168:171], v[116:119]
	s_waitcnt vmcnt(6) lgkmcnt(0)
	s_barrier
	s_waitcnt lgkmcnt(7)
	ds_read_b128 v[136:139], v15 offset:53248
	ds_read_b128 v[156:159], v17 offset:53248
	ds_read_b128 v[160:163], v17 offset:55296
	ds_read_b128 v[164:167], v17 offset:57344
	ds_read_b128 v[168:171], v17 offset:59392
	ds_read_b128 v[140:143], v15 offset:55296
	ds_read_b128 v[144:147], v15 offset:57344
	ds_read_b128 v[148:151], v15 offset:59392
	s_waitcnt lgkmcnt(14)
	v_mfma_f32_16x16x32_f16 v[56:59], v[172:175], v[192:195], v[56:59]
	s_add_u32 m0, s28, 0x0
	s_nop 0
	global_load_lds_dwordx4 v10, s[4:5]
	s_waitcnt lgkmcnt(13)
	v_mfma_f32_16x16x32_f16 v[60:63], v[172:175], v[196:199], v[60:63]
	s_waitcnt lgkmcnt(12)
	v_mfma_f32_16x16x32_f16 v[64:67], v[172:175], v[200:203], v[64:67]
	s_waitcnt lgkmcnt(11)
	v_mfma_f32_16x16x32_f16 v[68:71], v[172:175], v[204:207], v[68:71]
	s_waitcnt lgkmcnt(10)
	v_mfma_f32_16x16x32_f16 v[72:75], v[176:179], v[192:195], v[72:75]
	v_mfma_f32_16x16x32_f16 v[76:79], v[176:179], v[196:199], v[76:79]
	s_add_u32 m0, s28, 0x2000
	s_nop 0
	global_load_lds_dwordx4 v11, s[4:5]
	v_mfma_f32_16x16x32_f16 v[80:83], v[176:179], v[200:203], v[80:83]
	v_mfma_f32_16x16x32_f16 v[84:87], v[176:179], v[204:207], v[84:87]
	s_waitcnt lgkmcnt(9)
	v_mfma_f32_16x16x32_f16 v[88:91], v[180:183], v[192:195], v[88:91]
	v_mfma_f32_16x16x32_f16 v[92:95], v[180:183], v[196:199], v[92:95]
	v_mfma_f32_16x16x32_f16 v[96:99], v[180:183], v[200:203], v[96:99]
	s_add_u32 m0, s28, 0x4000
	s_nop 0
	global_load_lds_dwordx4 v12, s[4:5]
	v_mfma_f32_16x16x32_f16 v[100:103], v[180:183], v[204:207], v[100:103]
	s_waitcnt lgkmcnt(8)
	v_mfma_f32_16x16x32_f16 v[104:107], v[184:187], v[192:195], v[104:107]
	v_mfma_f32_16x16x32_f16 v[108:111], v[184:187], v[196:199], v[108:111]
	v_mfma_f32_16x16x32_f16 v[112:115], v[184:187], v[200:203], v[112:115]
	v_mfma_f32_16x16x32_f16 v[116:119], v[184:187], v[204:207], v[116:119]
	s_waitcnt lgkmcnt(7)
	ds_read_b128 v[172:175], v16 offset:53248
	ds_read_b128 v[192:195], v18 offset:53248
	ds_read_b128 v[196:199], v18 offset:55296
	ds_read_b128 v[200:203], v18 offset:57344
	ds_read_b128 v[204:207], v18 offset:59392
	ds_read_b128 v[176:179], v16 offset:55296
	ds_read_b128 v[180:183], v16 offset:57344
	ds_read_b128 v[184:187], v16 offset:59392
	s_waitcnt lgkmcnt(14)
	v_mfma_f32_16x16x32_f16 v[56:59], v[136:139], v[156:159], v[56:59]
	s_add_u32 m0, s28, 0x6000
	s_nop 0
	global_load_lds_dwordx4 v13, s[4:5]
	s_add_u32 s4, s4, s20
	s_addc_u32 s5, s5, 0
	s_waitcnt lgkmcnt(13)
	v_mfma_f32_16x16x32_f16 v[60:63], v[136:139], v[160:163], v[60:63]
	s_waitcnt lgkmcnt(12)
	v_mfma_f32_16x16x32_f16 v[64:67], v[136:139], v[164:167], v[64:67]
	s_waitcnt lgkmcnt(11)
	v_mfma_f32_16x16x32_f16 v[68:71], v[136:139], v[168:171], v[68:71]
	s_waitcnt lgkmcnt(10)
	v_mfma_f32_16x16x32_f16 v[72:75], v[140:143], v[156:159], v[72:75]
	v_mfma_f32_16x16x32_f16 v[76:79], v[140:143], v[160:163], v[76:79]
	s_add_u32 m0, s28, 0x9000
	s_nop 0
	global_load_lds_dwordx4 v10, s[6:7]
	v_mfma_f32_16x16x32_f16 v[80:83], v[140:143], v[164:167], v[80:83]
	v_mfma_f32_16x16x32_f16 v[84:87], v[140:143], v[168:171], v[84:87]
	s_waitcnt lgkmcnt(9)
	v_mfma_f32_16x16x32_f16 v[88:91], v[144:147], v[156:159], v[88:91]
	v_mfma_f32_16x16x32_f16 v[92:95], v[144:147], v[160:163], v[92:95]
	v_mfma_f32_16x16x32_f16 v[96:99], v[144:147], v[164:167], v[96:99]
	s_add_u32 m0, s28, 0xb000
	s_nop 0
	global_load_lds_dwordx4 v11, s[6:7]
	s_add_u32 s6, s6, s20
	s_addc_u32 s7, s7, 0
	v_mfma_f32_16x16x32_f16 v[100:103], v[144:147], v[168:171], v[100:103]
	s_waitcnt lgkmcnt(8)
	v_mfma_f32_16x16x32_f16 v[104:107], v[148:151], v[156:159], v[104:107]
	v_mfma_f32_16x16x32_f16 v[108:111], v[148:151], v[160:163], v[108:111]
	v_mfma_f32_16x16x32_f16 v[112:115], v[148:151], v[164:167], v[112:115]
	v_mfma_f32_16x16x32_f16 v[116:119], v[148:151], v[168:171], v[116:119]
	s_waitcnt vmcnt(6) lgkmcnt(0)
	s_barrier
	s_waitcnt lgkmcnt(7)
	ds_read_b128 v[136:139], v19
	ds_read_b128 v[156:159], v21
	ds_read_b128 v[160:163], v21 offset:2048
	ds_read_b128 v[164:167], v21 offset:4096
	ds_read_b128 v[168:171], v21 offset:6144
	ds_read_b128 v[140:143], v19 offset:2048
	ds_read_b128 v[144:147], v19 offset:4096
	ds_read_b128 v[148:151], v19 offset:6144
	s_waitcnt lgkmcnt(14)
	v_mfma_f32_16x16x32_f16 v[56:59], v[172:175], v[192:195], v[56:59]
	s_add_u32 m0, s28, 0xd000
	s_nop 0
	global_load_lds_dwordx4 v10, s[4:5]
	s_waitcnt lgkmcnt(13)
	v_mfma_f32_16x16x32_f16 v[60:63], v[172:175], v[196:199], v[60:63]
	s_waitcnt lgkmcnt(12)
	v_mfma_f32_16x16x32_f16 v[64:67], v[172:175], v[200:203], v[64:67]
	s_waitcnt lgkmcnt(11)
	v_mfma_f32_16x16x32_f16 v[68:71], v[172:175], v[204:207], v[68:71]
	s_waitcnt lgkmcnt(10)
	v_mfma_f32_16x16x32_f16 v[72:75], v[176:179], v[192:195], v[72:75]
	v_mfma_f32_16x16x32_f16 v[76:79], v[176:179], v[196:199], v[76:79]
	s_add_u32 m0, s28, 0xf000
	s_nop 0
	global_load_lds_dwordx4 v11, s[4:5]
	v_mfma_f32_16x16x32_f16 v[80:83], v[176:179], v[200:203], v[80:83]
	v_mfma_f32_16x16x32_f16 v[84:87], v[176:179], v[204:207], v[84:87]
	s_waitcnt lgkmcnt(9)
	v_mfma_f32_16x16x32_f16 v[88:91], v[180:183], v[192:195], v[88:91]
	v_mfma_f32_16x16x32_f16 v[92:95], v[180:183], v[196:199], v[92:95]
	v_mfma_f32_16x16x32_f16 v[96:99], v[180:183], v[200:203], v[96:99]
	s_add_u32 m0, s28, 0x11000
	s_nop 0
	global_load_lds_dwordx4 v12, s[4:5]
	v_mfma_f32_16x16x32_f16 v[100:103], v[180:183], v[204:207], v[100:103]
	s_waitcnt lgkmcnt(8)
	v_mfma_f32_16x16x32_f16 v[104:107], v[184:187], v[192:195], v[104:107]
	v_mfma_f32_16x16x32_f16 v[108:111], v[184:187], v[196:199], v[108:111]
	v_mfma_f32_16x16x32_f16 v[112:115], v[184:187], v[200:203], v[112:115]
	v_mfma_f32_16x16x32_f16 v[116:119], v[184:187], v[204:207], v[116:119]
	s_waitcnt lgkmcnt(7)
	ds_read_b128 v[172:175], v20
	ds_read_b128 v[192:195], v22
	ds_read_b128 v[196:199], v22 offset:2048
	ds_read_b128 v[200:203], v22 offset:4096
	ds_read_b128 v[204:207], v22 offset:6144
	ds_read_b128 v[176:179], v20 offset:2048
	ds_read_b128 v[180:183], v20 offset:4096
	ds_read_b128 v[184:187], v20 offset:6144
	s_waitcnt lgkmcnt(14)
	v_mfma_f32_16x16x32_f16 v[56:59], v[136:139], v[156:159], v[56:59]
	s_add_u32 m0, s28, 0x13000
	s_nop 0
	global_load_lds_dwordx4 v13, s[4:5]
	s_add_u32 s4, s4, s20
	s_addc_u32 s5, s5, 0
	s_waitcnt lgkmcnt(13)
	v_mfma_f32_16x16x32_f16 v[60:63], v[136:139], v[160:163], v[60:63]
	s_waitcnt lgkmcnt(12)
	v_mfma_f32_16x16x32_f16 v[64:67], v[136:139], v[164:167], v[64:67]
	s_waitcnt lgkmcnt(11)
	v_mfma_f32_16x16x32_f16 v[68:71], v[136:139], v[168:171], v[68:71]
	s_waitcnt lgkmcnt(10)
	v_mfma_f32_16x16x32_f16 v[72:75], v[140:143], v[156:159], v[72:75]
	v_mfma_f32_16x16x32_f16 v[76:79], v[140:143], v[160:163], v[76:79]
	s_add_u32 m0, s28, 0x16000
	s_nop 0
	global_load_lds_dwordx4 v10, s[6:7]
	v_mfma_f32_16x16x32_f16 v[80:83], v[140:143], v[164:167], v[80:83]
	v_mfma_f32_16x16x32_f16 v[84:87], v[140:143], v[168:171], v[84:87]
	s_waitcnt lgkmcnt(9)
	v_mfma_f32_16x16x32_f16 v[88:91], v[144:147], v[156:159], v[88:91]
	v_mfma_f32_16x16x32_f16 v[92:95], v[144:147], v[160:163], v[92:95]
	v_mfma_f32_16x16x32_f16 v[96:99], v[144:147], v[164:167], v[96:99]
	s_add_u32 m0, s28, 0x18000
	s_nop 0
	global_load_lds_dwordx4 v11, s[6:7]
	s_add_u32 s6, s6, s20
	s_addc_u32 s7, s7, 0
	v_mfma_f32_16x16x32_f16 v[100:103], v[144:147], v[168:171], v[100:103]
	s_waitcnt lgkmcnt(8)
	v_mfma_f32_16x16x32_f16 v[104:107], v[148:151], v[156:159], v[104:107]
	v_mfma_f32_16x16x32_f16 v[108:111], v[148:151], v[160:163], v[108:111]
	v_mfma_f32_16x16x32_f16 v[112:115], v[148:151], v[164:167], v[112:115]
	v_mfma_f32_16x16x32_f16 v[116:119], v[148:151], v[168:171], v[116:119]
	s_waitcnt vmcnt(6) lgkmcnt(0)
	s_barrier
	s_waitcnt lgkmcnt(7)
	ds_read_b128 v[136:139], v15
	ds_read_b128 v[156:159], v17
	ds_read_b128 v[160:163], v17 offset:2048
	ds_read_b128 v[164:167], v17 offset:4096
	ds_read_b128 v[168:171], v17 offset:6144
	ds_read_b128 v[140:143], v15 offset:2048
	ds_read_b128 v[144:147], v15 offset:4096
	ds_read_b128 v[148:151], v15 offset:6144
	s_waitcnt lgkmcnt(14)
	v_mfma_f32_16x16x32_f16 v[56:59], v[172:175], v[192:195], v[56:59]
	s_add_u32 m0, s28, 0x1a000
	s_nop 0
	global_load_lds_dwordx4 v10, s[4:5]
	s_waitcnt lgkmcnt(13)
	v_mfma_f32_16x16x32_f16 v[60:63], v[172:175], v[196:199], v[60:63]
	s_waitcnt lgkmcnt(12)
	v_mfma_f32_16x16x32_f16 v[64:67], v[172:175], v[200:203], v[64:67]
	s_waitcnt lgkmcnt(11)
	v_mfma_f32_16x16x32_f16 v[68:71], v[172:175], v[204:207], v[68:71]
	s_waitcnt lgkmcnt(10)
	v_mfma_f32_16x16x32_f16 v[72:75], v[176:179], v[192:195], v[72:75]
	v_mfma_f32_16x16x32_f16 v[76:79], v[176:179], v[196:199], v[76:79]
	s_add_u32 m0, s28, 0x1c000
	s_nop 0
	global_load_lds_dwordx4 v11, s[4:5]
	v_mfma_f32_16x16x32_f16 v[80:83], v[176:179], v[200:203], v[80:83]
	v_mfma_f32_16x16x32_f16 v[84:87], v[176:179], v[204:207], v[84:87]
	s_waitcnt lgkmcnt(9)
	v_mfma_f32_16x16x32_f16 v[88:91], v[180:183], v[192:195], v[88:91]
	v_mfma_f32_16x16x32_f16 v[92:95], v[180:183], v[196:199], v[92:95]
	v_mfma_f32_16x16x32_f16 v[96:99], v[180:183], v[200:203], v[96:99]
	s_add_u32 m0, s28, 0x1e000
	s_nop 0
	global_load_lds_dwordx4 v12, s[4:5]
	v_mfma_f32_16x16x32_f16 v[100:103], v[180:183], v[204:207], v[100:103]
	s_waitcnt lgkmcnt(8)
	v_mfma_f32_16x16x32_f16 v[104:107], v[184:187], v[192:195], v[104:107]
	v_mfma_f32_16x16x32_f16 v[108:111], v[184:187], v[196:199], v[108:111]
	v_mfma_f32_16x16x32_f16 v[112:115], v[184:187], v[200:203], v[112:115]
	v_mfma_f32_16x16x32_f16 v[116:119], v[184:187], v[204:207], v[116:119]
	s_waitcnt lgkmcnt(7)
	ds_read_b128 v[172:175], v16
	ds_read_b128 v[192:195], v18
	ds_read_b128 v[196:199], v18 offset:2048
	ds_read_b128 v[200:203], v18 offset:4096
	ds_read_b128 v[204:207], v18 offset:6144
	ds_read_b128 v[176:179], v16 offset:2048
	ds_read_b128 v[180:183], v16 offset:4096
	ds_read_b128 v[184:187], v16 offset:6144
	s_waitcnt lgkmcnt(14)
	v_mfma_f32_16x16x32_f16 v[56:59], v[136:139], v[156:159], v[56:59]
	s_add_u32 m0, s28, 0x20000
	s_nop 0
	global_load_lds_dwordx4 v13, s[4:5]
	s_add_u32 s4, s4, s20
	s_addc_u32 s5, s5, 0
	s_waitcnt lgkmcnt(13)
	v_mfma_f32_16x16x32_f16 v[60:63], v[136:139], v[160:163], v[60:63]
	s_waitcnt lgkmcnt(12)
	v_mfma_f32_16x16x32_f16 v[64:67], v[136:139], v[164:167], v[64:67]
	s_waitcnt lgkmcnt(11)
	v_mfma_f32_16x16x32_f16 v[68:71], v[136:139], v[168:171], v[68:71]
	s_waitcnt lgkmcnt(10)
	v_mfma_f32_16x16x32_f16 v[72:75], v[140:143], v[156:159], v[72:75]
	v_mfma_f32_16x16x32_f16 v[76:79], v[140:143], v[160:163], v[76:79]
	s_add_u32 m0, s28, 0x23000
	s_nop 0
	global_load_lds_dwordx4 v10, s[6:7]
	v_mfma_f32_16x16x32_f16 v[80:83], v[140:143], v[164:167], v[80:83]
	v_mfma_f32_16x16x32_f16 v[84:87], v[140:143], v[168:171], v[84:87]
	s_waitcnt lgkmcnt(9)
	v_mfma_f32_16x16x32_f16 v[88:91], v[144:147], v[156:159], v[88:91]
	v_mfma_f32_16x16x32_f16 v[92:95], v[144:147], v[160:163], v[92:95]
	v_mfma_f32_16x16x32_f16 v[96:99], v[144:147], v[164:167], v[96:99]
	s_add_u32 m0, s28, 0x25000
	s_nop 0
	global_load_lds_dwordx4 v11, s[6:7]
	s_add_u32 s6, s6, s20
	s_addc_u32 s7, s7, 0
	v_mfma_f32_16x16x32_f16 v[100:103], v[144:147], v[168:171], v[100:103]
	s_waitcnt lgkmcnt(8)
	v_mfma_f32_16x16x32_f16 v[104:107], v[148:151], v[156:159], v[104:107]
	v_mfma_f32_16x16x32_f16 v[108:111], v[148:151], v[160:163], v[108:111]
	v_mfma_f32_16x16x32_f16 v[112:115], v[148:151], v[164:167], v[112:115]
	v_mfma_f32_16x16x32_f16 v[116:119], v[148:151], v[168:171], v[116:119]
	s_waitcnt vmcnt(6) lgkmcnt(0)
	s_barrier
	s_waitcnt lgkmcnt(7)
	ds_read_b128 v[136:139], v15 offset:53248
	ds_read_b128 v[156:159], v17 offset:53248
	ds_read_b128 v[160:163], v17 offset:55296
	ds_read_b128 v[164:167], v17 offset:57344
	ds_read_b128 v[168:171], v17 offset:59392
	ds_read_b128 v[140:143], v15 offset:55296
	ds_read_b128 v[144:147], v15 offset:57344
	ds_read_b128 v[148:151], v15 offset:59392
	s_waitcnt lgkmcnt(14)
	v_mfma_f32_16x16x32_f16 v[56:59], v[172:175], v[192:195], v[56:59]
	s_add_u32 m0, s28, 0x0
	s_nop 0
	global_load_lds_dwordx4 v10, s[4:5]
	s_waitcnt lgkmcnt(13)
	v_mfma_f32_16x16x32_f16 v[60:63], v[172:175], v[196:199], v[60:63]
	s_waitcnt lgkmcnt(12)
	v_mfma_f32_16x16x32_f16 v[64:67], v[172:175], v[200:203], v[64:67]
	s_waitcnt lgkmcnt(11)
	v_mfma_f32_16x16x32_f16 v[68:71], v[172:175], v[204:207], v[68:71]
	s_waitcnt lgkmcnt(10)
	v_mfma_f32_16x16x32_f16 v[72:75], v[176:179], v[192:195], v[72:75]
	v_mfma_f32_16x16x32_f16 v[76:79], v[176:179], v[196:199], v[76:79]
	s_add_u32 m0, s28, 0x2000
	s_nop 0
	global_load_lds_dwordx4 v11, s[4:5]
	v_mfma_f32_16x16x32_f16 v[80:83], v[176:179], v[200:203], v[80:83]
	v_mfma_f32_16x16x32_f16 v[84:87], v[176:179], v[204:207], v[84:87]
	s_waitcnt lgkmcnt(9)
	v_mfma_f32_16x16x32_f16 v[88:91], v[180:183], v[192:195], v[88:91]
	v_mfma_f32_16x16x32_f16 v[92:95], v[180:183], v[196:199], v[92:95]
	v_mfma_f32_16x16x32_f16 v[96:99], v[180:183], v[200:203], v[96:99]
	s_add_u32 m0, s28, 0x4000
	s_nop 0
	global_load_lds_dwordx4 v12, s[4:5]
	v_mfma_f32_16x16x32_f16 v[100:103], v[180:183], v[204:207], v[100:103]
	s_waitcnt lgkmcnt(8)
	v_mfma_f32_16x16x32_f16 v[104:107], v[184:187], v[192:195], v[104:107]
	v_mfma_f32_16x16x32_f16 v[108:111], v[184:187], v[196:199], v[108:111]
	v_mfma_f32_16x16x32_f16 v[112:115], v[184:187], v[200:203], v[112:115]
	v_mfma_f32_16x16x32_f16 v[116:119], v[184:187], v[204:207], v[116:119]
	s_waitcnt lgkmcnt(7)
	ds_read_b128 v[172:175], v16 offset:53248
	ds_read_b128 v[192:195], v18 offset:53248
	ds_read_b128 v[196:199], v18 offset:55296
	ds_read_b128 v[200:203], v18 offset:57344
	ds_read_b128 v[204:207], v18 offset:59392
	ds_read_b128 v[176:179], v16 offset:55296
	ds_read_b128 v[180:183], v16 offset:57344
	ds_read_b128 v[184:187], v16 offset:59392
	s_waitcnt lgkmcnt(14)
	v_mfma_f32_16x16x32_f16 v[56:59], v[136:139], v[156:159], v[56:59]
	s_add_u32 m0, s28, 0x6000
	s_nop 0
	global_load_lds_dwordx4 v13, s[4:5]
	s_add_u32 s4, s4, s20
	s_addc_u32 s5, s5, 0
	s_waitcnt lgkmcnt(13)
	v_mfma_f32_16x16x32_f16 v[60:63], v[136:139], v[160:163], v[60:63]
	s_waitcnt lgkmcnt(12)
	v_mfma_f32_16x16x32_f16 v[64:67], v[136:139], v[164:167], v[64:67]
	s_waitcnt lgkmcnt(11)
	v_mfma_f32_16x16x32_f16 v[68:71], v[136:139], v[168:171], v[68:71]
	s_waitcnt lgkmcnt(10)
	v_mfma_f32_16x16x32_f16 v[72:75], v[140:143], v[156:159], v[72:75]
	v_mfma_f32_16x16x32_f16 v[76:79], v[140:143], v[160:163], v[76:79]
	s_add_u32 m0, s28, 0x9000
	s_nop 0
	global_load_lds_dwordx4 v10, s[6:7]
	v_mfma_f32_16x16x32_f16 v[80:83], v[140:143], v[164:167], v[80:83]
	v_mfma_f32_16x16x32_f16 v[84:87], v[140:143], v[168:171], v[84:87]
	s_waitcnt lgkmcnt(9)
	v_mfma_f32_16x16x32_f16 v[88:91], v[144:147], v[156:159], v[88:91]
	v_mfma_f32_16x16x32_f16 v[92:95], v[144:147], v[160:163], v[92:95]
	v_mfma_f32_16x16x32_f16 v[96:99], v[144:147], v[164:167], v[96:99]
	s_add_u32 m0, s28, 0xb000
	s_nop 0
	global_load_lds_dwordx4 v11, s[6:7]
	s_add_u32 s6, s6, s20
	s_addc_u32 s7, s7, 0
	v_mfma_f32_16x16x32_f16 v[100:103], v[144:147], v[168:171], v[100:103]
	s_waitcnt lgkmcnt(8)
	v_mfma_f32_16x16x32_f16 v[104:107], v[148:151], v[156:159], v[104:107]
	v_mfma_f32_16x16x32_f16 v[108:111], v[148:151], v[160:163], v[108:111]
	v_mfma_f32_16x16x32_f16 v[112:115], v[148:151], v[164:167], v[112:115]
	v_mfma_f32_16x16x32_f16 v[116:119], v[148:151], v[168:171], v[116:119]
	s_waitcnt vmcnt(6) lgkmcnt(0)
	s_barrier
	s_waitcnt lgkmcnt(7)
	ds_read_b128 v[136:139], v19
	ds_read_b128 v[156:159], v21
	ds_read_b128 v[160:163], v21 offset:2048
	ds_read_b128 v[164:167], v21 offset:4096
	ds_read_b128 v[168:171], v21 offset:6144
	ds_read_b128 v[140:143], v19 offset:2048
	ds_read_b128 v[144:147], v19 offset:4096
	ds_read_b128 v[148:151], v19 offset:6144
	s_waitcnt lgkmcnt(14)
	v_mfma_f32_16x16x32_f16 v[56:59], v[172:175], v[192:195], v[56:59]
	s_waitcnt lgkmcnt(13)
	v_mfma_f32_16x16x32_f16 v[60:63], v[172:175], v[196:199], v[60:63]
	s_waitcnt lgkmcnt(12)
	v_mfma_f32_16x16x32_f16 v[64:67], v[172:175], v[200:203], v[64:67]
	s_waitcnt lgkmcnt(11)
	v_mfma_f32_16x16x32_f16 v[68:71], v[172:175], v[204:207], v[68:71]
	s_waitcnt lgkmcnt(10)
	v_mfma_f32_16x16x32_f16 v[72:75], v[176:179], v[192:195], v[72:75]
	v_mfma_f32_16x16x32_f16 v[76:79], v[176:179], v[196:199], v[76:79]
	v_mfma_f32_16x16x32_f16 v[80:83], v[176:179], v[200:203], v[80:83]
	v_mfma_f32_16x16x32_f16 v[84:87], v[176:179], v[204:207], v[84:87]
	s_waitcnt lgkmcnt(9)
	v_mfma_f32_16x16x32_f16 v[88:91], v[180:183], v[192:195], v[88:91]
	v_mfma_f32_16x16x32_f16 v[92:95], v[180:183], v[196:199], v[92:95]
	v_mfma_f32_16x16x32_f16 v[96:99], v[180:183], v[200:203], v[96:99]
	v_mfma_f32_16x16x32_f16 v[100:103], v[180:183], v[204:207], v[100:103]
	s_waitcnt lgkmcnt(8)
	v_mfma_f32_16x16x32_f16 v[104:107], v[184:187], v[192:195], v[104:107]
	v_mfma_f32_16x16x32_f16 v[108:111], v[184:187], v[196:199], v[108:111]
	v_mfma_f32_16x16x32_f16 v[112:115], v[184:187], v[200:203], v[112:115]
	v_mfma_f32_16x16x32_f16 v[116:119], v[184:187], v[204:207], v[116:119]
	s_waitcnt lgkmcnt(7)
	ds_read_b128 v[172:175], v20
	ds_read_b128 v[192:195], v22
	ds_read_b128 v[196:199], v22 offset:2048
	ds_read_b128 v[200:203], v22 offset:4096
	ds_read_b128 v[204:207], v22 offset:6144
	ds_read_b128 v[176:179], v20 offset:2048
	ds_read_b128 v[180:183], v20 offset:4096
	ds_read_b128 v[184:187], v20 offset:6144
	s_waitcnt lgkmcnt(14)
	v_mfma_f32_16x16x32_f16 v[56:59], v[136:139], v[156:159], v[56:59]
	s_waitcnt lgkmcnt(13)
	v_mfma_f32_16x16x32_f16 v[60:63], v[136:139], v[160:163], v[60:63]
	s_waitcnt lgkmcnt(12)
	v_mfma_f32_16x16x32_f16 v[64:67], v[136:139], v[164:167], v[64:67]
	s_waitcnt lgkmcnt(11)
	v_mfma_f32_16x16x32_f16 v[68:71], v[136:139], v[168:171], v[68:71]
	s_waitcnt lgkmcnt(10)
	v_mfma_f32_16x16x32_f16 v[72:75], v[140:143], v[156:159], v[72:75]
	v_mfma_f32_16x16x32_f16 v[76:79], v[140:143], v[160:163], v[76:79]
	v_mfma_f32_16x16x32_f16 v[80:83], v[140:143], v[164:167], v[80:83]
	v_mfma_f32_16x16x32_f16 v[84:87], v[140:143], v[168:171], v[84:87]
	s_waitcnt lgkmcnt(9)
	v_mfma_f32_16x16x32_f16 v[88:91], v[144:147], v[156:159], v[88:91]
	v_mfma_f32_16x16x32_f16 v[92:95], v[144:147], v[160:163], v[92:95]
	v_mfma_f32_16x16x32_f16 v[96:99], v[144:147], v[164:167], v[96:99]
	v_mfma_f32_16x16x32_f16 v[100:103], v[144:147], v[168:171], v[100:103]
	s_waitcnt lgkmcnt(8)
	v_mfma_f32_16x16x32_f16 v[104:107], v[148:151], v[156:159], v[104:107]
	v_mfma_f32_16x16x32_f16 v[108:111], v[148:151], v[160:163], v[108:111]
	v_mfma_f32_16x16x32_f16 v[112:115], v[148:151], v[164:167], v[112:115]
	v_mfma_f32_16x16x32_f16 v[116:119], v[148:151], v[168:171], v[116:119]
	s_waitcnt vmcnt(0) lgkmcnt(0)
	s_barrier
	s_waitcnt lgkmcnt(7)
	ds_read_b128 v[136:139], v15
	ds_read_b128 v[156:159], v17
	ds_read_b128 v[160:163], v17 offset:2048
	ds_read_b128 v[164:167], v17 offset:4096
	ds_read_b128 v[168:171], v17 offset:6144
	ds_read_b128 v[140:143], v15 offset:2048
	ds_read_b128 v[144:147], v15 offset:4096
	ds_read_b128 v[148:151], v15 offset:6144
	s_waitcnt lgkmcnt(14)
	v_mfma_f32_16x16x32_f16 v[56:59], v[172:175], v[192:195], v[56:59]
	s_waitcnt lgkmcnt(13)
	v_mfma_f32_16x16x32_f16 v[60:63], v[172:175], v[196:199], v[60:63]
	s_waitcnt lgkmcnt(12)
	v_mfma_f32_16x16x32_f16 v[64:67], v[172:175], v[200:203], v[64:67]
	s_waitcnt lgkmcnt(11)
	v_mfma_f32_16x16x32_f16 v[68:71], v[172:175], v[204:207], v[68:71]
	s_waitcnt lgkmcnt(10)
	v_mfma_f32_16x16x32_f16 v[72:75], v[176:179], v[192:195], v[72:75]
	v_mfma_f32_16x16x32_f16 v[76:79], v[176:179], v[196:199], v[76:79]
	v_mfma_f32_16x16x32_f16 v[80:83], v[176:179], v[200:203], v[80:83]
	v_mfma_f32_16x16x32_f16 v[84:87], v[176:179], v[204:207], v[84:87]
	s_waitcnt lgkmcnt(9)
	v_mfma_f32_16x16x32_f16 v[88:91], v[180:183], v[192:195], v[88:91]
	v_mfma_f32_16x16x32_f16 v[92:95], v[180:183], v[196:199], v[92:95]
	v_mfma_f32_16x16x32_f16 v[96:99], v[180:183], v[200:203], v[96:99]
	v_mfma_f32_16x16x32_f16 v[100:103], v[180:183], v[204:207], v[100:103]
	s_waitcnt lgkmcnt(8)
	v_mfma_f32_16x16x32_f16 v[104:107], v[184:187], v[192:195], v[104:107]
	v_mfma_f32_16x16x32_f16 v[108:111], v[184:187], v[196:199], v[108:111]
	v_mfma_f32_16x16x32_f16 v[112:115], v[184:187], v[200:203], v[112:115]
	v_mfma_f32_16x16x32_f16 v[116:119], v[184:187], v[204:207], v[116:119]
	s_waitcnt lgkmcnt(7)
	ds_read_b128 v[172:175], v16
	ds_read_b128 v[192:195], v18
	ds_read_b128 v[196:199], v18 offset:2048
	ds_read_b128 v[200:203], v18 offset:4096
	ds_read_b128 v[204:207], v18 offset:6144
	ds_read_b128 v[176:179], v16 offset:2048
	ds_read_b128 v[180:183], v16 offset:4096
	ds_read_b128 v[184:187], v16 offset:6144
	s_waitcnt lgkmcnt(14)
	v_mfma_f32_16x16x32_f16 v[56:59], v[136:139], v[156:159], v[56:59]
	s_waitcnt lgkmcnt(13)
	v_mfma_f32_16x16x32_f16 v[60:63], v[136:139], v[160:163], v[60:63]
	s_waitcnt lgkmcnt(12)
	v_mfma_f32_16x16x32_f16 v[64:67], v[136:139], v[164:167], v[64:67]
	s_waitcnt lgkmcnt(11)
	v_mfma_f32_16x16x32_f16 v[68:71], v[136:139], v[168:171], v[68:71]
	s_waitcnt lgkmcnt(10)
	v_mfma_f32_16x16x32_f16 v[72:75], v[140:143], v[156:159], v[72:75]
	v_mfma_f32_16x16x32_f16 v[76:79], v[140:143], v[160:163], v[76:79]
	v_mfma_f32_16x16x32_f16 v[80:83], v[140:143], v[164:167], v[80:83]
	v_mfma_f32_16x16x32_f16 v[84:87], v[140:143], v[168:171], v[84:87]
	s_waitcnt lgkmcnt(9)
	v_mfma_f32_16x16x32_f16 v[88:91], v[144:147], v[156:159], v[88:91]
	v_mfma_f32_16x16x32_f16 v[92:95], v[144:147], v[160:163], v[92:95]
	v_mfma_f32_16x16x32_f16 v[96:99], v[144:147], v[164:167], v[96:99]
	v_mfma_f32_16x16x32_f16 v[100:103], v[144:147], v[168:171], v[100:103]
	s_waitcnt lgkmcnt(8)
	v_mfma_f32_16x16x32_f16 v[104:107], v[148:151], v[156:159], v[104:107]
	v_mfma_f32_16x16x32_f16 v[108:111], v[148:151], v[160:163], v[108:111]
	v_mfma_f32_16x16x32_f16 v[112:115], v[148:151], v[164:167], v[112:115]
	v_mfma_f32_16x16x32_f16 v[116:119], v[148:151], v[168:171], v[116:119]
	s_waitcnt lgkmcnt(6)
	v_mfma_f32_16x16x32_f16 v[56:59], v[172:175], v[192:195], v[56:59]
	s_waitcnt lgkmcnt(5)
	v_mfma_f32_16x16x32_f16 v[60:63], v[172:175], v[196:199], v[60:63]
	s_waitcnt lgkmcnt(4)
	v_mfma_f32_16x16x32_f16 v[64:67], v[172:175], v[200:203], v[64:67]
	s_waitcnt lgkmcnt(3)
	v_mfma_f32_16x16x32_f16 v[68:71], v[172:175], v[204:207], v[68:71]
	s_waitcnt lgkmcnt(2)
	v_mfma_f32_16x16x32_f16 v[72:75], v[176:179], v[192:195], v[72:75]
	v_mfma_f32_16x16x32_f16 v[76:79], v[176:179], v[196:199], v[76:79]
	v_mfma_f32_16x16x32_f16 v[80:83], v[176:179], v[200:203], v[80:83]
	v_mfma_f32_16x16x32_f16 v[84:87], v[176:179], v[204:207], v[84:87]
	s_waitcnt lgkmcnt(1)
	v_mfma_f32_16x16x32_f16 v[88:91], v[180:183], v[192:195], v[88:91]
	v_mfma_f32_16x16x32_f16 v[92:95], v[180:183], v[196:199], v[92:95]
	v_mfma_f32_16x16x32_f16 v[96:99], v[180:183], v[200:203], v[96:99]
	v_mfma_f32_16x16x32_f16 v[100:103], v[180:183], v[204:207], v[100:103]
	s_waitcnt lgkmcnt(0)
	v_mfma_f32_16x16x32_f16 v[104:107], v[184:187], v[192:195], v[104:107]
	v_mfma_f32_16x16x32_f16 v[108:111], v[184:187], v[196:199], v[108:111]
	v_mfma_f32_16x16x32_f16 v[112:115], v[184:187], v[200:203], v[112:115]
	v_mfma_f32_16x16x32_f16 v[116:119], v[184:187], v[204:207], v[116:119]
	s_nop 7
	s_nop 1
	s_add_u32 s24, s29, 0
	s_lshl_b32 s8, s24, 11
	v_add_u32_e32 v212, s8, v23
	v_pk_add_f32 v[56:57], v[56:57], v[24:25] op_sel_hi:[1,0]
	v_pk_add_f32 v[58:59], v[58:59], v[24:25] op_sel_hi:[1,0]
	v_cvt_pk_f16_f32 v56, v56, v57
	v_cvt_pk_f16_f32 v57, v58, v59
	global_store_dwordx2 v212, v[56:57], s[22:23] offset:0
	v_pk_add_f32 v[60:61], v[60:61], v[26:27] op_sel_hi:[1,0]
	v_pk_add_f32 v[62:63], v[62:63], v[26:27] op_sel_hi:[1,0]
	v_cvt_pk_f16_f32 v60, v60, v61
	v_cvt_pk_f16_f32 v61, v62, v63
	global_store_dwordx2 v212, v[60:61], s[22:23] offset:256
	v_pk_add_f32 v[64:65], v[64:65], v[28:29] op_sel_hi:[1,0]
	v_pk_add_f32 v[66:67], v[66:67], v[28:29] op_sel_hi:[1,0]
	v_cvt_pk_f16_f32 v64, v64, v65
	v_cvt_pk_f16_f32 v65, v66, v67
	global_store_dwordx2 v212, v[64:65], s[22:23] offset:1024
	v_pk_add_f32 v[68:69], v[68:69], v[30:31] op_sel_hi:[1,0]
	v_pk_add_f32 v[70:71], v[70:71], v[30:31] op_sel_hi:[1,0]
	v_cvt_pk_f16_f32 v68, v68, v69
	v_cvt_pk_f16_f32 v69, v70, v71
	global_store_dwordx2 v212, v[68:69], s[22:23] offset:1280
	s_add_u32 s24, s29, 1
	s_lshl_b32 s8, s24, 11
	v_add_u32_e32 v212, s8, v23
	v_pk_add_f32 v[72:73], v[72:73], v[24:25] op_sel_hi:[1,0]
	v_pk_add_f32 v[74:75], v[74:75], v[24:25] op_sel_hi:[1,0]
	v_cvt_pk_f16_f32 v72, v72, v73
	v_cvt_pk_f16_f32 v73, v74, v75
	global_store_dwordx2 v212, v[72:73], s[22:23] offset:0
	v_pk_add_f32 v[76:77], v[76:77], v[26:27] op_sel_hi:[1,0]
	v_pk_add_f32 v[78:79], v[78:79], v[26:27] op_sel_hi:[1,0]
	v_cvt_pk_f16_f32 v76, v76, v77
	v_cvt_pk_f16_f32 v77, v78, v79
	global_store_dwordx2 v212, v[76:77], s[22:23] offset:256
	v_pk_add_f32 v[80:81], v[80:81], v[28:29] op_sel_hi:[1,0]
	v_pk_add_f32 v[82:83], v[82:83], v[28:29] op_sel_hi:[1,0]
	v_cvt_pk_f16_f32 v80, v80, v81
	v_cvt_pk_f16_f32 v81, v82, v83
	global_store_dwordx2 v212, v[80:81], s[22:23] offset:1024
	v_pk_add_f32 v[84:85], v[84:85], v[30:31] op_sel_hi:[1,0]
	v_pk_add_f32 v[86:87], v[86:87], v[30:31] op_sel_hi:[1,0]
	v_cvt_pk_f16_f32 v84, v84, v85
	v_cvt_pk_f16_f32 v85, v86, v87
	global_store_dwordx2 v212, v[84:85], s[22:23] offset:1280
	s_add_u32 s24, s29, 2
	s_lshl_b32 s8, s24, 11
	v_add_u32_e32 v212, s8, v23
	v_pk_add_f32 v[88:89], v[88:89], v[24:25] op_sel_hi:[1,0]
	v_pk_add_f32 v[90:91], v[90:91], v[24:25] op_sel_hi:[1,0]
	v_cvt_pk_f16_f32 v88, v88, v89
	v_cvt_pk_f16_f32 v89, v90, v91
	global_store_dwordx2 v212, v[88:89], s[22:23] offset:0
	v_pk_add_f32 v[92:93], v[92:93], v[26:27] op_sel_hi:[1,0]
	v_pk_add_f32 v[94:95], v[94:95], v[26:27] op_sel_hi:[1,0]
	v_cvt_pk_f16_f32 v92, v92, v93
	v_cvt_pk_f16_f32 v93, v94, v95
	global_store_dwordx2 v212, v[92:93], s[22:23] offset:256
	v_pk_add_f32 v[96:97], v[96:97], v[28:29] op_sel_hi:[1,0]
	v_pk_add_f32 v[98:99], v[98:99], v[28:29] op_sel_hi:[1,0]
	v_cvt_pk_f16_f32 v96, v96, v97
	v_cvt_pk_f16_f32 v97, v98, v99
	global_store_dwordx2 v212, v[96:97], s[22:23] offset:1024
	v_pk_add_f32 v[100:101], v[100:101], v[30:31] op_sel_hi:[1,0]
	v_pk_add_f32 v[102:103], v[102:103], v[30:31] op_sel_hi:[1,0]
	v_cvt_pk_f16_f32 v100, v100, v101
	v_cvt_pk_f16_f32 v101, v102, v103
	global_store_dwordx2 v212, v[100:101], s[22:23] offset:1280
	s_add_u32 s24, s29, 3
	s_lshl_b32 s8, s24, 11
	v_add_u32_e32 v212, s8, v23
	v_pk_add_f32 v[104:105], v[104:105], v[24:25] op_sel_hi:[1,0]
	v_pk_add_f32 v[106:107], v[106:107], v[24:25] op_sel_hi:[1,0]
	v_cvt_pk_f16_f32 v104, v104, v105
	v_cvt_pk_f16_f32 v105, v106, v107
	global_store_dwordx2 v212, v[104:105], s[22:23] offset:0
	v_pk_add_f32 v[108:109], v[108:109], v[26:27] op_sel_hi:[1,0]
	v_pk_add_f32 v[110:111], v[110:111], v[26:27] op_sel_hi:[1,0]
	v_cvt_pk_f16_f32 v108, v108, v109
	v_cvt_pk_f16_f32 v109, v110, v111
	global_store_dwordx2 v212, v[108:109], s[22:23] offset:256
	v_pk_add_f32 v[112:113], v[112:113], v[28:29] op_sel_hi:[1,0]
	v_pk_add_f32 v[114:115], v[114:115], v[28:29] op_sel_hi:[1,0]
	v_cvt_pk_f16_f32 v112, v112, v113
	v_cvt_pk_f16_f32 v113, v114, v115
	global_store_dwordx2 v212, v[112:113], s[22:23] offset:1024
	v_pk_add_f32 v[116:117], v[116:117], v[30:31] op_sel_hi:[1,0]
	v_pk_add_f32 v[118:119], v[118:119], v[30:31] op_sel_hi:[1,0]
	v_cvt_pk_f16_f32 v116, v116, v117
	v_cvt_pk_f16_f32 v117, v118, v119
	global_store_dwordx2 v212, v[116:117], s[22:23] offset:1280
	s_branch .Lpf_done
